# GEMM main loops: per-phase s_setprio 1/0 toggles around the MFMA blocks removed (all waves at equal priority)
# speedup vs baseline: 1.0146x; 1.0024x over previous
.LBB0_310:
	s_add_u32 s31, s2, s6
	s_addc_u32 s38, s3, s7
	s_add_u32 s42, s31, 0x100
	s_addc_u32 s43, s38, 0
	ds_read_b128 v[132:135], v174
	ds_read_b128 v[136:139], v174 offset:1024
	ds_read_b128 v[140:143], v174 offset:2048
	ds_read_b128 v[144:147], v174 offset:3072
	s_add_u32 s39, s0, s6
	s_addc_u32 s40, s1, s7
	s_add_u32 s10, s39, 0x40080
	s_addc_u32 s11, s40, 0
	s_add_u32 s44, s39, 0x60080
	s_addc_u32 s45, s40, 0
	ds_read_b128 v[148:151], v175
	ds_read_b128 v[152:155], v175 offset:1024
	ds_read_b128 v[156:159], v175 offset:2048
	ds_read_b128 v[160:163], v175 offset:3072
	ds_read_b128 v[168:171], v175 offset:4096
	ds_read_b128 v[180:183], v175 offset:5120
	ds_read_b128 v[184:187], v175 offset:6144
	ds_read_b128 v[188:191], v175 offset:7168
	s_nop 0
	v_lshl_add_u64 v[164:165], s[10:11], 0, v[166:167]
	s_add_i32 s11, s65, 0xc000
	s_mov_b32 m0, s11
	s_add_i32 s10, s65, 0xe000
	global_load_lds_dwordx4 v[164:165], off
	v_lshl_add_u64 v[164:165], s[44:45], 0, v[166:167]
	s_mov_b32 m0, s10
	s_nop 0
	global_load_lds_dwordx4 v[164:165], off
	s_waitcnt lgkmcnt(8)
	s_barrier
	s_waitcnt lgkmcnt(0)
	s_waitcnt lgkmcnt(0)
	v_mfma_f32_16x16x32_bf16 v[128:131], v[132:135], v[148:151], v[128:131]
	v_mfma_f32_16x16x32_bf16 v[124:127], v[140:143], v[148:151], v[124:127]
	v_mfma_f32_16x16x32_bf16 v[120:123], v[132:135], v[156:159], v[120:123]
	v_mfma_f32_16x16x32_bf16 v[116:119], v[140:143], v[156:159], v[116:119]
	v_mfma_f32_16x16x32_bf16 v[112:115], v[132:135], v[168:171], v[112:115]
	v_mfma_f32_16x16x32_bf16 v[108:111], v[140:143], v[168:171], v[108:111]
	v_mfma_f32_16x16x32_bf16 v[104:107], v[132:135], v[184:187], v[104:107]
	v_mfma_f32_16x16x32_bf16 v[100:103], v[140:143], v[184:187], v[100:103]
	v_mfma_f32_16x16x32_bf16 v[128:131], v[136:139], v[152:155], v[128:131]
	v_mfma_f32_16x16x32_bf16 v[124:127], v[144:147], v[152:155], v[124:127]
	v_mfma_f32_16x16x32_bf16 v[120:123], v[136:139], v[160:163], v[120:123]
	v_mfma_f32_16x16x32_bf16 v[116:119], v[144:147], v[160:163], v[116:119]
	v_mfma_f32_16x16x32_bf16 v[112:115], v[136:139], v[180:183], v[112:115]
	v_mfma_f32_16x16x32_bf16 v[108:111], v[144:147], v[180:183], v[108:111]
	v_mfma_f32_16x16x32_bf16 v[104:107], v[136:139], v[188:191], v[104:107]
	v_mfma_f32_16x16x32_bf16 v[100:103], v[144:147], v[188:191], v[100:103]
	s_barrier
	s_add_u32 s44, s31, 0x20100
	s_addc_u32 s45, s38, 0
	s_mov_b32 m0, s63
	ds_read_b128 v[192:195], v176
	ds_read_b128 v[196:199], v176 offset:1024
	ds_read_b128 v[200:203], v176 offset:2048
	ds_read_b128 v[204:207], v176 offset:3072
	s_nop 0
	v_lshl_add_u64 v[164:165], s[42:43], 0, v[166:167]
	global_load_lds_dwordx4 v[164:165], off
	v_lshl_add_u64 v[164:165], s[44:45], 0, v[166:167]
	s_mov_b32 m0, s64
	s_nop 0
	global_load_lds_dwordx4 v[164:165], off
	s_barrier
	s_waitcnt lgkmcnt(0)
	s_waitcnt lgkmcnt(0)
	v_mfma_f32_16x16x32_bf16 v[96:99], v[192:195], v[148:151], v[96:99]
	v_mfma_f32_16x16x32_bf16 v[92:95], v[200:203], v[148:151], v[92:95]
	v_mfma_f32_16x16x32_bf16 v[88:91], v[192:195], v[156:159], v[88:91]
	v_mfma_f32_16x16x32_bf16 v[84:87], v[200:203], v[156:159], v[84:87]
	v_mfma_f32_16x16x32_bf16 v[80:83], v[192:195], v[168:171], v[80:83]
	v_mfma_f32_16x16x32_bf16 v[76:79], v[200:203], v[168:171], v[76:79]
	v_mfma_f32_16x16x32_bf16 v[72:75], v[192:195], v[184:187], v[72:75]
	v_mfma_f32_16x16x32_bf16 v[68:71], v[200:203], v[184:187], v[68:71]
	v_mfma_f32_16x16x32_bf16 v[96:99], v[196:199], v[152:155], v[96:99]
	v_mfma_f32_16x16x32_bf16 v[92:95], v[204:207], v[152:155], v[92:95]
	v_mfma_f32_16x16x32_bf16 v[88:91], v[196:199], v[160:163], v[88:91]
	v_mfma_f32_16x16x32_bf16 v[84:87], v[204:207], v[160:163], v[84:87]
	v_mfma_f32_16x16x32_bf16 v[80:83], v[196:199], v[180:183], v[80:83]
	v_mfma_f32_16x16x32_bf16 v[76:79], v[204:207], v[180:183], v[76:79]
	v_mfma_f32_16x16x32_bf16 v[72:75], v[196:199], v[188:191], v[72:75]
	v_mfma_f32_16x16x32_bf16 v[68:71], v[204:207], v[188:191], v[68:71]
	s_barrier
	s_add_u32 s42, s39, 0x100
	s_addc_u32 s43, s40, 0
	s_add_u32 s44, s39, 0x20100
	s_addc_u32 s45, s40, 0
	s_mov_b32 m0, s65
	ds_read_b128 v[148:151], v175 offset:16384
	ds_read_b128 v[152:155], v175 offset:17408
	ds_read_b128 v[156:159], v175 offset:18432
	ds_read_b128 v[160:163], v175 offset:19456
	ds_read_b128 v[168:171], v175 offset:20480
	ds_read_b128 v[180:183], v175 offset:21504
	ds_read_b128 v[184:187], v175 offset:22528
	ds_read_b128 v[188:191], v175 offset:23552
	s_nop 0
	v_lshl_add_u64 v[164:165], s[42:43], 0, v[166:167]
	global_load_lds_dwordx4 v[164:165], off
	v_lshl_add_u64 v[164:165], s[44:45], 0, v[166:167]
	s_mov_b32 m0, s66
	s_nop 0
	global_load_lds_dwordx4 v[164:165], off
	s_barrier
	s_waitcnt lgkmcnt(0)
	s_waitcnt lgkmcnt(0)
	v_mfma_f32_16x16x32_bf16 v[64:67], v[132:135], v[148:151], v[64:67]
	v_mfma_f32_16x16x32_bf16 v[60:63], v[140:143], v[148:151], v[60:63]
	v_mfma_f32_16x16x32_bf16 v[56:59], v[132:135], v[156:159], v[56:59]
	v_mfma_f32_16x16x32_bf16 v[52:55], v[140:143], v[156:159], v[52:55]
	v_mfma_f32_16x16x32_bf16 v[48:51], v[132:135], v[168:171], v[48:51]
	v_mfma_f32_16x16x32_bf16 v[44:47], v[140:143], v[168:171], v[44:47]
	v_mfma_f32_16x16x32_bf16 v[40:43], v[132:135], v[184:187], v[40:43]
	v_mfma_f32_16x16x32_bf16 v[36:39], v[140:143], v[184:187], v[36:39]
	v_mfma_f32_16x16x32_bf16 v[64:67], v[136:139], v[152:155], v[64:67]
	v_mfma_f32_16x16x32_bf16 v[60:63], v[144:147], v[152:155], v[60:63]
	v_mfma_f32_16x16x32_bf16 v[56:59], v[136:139], v[160:163], v[56:59]
	v_mfma_f32_16x16x32_bf16 v[52:55], v[144:147], v[160:163], v[52:55]
	v_mfma_f32_16x16x32_bf16 v[48:51], v[136:139], v[180:183], v[48:51]
	v_mfma_f32_16x16x32_bf16 v[44:47], v[144:147], v[180:183], v[44:47]
	v_mfma_f32_16x16x32_bf16 v[40:43], v[136:139], v[188:191], v[40:43]
	v_mfma_f32_16x16x32_bf16 v[36:39], v[144:147], v[188:191], v[36:39]
	s_barrier
	s_add_u32 s42, s31, 0x40100
	s_addc_u32 s43, s38, 0
	s_add_u32 s44, s31, 0x60100
	s_addc_u32 s45, s38, 0
	s_mov_b32 m0, s67
	s_nop 0
	v_lshl_add_u64 v[132:133], s[42:43], 0, v[166:167]
	global_load_lds_dwordx4 v[132:133], off
	v_lshl_add_u64 v[132:133], s[44:45], 0, v[166:167]
	s_mov_b32 m0, s68
	s_nop 0
	global_load_lds_dwordx4 v[132:133], off
	s_waitcnt vmcnt(6)
	s_barrier
	v_mfma_f32_16x16x32_bf16 v[30:33], v[192:195], v[148:151], v[30:33]
	v_mfma_f32_16x16x32_bf16 v[26:29], v[200:203], v[148:151], v[26:29]
	v_mfma_f32_16x16x32_bf16 v[22:25], v[192:195], v[156:159], v[22:25]
	v_mfma_f32_16x16x32_bf16 v[18:21], v[200:203], v[156:159], v[18:21]
	v_mfma_f32_16x16x32_bf16 v[14:17], v[192:195], v[168:171], v[14:17]
	v_mfma_f32_16x16x32_bf16 v[10:13], v[200:203], v[168:171], v[10:13]
	v_mfma_f32_16x16x32_bf16 v[6:9], v[192:195], v[184:187], v[6:9]
	v_mfma_f32_16x16x32_bf16 v[2:5], v[200:203], v[184:187], v[2:5]
	v_mfma_f32_16x16x32_bf16 v[30:33], v[196:199], v[152:155], v[30:33]
	v_mfma_f32_16x16x32_bf16 v[26:29], v[204:207], v[152:155], v[26:29]
	v_mfma_f32_16x16x32_bf16 v[22:25], v[196:199], v[160:163], v[22:25]
	v_mfma_f32_16x16x32_bf16 v[18:21], v[204:207], v[160:163], v[18:21]
	v_mfma_f32_16x16x32_bf16 v[14:17], v[196:199], v[180:183], v[14:17]
	v_mfma_f32_16x16x32_bf16 v[10:13], v[204:207], v[180:183], v[10:13]
	v_mfma_f32_16x16x32_bf16 v[6:9], v[196:199], v[188:191], v[6:9]
	v_mfma_f32_16x16x32_bf16 v[2:5], v[204:207], v[188:191], v[2:5]
	s_barrier
	ds_read_b128 v[132:135], v177
	ds_read_b128 v[136:139], v177 offset:1024
	ds_read_b128 v[140:143], v177 offset:2048
	ds_read_b128 v[144:147], v177 offset:3072
	s_add_u32 s42, s39, 0x40100
	s_addc_u32 s43, s40, 0
	s_add_u32 s44, s39, 0x60100
	s_addc_u32 s45, s40, 0
	s_mov_b32 m0, s69
	ds_read_b128 v[148:151], v175 offset:32768
	ds_read_b128 v[152:155], v175 offset:33792
	ds_read_b128 v[156:159], v175 offset:34816
	ds_read_b128 v[160:163], v175 offset:35840
	ds_read_b128 v[168:171], v175 offset:36864
	ds_read_b128 v[180:183], v175 offset:37888
	ds_read_b128 v[184:187], v175 offset:38912
	ds_read_b128 v[188:191], v175 offset:39936
	s_nop 0
	v_lshl_add_u64 v[164:165], s[42:43], 0, v[166:167]
	global_load_lds_dwordx4 v[164:165], off
	v_lshl_add_u64 v[164:165], s[44:45], 0, v[166:167]
	s_mov_b32 m0, s70
	s_nop 0
	global_load_lds_dwordx4 v[164:165], off
	s_waitcnt lgkmcnt(8)
	s_barrier
	s_waitcnt lgkmcnt(0)
	s_waitcnt lgkmcnt(0)
	v_mfma_f32_16x16x32_bf16 v[128:131], v[132:135], v[148:151], v[128:131]
	v_mfma_f32_16x16x32_bf16 v[124:127], v[140:143], v[148:151], v[124:127]
	v_mfma_f32_16x16x32_bf16 v[120:123], v[132:135], v[156:159], v[120:123]
	v_mfma_f32_16x16x32_bf16 v[116:119], v[140:143], v[156:159], v[116:119]
	v_mfma_f32_16x16x32_bf16 v[112:115], v[132:135], v[168:171], v[112:115]
	v_mfma_f32_16x16x32_bf16 v[108:111], v[140:143], v[168:171], v[108:111]
	v_mfma_f32_16x16x32_bf16 v[104:107], v[132:135], v[184:187], v[104:107]
	v_mfma_f32_16x16x32_bf16 v[100:103], v[140:143], v[184:187], v[100:103]
	v_mfma_f32_16x16x32_bf16 v[128:131], v[136:139], v[152:155], v[128:131]
	v_mfma_f32_16x16x32_bf16 v[124:127], v[144:147], v[152:155], v[124:127]
	v_mfma_f32_16x16x32_bf16 v[120:123], v[136:139], v[160:163], v[120:123]
	v_mfma_f32_16x16x32_bf16 v[116:119], v[144:147], v[160:163], v[116:119]
	v_mfma_f32_16x16x32_bf16 v[112:115], v[136:139], v[180:183], v[112:115]
	v_mfma_f32_16x16x32_bf16 v[108:111], v[144:147], v[180:183], v[108:111]
	v_mfma_f32_16x16x32_bf16 v[104:107], v[136:139], v[188:191], v[104:107]
	v_mfma_f32_16x16x32_bf16 v[100:103], v[144:147], v[188:191], v[100:103]
	s_barrier
	s_add_u32 s42, s31, 0x180
	s_addc_u32 s43, s38, 0
	s_add_u32 s44, s31, 0x20180
	s_addc_u32 s45, s38, 0
	s_mov_b32 m0, s71
	ds_read_b128 v[192:195], v178
	ds_read_b128 v[196:199], v178 offset:1024
	ds_read_b128 v[200:203], v178 offset:2048
	ds_read_b128 v[204:207], v178 offset:3072
	s_nop 0
	v_lshl_add_u64 v[164:165], s[42:43], 0, v[166:167]
	global_load_lds_dwordx4 v[164:165], off
	v_lshl_add_u64 v[164:165], s[44:45], 0, v[166:167]
	s_mov_b32 m0, s72
	s_nop 0
	global_load_lds_dwordx4 v[164:165], off
	s_barrier
	s_waitcnt lgkmcnt(0)
	s_waitcnt lgkmcnt(0)
	v_mfma_f32_16x16x32_bf16 v[96:99], v[192:195], v[148:151], v[96:99]
	v_mfma_f32_16x16x32_bf16 v[92:95], v[200:203], v[148:151], v[92:95]
	v_mfma_f32_16x16x32_bf16 v[88:91], v[192:195], v[156:159], v[88:91]
	v_mfma_f32_16x16x32_bf16 v[84:87], v[200:203], v[156:159], v[84:87]
	v_mfma_f32_16x16x32_bf16 v[80:83], v[192:195], v[168:171], v[80:83]
	v_mfma_f32_16x16x32_bf16 v[76:79], v[200:203], v[168:171], v[76:79]
	v_mfma_f32_16x16x32_bf16 v[72:75], v[192:195], v[184:187], v[72:75]
	v_mfma_f32_16x16x32_bf16 v[68:71], v[200:203], v[184:187], v[68:71]
	v_mfma_f32_16x16x32_bf16 v[96:99], v[196:199], v[152:155], v[96:99]
	v_mfma_f32_16x16x32_bf16 v[92:95], v[204:207], v[152:155], v[92:95]
	v_mfma_f32_16x16x32_bf16 v[88:91], v[196:199], v[160:163], v[88:91]
	v_mfma_f32_16x16x32_bf16 v[84:87], v[204:207], v[160:163], v[84:87]
	v_mfma_f32_16x16x32_bf16 v[80:83], v[196:199], v[180:183], v[80:83]
	v_mfma_f32_16x16x32_bf16 v[76:79], v[204:207], v[180:183], v[76:79]
	v_mfma_f32_16x16x32_bf16 v[72:75], v[196:199], v[188:191], v[72:75]
	v_mfma_f32_16x16x32_bf16 v[68:71], v[204:207], v[188:191], v[68:71]
	s_barrier
	s_add_u32 s42, s39, 0x180
	s_addc_u32 s43, s40, 0
	s_add_u32 s44, s39, 0x20180
	s_addc_u32 s45, s40, 0
	s_mov_b32 m0, s73
	ds_read_b128 v[148:151], v175 offset:49152
	ds_read_b128 v[152:155], v175 offset:50176
	ds_read_b128 v[156:159], v175 offset:51200
	ds_read_b128 v[160:163], v175 offset:52224
	ds_read_b128 v[168:171], v175 offset:53248
	ds_read_b128 v[180:183], v175 offset:54272
	ds_read_b128 v[184:187], v175 offset:55296
	ds_read_b128 v[188:191], v175 offset:56320
	s_nop 0
	v_lshl_add_u64 v[164:165], s[42:43], 0, v[166:167]
	global_load_lds_dwordx4 v[164:165], off
	v_lshl_add_u64 v[164:165], s[44:45], 0, v[166:167]
	s_mov_b32 m0, s74
	s_nop 0
	global_load_lds_dwordx4 v[164:165], off
	s_barrier
; __device__ __forceinline__ int tid_hidden() { int t = threadIdx.x; asm volatile("" : "+v"(t)); return t; }
; #define lds lds_hidden(lds0)
; template <class Epi, class Src>
; __device__ __forceinline__ void gemm_phase(LAS unsigned char* lds, const Src S, const Epi E) {
;     ...
;         { const int tp = tid_hidden(); E.prefetch(cur, lds, par, tp, __builtin_amdgcn_readfirstlane(tp >> 6)); }
;         if (Src::GATHER && has_next) { const int tp = tid_hidden(); tab_fill(S, nxt, tp, __builtin_amdgcn_readfirstlane(tp >> 6), lds, par ^ 1); }
;         for (int t = 0; t < NKTR - 2; t += 2) {
;             const size_t k1 = (size_t)(t + 1) * kstep, k2 = (size_t)(t + 2) * kstep;
;             const char* b2 = cB + k2; const char* b3 = b2 + kstep;
;             G8_ITER(cA, par, k1, cA, par, k2, b2, b3);
;         }
;         {
;             const int par2 = has_next ? (par ^ 1) : par;
;             const char* b3 = nB + kstep;
;             G8_ITER(cA, par, (size_t)(NKTR - 1) * kstep, nA, par2, (size_t)0, nB, b3);
	s_waitcnt lgkmcnt(0)
	s_waitcnt lgkmcnt(0)
	v_mfma_f32_16x16x32_bf16 v[64:67], v[132:135], v[148:151], v[64:67]
	v_mfma_f32_16x16x32_bf16 v[60:63], v[140:143], v[148:151], v[60:63]
	v_mfma_f32_16x16x32_bf16 v[56:59], v[132:135], v[156:159], v[56:59]
	v_mfma_f32_16x16x32_bf16 v[52:55], v[140:143], v[156:159], v[52:55]
	v_mfma_f32_16x16x32_bf16 v[48:51], v[132:135], v[168:171], v[48:51]
	v_mfma_f32_16x16x32_bf16 v[44:47], v[140:143], v[168:171], v[44:47]
	v_mfma_f32_16x16x32_bf16 v[40:43], v[132:135], v[184:187], v[40:43]
	v_mfma_f32_16x16x32_bf16 v[36:39], v[140:143], v[184:187], v[36:39]
	v_mfma_f32_16x16x32_bf16 v[64:67], v[136:139], v[152:155], v[64:67]
	v_mfma_f32_16x16x32_bf16 v[60:63], v[144:147], v[152:155], v[60:63]
	v_mfma_f32_16x16x32_bf16 v[56:59], v[136:139], v[160:163], v[56:59]
	v_mfma_f32_16x16x32_bf16 v[52:55], v[144:147], v[160:163], v[52:55]
	v_mfma_f32_16x16x32_bf16 v[48:51], v[136:139], v[180:183], v[48:51]
	v_mfma_f32_16x16x32_bf16 v[44:47], v[144:147], v[180:183], v[44:47]
	v_mfma_f32_16x16x32_bf16 v[40:43], v[136:139], v[188:191], v[40:43]
	v_mfma_f32_16x16x32_bf16 v[36:39], v[144:147], v[188:191], v[36:39]
	s_barrier
	s_add_u32 s40, s31, 0x40180
	s_addc_u32 s41, s38, 0
	s_add_u32 s42, s31, 0x60180
	s_addc_u32 s43, s38, 0
	s_mov_b32 m0, s75
	s_nop 0
	v_lshl_add_u64 v[132:133], s[40:41], 0, v[166:167]
	global_load_lds_dwordx4 v[132:133], off
	v_lshl_add_u64 v[132:133], s[42:43], 0, v[166:167]
	s_mov_b32 m0, s76
	s_nop 0
	global_load_lds_dwordx4 v[132:133], off
	s_waitcnt vmcnt(6)
	s_barrier
	v_mfma_f32_16x16x32_bf16 v[30:33], v[192:195], v[148:151], v[30:33]
	v_mfma_f32_16x16x32_bf16 v[26:29], v[200:203], v[148:151], v[26:29]
	v_mfma_f32_16x16x32_bf16 v[22:25], v[192:195], v[156:159], v[22:25]
	v_mfma_f32_16x16x32_bf16 v[18:21], v[200:203], v[156:159], v[18:21]
	v_mfma_f32_16x16x32_bf16 v[14:17], v[192:195], v[168:171], v[14:17]
	v_mfma_f32_16x16x32_bf16 v[10:13], v[200:203], v[168:171], v[10:13]
	v_mfma_f32_16x16x32_bf16 v[6:9], v[192:195], v[184:187], v[6:9]
	v_mfma_f32_16x16x32_bf16 v[2:5], v[200:203], v[184:187], v[2:5]
	v_mfma_f32_16x16x32_bf16 v[30:33], v[196:199], v[152:155], v[30:33]
	v_mfma_f32_16x16x32_bf16 v[26:29], v[204:207], v[152:155], v[26:29]
	v_mfma_f32_16x16x32_bf16 v[22:25], v[196:199], v[160:163], v[22:25]
	v_mfma_f32_16x16x32_bf16 v[18:21], v[204:207], v[160:163], v[18:21]
	v_mfma_f32_16x16x32_bf16 v[14:17], v[196:199], v[180:183], v[14:17]
	v_mfma_f32_16x16x32_bf16 v[10:13], v[204:207], v[180:183], v[10:13]
	v_mfma_f32_16x16x32_bf16 v[6:9], v[196:199], v[188:191], v[6:9]
	v_mfma_f32_16x16x32_bf16 v[2:5], v[204:207], v[188:191], v[2:5]
	s_add_i32 s9, s9, 2
	s_add_u32 s6, s6, 0x100
	s_addc_u32 s7, s7, 0
	s_cmp_gt_u32 s9, 11
	s_barrier
	s_cbranch_scc0 .LBB0_310
	s_lshl_b32 s38, s62, 8
	s_ashr_i32 s31, s30, 31
	s_ashr_i32 s39, s38, 31
	s_lshl_b64 s[6:7], s[30:31], 19
	s_lshl_b64 s[40:41], s[38:39], 11
	s_add_u32 s38, s60, s6
	s_addc_u32 s39, s61, s7
	s_add_u32 s40, s12, s40
	s_addc_u32 s41, s13, s41
	s_and_b64 s[4:5], s[4:5], exec
	s_cselect_b32 s5, s41, s1
	s_cselect_b32 s4, s40, s0
	ds_read_b128 v[132:135], v174
	ds_read_b128 v[136:139], v174 offset:1024
	ds_read_b128 v[140:143], v174 offset:2048
	ds_read_b128 v[144:147], v174 offset:3072
	s_cselect_b32 s3, s39, s3
	s_cselect_b32 s2, s38, s2
	s_add_u32 s6, s0, 0x40780
	s_addc_u32 s7, s1, 0
	s_add_u32 s0, s0, 0x60780
	s_addc_u32 s1, s1, 0
	s_mov_b32 m0, s11
	ds_read_b128 v[148:151], v175
	ds_read_b128 v[152:155], v175 offset:1024
	ds_read_b128 v[156:159], v175 offset:2048
	ds_read_b128 v[160:163], v175 offset:3072
	ds_read_b128 v[168:171], v175 offset:4096
	ds_read_b128 v[180:183], v175 offset:5120
	ds_read_b128 v[184:187], v175 offset:6144
	ds_read_b128 v[188:191], v175 offset:7168
	s_nop 0
	v_lshl_add_u64 v[164:165], s[6:7], 0, v[166:167]
	global_load_lds_dwordx4 v[164:165], off
	v_lshl_add_u64 v[164:165], s[0:1], 0, v[166:167]
	s_mov_b32 m0, s10
	s_nop 0
	global_load_lds_dwordx4 v[164:165], off
	s_waitcnt lgkmcnt(8)
	s_barrier
	s_waitcnt lgkmcnt(0)
	s_waitcnt lgkmcnt(0)
	v_mfma_f32_16x16x32_bf16 v[128:131], v[132:135], v[148:151], v[128:131]
	v_mfma_f32_16x16x32_bf16 v[124:127], v[140:143], v[148:151], v[124:127]
	v_mfma_f32_16x16x32_bf16 v[120:123], v[132:135], v[156:159], v[120:123]
	v_mfma_f32_16x16x32_bf16 v[116:119], v[140:143], v[156:159], v[116:119]
	v_mfma_f32_16x16x32_bf16 v[112:115], v[132:135], v[168:171], v[112:115]
	v_mfma_f32_16x16x32_bf16 v[108:111], v[140:143], v[168:171], v[108:111]
	v_mfma_f32_16x16x32_bf16 v[104:107], v[132:135], v[184:187], v[104:107]
	v_mfma_f32_16x16x32_bf16 v[100:103], v[140:143], v[184:187], v[100:103]
	v_mfma_f32_16x16x32_bf16 v[128:131], v[136:139], v[152:155], v[128:131]
	v_mfma_f32_16x16x32_bf16 v[124:127], v[144:147], v[152:155], v[124:127]
	v_mfma_f32_16x16x32_bf16 v[120:123], v[136:139], v[160:163], v[120:123]
	v_mfma_f32_16x16x32_bf16 v[116:119], v[144:147], v[160:163], v[116:119]
	v_mfma_f32_16x16x32_bf16 v[112:115], v[136:139], v[180:183], v[112:115]
	v_mfma_f32_16x16x32_bf16 v[108:111], v[144:147], v[180:183], v[108:111]
	v_mfma_f32_16x16x32_bf16 v[104:107], v[136:139], v[188:191], v[104:107]
	v_mfma_f32_16x16x32_bf16 v[100:103], v[144:147], v[188:191], v[100:103]
	s_barrier
	s_add_u32 s0, s2, 0x20000
	s_addc_u32 s1, s3, 0
	s_mov_b64 s[6:7], s[2:3]
	s_mov_b32 m0, s63
	ds_read_b128 v[192:195], v176
	ds_read_b128 v[196:199], v176 offset:1024
	ds_read_b128 v[200:203], v176 offset:2048
	ds_read_b128 v[204:207], v176 offset:3072
	s_nop 0
	v_lshl_add_u64 v[164:165], s[6:7], 0, v[166:167]
	global_load_lds_dwordx4 v[164:165], off
	v_lshl_add_u64 v[164:165], s[0:1], 0, v[166:167]
	s_mov_b32 m0, s64
	s_nop 0
	global_load_lds_dwordx4 v[164:165], off
	s_barrier
; template <class Epi, class Src>
; __device__ __forceinline__ void gemm_phase(LAS unsigned char* lds, const Src S, const Epi E) {
;     ...
;         {
;             const int par2 = has_next ? (par ^ 1) : par;
;             const char* b3 = nB + kstep;
;             G8_ITER(cA, par, (size_t)(NKTR - 1) * kstep, nA, par2, (size_t)0, nB, b3);
	s_waitcnt lgkmcnt(0)
	s_waitcnt lgkmcnt(0)
	v_mfma_f32_16x16x32_bf16 v[96:99], v[192:195], v[148:151], v[96:99]
	v_mfma_f32_16x16x32_bf16 v[92:95], v[200:203], v[148:151], v[92:95]
	v_mfma_f32_16x16x32_bf16 v[88:91], v[192:195], v[156:159], v[88:91]
	v_mfma_f32_16x16x32_bf16 v[84:87], v[200:203], v[156:159], v[84:87]
	v_mfma_f32_16x16x32_bf16 v[80:83], v[192:195], v[168:171], v[80:83]
	v_mfma_f32_16x16x32_bf16 v[76:79], v[200:203], v[168:171], v[76:79]
	v_mfma_f32_16x16x32_bf16 v[72:75], v[192:195], v[184:187], v[72:75]
	v_mfma_f32_16x16x32_bf16 v[96:99], v[196:199], v[152:155], v[96:99]
	v_mfma_f32_16x16x32_bf16 v[92:95], v[204:207], v[152:155], v[92:95]
	v_mfma_f32_16x16x32_bf16 v[88:91], v[196:199], v[160:163], v[88:91]
	v_mfma_f32_16x16x32_bf16 v[84:87], v[204:207], v[160:163], v[84:87]
	v_mfma_f32_16x16x32_bf16 v[80:83], v[196:199], v[180:183], v[80:83]
	v_mfma_f32_16x16x32_bf16 v[76:79], v[204:207], v[180:183], v[76:79]
	v_mfma_f32_16x16x32_bf16 v[72:75], v[196:199], v[188:191], v[72:75]
	v_mfma_f32_16x16x32_bf16 v[68:71], v[200:203], v[184:187], v[68:71]
	v_mfma_f32_16x16x32_bf16 v[148:151], v[204:207], v[188:191], v[68:71]
	s_barrier
	s_add_u32 s0, s4, 0x20000
	s_addc_u32 s1, s5, 0
	s_mov_b64 s[6:7], s[4:5]
	s_mov_b32 m0, s65
	s_nop 0
	ds_read_b128 v[68:71], v175 offset:16384
	ds_read_b128 v[152:155], v175 offset:17408
	ds_read_b128 v[156:159], v175 offset:18432
	ds_read_b128 v[160:163], v175 offset:19456
	ds_read_b128 v[168:171], v175 offset:20480
	ds_read_b128 v[180:183], v175 offset:21504
	ds_read_b128 v[184:187], v175 offset:22528
	ds_read_b128 v[188:191], v175 offset:23552
	s_nop 0
	v_lshl_add_u64 v[164:165], s[6:7], 0, v[166:167]
	global_load_lds_dwordx4 v[164:165], off
	v_lshl_add_u64 v[164:165], s[0:1], 0, v[166:167]
	s_mov_b32 m0, s66
	s_nop 0
	global_load_lds_dwordx4 v[164:165], off
	s_barrier
	s_waitcnt lgkmcnt(0)
	s_waitcnt lgkmcnt(0)
	v_mfma_f32_16x16x32_bf16 v[64:67], v[132:135], v[68:71], v[64:67]
	v_mfma_f32_16x16x32_bf16 v[60:63], v[140:143], v[68:71], v[60:63]
	v_mfma_f32_16x16x32_bf16 v[56:59], v[132:135], v[156:159], v[56:59]
	v_mfma_f32_16x16x32_bf16 v[52:55], v[140:143], v[156:159], v[52:55]
	v_mfma_f32_16x16x32_bf16 v[48:51], v[132:135], v[168:171], v[48:51]
	v_mfma_f32_16x16x32_bf16 v[44:47], v[140:143], v[168:171], v[44:47]
	v_mfma_f32_16x16x32_bf16 v[40:43], v[132:135], v[184:187], v[40:43]
	v_mfma_f32_16x16x32_bf16 v[36:39], v[140:143], v[184:187], v[36:39]
	v_mfma_f32_16x16x32_bf16 v[208:211], v[136:139], v[152:155], v[64:67]
	v_mfma_f32_16x16x32_bf16 v[212:215], v[144:147], v[152:155], v[60:63]
	v_mfma_f32_16x16x32_bf16 v[216:219], v[136:139], v[160:163], v[56:59]
	v_mfma_f32_16x16x32_bf16 v[220:223], v[144:147], v[160:163], v[52:55]
	v_mfma_f32_16x16x32_bf16 v[224:227], v[136:139], v[180:183], v[48:51]
	v_mfma_f32_16x16x32_bf16 v[228:231], v[144:147], v[180:183], v[44:47]
	v_mfma_f32_16x16x32_bf16 v[134:137], v[136:139], v[188:191], v[40:43]
	v_mfma_f32_16x16x32_bf16 v[138:141], v[144:147], v[188:191], v[36:39]
	s_barrier
	s_add_u32 s0, s2, 0x40000
	s_addc_u32 s1, s3, 0
	s_add_u32 s6, s2, 0x60000
	s_addc_u32 s7, s3, 0
	s_mov_b32 m0, s67
	s_nop 0
	v_lshl_add_u64 v[36:37], s[0:1], 0, v[166:167]
	global_load_lds_dwordx4 v[36:37], off
	v_lshl_add_u64 v[36:37], s[6:7], 0, v[166:167]
	s_mov_b32 m0, s68
	s_nop 0
	global_load_lds_dwordx4 v[36:37], off
	s_waitcnt vmcnt(6)
	s_barrier
	v_mfma_f32_16x16x32_bf16 v[30:33], v[192:195], v[68:71], v[30:33]
	v_mfma_f32_16x16x32_bf16 v[26:29], v[200:203], v[68:71], v[26:29]
	v_mfma_f32_16x16x32_bf16 v[22:25], v[192:195], v[156:159], v[22:25]
	v_mfma_f32_16x16x32_bf16 v[18:21], v[200:203], v[156:159], v[18:21]
	v_mfma_f32_16x16x32_bf16 v[14:17], v[192:195], v[168:171], v[14:17]
	v_mfma_f32_16x16x32_bf16 v[10:13], v[200:203], v[168:171], v[10:13]
	v_mfma_f32_16x16x32_bf16 v[6:9], v[192:195], v[184:187], v[6:9]
	v_mfma_f32_16x16x32_bf16 v[2:5], v[200:203], v[184:187], v[2:5]
	v_mfma_f32_16x16x32_bf16 v[30:33], v[196:199], v[152:155], v[30:33]
	v_mfma_f32_16x16x32_bf16 v[26:29], v[204:207], v[152:155], v[26:29]
	v_mfma_f32_16x16x32_bf16 v[22:25], v[196:199], v[160:163], v[22:25]
	v_mfma_f32_16x16x32_bf16 v[18:21], v[204:207], v[160:163], v[18:21]
	v_mfma_f32_16x16x32_bf16 v[14:17], v[196:199], v[180:183], v[14:17]
	v_mfma_f32_16x16x32_bf16 v[10:13], v[204:207], v[180:183], v[10:13]
	v_mfma_f32_16x16x32_bf16 v[6:9], v[196:199], v[188:191], v[6:9]
	v_mfma_f32_16x16x32_bf16 v[2:5], v[204:207], v[188:191], v[2:5]
	s_barrier
	ds_read_b128 v[142:145], v177
	ds_read_b128 v[152:155], v177 offset:1024
	ds_read_b128 v[156:159], v177 offset:2048
	ds_read_b128 v[160:163], v177 offset:3072
	s_add_u32 s0, s4, 0x40000
	s_addc_u32 s1, s5, 0
	s_add_u32 s6, s4, 0x60000
	s_addc_u32 s7, s5, 0
	s_mov_b32 m0, s69
	ds_read_b128 v[36:39], v175 offset:32768
	ds_read_b128 v[40:43], v175 offset:33792
	ds_read_b128 v[44:47], v175 offset:34816
	ds_read_b128 v[48:51], v175 offset:35840
	ds_read_b128 v[168:171], v175 offset:36864
	ds_read_b128 v[180:183], v175 offset:37888
	ds_read_b128 v[184:187], v175 offset:38912
	ds_read_b128 v[188:191], v175 offset:39936
	s_nop 0
	v_lshl_add_u64 v[52:53], s[0:1], 0, v[166:167]
	global_load_lds_dwordx4 v[52:53], off
	v_lshl_add_u64 v[52:53], s[6:7], 0, v[166:167]
	s_mov_b32 m0, s70
	s_nop 0
	global_load_lds_dwordx4 v[52:53], off
	s_waitcnt lgkmcnt(8)
	s_barrier
; __device__ __forceinline__ int tid_hidden() { int t = threadIdx.x; asm volatile("" : "+v"(t)); return t; }
; #define lds lds_hidden(lds0)
; template <class Epi, class Src>
; __device__ __forceinline__ void gemm_phase(LAS unsigned char* lds, const Src S, const Epi E) {
;     ...
;         { const int tp = tid_hidden(); E.prefetch(cur, lds, par, tp, __builtin_amdgcn_readfirstlane(tp >> 6)); }
;         if (Src::GATHER && has_next) { const int tp = tid_hidden(); tab_fill(S, nxt, tp, __builtin_amdgcn_readfirstlane(tp >> 6), lds, par ^ 1); }
;         for (int t = 0; t < NKTR - 2; t += 2) {
;             const size_t k1 = (size_t)(t + 1) * kstep, k2 = (size_t)(t + 2) * kstep;
;             const char* b2 = cB + k2; const char* b3 = b2 + kstep;
;             G8_ITER(cA, par, k1, cA, par, k2, b2, b3);
;         }
;         {
;             const int par2 = has_next ? (par ^ 1) : par;
;             const char* b3 = nB + kstep;
;             G8_ITER(cA, par, (size_t)(NKTR - 1) * kstep, nA, par2, (size_t)0, nB, b3);
	s_waitcnt lgkmcnt(0)
	s_waitcnt lgkmcnt(0)
	v_mfma_f32_16x16x32_bf16 v[52:55], v[142:145], v[36:39], v[128:131]
	v_mfma_f32_16x16x32_bf16 v[130:133], v[152:155], v[40:43], v[52:55]
	v_mfma_f32_16x16x32_bf16 v[52:55], v[156:159], v[36:39], v[124:127]
	v_mfma_f32_16x16x32_bf16 v[126:129], v[160:163], v[40:43], v[52:55]
	v_mfma_f32_16x16x32_bf16 v[52:55], v[142:145], v[44:47], v[120:123]
	v_mfma_f32_16x16x32_bf16 v[122:125], v[152:155], v[48:51], v[52:55]
	v_mfma_f32_16x16x32_bf16 v[52:55], v[156:159], v[44:47], v[116:119]
	v_mfma_f32_16x16x32_bf16 v[118:121], v[160:163], v[48:51], v[52:55]
	v_mfma_f32_16x16x32_bf16 v[52:55], v[142:145], v[168:171], v[112:115]
	v_mfma_f32_16x16x32_bf16 v[114:117], v[152:155], v[180:183], v[52:55]
	v_mfma_f32_16x16x32_bf16 v[52:55], v[156:159], v[168:171], v[108:111]
	v_mfma_f32_16x16x32_bf16 v[110:113], v[160:163], v[180:183], v[52:55]
	v_mfma_f32_16x16x32_bf16 v[52:55], v[142:145], v[184:187], v[104:107]
	v_mfma_f32_16x16x32_bf16 v[106:109], v[152:155], v[188:191], v[52:55]
	v_mfma_f32_16x16x32_bf16 v[52:55], v[156:159], v[184:187], v[100:103]
	v_mfma_f32_16x16x32_bf16 v[102:105], v[160:163], v[188:191], v[52:55]
	s_barrier
	s_add_u32 s0, s2, 0x80
	s_addc_u32 s1, s3, 0
	s_add_u32 s6, s2, 0x20080
	s_addc_u32 s7, s3, 0
	s_mov_b32 m0, s71
	ds_read_b128 v[192:195], v178
	ds_read_b128 v[196:199], v178 offset:1024
	ds_read_b128 v[200:203], v178 offset:2048
	ds_read_b128 v[204:207], v178 offset:3072
	s_nop 0
	v_lshl_add_u64 v[52:53], s[0:1], 0, v[166:167]
	global_load_lds_dwordx4 v[52:53], off
	v_lshl_add_u64 v[52:53], s[6:7], 0, v[166:167]
	s_mov_b32 m0, s72
	s_nop 0
	global_load_lds_dwordx4 v[52:53], off
	s_barrier
	s_waitcnt lgkmcnt(0)
	s_waitcnt lgkmcnt(0)
	v_mfma_f32_16x16x32_bf16 v[52:55], v[192:195], v[36:39], v[96:99]
	v_mfma_f32_16x16x32_bf16 v[36:39], v[200:203], v[36:39], v[92:95]
	v_mfma_f32_16x16x32_bf16 v[62:65], v[204:207], v[40:43], v[36:39]
	v_mfma_f32_16x16x32_bf16 v[36:39], v[192:195], v[44:47], v[88:91]
	v_mfma_f32_16x16x32_bf16 v[58:61], v[196:199], v[48:51], v[36:39]
	v_mfma_f32_16x16x32_bf16 v[36:39], v[200:203], v[44:47], v[84:87]
	v_mfma_f32_16x16x32_bf16 v[66:69], v[196:199], v[40:43], v[52:55]
	v_mfma_f32_16x16x32_bf16 v[54:57], v[204:207], v[48:51], v[36:39]
	v_mfma_f32_16x16x32_bf16 v[36:39], v[192:195], v[168:171], v[80:83]
	v_mfma_f32_16x16x32_bf16 v[50:53], v[196:199], v[180:183], v[36:39]
	v_mfma_f32_16x16x32_bf16 v[36:39], v[200:203], v[168:171], v[76:79]
	v_mfma_f32_16x16x32_bf16 v[46:49], v[204:207], v[180:183], v[36:39]
	v_mfma_f32_16x16x32_bf16 v[36:39], v[192:195], v[184:187], v[72:75]
	v_mfma_f32_16x16x32_bf16 v[42:45], v[196:199], v[188:191], v[36:39]
	v_mfma_f32_16x16x32_bf16 v[36:39], v[200:203], v[184:187], v[148:151]
	v_mfma_f32_16x16x32_bf16 v[38:41], v[204:207], v[188:191], v[36:39]
	s_barrier
	s_add_u32 s0, s4, 0x80
	s_addc_u32 s1, s5, 0
	s_add_u32 s4, s4, 0x20080
	s_addc_u32 s5, s5, 0
	s_mov_b32 m0, s73
	ds_read_b128 v[146:149], v175 offset:49152
	ds_read_b128 v[168:171], v175 offset:50176
	ds_read_b128 v[180:183], v175 offset:51200
	ds_read_b128 v[184:187], v175 offset:52224
	ds_read_b128 v[188:191], v175 offset:53248
	ds_read_b128 v[232:235], v175 offset:54272
	ds_read_b128 v[236:239], v175 offset:55296
	ds_read_b128 v[240:243], v175 offset:56320
	s_nop 0
	v_lshl_add_u64 v[36:37], s[0:1], 0, v[166:167]
	global_load_lds_dwordx4 v[36:37], off
	v_lshl_add_u64 v[36:37], s[4:5], 0, v[166:167]
	s_mov_b32 m0, s74
	s_nop 0
	global_load_lds_dwordx4 v[36:37], off
	s_barrier
	s_waitcnt lgkmcnt(0)
	s_waitcnt lgkmcnt(0)
	v_mfma_f32_16x16x32_bf16 v[70:73], v[142:145], v[146:149], v[208:211]
	v_mfma_f32_16x16x32_bf16 v[98:101], v[152:155], v[168:171], v[70:73]
	v_mfma_f32_16x16x32_bf16 v[70:73], v[156:159], v[146:149], v[212:215]
	v_mfma_f32_16x16x32_bf16 v[94:97], v[160:163], v[168:171], v[70:73]
	v_mfma_f32_16x16x32_bf16 v[70:73], v[142:145], v[180:183], v[216:219]
	v_mfma_f32_16x16x32_bf16 v[90:93], v[152:155], v[184:187], v[70:73]
	v_mfma_f32_16x16x32_bf16 v[70:73], v[156:159], v[180:183], v[220:223]
	v_mfma_f32_16x16x32_bf16 v[86:89], v[160:163], v[184:187], v[70:73]
	v_mfma_f32_16x16x32_bf16 v[70:73], v[142:145], v[188:191], v[224:227]
	v_mfma_f32_16x16x32_bf16 v[82:85], v[152:155], v[232:235], v[70:73]
	v_mfma_f32_16x16x32_bf16 v[70:73], v[156:159], v[188:191], v[228:231]
	v_mfma_f32_16x16x32_bf16 v[78:81], v[160:163], v[232:235], v[70:73]
	v_mfma_f32_16x16x32_bf16 v[70:73], v[142:145], v[236:239], v[134:137]
	v_mfma_f32_16x16x32_bf16 v[74:77], v[152:155], v[240:243], v[70:73]
	v_mfma_f32_16x16x32_bf16 v[70:73], v[156:159], v[236:239], v[138:141]
	v_mfma_f32_16x16x32_bf16 v[70:73], v[160:163], v[240:243], v[70:73]
	s_barrier
	s_add_u32 s0, s2, 0x40080
	s_addc_u32 s1, s3, 0
	s_add_u32 s2, s2, 0x60080
	s_addc_u32 s3, s3, 0
	s_mov_b32 m0, s75
	s_nop 0
	v_lshl_add_u64 v[36:37], s[0:1], 0, v[166:167]
	global_load_lds_dwordx4 v[36:37], off
	v_lshl_add_u64 v[36:37], s[2:3], 0, v[166:167]
	s_mov_b32 m0, s76
	s_nop 0
	global_load_lds_dwordx4 v[36:37], off
	s_waitcnt vmcnt(6)
	s_barrier
	v_mfma_f32_16x16x32_bf16 v[30:33], v[192:195], v[146:149], v[30:33]
	v_mfma_f32_16x16x32_bf16 v[26:29], v[200:203], v[146:149], v[26:29]
	v_mfma_f32_16x16x32_bf16 v[22:25], v[192:195], v[180:183], v[22:25]
	v_mfma_f32_16x16x32_bf16 v[18:21], v[200:203], v[180:183], v[18:21]
	v_mfma_f32_16x16x32_bf16 v[14:17], v[192:195], v[188:191], v[14:17]
	v_mfma_f32_16x16x32_bf16 v[10:13], v[200:203], v[188:191], v[10:13]
	v_mfma_f32_16x16x32_bf16 v[6:9], v[192:195], v[236:239], v[6:9]
	v_mfma_f32_16x16x32_bf16 v[2:5], v[200:203], v[236:239], v[2:5]
	v_mfma_f32_16x16x32_bf16 v[30:33], v[196:199], v[168:171], v[30:33]
	v_mfma_f32_16x16x32_bf16 v[26:29], v[204:207], v[168:171], v[26:29]
	v_mfma_f32_16x16x32_bf16 v[22:25], v[196:199], v[184:187], v[22:25]
	v_mfma_f32_16x16x32_bf16 v[18:21], v[204:207], v[184:187], v[18:21]
	v_mfma_f32_16x16x32_bf16 v[14:17], v[196:199], v[232:235], v[14:17]
	v_mfma_f32_16x16x32_bf16 v[10:13], v[204:207], v[232:235], v[10:13]
	v_mfma_f32_16x16x32_bf16 v[6:9], v[196:199], v[240:243], v[6:9]
	v_mfma_f32_16x16x32_bf16 v[2:5], v[204:207], v[240:243], v[2:5]
	v_mov_b32_e32 v34, v0
	s_barrier
; __device__ __forceinline__ bf16_t f2bf(float f) { unsigned u = __float_as_uint(f); u += 0x7FFFu + ((u >> 16) & 1u); return (bf16_t)(u >> 16); }
; #define EP_FENCE() asm volatile("" ::: "memory")
;     __device__ __forceinline__ void store_vt(bf16_t* base, unsigned voff0, const f32x4 (&acc)[2][2][4][2], int bj0, int bj1) const {
; #pragma unroll
;         for (int ai = 0; ai < 2; ++ai)
; #pragma unroll
;             for (int m = 0; m < 4; ++m) {
; #pragma unroll
;                 for (int bj = 0; bj < 2; ++bj) {
;                     if (bj < bj0 || bj > bj1) continue;
; #pragma unroll
;                     for (int n = 0; n < 2; ++n)
; #pragma unroll
;                         for (int j = 0; j < 4; ++j) {
;                             const unsigned off = voff0 + (unsigned)((ai * HALF + m * 16) * 2 + ((bj - bj0) * HALF + n * 4 + j) * SEQ * 2);
;                             *(bf16_t*)((char*)base + off) = f2bf(acc[ai][bj][m][n][j]);
;                         }
;                 }
;                 EP_FENCE();
;             }
;     }
;     __device__ __forceinline__ void operator()(const f32x4 (&acc)[2][2][4][2], const Unit& u, int wr, int wc, int fr, int fq, LAS unsigned char*, int) const {
;     ...
;         } else {
;             const int b = row0 / SEQ, sp = row0 % SEQ;
;             store_vt(VTH, (unsigned)(((b * 512 + (pn - 9) * BM + wc * 32 + 8 * fq) * SEQ + sp) * 2), acc, 0, 1);
	s_lshl_b32 s0, s8, 8
	v_readfirstlane_b32 s7, v34
	s_ashr_i32 s1, s7, 2
	s_andn2_b32 s1, s1, 63
	s_bfe_u32 s31, s7, 0x20006
	s_add_i32 s1, s1, s0
	v_bfe_u32 v179, v34, 4, 2
	v_and_or_b32 v168, v34, 15, s1
	s_cmp_gt_i32 s48, 2
	s_mov_b64 s[0:1], -1
	s_cbranch_scc0 .LBB0_321
	s_add_i32 s0, s48, -11
	s_cmp_gt_u32 s0, -7
	s_mov_b64 s[0:1], -1
	s_cbranch_scc0 .LBB0_318
	s_cmp_gt_u32 s48, 8
	s_cbranch_scc0 .LBB0_315
	v_ashrrev_i32_e32 v34, 31, v168
	v_lshrrev_b32_e32 v34, 21, v34
	v_add_u32_e32 v34, v168, v34
	s_lshl_b32 s0, s48, 19
	v_ashrrev_i32_e32 v34, 11, v34
	s_add_i32 s0, s0, 0x7fb80000
	v_mul_i32_i24_e32 v36, 0x800, v34
	v_lshl_or_b32 v37, v179, 14, s0
	v_sub_u32_e32 v36, v168, v36
	v_lshl_or_b32 v37, s31, 16, v37
	v_add_u32_e32 v36, v37, v36
	v_lshlrev_b32_e32 v34, 21, v34
	v_lshl_add_u32 v34, v36, 1, v34
	v_bfe_u32 v36, v130, 16, 1
	v_add3_u32 v36, v130, v36, s88
	v_bfe_u32 v37, v131, 16, 1
	global_store_short_d16_hi v34, v36, s[24:25]
	v_add_u32_e32 v36, 0x1000, v34
	v_add3_u32 v37, v131, v37, s88
	global_store_short_d16_hi v36, v37, s[24:25]
	v_bfe_u32 v37, v132, 16, 1
	v_add_u32_e32 v36, 0x2000, v34
	v_add3_u32 v37, v132, v37, s88
	global_store_short_d16_hi v36, v37, s[24:25]
	v_bfe_u32 v37, v133, 16, 1
	v_add_u32_e32 v36, 0x3000, v34
	v_add3_u32 v37, v133, v37, s88
	global_store_short_d16_hi v36, v37, s[24:25]
	v_bfe_u32 v37, v126, 16, 1
	v_add_u32_e32 v36, 0x4000, v34
	v_add3_u32 v37, v126, v37, s88
	global_store_short_d16_hi v36, v37, s[24:25]
	v_bfe_u32 v37, v127, 16, 1
	v_add_u32_e32 v36, 0x5000, v34
	v_add3_u32 v37, v127, v37, s88
	global_store_short_d16_hi v36, v37, s[24:25]
	v_bfe_u32 v37, v128, 16, 1
	v_add_u32_e32 v36, 0x6000, v34
	v_add3_u32 v37, v128, v37, s88
	global_store_short_d16_hi v36, v37, s[24:25]
	v_bfe_u32 v37, v129, 16, 1
	v_add_u32_e32 v36, 0x7000, v34
	v_add3_u32 v37, v129, v37, s88
	global_store_short_d16_hi v36, v37, s[24:25]
	v_bfe_u32 v37, v66, 16, 1
	v_add_u32_e32 v36, 0x80000, v34
	v_add3_u32 v37, v66, v37, s88
	global_store_short_d16_hi v36, v37, s[24:25]
	v_bfe_u32 v37, v67, 16, 1
	v_add_u32_e32 v36, 0x81000, v34
	v_add3_u32 v37, v67, v37, s88
	global_store_short_d16_hi v36, v37, s[24:25]
	v_bfe_u32 v37, v68, 16, 1
	v_add_u32_e32 v36, 0x82000, v34
	v_add3_u32 v37, v68, v37, s88
	global_store_short_d16_hi v36, v37, s[24:25]
	v_bfe_u32 v37, v69, 16, 1
	v_add_u32_e32 v36, 0x83000, v34
	v_add3_u32 v37, v69, v37, s88
	global_store_short_d16_hi v36, v37, s[24:25]
	v_bfe_u32 v37, v62, 16, 1
	v_add_u32_e32 v36, 0x84000, v34
	v_add3_u32 v37, v62, v37, s88
	global_store_short_d16_hi v36, v37, s[24:25]
	v_bfe_u32 v37, v63, 16, 1
	v_add_u32_e32 v36, 0x85000, v34
	v_add3_u32 v37, v63, v37, s88
	global_store_short_d16_hi v36, v37, s[24:25]
	v_bfe_u32 v37, v64, 16, 1
	v_add_u32_e32 v36, 0x86000, v34
	v_add3_u32 v37, v64, v37, s88
	global_store_short_d16_hi v36, v37, s[24:25]
	v_bfe_u32 v37, v65, 16, 1
	v_add_u32_e32 v36, 0x87000, v34
	v_add3_u32 v37, v65, v37, s88
	global_store_short_d16_hi v36, v37, s[24:25]
	v_bfe_u32 v37, v122, 16, 1
	v_add_u32_e32 v36, 32, v34
	v_add3_u32 v37, v122, v37, s88
	global_store_short_d16_hi v36, v37, s[24:25]
	v_bfe_u32 v37, v123, 16, 1
	v_add_u32_e32 v36, 0x1020, v34
	v_add3_u32 v37, v123, v37, s88
	global_store_short_d16_hi v36, v37, s[24:25]
	v_bfe_u32 v37, v124, 16, 1
	v_add_u32_e32 v36, 0x2020, v34
	v_add3_u32 v37, v124, v37, s88
	global_store_short_d16_hi v36, v37, s[24:25]
	v_bfe_u32 v37, v125, 16, 1
	v_add_u32_e32 v36, 0x3020, v34
	v_add3_u32 v37, v125, v37, s88
	global_store_short_d16_hi v36, v37, s[24:25]
	v_bfe_u32 v37, v118, 16, 1
	v_add_u32_e32 v36, 0x4020, v34
	v_add3_u32 v37, v118, v37, s88
	global_store_short_d16_hi v36, v37, s[24:25]
	v_bfe_u32 v37, v119, 16, 1
	v_add_u32_e32 v36, 0x5020, v34
	v_add3_u32 v37, v119, v37, s88
	global_store_short_d16_hi v36, v37, s[24:25]
	v_bfe_u32 v37, v120, 16, 1
	v_add_u32_e32 v36, 0x6020, v34
	v_add3_u32 v37, v120, v37, s88
	global_store_short_d16_hi v36, v37, s[24:25]
	v_bfe_u32 v37, v121, 16, 1
	v_add_u32_e32 v36, 0x7020, v34
	v_add3_u32 v37, v121, v37, s88
	global_store_short_d16_hi v36, v37, s[24:25]
	v_bfe_u32 v37, v58, 16, 1
	v_add_u32_e32 v36, 0x80020, v34
	v_add3_u32 v37, v58, v37, s88
	global_store_short_d16_hi v36, v37, s[24:25]
	v_bfe_u32 v37, v59, 16, 1
	v_add_u32_e32 v36, 0x81020, v34
	v_add3_u32 v37, v59, v37, s88
	global_store_short_d16_hi v36, v37, s[24:25]
	v_bfe_u32 v37, v60, 16, 1
	v_add_u32_e32 v36, 0x82020, v34
	v_add3_u32 v37, v60, v37, s88
	global_store_short_d16_hi v36, v37, s[24:25]
	v_bfe_u32 v37, v61, 16, 1
	v_add_u32_e32 v36, 0x83020, v34
	v_add3_u32 v37, v61, v37, s88
	global_store_short_d16_hi v36, v37, s[24:25]
	v_bfe_u32 v37, v54, 16, 1
	v_add_u32_e32 v36, 0x84020, v34
	v_add3_u32 v37, v54, v37, s88
	global_store_short_d16_hi v36, v37, s[24:25]
	v_bfe_u32 v37, v55, 16, 1
	v_add_u32_e32 v36, 0x85020, v34
	v_add3_u32 v37, v55, v37, s88
	global_store_short_d16_hi v36, v37, s[24:25]
	v_bfe_u32 v37, v56, 16, 1
	v_add_u32_e32 v36, 0x86020, v34
	v_add3_u32 v37, v56, v37, s88
	global_store_short_d16_hi v36, v37, s[24:25]
	v_bfe_u32 v37, v57, 16, 1
	v_add_u32_e32 v36, 0x87020, v34
	v_add3_u32 v37, v57, v37, s88
	global_store_short_d16_hi v36, v37, s[24:25]
	v_bfe_u32 v37, v114, 16, 1
	v_add_u32_e32 v36, 64, v34
	v_add3_u32 v37, v114, v37, s88
	global_store_short_d16_hi v36, v37, s[24:25]
	v_bfe_u32 v37, v115, 16, 1
	v_add_u32_e32 v36, 0x1040, v34
	v_add3_u32 v37, v115, v37, s88
	global_store_short_d16_hi v36, v37, s[24:25]
	v_bfe_u32 v37, v116, 16, 1
	v_add_u32_e32 v36, 0x2040, v34
	v_add3_u32 v37, v116, v37, s88
	global_store_short_d16_hi v36, v37, s[24:25]
	v_bfe_u32 v37, v117, 16, 1
	v_add_u32_e32 v36, 0x3040, v34
; __device__ __forceinline__ bf16_t f2bf(float f) { unsigned u = __float_as_uint(f); u += 0x7FFFu + ((u >> 16) & 1u); return (bf16_t)(u >> 16); }
; #define EP_FENCE() asm volatile("" ::: "memory")
;     __device__ __forceinline__ void store_vt(bf16_t* base, unsigned voff0, const f32x4 (&acc)[2][2][4][2], int bj0, int bj1) const {
; #pragma unroll
;         for (int ai = 0; ai < 2; ++ai)
; #pragma unroll
;             for (int m = 0; m < 4; ++m) {
; #pragma unroll
;                 for (int bj = 0; bj < 2; ++bj) {
;                     if (bj < bj0 || bj > bj1) continue;
; #pragma unroll
;                     for (int n = 0; n < 2; ++n)
; #pragma unroll
;                         for (int j = 0; j < 4; ++j) {
;                             const unsigned off = voff0 + (unsigned)((ai * HALF + m * 16) * 2 + ((bj - bj0) * HALF + n * 4 + j) * SEQ * 2);
;                             *(bf16_t*)((char*)base + off) = f2bf(acc[ai][bj][m][n][j]);
;                         }
;                 }
;                 EP_FENCE();
;             }
;     }
	v_add3_u32 v37, v117, v37, s88
	global_store_short_d16_hi v36, v37, s[24:25]
	v_bfe_u32 v37, v110, 16, 1
	v_add_u32_e32 v36, 0x4040, v34
	v_add3_u32 v37, v110, v37, s88
	global_store_short_d16_hi v36, v37, s[24:25]
	v_bfe_u32 v37, v111, 16, 1
	v_add_u32_e32 v36, 0x5040, v34
	v_add3_u32 v37, v111, v37, s88
	global_store_short_d16_hi v36, v37, s[24:25]
	v_bfe_u32 v37, v112, 16, 1
	v_add_u32_e32 v36, 0x6040, v34
	v_add3_u32 v37, v112, v37, s88
	global_store_short_d16_hi v36, v37, s[24:25]
	v_bfe_u32 v37, v113, 16, 1
	v_add_u32_e32 v36, 0x7040, v34
	v_add3_u32 v37, v113, v37, s88
	global_store_short_d16_hi v36, v37, s[24:25]
	v_bfe_u32 v37, v50, 16, 1
	v_add_u32_e32 v36, 0x80040, v34
	v_add3_u32 v37, v50, v37, s88
	global_store_short_d16_hi v36, v37, s[24:25]
	v_bfe_u32 v37, v51, 16, 1
	v_add_u32_e32 v36, 0x81040, v34
	v_add3_u32 v37, v51, v37, s88
	global_store_short_d16_hi v36, v37, s[24:25]
	v_bfe_u32 v37, v52, 16, 1
	v_add_u32_e32 v36, 0x82040, v34
	v_add3_u32 v37, v52, v37, s88
	global_store_short_d16_hi v36, v37, s[24:25]
	v_bfe_u32 v37, v53, 16, 1
	v_add_u32_e32 v36, 0x83040, v34
	v_add3_u32 v37, v53, v37, s88
	global_store_short_d16_hi v36, v37, s[24:25]
	v_bfe_u32 v37, v46, 16, 1
	v_add_u32_e32 v36, 0x84040, v34
	v_add3_u32 v37, v46, v37, s88
	global_store_short_d16_hi v36, v37, s[24:25]
	v_bfe_u32 v37, v47, 16, 1
	v_add_u32_e32 v36, 0x85040, v34
	v_add3_u32 v37, v47, v37, s88
	global_store_short_d16_hi v36, v37, s[24:25]
	v_bfe_u32 v37, v48, 16, 1
	v_add_u32_e32 v36, 0x86040, v34
	v_add3_u32 v37, v48, v37, s88
	global_store_short_d16_hi v36, v37, s[24:25]
	v_bfe_u32 v37, v49, 16, 1
	v_add_u32_e32 v36, 0x87040, v34
	v_add3_u32 v37, v49, v37, s88
	global_store_short_d16_hi v36, v37, s[24:25]
	v_bfe_u32 v37, v106, 16, 1
	v_add_u32_e32 v36, 0x60, v34
	v_add3_u32 v37, v106, v37, s88
	global_store_short_d16_hi v36, v37, s[24:25]
	v_bfe_u32 v37, v107, 16, 1
	v_add_u32_e32 v36, 0x1060, v34
	v_add3_u32 v37, v107, v37, s88
	global_store_short_d16_hi v36, v37, s[24:25]
	v_bfe_u32 v37, v108, 16, 1
	v_add_u32_e32 v36, 0x2060, v34
	v_add3_u32 v37, v108, v37, s88
	global_store_short_d16_hi v36, v37, s[24:25]
	v_bfe_u32 v37, v109, 16, 1
	v_add_u32_e32 v36, 0x3060, v34
	v_add3_u32 v37, v109, v37, s88
	global_store_short_d16_hi v36, v37, s[24:25]
	v_bfe_u32 v37, v102, 16, 1
	v_add_u32_e32 v36, 0x4060, v34
	v_add3_u32 v37, v102, v37, s88
	global_store_short_d16_hi v36, v37, s[24:25]
	v_bfe_u32 v37, v103, 16, 1
	v_add_u32_e32 v36, 0x5060, v34
	v_add3_u32 v37, v103, v37, s88
	global_store_short_d16_hi v36, v37, s[24:25]
	v_bfe_u32 v37, v104, 16, 1
	v_add_u32_e32 v36, 0x6060, v34
	v_add3_u32 v37, v104, v37, s88
	global_store_short_d16_hi v36, v37, s[24:25]
	v_bfe_u32 v37, v105, 16, 1
	v_add_u32_e32 v36, 0x7060, v34
	v_add3_u32 v37, v105, v37, s88
	global_store_short_d16_hi v36, v37, s[24:25]
	v_bfe_u32 v37, v42, 16, 1
	v_add_u32_e32 v36, 0x80060, v34
	v_add3_u32 v37, v42, v37, s88
	global_store_short_d16_hi v36, v37, s[24:25]
	v_bfe_u32 v37, v43, 16, 1
	v_add_u32_e32 v36, 0x81060, v34
	v_add3_u32 v37, v43, v37, s88
	global_store_short_d16_hi v36, v37, s[24:25]
	v_bfe_u32 v37, v44, 16, 1
	v_add_u32_e32 v36, 0x82060, v34
	v_add3_u32 v37, v44, v37, s88
	global_store_short_d16_hi v36, v37, s[24:25]
	v_bfe_u32 v37, v45, 16, 1
	v_add_u32_e32 v36, 0x83060, v34
	v_add3_u32 v37, v45, v37, s88
	global_store_short_d16_hi v36, v37, s[24:25]
	v_bfe_u32 v37, v38, 16, 1
	v_add_u32_e32 v36, 0x84060, v34
	v_add3_u32 v37, v38, v37, s88
	global_store_short_d16_hi v36, v37, s[24:25]
	v_bfe_u32 v37, v39, 16, 1
	v_add_u32_e32 v36, 0x85060, v34
	v_add3_u32 v37, v39, v37, s88
	global_store_short_d16_hi v36, v37, s[24:25]
	v_bfe_u32 v37, v40, 16, 1
	v_add_u32_e32 v36, 0x86060, v34
	v_add3_u32 v37, v40, v37, s88
	global_store_short_d16_hi v36, v37, s[24:25]
	v_bfe_u32 v37, v41, 16, 1
	v_add_u32_e32 v36, 0x87060, v34
	v_add3_u32 v37, v41, v37, s88
	global_store_short_d16_hi v36, v37, s[24:25]
	v_bfe_u32 v37, v98, 16, 1
	v_add_u32_e32 v36, 0x100, v34
	v_add3_u32 v37, v98, v37, s88
	global_store_short_d16_hi v36, v37, s[24:25]
	v_bfe_u32 v37, v99, 16, 1
	v_add_u32_e32 v36, 0x1100, v34
	v_add3_u32 v37, v99, v37, s88
	global_store_short_d16_hi v36, v37, s[24:25]
	v_bfe_u32 v37, v100, 16, 1
	v_add_u32_e32 v36, 0x2100, v34
	v_add3_u32 v37, v100, v37, s88
	global_store_short_d16_hi v36, v37, s[24:25]
	v_bfe_u32 v37, v101, 16, 1
	v_add_u32_e32 v36, 0x3100, v34
	v_add3_u32 v37, v101, v37, s88
	global_store_short_d16_hi v36, v37, s[24:25]
	v_bfe_u32 v37, v94, 16, 1
	v_add_u32_e32 v36, 0x4100, v34
	v_add3_u32 v37, v94, v37, s88
	global_store_short_d16_hi v36, v37, s[24:25]
	v_bfe_u32 v37, v95, 16, 1
	v_add_u32_e32 v36, 0x5100, v34
	v_add3_u32 v37, v95, v37, s88
	global_store_short_d16_hi v36, v37, s[24:25]
	v_bfe_u32 v37, v96, 16, 1
	v_add_u32_e32 v36, 0x6100, v34
	v_add3_u32 v37, v96, v37, s88
	global_store_short_d16_hi v36, v37, s[24:25]
	v_bfe_u32 v37, v97, 16, 1
	v_add_u32_e32 v36, 0x7100, v34
	v_add3_u32 v37, v97, v37, s88
	global_store_short_d16_hi v36, v37, s[24:25]
	v_bfe_u32 v37, v30, 16, 1
	v_add_u32_e32 v36, 0x80100, v34
	v_add3_u32 v37, v30, v37, s88
	global_store_short_d16_hi v36, v37, s[24:25]
	v_bfe_u32 v37, v31, 16, 1
	v_add_u32_e32 v36, 0x81100, v34
	v_add3_u32 v37, v31, v37, s88
	global_store_short_d16_hi v36, v37, s[24:25]
	v_bfe_u32 v37, v32, 16, 1
	v_add_u32_e32 v36, 0x82100, v34
	v_add3_u32 v37, v32, v37, s88
	global_store_short_d16_hi v36, v37, s[24:25]
	v_bfe_u32 v37, v33, 16, 1
	v_add_u32_e32 v36, 0x83100, v34
	v_add3_u32 v37, v33, v37, s88
	global_store_short_d16_hi v36, v37, s[24:25]
	v_bfe_u32 v37, v26, 16, 1
	v_add_u32_e32 v36, 0x84100, v34
	v_add3_u32 v37, v26, v37, s88
; __device__ __forceinline__ bf16_t f2bf(float f) { unsigned u = __float_as_uint(f); u += 0x7FFFu + ((u >> 16) & 1u); return (bf16_t)(u >> 16); }
; #define EP_FENCE() asm volatile("" ::: "memory")
;     __device__ __forceinline__ void store_vt(bf16_t* base, unsigned voff0, const f32x4 (&acc)[2][2][4][2], int bj0, int bj1) const {
; #pragma unroll
;         for (int ai = 0; ai < 2; ++ai)
; #pragma unroll
;             for (int m = 0; m < 4; ++m) {
; #pragma unroll
;                 for (int bj = 0; bj < 2; ++bj) {
;                     if (bj < bj0 || bj > bj1) continue;
; #pragma unroll
;                     for (int n = 0; n < 2; ++n)
; #pragma unroll
;                         for (int j = 0; j < 4; ++j) {
;                             const unsigned off = voff0 + (unsigned)((ai * HALF + m * 16) * 2 + ((bj - bj0) * HALF + n * 4 + j) * SEQ * 2);
;                             *(bf16_t*)((char*)base + off) = f2bf(acc[ai][bj][m][n][j]);
;                         }
;                 }
;                 EP_FENCE();
;             }
;     }
	global_store_short_d16_hi v36, v37, s[24:25]
	v_bfe_u32 v37, v27, 16, 1
	v_add_u32_e32 v36, 0x85100, v34
	v_add3_u32 v37, v27, v37, s88
	global_store_short_d16_hi v36, v37, s[24:25]
	v_bfe_u32 v37, v28, 16, 1
	v_add_u32_e32 v36, 0x86100, v34
	v_add3_u32 v37, v28, v37, s88
	global_store_short_d16_hi v36, v37, s[24:25]
	v_bfe_u32 v37, v29, 16, 1
	v_add_u32_e32 v36, 0x87100, v34
	v_add3_u32 v37, v29, v37, s88
	global_store_short_d16_hi v36, v37, s[24:25]
	v_bfe_u32 v37, v90, 16, 1
	v_add_u32_e32 v36, 0x120, v34
	v_add3_u32 v37, v90, v37, s88
	global_store_short_d16_hi v36, v37, s[24:25]
	v_bfe_u32 v37, v91, 16, 1
	v_add_u32_e32 v36, 0x1120, v34
	v_add3_u32 v37, v91, v37, s88
	global_store_short_d16_hi v36, v37, s[24:25]
	v_bfe_u32 v37, v92, 16, 1
	v_add_u32_e32 v36, 0x2120, v34
	v_add3_u32 v37, v92, v37, s88
	global_store_short_d16_hi v36, v37, s[24:25]
	v_bfe_u32 v37, v93, 16, 1
	v_add_u32_e32 v36, 0x3120, v34
	v_add3_u32 v37, v93, v37, s88
	global_store_short_d16_hi v36, v37, s[24:25]
	v_bfe_u32 v37, v86, 16, 1
	v_add_u32_e32 v36, 0x4120, v34
	v_add3_u32 v37, v86, v37, s88
	global_store_short_d16_hi v36, v37, s[24:25]
	v_bfe_u32 v37, v87, 16, 1
	v_add_u32_e32 v36, 0x5120, v34
	v_add3_u32 v37, v87, v37, s88
	global_store_short_d16_hi v36, v37, s[24:25]
	v_bfe_u32 v37, v88, 16, 1
	v_add_u32_e32 v36, 0x6120, v34
	v_add3_u32 v37, v88, v37, s88
	global_store_short_d16_hi v36, v37, s[24:25]
	v_bfe_u32 v37, v89, 16, 1
	v_add_u32_e32 v36, 0x7120, v34
	v_add3_u32 v37, v89, v37, s88
	global_store_short_d16_hi v36, v37, s[24:25]
	v_bfe_u32 v37, v22, 16, 1
	v_add_u32_e32 v36, 0x80120, v34
	v_add3_u32 v37, v22, v37, s88
	global_store_short_d16_hi v36, v37, s[24:25]
	v_bfe_u32 v37, v23, 16, 1
	v_add_u32_e32 v36, 0x81120, v34
	v_add3_u32 v37, v23, v37, s88
	global_store_short_d16_hi v36, v37, s[24:25]
	v_bfe_u32 v37, v24, 16, 1
	v_add_u32_e32 v36, 0x82120, v34
	v_add3_u32 v37, v24, v37, s88
	global_store_short_d16_hi v36, v37, s[24:25]
	v_bfe_u32 v37, v25, 16, 1
	v_add_u32_e32 v36, 0x83120, v34
	v_add3_u32 v37, v25, v37, s88
	global_store_short_d16_hi v36, v37, s[24:25]
	v_bfe_u32 v37, v18, 16, 1
	v_add_u32_e32 v36, 0x84120, v34
	v_add3_u32 v37, v18, v37, s88
	global_store_short_d16_hi v36, v37, s[24:25]
	v_bfe_u32 v37, v19, 16, 1
	v_add_u32_e32 v36, 0x85120, v34
	v_add3_u32 v37, v19, v37, s88
	global_store_short_d16_hi v36, v37, s[24:25]
	v_bfe_u32 v37, v20, 16, 1
	v_add_u32_e32 v36, 0x86120, v34
	v_add3_u32 v37, v20, v37, s88
	global_store_short_d16_hi v36, v37, s[24:25]
	v_bfe_u32 v37, v21, 16, 1
	v_add_u32_e32 v36, 0x87120, v34
	v_add3_u32 v37, v21, v37, s88
	global_store_short_d16_hi v36, v37, s[24:25]
	v_bfe_u32 v37, v82, 16, 1
	v_add_u32_e32 v36, 0x140, v34
	v_add3_u32 v37, v82, v37, s88
	global_store_short_d16_hi v36, v37, s[24:25]
	v_bfe_u32 v37, v83, 16, 1
	v_add_u32_e32 v36, 0x1140, v34
	v_add3_u32 v37, v83, v37, s88
	global_store_short_d16_hi v36, v37, s[24:25]
	v_bfe_u32 v37, v84, 16, 1
	v_add_u32_e32 v36, 0x2140, v34
	v_add3_u32 v37, v84, v37, s88
	global_store_short_d16_hi v36, v37, s[24:25]
	v_bfe_u32 v37, v85, 16, 1
	v_add_u32_e32 v36, 0x3140, v34
	v_add3_u32 v37, v85, v37, s88
	global_store_short_d16_hi v36, v37, s[24:25]
	v_bfe_u32 v37, v78, 16, 1
	v_add_u32_e32 v36, 0x4140, v34
	v_add3_u32 v37, v78, v37, s88
	global_store_short_d16_hi v36, v37, s[24:25]
	v_bfe_u32 v37, v79, 16, 1
	v_add_u32_e32 v36, 0x5140, v34
	v_add3_u32 v37, v79, v37, s88
	global_store_short_d16_hi v36, v37, s[24:25]
	v_bfe_u32 v37, v80, 16, 1
	v_add_u32_e32 v36, 0x6140, v34
	v_add3_u32 v37, v80, v37, s88
	global_store_short_d16_hi v36, v37, s[24:25]
	v_bfe_u32 v37, v81, 16, 1
	v_add_u32_e32 v36, 0x7140, v34
	v_add3_u32 v37, v81, v37, s88
	global_store_short_d16_hi v36, v37, s[24:25]
	v_bfe_u32 v37, v14, 16, 1
	v_add_u32_e32 v36, 0x80140, v34
	v_add3_u32 v37, v14, v37, s88
	global_store_short_d16_hi v36, v37, s[24:25]
	v_bfe_u32 v37, v15, 16, 1
	v_add_u32_e32 v36, 0x81140, v34
	v_add3_u32 v37, v15, v37, s88
	global_store_short_d16_hi v36, v37, s[24:25]
	v_bfe_u32 v37, v16, 16, 1
	v_add_u32_e32 v36, 0x82140, v34
	v_add3_u32 v37, v16, v37, s88
	global_store_short_d16_hi v36, v37, s[24:25]
	v_bfe_u32 v37, v17, 16, 1
	v_add_u32_e32 v36, 0x83140, v34
	v_add3_u32 v37, v17, v37, s88
	global_store_short_d16_hi v36, v37, s[24:25]
	v_bfe_u32 v37, v10, 16, 1
	v_add_u32_e32 v36, 0x84140, v34
	v_add3_u32 v37, v10, v37, s88
	global_store_short_d16_hi v36, v37, s[24:25]
	v_bfe_u32 v37, v11, 16, 1
	v_add_u32_e32 v36, 0x85140, v34
	v_add3_u32 v37, v11, v37, s88
	global_store_short_d16_hi v36, v37, s[24:25]
	v_bfe_u32 v37, v12, 16, 1
	v_add_u32_e32 v36, 0x86140, v34
	v_add3_u32 v37, v12, v37, s88
	global_store_short_d16_hi v36, v37, s[24:25]
	v_bfe_u32 v37, v13, 16, 1
	v_add_u32_e32 v36, 0x87140, v34
	v_add3_u32 v37, v13, v37, s88
	global_store_short_d16_hi v36, v37, s[24:25]
	v_bfe_u32 v37, v74, 16, 1
	v_add_u32_e32 v36, 0x160, v34
	v_add3_u32 v37, v74, v37, s88
	global_store_short_d16_hi v36, v37, s[24:25]
	v_bfe_u32 v37, v75, 16, 1
	v_add_u32_e32 v36, 0x1160, v34
	v_add3_u32 v37, v75, v37, s88
	global_store_short_d16_hi v36, v37, s[24:25]
	v_bfe_u32 v37, v76, 16, 1
	v_add_u32_e32 v36, 0x2160, v34
	v_add3_u32 v37, v76, v37, s88
	global_store_short_d16_hi v36, v37, s[24:25]
	v_bfe_u32 v37, v77, 16, 1
	v_add_u32_e32 v36, 0x3160, v34
	v_add3_u32 v37, v77, v37, s88
	global_store_short_d16_hi v36, v37, s[24:25]
	v_bfe_u32 v37, v70, 16, 1
	v_add_u32_e32 v36, 0x4160, v34
	v_add3_u32 v37, v70, v37, s88
	global_store_short_d16_hi v36, v37, s[24:25]
	v_bfe_u32 v37, v71, 16, 1
	v_add_u32_e32 v36, 0x5160, v34
	v_add3_u32 v37, v71, v37, s88
	global_store_short_d16_hi v36, v37, s[24:25]
	v_bfe_u32 v37, v72, 16, 1
	v_add_u32_e32 v36, 0x6160, v34
	v_add3_u32 v37, v72, v37, s88
	global_store_short_d16_hi v36, v37, s[24:25]
	v_bfe_u32 v37, v73, 16, 1
	v_add_u32_e32 v36, 0x7160, v34
	v_add3_u32 v37, v73, v37, s88
	global_store_short_d16_hi v36, v37, s[24:25]
	v_bfe_u32 v37, v6, 16, 1
	v_add_u32_e32 v36, 0x80160, v34
	v_add3_u32 v37, v6, v37, s88
	global_store_short_d16_hi v36, v37, s[24:25]
	v_bfe_u32 v37, v7, 16, 1
	v_add_u32_e32 v36, 0x81160, v34
	v_add3_u32 v37, v7, v37, s88
	global_store_short_d16_hi v36, v37, s[24:25]
	v_bfe_u32 v37, v8, 16, 1
	v_add_u32_e32 v36, 0x82160, v34
	v_add3_u32 v37, v8, v37, s88
	global_store_short_d16_hi v36, v37, s[24:25]
	v_bfe_u32 v37, v9, 16, 1
	v_add_u32_e32 v36, 0x83160, v34
	v_add3_u32 v37, v9, v37, s88
	global_store_short_d16_hi v36, v37, s[24:25]
	v_bfe_u32 v37, v2, 16, 1
	v_add_u32_e32 v36, 0x84160, v34
	v_add3_u32 v37, v2, v37, s88
	global_store_short_d16_hi v36, v37, s[24:25]
	v_bfe_u32 v37, v3, 16, 1
	v_add_u32_e32 v36, 0x85160, v34
	v_add3_u32 v37, v3, v37, s88
	global_store_short_d16_hi v36, v37, s[24:25]
	v_bfe_u32 v37, v4, 16, 1
	v_add_u32_e32 v36, 0x86160, v34
	v_add3_u32 v37, v4, v37, s88
	global_store_short_d16_hi v36, v37, s[24:25]
	v_bfe_u32 v36, v5, 16, 1
	v_add_u32_e32 v34, 0x87160, v34
	v_add3_u32 v36, v5, v36, s88
	global_store_short_d16_hi v34, v36, s[24:25]
	s_mov_b64 s[0:1], 0

; __device__ __forceinline__ int tid_hidden() { int t = threadIdx.x; asm volatile("" : "+v"(t)); return t; }
; #define lds lds_hidden(lds0)
; template <class Epi, class Src>
; __device__ __forceinline__ void gemm_phase(LAS unsigned char* lds, const Src S, const Epi E) {
;     ...
;         { const int tp = tid_hidden(); E.prefetch(cur, lds, par, tp, __builtin_amdgcn_readfirstlane(tp >> 6)); }
;         if (Src::GATHER && has_next) { const int tp = tid_hidden(); tab_fill(S, nxt, tp, __builtin_amdgcn_readfirstlane(tp >> 6), lds, par ^ 1); }
;         for (int t = 0; t < NKTR - 2; t += 2) {
;             const size_t k1 = (size_t)(t + 1) * kstep, k2 = (size_t)(t + 2) * kstep;
;             const char* b2 = cB + k2; const char* b3 = b2 + kstep;
;             G8_ITER(cA, par, k1, cA, par, k2, b2, b3);
;         }
.LBB0_727:
	s_add_u32 s34, s56, s0
	s_addc_u32 s35, s57, s1
	v_add_u32_e32 v34, s38, v134
	ds_read_b128 v[138:141], v34
	ds_read_b128 v[142:145], v34 offset:1024
	ds_read_b128 v[146:149], v34 offset:2048
	ds_read_b128 v[150:153], v34 offset:3072
	s_add_u32 s64, s2, s0
	s_addc_u32 s65, s3, s1
	s_add_u32 s62, s64, 0x40080
	s_addc_u32 s63, s65, 0
	s_add_u32 s66, s64, 0x60080
	s_addc_u32 s67, s65, 0
	ds_read_b128 v[154:157], v135
	ds_read_b128 v[158:161], v135 offset:1024
	ds_read_b128 v[162:165], v135 offset:2048
	ds_read_b128 v[166:169], v135 offset:3072
	ds_read_b128 v[170:173], v135 offset:4096
	ds_read_b128 v[174:177], v135 offset:5120
	ds_read_b128 v[178:181], v135 offset:6144
	ds_read_b128 v[182:185], v135 offset:7168
	s_nop 0
	v_lshl_add_u64 v[136:137], s[62:63], 0, v[132:133]
	s_add_i32 s63, s41, 0xc000
	s_mov_b32 m0, s63
	s_add_i32 s62, s41, 0xe000
	global_load_lds_dwordx4 v[136:137], off
	v_lshl_add_u64 v[136:137], s[66:67], 0, v[132:133]
	s_mov_b32 m0, s62
	s_nop 0
	global_load_lds_dwordx4 v[136:137], off
	s_waitcnt lgkmcnt(8)
	s_barrier
	s_waitcnt lgkmcnt(0)
	s_waitcnt lgkmcnt(0)
	v_mfma_f32_16x16x32_bf16 v[128:131], v[138:141], v[154:157], v[128:131]
	v_mfma_f32_16x16x32_bf16 v[124:127], v[146:149], v[154:157], v[124:127]
	v_mfma_f32_16x16x32_bf16 v[120:123], v[138:141], v[162:165], v[120:123]
	v_mfma_f32_16x16x32_bf16 v[116:119], v[146:149], v[162:165], v[116:119]
	v_mfma_f32_16x16x32_bf16 v[112:115], v[138:141], v[170:173], v[112:115]
	v_mfma_f32_16x16x32_bf16 v[108:111], v[146:149], v[170:173], v[108:111]
	v_mfma_f32_16x16x32_bf16 v[104:107], v[138:141], v[178:181], v[104:107]
	v_mfma_f32_16x16x32_bf16 v[100:103], v[146:149], v[178:181], v[100:103]
	v_mfma_f32_16x16x32_bf16 v[128:131], v[142:145], v[158:161], v[128:131]
	v_mfma_f32_16x16x32_bf16 v[124:127], v[150:153], v[158:161], v[124:127]
	v_mfma_f32_16x16x32_bf16 v[120:123], v[142:145], v[166:169], v[120:123]
	v_mfma_f32_16x16x32_bf16 v[116:119], v[150:153], v[166:169], v[116:119]
	v_mfma_f32_16x16x32_bf16 v[112:115], v[142:145], v[174:177], v[112:115]
	v_mfma_f32_16x16x32_bf16 v[108:111], v[150:153], v[174:177], v[108:111]
	v_mfma_f32_16x16x32_bf16 v[104:107], v[142:145], v[182:185], v[104:107]
	v_mfma_f32_16x16x32_bf16 v[100:103], v[150:153], v[182:185], v[100:103]
	s_barrier
	s_add_u32 s66, s34, 0x20000
	v_add_u32_e32 v136, s43, v134
	s_addc_u32 s67, s35, 0
	s_mov_b64 s[68:69], s[34:35]
	s_mov_b32 m0, s39
	ds_read_b128 v[186:189], v136
	ds_read_b128 v[190:193], v136 offset:1024
	ds_read_b128 v[194:197], v136 offset:2048
	ds_read_b128 v[198:201], v136 offset:3072
	s_nop 0
	v_lshl_add_u64 v[202:203], s[68:69], 0, v[132:133]
	global_load_lds_dwordx4 v[202:203], off
	v_lshl_add_u64 v[202:203], s[66:67], 0, v[132:133]
	s_mov_b32 m0, s40
	s_nop 0
	global_load_lds_dwordx4 v[202:203], off
	s_barrier
	s_waitcnt lgkmcnt(0)
	s_waitcnt lgkmcnt(0)
	v_mfma_f32_16x16x32_bf16 v[96:99], v[186:189], v[154:157], v[96:99]
	v_mfma_f32_16x16x32_bf16 v[92:95], v[194:197], v[154:157], v[92:95]
	v_mfma_f32_16x16x32_bf16 v[88:91], v[186:189], v[162:165], v[88:91]
	v_mfma_f32_16x16x32_bf16 v[84:87], v[194:197], v[162:165], v[84:87]
	v_mfma_f32_16x16x32_bf16 v[80:83], v[186:189], v[170:173], v[80:83]
	v_mfma_f32_16x16x32_bf16 v[76:79], v[194:197], v[170:173], v[76:79]
	v_mfma_f32_16x16x32_bf16 v[72:75], v[186:189], v[178:181], v[72:75]
	v_mfma_f32_16x16x32_bf16 v[68:71], v[194:197], v[178:181], v[68:71]
	v_mfma_f32_16x16x32_bf16 v[96:99], v[190:193], v[158:161], v[96:99]
	v_mfma_f32_16x16x32_bf16 v[92:95], v[198:201], v[158:161], v[92:95]
	v_mfma_f32_16x16x32_bf16 v[88:91], v[190:193], v[166:169], v[88:91]
	v_mfma_f32_16x16x32_bf16 v[84:87], v[198:201], v[166:169], v[84:87]
	v_mfma_f32_16x16x32_bf16 v[80:83], v[190:193], v[174:177], v[80:83]
	v_mfma_f32_16x16x32_bf16 v[76:79], v[198:201], v[174:177], v[76:79]
	v_mfma_f32_16x16x32_bf16 v[72:75], v[190:193], v[182:185], v[72:75]
	v_mfma_f32_16x16x32_bf16 v[68:71], v[198:201], v[182:185], v[68:71]
	s_barrier
	s_add_u32 s66, s64, 0x100
	s_addc_u32 s67, s65, 0
	s_add_u32 s68, s64, 0x20100
	s_addc_u32 s69, s65, 0
	s_mov_b32 m0, s41
	ds_read_b128 v[154:157], v135 offset:16384
	ds_read_b128 v[158:161], v135 offset:17408
	ds_read_b128 v[162:165], v135 offset:18432
	ds_read_b128 v[166:169], v135 offset:19456
	ds_read_b128 v[170:173], v135 offset:20480
	ds_read_b128 v[174:177], v135 offset:21504
	ds_read_b128 v[178:181], v135 offset:22528
	ds_read_b128 v[182:185], v135 offset:23552
	s_nop 0
	v_lshl_add_u64 v[202:203], s[66:67], 0, v[132:133]
	global_load_lds_dwordx4 v[202:203], off
	v_lshl_add_u64 v[202:203], s[68:69], 0, v[132:133]
	s_mov_b32 m0, s42
	s_nop 0
	global_load_lds_dwordx4 v[202:203], off
	s_barrier
	s_waitcnt lgkmcnt(0)
	s_waitcnt lgkmcnt(0)
	v_mfma_f32_16x16x32_bf16 v[64:67], v[138:141], v[154:157], v[64:67]
	v_mfma_f32_16x16x32_bf16 v[60:63], v[146:149], v[154:157], v[60:63]
	v_mfma_f32_16x16x32_bf16 v[56:59], v[138:141], v[162:165], v[56:59]
	v_mfma_f32_16x16x32_bf16 v[52:55], v[146:149], v[162:165], v[52:55]
	v_mfma_f32_16x16x32_bf16 v[48:51], v[138:141], v[170:173], v[48:51]
	v_mfma_f32_16x16x32_bf16 v[44:47], v[146:149], v[170:173], v[44:47]
	v_mfma_f32_16x16x32_bf16 v[40:43], v[138:141], v[178:181], v[40:43]
	v_mfma_f32_16x16x32_bf16 v[36:39], v[146:149], v[178:181], v[36:39]
	v_mfma_f32_16x16x32_bf16 v[64:67], v[142:145], v[158:161], v[64:67]
	v_mfma_f32_16x16x32_bf16 v[60:63], v[150:153], v[158:161], v[60:63]
	v_mfma_f32_16x16x32_bf16 v[56:59], v[142:145], v[166:169], v[56:59]
	v_mfma_f32_16x16x32_bf16 v[52:55], v[150:153], v[166:169], v[52:55]
	v_mfma_f32_16x16x32_bf16 v[48:51], v[142:145], v[174:177], v[48:51]
	v_mfma_f32_16x16x32_bf16 v[44:47], v[150:153], v[174:177], v[44:47]
	v_mfma_f32_16x16x32_bf16 v[40:43], v[142:145], v[182:185], v[40:43]
	v_mfma_f32_16x16x32_bf16 v[36:39], v[150:153], v[182:185], v[36:39]
	s_barrier
; __device__ __forceinline__ int tid_hidden() { int t = threadIdx.x; asm volatile("" : "+v"(t)); return t; }
; #define lds lds_hidden(lds0)
; template <class Epi, class Src>
; __device__ __forceinline__ void gemm_phase(LAS unsigned char* lds, const Src S, const Epi E) {
;     ...
;         { const int tp = tid_hidden(); E.prefetch(cur, lds, par, tp, __builtin_amdgcn_readfirstlane(tp >> 6)); }
;         if (Src::GATHER && has_next) { const int tp = tid_hidden(); tab_fill(S, nxt, tp, __builtin_amdgcn_readfirstlane(tp >> 6), lds, par ^ 1); }
;         for (int t = 0; t < NKTR - 2; t += 2) {
;             const size_t k1 = (size_t)(t + 1) * kstep, k2 = (size_t)(t + 2) * kstep;
;             const char* b2 = cB + k2; const char* b3 = b2 + kstep;
;             G8_ITER(cA, par, k1, cA, par, k2, b2, b3);
;         }
	s_add_u32 s66, s34, 0x40000
	s_addc_u32 s67, s35, 0
	s_add_u32 s68, s34, 0x60000
	s_addc_u32 s69, s35, 0
	s_mov_b32 m0, s44
	s_nop 0
	v_lshl_add_u64 v[138:139], s[66:67], 0, v[132:133]
	global_load_lds_dwordx4 v[138:139], off
	v_lshl_add_u64 v[138:139], s[68:69], 0, v[132:133]
	s_mov_b32 m0, s45
	s_nop 0
	global_load_lds_dwordx4 v[138:139], off
	s_waitcnt vmcnt(6)
	s_barrier
	v_mfma_f32_16x16x32_bf16 v[30:33], v[186:189], v[154:157], v[30:33]
	v_mfma_f32_16x16x32_bf16 v[26:29], v[194:197], v[154:157], v[26:29]
	v_mfma_f32_16x16x32_bf16 v[22:25], v[186:189], v[162:165], v[22:25]
	v_mfma_f32_16x16x32_bf16 v[18:21], v[194:197], v[162:165], v[18:21]
	v_mfma_f32_16x16x32_bf16 v[14:17], v[186:189], v[170:173], v[14:17]
	v_mfma_f32_16x16x32_bf16 v[10:13], v[194:197], v[170:173], v[10:13]
	v_mfma_f32_16x16x32_bf16 v[6:9], v[186:189], v[178:181], v[6:9]
	v_mfma_f32_16x16x32_bf16 v[2:5], v[194:197], v[178:181], v[2:5]
	v_mfma_f32_16x16x32_bf16 v[30:33], v[190:193], v[158:161], v[30:33]
	v_mfma_f32_16x16x32_bf16 v[26:29], v[198:201], v[158:161], v[26:29]
	v_mfma_f32_16x16x32_bf16 v[22:25], v[190:193], v[166:169], v[22:25]
	v_mfma_f32_16x16x32_bf16 v[18:21], v[198:201], v[166:169], v[18:21]
	v_mfma_f32_16x16x32_bf16 v[14:17], v[190:193], v[174:177], v[14:17]
	v_mfma_f32_16x16x32_bf16 v[10:13], v[198:201], v[174:177], v[10:13]
	v_mfma_f32_16x16x32_bf16 v[6:9], v[190:193], v[182:185], v[6:9]
	v_mfma_f32_16x16x32_bf16 v[2:5], v[198:201], v[182:185], v[2:5]
	s_barrier
	v_add_u32_e32 v137, s48, v134
	ds_read_b128 v[140:143], v137
	ds_read_b128 v[144:147], v137 offset:1024
	ds_read_b128 v[148:151], v137 offset:2048
	ds_read_b128 v[152:155], v137 offset:3072
	s_add_u32 s66, s64, 0x40100
	s_addc_u32 s67, s65, 0
	s_add_u32 s68, s64, 0x60100
	s_addc_u32 s69, s65, 0
	s_mov_b32 m0, s46
	ds_read_b128 v[156:159], v135 offset:32768
	ds_read_b128 v[160:163], v135 offset:33792
	ds_read_b128 v[164:167], v135 offset:34816
	ds_read_b128 v[168:171], v135 offset:35840
	ds_read_b128 v[172:175], v135 offset:36864
	ds_read_b128 v[176:179], v135 offset:37888
	ds_read_b128 v[180:183], v135 offset:38912
	ds_read_b128 v[184:187], v135 offset:39936
	s_nop 0
	v_lshl_add_u64 v[138:139], s[66:67], 0, v[132:133]
	global_load_lds_dwordx4 v[138:139], off
	v_lshl_add_u64 v[138:139], s[68:69], 0, v[132:133]
	s_mov_b32 m0, s47
	s_nop 0
	global_load_lds_dwordx4 v[138:139], off
	s_waitcnt lgkmcnt(8)
	s_barrier
	s_waitcnt lgkmcnt(0)
	s_waitcnt lgkmcnt(0)
	v_mfma_f32_16x16x32_bf16 v[128:131], v[140:143], v[156:159], v[128:131]
	v_mfma_f32_16x16x32_bf16 v[124:127], v[148:151], v[156:159], v[124:127]
	v_mfma_f32_16x16x32_bf16 v[120:123], v[140:143], v[164:167], v[120:123]
	v_mfma_f32_16x16x32_bf16 v[116:119], v[148:151], v[164:167], v[116:119]
	v_mfma_f32_16x16x32_bf16 v[112:115], v[140:143], v[172:175], v[112:115]
	v_mfma_f32_16x16x32_bf16 v[108:111], v[148:151], v[172:175], v[108:111]
	v_mfma_f32_16x16x32_bf16 v[104:107], v[140:143], v[180:183], v[104:107]
	v_mfma_f32_16x16x32_bf16 v[100:103], v[148:151], v[180:183], v[100:103]
	v_mfma_f32_16x16x32_bf16 v[128:131], v[144:147], v[160:163], v[128:131]
	v_mfma_f32_16x16x32_bf16 v[124:127], v[152:155], v[160:163], v[124:127]
	v_mfma_f32_16x16x32_bf16 v[120:123], v[144:147], v[168:171], v[120:123]
	v_mfma_f32_16x16x32_bf16 v[116:119], v[152:155], v[168:171], v[116:119]
	v_mfma_f32_16x16x32_bf16 v[112:115], v[144:147], v[176:179], v[112:115]
	v_mfma_f32_16x16x32_bf16 v[108:111], v[152:155], v[176:179], v[108:111]
	v_mfma_f32_16x16x32_bf16 v[104:107], v[144:147], v[184:187], v[104:107]
	v_mfma_f32_16x16x32_bf16 v[100:103], v[152:155], v[184:187], v[100:103]
	s_barrier
	s_add_u32 s66, s34, 0x80
	s_addc_u32 s67, s35, 0
	s_add_u32 s68, s34, 0x20080
	v_add_u32_e32 v138, s53, v134
	s_addc_u32 s69, s35, 0
	s_mov_b32 m0, s49
	ds_read_b128 v[188:191], v138
	ds_read_b128 v[192:195], v138 offset:1024
	ds_read_b128 v[196:199], v138 offset:2048
	ds_read_b128 v[200:203], v138 offset:3072
	s_nop 0
	v_lshl_add_u64 v[204:205], s[66:67], 0, v[132:133]
	global_load_lds_dwordx4 v[204:205], off
	v_lshl_add_u64 v[204:205], s[68:69], 0, v[132:133]
	s_mov_b32 m0, s50
	s_nop 0
	global_load_lds_dwordx4 v[204:205], off
	s_barrier
	s_waitcnt lgkmcnt(0)
	s_waitcnt lgkmcnt(0)
	v_mfma_f32_16x16x32_bf16 v[96:99], v[188:191], v[156:159], v[96:99]
	v_mfma_f32_16x16x32_bf16 v[92:95], v[196:199], v[156:159], v[92:95]
	v_mfma_f32_16x16x32_bf16 v[88:91], v[188:191], v[164:167], v[88:91]
	v_mfma_f32_16x16x32_bf16 v[84:87], v[196:199], v[164:167], v[84:87]
	v_mfma_f32_16x16x32_bf16 v[80:83], v[188:191], v[172:175], v[80:83]
	v_mfma_f32_16x16x32_bf16 v[76:79], v[196:199], v[172:175], v[76:79]
	v_mfma_f32_16x16x32_bf16 v[72:75], v[188:191], v[180:183], v[72:75]
	v_mfma_f32_16x16x32_bf16 v[68:71], v[196:199], v[180:183], v[68:71]
	v_mfma_f32_16x16x32_bf16 v[96:99], v[192:195], v[160:163], v[96:99]
	v_mfma_f32_16x16x32_bf16 v[92:95], v[200:203], v[160:163], v[92:95]
	v_mfma_f32_16x16x32_bf16 v[88:91], v[192:195], v[168:171], v[88:91]
	v_mfma_f32_16x16x32_bf16 v[84:87], v[200:203], v[168:171], v[84:87]
	v_mfma_f32_16x16x32_bf16 v[80:83], v[192:195], v[176:179], v[80:83]
	v_mfma_f32_16x16x32_bf16 v[76:79], v[200:203], v[176:179], v[76:79]
	v_mfma_f32_16x16x32_bf16 v[72:75], v[192:195], v[184:187], v[72:75]
	v_mfma_f32_16x16x32_bf16 v[68:71], v[200:203], v[184:187], v[68:71]
	s_barrier
; __device__ __forceinline__ int tid_hidden() { int t = threadIdx.x; asm volatile("" : "+v"(t)); return t; }
; #define lds lds_hidden(lds0)
; template <class Epi, class Src>
; __device__ __forceinline__ void gemm_phase(LAS unsigned char* lds, const Src S, const Epi E) {
;     ...
;         { const int tp = tid_hidden(); E.prefetch(cur, lds, par, tp, __builtin_amdgcn_readfirstlane(tp >> 6)); }
;         if (Src::GATHER && has_next) { const int tp = tid_hidden(); tab_fill(S, nxt, tp, __builtin_amdgcn_readfirstlane(tp >> 6), lds, par ^ 1); }
;         for (int t = 0; t < NKTR - 2; t += 2) {
;             const size_t k1 = (size_t)(t + 1) * kstep, k2 = (size_t)(t + 2) * kstep;
;             const char* b2 = cB + k2; const char* b3 = b2 + kstep;
;             G8_ITER(cA, par, k1, cA, par, k2, b2, b3);
;         }
;         {
;             const int par2 = has_next ? (par ^ 1) : par;
;             const char* b3 = nB + kstep;
;             G8_ITER(cA, par, (size_t)(NKTR - 1) * kstep, nA, par2, (size_t)0, nB, b3);
	s_add_u32 s66, s64, 0x180
	s_addc_u32 s67, s65, 0
	s_add_u32 s64, s64, 0x20180
	s_addc_u32 s65, s65, 0
	s_mov_b32 m0, s51
	ds_read_b128 v[156:159], v135 offset:49152
	ds_read_b128 v[160:163], v135 offset:50176
	ds_read_b128 v[164:167], v135 offset:51200
	ds_read_b128 v[168:171], v135 offset:52224
	ds_read_b128 v[172:175], v135 offset:53248
	ds_read_b128 v[176:179], v135 offset:54272
	ds_read_b128 v[180:183], v135 offset:55296
	ds_read_b128 v[184:187], v135 offset:56320
	s_nop 0
	v_lshl_add_u64 v[204:205], s[66:67], 0, v[132:133]
	global_load_lds_dwordx4 v[204:205], off
	v_lshl_add_u64 v[204:205], s[64:65], 0, v[132:133]
	s_mov_b32 m0, s52
	s_nop 0
	global_load_lds_dwordx4 v[204:205], off
	s_barrier
	s_waitcnt lgkmcnt(0)
	s_waitcnt lgkmcnt(0)
	v_mfma_f32_16x16x32_bf16 v[64:67], v[140:143], v[156:159], v[64:67]
	v_mfma_f32_16x16x32_bf16 v[60:63], v[148:151], v[156:159], v[60:63]
	v_mfma_f32_16x16x32_bf16 v[56:59], v[140:143], v[164:167], v[56:59]
	v_mfma_f32_16x16x32_bf16 v[52:55], v[148:151], v[164:167], v[52:55]
	v_mfma_f32_16x16x32_bf16 v[48:51], v[140:143], v[172:175], v[48:51]
	v_mfma_f32_16x16x32_bf16 v[44:47], v[148:151], v[172:175], v[44:47]
	v_mfma_f32_16x16x32_bf16 v[40:43], v[140:143], v[180:183], v[40:43]
	v_mfma_f32_16x16x32_bf16 v[36:39], v[148:151], v[180:183], v[36:39]
	v_mfma_f32_16x16x32_bf16 v[64:67], v[144:147], v[160:163], v[64:67]
	v_mfma_f32_16x16x32_bf16 v[60:63], v[152:155], v[160:163], v[60:63]
	v_mfma_f32_16x16x32_bf16 v[56:59], v[144:147], v[168:171], v[56:59]
	v_mfma_f32_16x16x32_bf16 v[52:55], v[152:155], v[168:171], v[52:55]
	v_mfma_f32_16x16x32_bf16 v[48:51], v[144:147], v[176:179], v[48:51]
	v_mfma_f32_16x16x32_bf16 v[44:47], v[152:155], v[176:179], v[44:47]
	v_mfma_f32_16x16x32_bf16 v[40:43], v[144:147], v[184:187], v[40:43]
	v_mfma_f32_16x16x32_bf16 v[36:39], v[152:155], v[184:187], v[36:39]
	s_barrier
	s_add_u32 s64, s34, 0x40080
	s_addc_u32 s65, s35, 0
	s_add_u32 s34, s34, 0x60080
	s_addc_u32 s35, s35, 0
	s_mov_b32 m0, s54
	s_nop 0
	v_lshl_add_u64 v[140:141], s[64:65], 0, v[132:133]
	global_load_lds_dwordx4 v[140:141], off
	v_lshl_add_u64 v[140:141], s[34:35], 0, v[132:133]
	s_mov_b32 m0, s55
	s_nop 0
	global_load_lds_dwordx4 v[140:141], off
	s_waitcnt vmcnt(6)
	s_barrier
	v_mfma_f32_16x16x32_bf16 v[30:33], v[188:191], v[156:159], v[30:33]
	v_mfma_f32_16x16x32_bf16 v[26:29], v[196:199], v[156:159], v[26:29]
	v_mfma_f32_16x16x32_bf16 v[22:25], v[188:191], v[164:167], v[22:25]
	v_mfma_f32_16x16x32_bf16 v[18:21], v[196:199], v[164:167], v[18:21]
	v_mfma_f32_16x16x32_bf16 v[14:17], v[188:191], v[172:175], v[14:17]
	v_mfma_f32_16x16x32_bf16 v[10:13], v[196:199], v[172:175], v[10:13]
	v_mfma_f32_16x16x32_bf16 v[6:9], v[188:191], v[180:183], v[6:9]
	v_mfma_f32_16x16x32_bf16 v[2:5], v[196:199], v[180:183], v[2:5]
	v_mfma_f32_16x16x32_bf16 v[30:33], v[192:195], v[160:163], v[30:33]
	v_mfma_f32_16x16x32_bf16 v[26:29], v[200:203], v[160:163], v[26:29]
	v_mfma_f32_16x16x32_bf16 v[22:25], v[192:195], v[168:171], v[22:25]
	v_mfma_f32_16x16x32_bf16 v[18:21], v[200:203], v[168:171], v[18:21]
	v_mfma_f32_16x16x32_bf16 v[14:17], v[192:195], v[176:179], v[14:17]
	v_mfma_f32_16x16x32_bf16 v[10:13], v[200:203], v[176:179], v[10:13]
	v_mfma_f32_16x16x32_bf16 v[6:9], v[192:195], v[184:187], v[6:9]
	v_mfma_f32_16x16x32_bf16 v[2:5], v[200:203], v[184:187], v[2:5]
	s_add_i32 s61, s61, 2
	s_add_u32 s0, s0, 0x100
	s_addc_u32 s1, s1, 0
	s_cmp_gt_u32 s61, 11
	s_barrier
	s_cbranch_scc0 .LBB0_727
	s_lshl_b32 s0, s59, 8
	s_ashr_i32 s1, s0, 31
	s_lshl_b64 s[0:1], s[0:1], 11
	s_add_u32 s0, s6, s0
	s_addc_u32 s1, s7, s1
	s_and_b64 s[30:31], s[30:31], exec
	s_cselect_b32 s31, s1, s3
	s_cselect_b32 s30, s0, s2
	ds_read_b128 v[140:143], v34
	ds_read_b128 v[144:147], v34 offset:1024
	ds_read_b128 v[148:151], v34 offset:2048
	ds_read_b128 v[152:155], v34 offset:3072
	s_add_u32 s34, s2, 0x40780
	s_addc_u32 s35, s3, 0
	s_add_u32 s2, s2, 0x60780
	s_addc_u32 s3, s3, 0
	s_mov_b32 m0, s63
	ds_read_b128 v[156:159], v135
	ds_read_b128 v[160:163], v135 offset:1024
	ds_read_b128 v[164:167], v135 offset:2048
	ds_read_b128 v[168:171], v135 offset:3072
	ds_read_b128 v[172:175], v135 offset:4096
	ds_read_b128 v[176:179], v135 offset:5120
	ds_read_b128 v[180:183], v135 offset:6144
	ds_read_b128 v[184:187], v135 offset:7168
	s_nop 0
	v_lshl_add_u64 v[188:189], s[34:35], 0, v[132:133]
	global_load_lds_dwordx4 v[188:189], off
	v_lshl_add_u64 v[188:189], s[2:3], 0, v[132:133]
	s_mov_b32 m0, s62
	s_nop 0
	global_load_lds_dwordx4 v[188:189], off
	s_waitcnt lgkmcnt(8)
	s_barrier
	s_waitcnt lgkmcnt(0)
	s_waitcnt lgkmcnt(0)
	v_mfma_f32_16x16x32_bf16 v[128:131], v[140:143], v[156:159], v[128:131]
	v_mfma_f32_16x16x32_bf16 v[124:127], v[148:151], v[156:159], v[124:127]
	v_mfma_f32_16x16x32_bf16 v[120:123], v[140:143], v[164:167], v[120:123]
	v_mfma_f32_16x16x32_bf16 v[116:119], v[148:151], v[164:167], v[116:119]
	v_mfma_f32_16x16x32_bf16 v[112:115], v[140:143], v[172:175], v[112:115]
	v_mfma_f32_16x16x32_bf16 v[108:111], v[148:151], v[172:175], v[108:111]
	v_mfma_f32_16x16x32_bf16 v[104:107], v[140:143], v[180:183], v[104:107]
	v_mfma_f32_16x16x32_bf16 v[100:103], v[148:151], v[180:183], v[100:103]
	v_mfma_f32_16x16x32_bf16 v[128:131], v[144:147], v[160:163], v[128:131]
	v_mfma_f32_16x16x32_bf16 v[124:127], v[152:155], v[160:163], v[124:127]
	v_mfma_f32_16x16x32_bf16 v[120:123], v[144:147], v[168:171], v[120:123]
	v_mfma_f32_16x16x32_bf16 v[116:119], v[152:155], v[168:171], v[116:119]
	v_mfma_f32_16x16x32_bf16 v[188:191], v[144:147], v[176:179], v[112:115]
	v_mfma_f32_16x16x32_bf16 v[192:195], v[152:155], v[176:179], v[108:111]
	v_mfma_f32_16x16x32_bf16 v[104:107], v[144:147], v[184:187], v[104:107]
	v_mfma_f32_16x16x32_bf16 v[100:103], v[152:155], v[184:187], v[100:103]
	s_barrier
; __device__ __forceinline__ int tid_hidden() { int t = threadIdx.x; asm volatile("" : "+v"(t)); return t; }
; #define lds lds_hidden(lds0)
; template <class Epi, class Src>
; __device__ __forceinline__ void gemm_phase(LAS unsigned char* lds, const Src S, const Epi E) {
;     ...
;         { const int tp = tid_hidden(); E.prefetch(cur, lds, par, tp, __builtin_amdgcn_readfirstlane(tp >> 6)); }
;         if (Src::GATHER && has_next) { const int tp = tid_hidden(); tab_fill(S, nxt, tp, __builtin_amdgcn_readfirstlane(tp >> 6), lds, par ^ 1); }
;         for (int t = 0; t < NKTR - 2; t += 2) {
;             const size_t k1 = (size_t)(t + 1) * kstep, k2 = (size_t)(t + 2) * kstep;
;             const char* b2 = cB + k2; const char* b3 = b2 + kstep;
;             G8_ITER(cA, par, k1, cA, par, k2, b2, b3);
;         }
;         {
;             const int par2 = has_next ? (par ^ 1) : par;
;             const char* b3 = nB + kstep;
;             G8_ITER(cA, par, (size_t)(NKTR - 1) * kstep, nA, par2, (size_t)0, nB, b3);
	s_mov_b64 s[2:3], s[12:13]
	s_mov_b64 s[34:35], s[14:15]
	s_mov_b32 m0, s39
	ds_read_b128 v[108:111], v136
	ds_read_b128 v[112:115], v136 offset:1024
	ds_read_b128 v[196:199], v136 offset:2048
	ds_read_b128 v[200:203], v136 offset:3072
	s_nop 0
	v_lshl_add_u64 v[204:205], s[2:3], 0, v[132:133]
	global_load_lds_dwordx4 v[204:205], off
	v_lshl_add_u64 v[204:205], s[34:35], 0, v[132:133]
	s_mov_b32 m0, s40
	s_nop 0
	global_load_lds_dwordx4 v[204:205], off
	s_barrier
	s_waitcnt lgkmcnt(0)
	s_waitcnt lgkmcnt(0)
	v_mfma_f32_16x16x32_bf16 v[96:99], v[108:111], v[156:159], v[96:99]
	v_mfma_f32_16x16x32_bf16 v[92:95], v[196:199], v[156:159], v[92:95]
	v_mfma_f32_16x16x32_bf16 v[88:91], v[108:111], v[164:167], v[88:91]
	v_mfma_f32_16x16x32_bf16 v[84:87], v[196:199], v[164:167], v[84:87]
	v_mfma_f32_16x16x32_bf16 v[80:83], v[108:111], v[172:175], v[80:83]
	v_mfma_f32_16x16x32_bf16 v[76:79], v[196:199], v[172:175], v[76:79]
	v_mfma_f32_16x16x32_bf16 v[72:75], v[108:111], v[180:183], v[72:75]
	v_mfma_f32_16x16x32_bf16 v[68:71], v[196:199], v[180:183], v[68:71]
	v_mfma_f32_16x16x32_bf16 v[204:207], v[112:115], v[160:163], v[96:99]
	v_mfma_f32_16x16x32_bf16 v[156:159], v[200:203], v[160:163], v[92:95]
	v_mfma_f32_16x16x32_bf16 v[88:91], v[112:115], v[168:171], v[88:91]
	v_mfma_f32_16x16x32_bf16 v[84:87], v[200:203], v[168:171], v[84:87]
	v_mfma_f32_16x16x32_bf16 v[160:163], v[112:115], v[176:179], v[80:83]
	v_mfma_f32_16x16x32_bf16 v[164:167], v[200:203], v[176:179], v[76:79]
	v_mfma_f32_16x16x32_bf16 v[72:75], v[112:115], v[184:187], v[72:75]
	v_mfma_f32_16x16x32_bf16 v[68:71], v[200:203], v[184:187], v[68:71]
	s_barrier
	s_add_u32 s2, s30, 0x20000
	s_addc_u32 s3, s31, 0
	s_mov_b64 s[34:35], s[30:31]
	s_mov_b32 m0, s41
	ds_read_b128 v[76:79], v135 offset:16384
	ds_read_b128 v[80:83], v135 offset:17408
	ds_read_b128 v[92:95], v135 offset:18432
	ds_read_b128 v[96:99], v135 offset:19456
	ds_read_b128 v[168:171], v135 offset:20480
	ds_read_b128 v[172:175], v135 offset:21504
	ds_read_b128 v[176:179], v135 offset:22528
	ds_read_b128 v[180:183], v135 offset:23552
	s_nop 0
	v_lshl_add_u64 v[184:185], s[34:35], 0, v[132:133]
	global_load_lds_dwordx4 v[184:185], off
	v_lshl_add_u64 v[184:185], s[2:3], 0, v[132:133]
	s_mov_b32 m0, s42
	s_nop 0
	global_load_lds_dwordx4 v[184:185], off
	s_barrier
	s_waitcnt lgkmcnt(0)
	s_waitcnt lgkmcnt(0)
	v_mfma_f32_16x16x32_bf16 v[64:67], v[140:143], v[76:79], v[64:67]
	v_mfma_f32_16x16x32_bf16 v[60:63], v[148:151], v[76:79], v[60:63]
	v_mfma_f32_16x16x32_bf16 v[56:59], v[140:143], v[92:95], v[56:59]
	v_mfma_f32_16x16x32_bf16 v[52:55], v[148:151], v[92:95], v[52:55]
	v_mfma_f32_16x16x32_bf16 v[48:51], v[140:143], v[168:171], v[48:51]
	v_mfma_f32_16x16x32_bf16 v[44:47], v[148:151], v[168:171], v[44:47]
	v_mfma_f32_16x16x32_bf16 v[40:43], v[140:143], v[176:179], v[40:43]
	v_mfma_f32_16x16x32_bf16 v[36:39], v[148:151], v[176:179], v[36:39]
	v_mfma_f32_16x16x32_bf16 v[64:67], v[144:147], v[80:83], v[64:67]
	v_mfma_f32_16x16x32_bf16 v[60:63], v[152:155], v[80:83], v[60:63]
	v_mfma_f32_16x16x32_bf16 v[56:59], v[144:147], v[96:99], v[56:59]
	v_mfma_f32_16x16x32_bf16 v[52:55], v[152:155], v[96:99], v[52:55]
	v_mfma_f32_16x16x32_bf16 v[184:187], v[144:147], v[172:175], v[48:51]
	v_mfma_f32_16x16x32_bf16 v[208:211], v[152:155], v[172:175], v[44:47]
	v_mfma_f32_16x16x32_bf16 v[40:43], v[144:147], v[180:183], v[40:43]
	v_mfma_f32_16x16x32_bf16 v[36:39], v[152:155], v[180:183], v[36:39]
	s_barrier
	s_mov_b64 s[2:3], s[16:17]
	s_mov_b64 s[34:35], s[18:19]
	s_mov_b32 m0, s44
	s_nop 0
	v_lshl_add_u64 v[44:45], s[2:3], 0, v[132:133]
	global_load_lds_dwordx4 v[44:45], off
	v_lshl_add_u64 v[44:45], s[34:35], 0, v[132:133]
	s_mov_b32 m0, s45
	s_nop 0
	global_load_lds_dwordx4 v[44:45], off
	s_waitcnt vmcnt(6)
	s_barrier
	v_mfma_f32_16x16x32_bf16 v[30:33], v[108:111], v[76:79], v[30:33]
	v_mfma_f32_16x16x32_bf16 v[26:29], v[196:199], v[76:79], v[26:29]
	v_mfma_f32_16x16x32_bf16 v[22:25], v[108:111], v[92:95], v[22:25]
	v_mfma_f32_16x16x32_bf16 v[18:21], v[196:199], v[92:95], v[18:21]
	v_mfma_f32_16x16x32_bf16 v[14:17], v[108:111], v[168:171], v[14:17]
	v_mfma_f32_16x16x32_bf16 v[10:13], v[196:199], v[168:171], v[10:13]
	v_mfma_f32_16x16x32_bf16 v[6:9], v[108:111], v[176:179], v[6:9]
	v_mfma_f32_16x16x32_bf16 v[2:5], v[196:199], v[176:179], v[2:5]
	v_mfma_f32_16x16x32_bf16 v[140:143], v[112:115], v[80:83], v[30:33]
	v_mfma_f32_16x16x32_bf16 v[144:147], v[200:203], v[80:83], v[26:29]
	v_mfma_f32_16x16x32_bf16 v[22:25], v[112:115], v[96:99], v[22:25]
	v_mfma_f32_16x16x32_bf16 v[18:21], v[200:203], v[96:99], v[18:21]
	v_mfma_f32_16x16x32_bf16 v[148:151], v[112:115], v[172:175], v[14:17]
	v_mfma_f32_16x16x32_bf16 v[152:155], v[200:203], v[172:175], v[10:13]
	v_mfma_f32_16x16x32_bf16 v[6:9], v[112:115], v[180:183], v[6:9]
	v_mfma_f32_16x16x32_bf16 v[2:5], v[200:203], v[180:183], v[2:5]
	s_barrier
	ds_read_b128 v[10:13], v137
	ds_read_b128 v[14:17], v137 offset:1024
	ds_read_b128 v[168:171], v137 offset:2048
	ds_read_b128 v[172:175], v137 offset:3072
	s_add_u32 s2, s30, 0x40000
	s_addc_u32 s3, s31, 0
	s_add_u32 s34, s30, 0x60000
	s_addc_u32 s35, s31, 0
	s_mov_b32 m0, s46
	ds_read_b128 v[26:29], v135 offset:32768
	ds_read_b128 v[30:33], v135 offset:33792
	ds_read_b128 v[44:47], v135 offset:34816
	ds_read_b128 v[48:51], v135 offset:35840
	ds_read_b128 v[176:179], v135 offset:36864
	ds_read_b128 v[180:183], v135 offset:37888
	ds_read_b128 v[196:199], v135 offset:38912
	ds_read_b128 v[200:203], v135 offset:39936
	s_nop 0
	v_lshl_add_u64 v[76:77], s[2:3], 0, v[132:133]
	global_load_lds_dwordx4 v[76:77], off
	v_lshl_add_u64 v[76:77], s[34:35], 0, v[132:133]
	s_mov_b32 m0, s47
	s_nop 0
	global_load_lds_dwordx4 v[76:77], off
	s_waitcnt lgkmcnt(8)
	s_barrier
; __device__ __forceinline__ int tid_hidden() { int t = threadIdx.x; asm volatile("" : "+v"(t)); return t; }
; #define lds lds_hidden(lds0)
; template <class Epi, class Src>
; __device__ __forceinline__ void gemm_phase(LAS unsigned char* lds, const Src S, const Epi E) {
;     ...
;         { const int tp = tid_hidden(); E.prefetch(cur, lds, par, tp, __builtin_amdgcn_readfirstlane(tp >> 6)); }
;         if (Src::GATHER && has_next) { const int tp = tid_hidden(); tab_fill(S, nxt, tp, __builtin_amdgcn_readfirstlane(tp >> 6), lds, par ^ 1); }
;         for (int t = 0; t < NKTR - 2; t += 2) {
;             const size_t k1 = (size_t)(t + 1) * kstep, k2 = (size_t)(t + 2) * kstep;
;             const char* b2 = cB + k2; const char* b3 = b2 + kstep;
;             G8_ITER(cA, par, k1, cA, par, k2, b2, b3);
;         }
;         {
;             const int par2 = has_next ? (par ^ 1) : par;
;             const char* b3 = nB + kstep;
;             G8_ITER(cA, par, (size_t)(NKTR - 1) * kstep, nA, par2, (size_t)0, nB, b3);
	s_waitcnt lgkmcnt(0)
	s_waitcnt lgkmcnt(0)
	v_mfma_f32_16x16x32_bf16 v[76:79], v[10:13], v[26:29], v[128:131]
	v_mfma_f32_16x16x32_bf16 v[212:215], v[14:17], v[30:33], v[76:79]
	v_mfma_f32_16x16x32_bf16 v[76:79], v[168:171], v[26:29], v[124:127]
	v_mfma_f32_16x16x32_bf16 v[124:127], v[172:175], v[30:33], v[76:79]
	v_mfma_f32_16x16x32_bf16 v[76:79], v[10:13], v[44:47], v[120:123]
	v_mfma_f32_16x16x32_bf16 v[112:115], v[14:17], v[48:51], v[76:79]
	v_mfma_f32_16x16x32_bf16 v[76:79], v[168:171], v[44:47], v[116:119]
	v_mfma_f32_16x16x32_bf16 v[108:111], v[172:175], v[48:51], v[76:79]
	v_mfma_f32_16x16x32_bf16 v[76:79], v[10:13], v[176:179], v[188:191]
	v_mfma_f32_16x16x32_bf16 v[96:99], v[14:17], v[180:183], v[76:79]
	v_mfma_f32_16x16x32_bf16 v[76:79], v[168:171], v[176:179], v[192:195]
	v_mfma_f32_16x16x32_bf16 v[92:95], v[172:175], v[180:183], v[76:79]
	v_mfma_f32_16x16x32_bf16 v[76:79], v[10:13], v[196:199], v[104:107]
	v_mfma_f32_16x16x32_bf16 v[80:83], v[14:17], v[200:203], v[76:79]
	v_mfma_f32_16x16x32_bf16 v[76:79], v[168:171], v[196:199], v[100:103]
	v_mfma_f32_16x16x32_bf16 v[76:79], v[172:175], v[200:203], v[76:79]
	s_barrier
	s_mov_b64 s[2:3], s[20:21]
	s_mov_b64 s[34:35], s[22:23]
	s_mov_b32 m0, s49
	ds_read_b128 v[128:131], v138
	ds_read_b128 v[188:191], v138 offset:1024
	ds_read_b128 v[192:195], v138 offset:2048
	ds_read_b128 v[136:139], v138 offset:3072
	s_nop 0
	v_lshl_add_u64 v[100:101], s[2:3], 0, v[132:133]
	global_load_lds_dwordx4 v[100:101], off
	v_lshl_add_u64 v[100:101], s[34:35], 0, v[132:133]
	s_mov_b32 m0, s50
	s_nop 0
	global_load_lds_dwordx4 v[100:101], off
	s_barrier
	s_waitcnt lgkmcnt(0)
	s_waitcnt lgkmcnt(0)
	v_mfma_f32_16x16x32_bf16 v[100:103], v[128:131], v[26:29], v[204:207]
	v_mfma_f32_16x16x32_bf16 v[26:29], v[192:195], v[26:29], v[156:159]
	v_mfma_f32_16x16x32_bf16 v[116:119], v[136:139], v[30:33], v[26:29]
	v_mfma_f32_16x16x32_bf16 v[26:29], v[128:131], v[44:47], v[88:91]
	v_mfma_f32_16x16x32_bf16 v[104:107], v[188:191], v[48:51], v[26:29]
	v_mfma_f32_16x16x32_bf16 v[26:29], v[192:195], v[44:47], v[84:87]
	v_mfma_f32_16x16x32_bf16 v[120:123], v[188:191], v[30:33], v[100:103]
	v_mfma_f32_16x16x32_bf16 v[100:103], v[136:139], v[48:51], v[26:29]
	v_mfma_f32_16x16x32_bf16 v[26:29], v[128:131], v[176:179], v[160:163]
	v_mfma_f32_16x16x32_bf16 v[88:91], v[188:191], v[180:183], v[26:29]
	v_mfma_f32_16x16x32_bf16 v[26:29], v[192:195], v[176:179], v[164:167]
	v_mfma_f32_16x16x32_bf16 v[84:87], v[136:139], v[180:183], v[26:29]
	v_mfma_f32_16x16x32_bf16 v[26:29], v[128:131], v[196:199], v[72:75]
	v_mfma_f32_16x16x32_bf16 v[72:75], v[188:191], v[200:203], v[26:29]
	v_mfma_f32_16x16x32_bf16 v[26:29], v[192:195], v[196:199], v[68:71]
	v_mfma_f32_16x16x32_bf16 v[68:71], v[136:139], v[200:203], v[26:29]
	s_barrier
	s_add_u32 s2, s30, 0x80
	s_addc_u32 s3, s31, 0
	s_add_u32 s30, s30, 0x20080
	s_addc_u32 s31, s31, 0
	s_mov_b32 m0, s51
	ds_read_b128 v[156:159], v135 offset:49152
	ds_read_b128 v[160:163], v135 offset:50176
	ds_read_b128 v[164:167], v135 offset:51200
	ds_read_b128 v[176:179], v135 offset:52224
	ds_read_b128 v[180:183], v135 offset:53248
	ds_read_b128 v[196:199], v135 offset:54272
	ds_read_b128 v[200:203], v135 offset:55296
	ds_read_b128 v[204:207], v135 offset:56320
	s_nop 0
	v_lshl_add_u64 v[26:27], s[2:3], 0, v[132:133]
	global_load_lds_dwordx4 v[26:27], off
	v_lshl_add_u64 v[26:27], s[30:31], 0, v[132:133]
	s_mov_b32 m0, s52
	s_nop 0
	global_load_lds_dwordx4 v[26:27], off
	s_barrier
	s_waitcnt lgkmcnt(0)
	s_waitcnt lgkmcnt(0)
	v_mfma_f32_16x16x32_bf16 v[26:29], v[10:13], v[156:159], v[64:67]
	v_mfma_f32_16x16x32_bf16 v[64:67], v[14:17], v[160:163], v[26:29]
	v_mfma_f32_16x16x32_bf16 v[26:29], v[168:171], v[156:159], v[60:63]
	v_mfma_f32_16x16x32_bf16 v[60:63], v[172:175], v[160:163], v[26:29]
	v_mfma_f32_16x16x32_bf16 v[26:29], v[10:13], v[164:167], v[56:59]
	v_mfma_f32_16x16x32_bf16 v[48:51], v[14:17], v[176:179], v[26:29]
	v_mfma_f32_16x16x32_bf16 v[26:29], v[168:171], v[164:167], v[52:55]
	v_mfma_f32_16x16x32_bf16 v[44:47], v[172:175], v[176:179], v[26:29]
	v_mfma_f32_16x16x32_bf16 v[26:29], v[10:13], v[180:183], v[184:187]
	v_mfma_f32_16x16x32_bf16 v[10:13], v[10:13], v[200:203], v[40:43]
	v_mfma_f32_16x16x32_bf16 v[30:33], v[14:17], v[196:199], v[26:29]
	v_mfma_f32_16x16x32_bf16 v[26:29], v[168:171], v[180:183], v[208:211]
	v_mfma_f32_16x16x32_bf16 v[14:17], v[14:17], v[204:207], v[10:13]
	v_mfma_f32_16x16x32_bf16 v[10:13], v[168:171], v[200:203], v[36:39]
	v_mfma_f32_16x16x32_bf16 v[26:29], v[172:175], v[196:199], v[26:29]
	v_mfma_f32_16x16x32_bf16 v[10:13], v[172:175], v[204:207], v[10:13]
	s_barrier
	s_mov_b64 s[2:3], s[24:25]
	s_mov_b64 s[30:31], s[26:27]
	s_mov_b32 m0, s54
	s_nop 0
	v_lshl_add_u64 v[36:37], s[2:3], 0, v[132:133]
	global_load_lds_dwordx4 v[36:37], off
	v_lshl_add_u64 v[36:37], s[30:31], 0, v[132:133]
	s_mov_b32 m0, s55
	s_nop 0
	global_load_lds_dwordx4 v[36:37], off
	s_waitcnt vmcnt(6)
	s_barrier
	v_mfma_f32_16x16x32_bf16 v[36:39], v[128:131], v[156:159], v[140:143]
	v_mfma_f32_16x16x32_bf16 v[56:59], v[188:191], v[160:163], v[36:39]
	v_mfma_f32_16x16x32_bf16 v[36:39], v[192:195], v[156:159], v[144:147]
	v_mfma_f32_16x16x32_bf16 v[18:21], v[192:195], v[164:167], v[18:21]
	v_mfma_f32_16x16x32_bf16 v[52:55], v[136:139], v[160:163], v[36:39]
	v_mfma_f32_16x16x32_bf16 v[22:25], v[128:131], v[164:167], v[22:25]
	v_mfma_f32_16x16x32_bf16 v[36:39], v[136:139], v[176:179], v[18:21]
	v_mfma_f32_16x16x32_bf16 v[18:21], v[128:131], v[180:183], v[148:151]
	v_mfma_f32_16x16x32_bf16 v[40:43], v[188:191], v[176:179], v[22:25]
	v_mfma_f32_16x16x32_bf16 v[22:25], v[188:191], v[196:199], v[18:21]
	v_mfma_f32_16x16x32_bf16 v[18:21], v[192:195], v[180:183], v[152:155]
	v_mfma_f32_16x16x32_bf16 v[6:9], v[128:131], v[200:203], v[6:9]
	v_mfma_f32_16x16x32_bf16 v[2:5], v[192:195], v[200:203], v[2:5]
	v_mfma_f32_16x16x32_bf16 v[18:21], v[136:139], v[196:199], v[18:21]
	v_mfma_f32_16x16x32_bf16 v[6:9], v[188:191], v[204:207], v[6:9]
	v_mfma_f32_16x16x32_bf16 v[2:5], v[136:139], v[204:207], v[2:5]
	v_mov_b32_e32 v34, v0
	s_barrier
; __device__ __forceinline__ unsigned cvt_pk_bf16(float lo, float hi) { const bf16x2_t r = __builtin_convertvector((f32x2_t){lo, hi}, bf16x2_t); return __builtin_bit_cast(unsigned, r); }
; __device__ __forceinline__ float kf(float x) { asm volatile("" : "+s"(x)); return x; }
; #define EP_FENCE() asm volatile("" ::: "memory")
;     __device__ __forceinline__ void operator()(const f32x4 (&acc)[2][2][4][2], const Unit& u, int wr, int wc, int fr, int fq, LAS unsigned char*, int) const {
;     ...
;         } else if (pn <= 4 || pn >= 11) {
;             bf16_t* dst = (pn <= 4) ? QH : GS;
;             const unsigned off0 = (unsigned)((row0 * 512 + (pn <= 4 ? (pn - 3) : (pn - 11)) * BM + wc * 32 + 8 * fq) * 2);
;             const float nl = kf(-1.4426950408889634f), on = kf(1.f); const f32x2_t nl2 = (f32x2_t){nl, nl}, one2 = (f32x2_t){on, on};
; #pragma unroll
;             for (int ai = 0; ai < 2; ++ai)
; #pragma unroll
;                 for (int m = 0; m < 4; ++m) {
; #pragma unroll
;                     for (int bj = 0; bj < 2; ++bj) {
;                         const f32x4 v0 = acc[ai][bj][m][0], v1 = acc[ai][bj][m][1];
;                         unsigned wq[4];
; #pragma unroll
;                         for (int q = 0; q < 4; ++q) {
;                             const f32x2_t x = q < 2 ? (f32x2_t){v0[2 * q], v0[2 * q + 1]} : (f32x2_t){v1[2 * q - 4], v1[2 * q - 3]};
;                             const f32x2_t t = x * nl2;
;                             const f32x2_t d = (f32x2_t){__builtin_amdgcn_exp2f(t.x), __builtin_amdgcn_exp2f(t.y)} + one2;
;                             const f32x2_t o = x * (f32x2_t){__builtin_amdgcn_rcpf(d.x), __builtin_amdgcn_rcpf(d.y)};
;                             wq[q] = cvt_pk_bf16(o.x, o.y);
;                         }
;                         *(u32x4*)((char*)dst + off0 + (unsigned)(((ai * HALF + m * 16) * 512 + bj * HALF) * 2)) = (u32x4){wq[0], wq[1], wq[2], wq[3]};
;                     }
;                     EP_FENCE();
;                 }
	s_lshl_b32 s30, s60, 8
	v_readfirstlane_b32 s2, v34
	s_and_b32 s3, s2, 0xc0
	s_lshr_b32 s2, s2, 2
	s_and_b32 s2, s2, 0x3fffc0
	s_add_i32 s2, s2, s30
	s_mov_b32 s30, 0xbfb8aa3b
	v_and_b32_e32 v128, 48, v34
	v_pk_mul_f32 v[130:131], v[212:213], s[30:31] op_sel_hi:[1,0]
	v_and_or_b32 v34, v34, 15, s2
	v_exp_f32_e32 v130, v130
	v_exp_f32_e32 v131, v131
	s_mov_b32 s2, 1.0
	v_lshlrev_b32_e32 v34, 10, v34
	v_pk_add_f32 v[130:131], s[2:3], v[130:131] op_sel_hi:[0,1]
	v_rcp_f32_e32 v130, v130
	v_rcp_f32_e32 v131, v131
	v_or3_b32 v34, v34, s3, v128
	v_lshl_add_u64 v[128:129], s[8:9], 0, v[34:35]
	s_mov_b32 s60, s59
	v_pk_mul_f32 v[130:131], v[212:213], v[130:131]
	s_nop 0
	v_cvt_pk_bf16_f32 v136, v130, v131
	v_pk_mul_f32 v[130:131], v[214:215], s[30:31] op_sel_hi:[1,0]
	s_nop 0
	v_exp_f32_e32 v130, v130
	v_exp_f32_e32 v131, v131
	s_nop 0
	v_pk_add_f32 v[130:131], s[2:3], v[130:131] op_sel_hi:[0,1]
	v_rcp_f32_e32 v130, v130
	v_rcp_f32_e32 v131, v131
	s_nop 0
	v_pk_mul_f32 v[130:131], v[214:215], v[130:131]
	s_nop 0
	v_cvt_pk_bf16_f32 v137, v130, v131
	v_pk_mul_f32 v[130:131], v[124:125], s[30:31] op_sel_hi:[1,0]
	s_nop 0
	v_exp_f32_e32 v130, v130
	v_exp_f32_e32 v131, v131
	s_nop 0
	v_pk_add_f32 v[130:131], s[2:3], v[130:131] op_sel_hi:[0,1]
	v_rcp_f32_e32 v130, v130
	v_rcp_f32_e32 v131, v131
	s_nop 0
	v_pk_mul_f32 v[124:125], v[124:125], v[130:131]
	s_nop 0
	v_cvt_pk_bf16_f32 v138, v124, v125
	v_pk_mul_f32 v[124:125], v[126:127], s[30:31] op_sel_hi:[1,0]
	s_nop 0
	v_exp_f32_e32 v124, v124
	v_exp_f32_e32 v125, v125
	s_nop 0
	v_pk_add_f32 v[124:125], s[2:3], v[124:125] op_sel_hi:[0,1]
	v_rcp_f32_e32 v124, v124
	v_rcp_f32_e32 v125, v125
	s_nop 0
	v_pk_mul_f32 v[124:125], v[126:127], v[124:125]
	s_nop 0
	v_cvt_pk_bf16_f32 v139, v124, v125
	v_pk_mul_f32 v[124:125], v[120:121], s[30:31] op_sel_hi:[1,0]
	global_store_dwordx4 v34, v[136:139], s[8:9] offset:512
	v_exp_f32_e32 v124, v124
	v_exp_f32_e32 v125, v125
	s_nop 0
	v_pk_add_f32 v[124:125], s[2:3], v[124:125] op_sel_hi:[0,1]
	v_rcp_f32_e32 v124, v124
	v_rcp_f32_e32 v125, v125
	s_nop 0
	v_pk_mul_f32 v[120:121], v[120:121], v[124:125]
	v_pk_mul_f32 v[124:125], v[122:123], s[30:31] op_sel_hi:[1,0]
	v_cvt_pk_bf16_f32 v120, v120, v121
	v_exp_f32_e32 v124, v124
	v_exp_f32_e32 v125, v125
	s_nop 0
	v_pk_add_f32 v[124:125], s[2:3], v[124:125] op_sel_hi:[0,1]
	v_rcp_f32_e32 v124, v124
	v_rcp_f32_e32 v125, v125
	s_nop 0
	v_pk_mul_f32 v[122:123], v[122:123], v[124:125]
	s_nop 0
	v_cvt_pk_bf16_f32 v121, v122, v123
	v_pk_mul_f32 v[122:123], v[116:117], s[30:31] op_sel_hi:[1,0]
	s_nop 0
	v_exp_f32_e32 v122, v122
	v_exp_f32_e32 v123, v123
	s_nop 0
	v_pk_add_f32 v[122:123], s[2:3], v[122:123] op_sel_hi:[0,1]
	v_rcp_f32_e32 v122, v122
	v_rcp_f32_e32 v123, v123
	s_nop 0
	v_pk_mul_f32 v[116:117], v[116:117], v[122:123]
	s_nop 0
	v_cvt_pk_bf16_f32 v122, v116, v117
	v_pk_mul_f32 v[116:117], v[118:119], s[30:31] op_sel_hi:[1,0]
	s_nop 0
	v_exp_f32_e32 v116, v116
	v_exp_f32_e32 v117, v117
	s_nop 0
	v_pk_add_f32 v[116:117], s[2:3], v[116:117] op_sel_hi:[0,1]
	v_rcp_f32_e32 v116, v116
	v_rcp_f32_e32 v117, v117
	s_nop 0
	v_pk_mul_f32 v[116:117], v[118:119], v[116:117]
	s_nop 0
	v_cvt_pk_bf16_f32 v123, v116, v117
	v_pk_mul_f32 v[116:117], v[112:113], s[30:31] op_sel_hi:[1,0]
	global_store_dwordx4 v34, v[120:123], s[8:9] offset:768
	v_exp_f32_e32 v116, v116
	v_exp_f32_e32 v117, v117
	s_nop 0
	v_pk_add_f32 v[116:117], s[2:3], v[116:117] op_sel_hi:[0,1]
	v_rcp_f32_e32 v116, v116
	v_rcp_f32_e32 v117, v117
	s_nop 0
	v_pk_mul_f32 v[112:113], v[112:113], v[116:117]
	v_pk_mul_f32 v[116:117], v[114:115], s[30:31] op_sel_hi:[1,0]
	v_cvt_pk_bf16_f32 v112, v112, v113
	v_exp_f32_e32 v116, v116
	v_exp_f32_e32 v117, v117
	s_nop 0
	v_pk_add_f32 v[116:117], s[2:3], v[116:117] op_sel_hi:[0,1]
	v_rcp_f32_e32 v116, v116
	v_rcp_f32_e32 v117, v117
	s_nop 0
	v_pk_mul_f32 v[114:115], v[114:115], v[116:117]
	s_nop 0
	v_cvt_pk_bf16_f32 v113, v114, v115
	v_pk_mul_f32 v[114:115], v[108:109], s[30:31] op_sel_hi:[1,0]
	s_nop 0
	v_exp_f32_e32 v114, v114
	v_exp_f32_e32 v115, v115
	s_nop 0
	v_pk_add_f32 v[114:115], s[2:3], v[114:115] op_sel_hi:[0,1]
	v_rcp_f32_e32 v114, v114
	v_rcp_f32_e32 v115, v115
	s_nop 0
	v_pk_mul_f32 v[108:109], v[108:109], v[114:115]
	s_nop 0
	v_cvt_pk_bf16_f32 v114, v108, v109
	v_pk_mul_f32 v[108:109], v[110:111], s[30:31] op_sel_hi:[1,0]
	s_nop 0
	v_exp_f32_e32 v108, v108
	v_exp_f32_e32 v109, v109
	s_nop 0
	v_pk_add_f32 v[108:109], s[2:3], v[108:109] op_sel_hi:[0,1]
	v_rcp_f32_e32 v108, v108
	v_rcp_f32_e32 v109, v109
	s_nop 0
	v_pk_mul_f32 v[108:109], v[110:111], v[108:109]
	v_pk_mul_f32 v[110:111], v[104:105], s[30:31] op_sel_hi:[1,0]
	v_cvt_pk_bf16_f32 v115, v108, v109
	v_exp_f32_e32 v110, v110
	v_exp_f32_e32 v111, v111
	v_add_co_u32_e32 v108, vcc, s92, v128
	v_pk_add_f32 v[110:111], s[2:3], v[110:111] op_sel_hi:[0,1]
	v_rcp_f32_e32 v110, v110
	v_rcp_f32_e32 v111, v111
	v_addc_co_u32_e32 v109, vcc, 0, v129, vcc
	global_store_dwordx4 v[108:109], v[112:115], off offset:512
	v_pk_mul_f32 v[104:105], v[104:105], v[110:111]
	v_pk_mul_f32 v[110:111], v[106:107], s[30:31] op_sel_hi:[1,0]
	v_cvt_pk_bf16_f32 v104, v104, v105
	v_exp_f32_e32 v110, v110
	v_exp_f32_e32 v111, v111
	s_nop 0
	v_pk_add_f32 v[110:111], s[2:3], v[110:111] op_sel_hi:[0,1]
	v_rcp_f32_e32 v110, v110
	v_rcp_f32_e32 v111, v111
	s_nop 0
	v_pk_mul_f32 v[106:107], v[106:107], v[110:111]
	s_nop 0
	v_cvt_pk_bf16_f32 v105, v106, v107
	v_pk_mul_f32 v[106:107], v[100:101], s[30:31] op_sel_hi:[1,0]
	s_nop 0
	v_exp_f32_e32 v106, v106
	v_exp_f32_e32 v107, v107
	s_nop 0
	v_pk_add_f32 v[106:107], s[2:3], v[106:107] op_sel_hi:[0,1]
	v_rcp_f32_e32 v106, v106
	v_rcp_f32_e32 v107, v107
; __device__ __forceinline__ unsigned cvt_pk_bf16(float lo, float hi) { const bf16x2_t r = __builtin_convertvector((f32x2_t){lo, hi}, bf16x2_t); return __builtin_bit_cast(unsigned, r); }
; __device__ __forceinline__ float kf(float x) { asm volatile("" : "+s"(x)); return x; }
; #define EP_FENCE() asm volatile("" ::: "memory")
;     __device__ __forceinline__ void operator()(const f32x4 (&acc)[2][2][4][2], const Unit& u, int wr, int wc, int fr, int fq, LAS unsigned char*, int) const {
;     ...
;         } else if (pn <= 4 || pn >= 11) {
;             bf16_t* dst = (pn <= 4) ? QH : GS;
;             const unsigned off0 = (unsigned)((row0 * 512 + (pn <= 4 ? (pn - 3) : (pn - 11)) * BM + wc * 32 + 8 * fq) * 2);
;             const float nl = kf(-1.4426950408889634f), on = kf(1.f); const f32x2_t nl2 = (f32x2_t){nl, nl}, one2 = (f32x2_t){on, on};
; #pragma unroll
;             for (int ai = 0; ai < 2; ++ai)
; #pragma unroll
;                 for (int m = 0; m < 4; ++m) {
; #pragma unroll
;                     for (int bj = 0; bj < 2; ++bj) {
;                         const f32x4 v0 = acc[ai][bj][m][0], v1 = acc[ai][bj][m][1];
;                         unsigned wq[4];
; #pragma unroll
;                         for (int q = 0; q < 4; ++q) {
;                             const f32x2_t x = q < 2 ? (f32x2_t){v0[2 * q], v0[2 * q + 1]} : (f32x2_t){v1[2 * q - 4], v1[2 * q - 3]};
;                             const f32x2_t t = x * nl2;
;                             const f32x2_t d = (f32x2_t){__builtin_amdgcn_exp2f(t.x), __builtin_amdgcn_exp2f(t.y)} + one2;
;                             const f32x2_t o = x * (f32x2_t){__builtin_amdgcn_rcpf(d.x), __builtin_amdgcn_rcpf(d.y)};
;                             wq[q] = cvt_pk_bf16(o.x, o.y);
;                         }
;                         *(u32x4*)((char*)dst + off0 + (unsigned)(((ai * HALF + m * 16) * 512 + bj * HALF) * 2)) = (u32x4){wq[0], wq[1], wq[2], wq[3]};
;                     }
;                     EP_FENCE();
;                 }
	s_nop 0
	v_pk_mul_f32 v[100:101], v[100:101], v[106:107]
	s_nop 0
	v_cvt_pk_bf16_f32 v106, v100, v101
	v_pk_mul_f32 v[100:101], v[102:103], s[30:31] op_sel_hi:[1,0]
	s_nop 0
	v_exp_f32_e32 v100, v100
	v_exp_f32_e32 v101, v101
	s_nop 0
	v_pk_add_f32 v[100:101], s[2:3], v[100:101] op_sel_hi:[0,1]
	v_rcp_f32_e32 v100, v100
	v_rcp_f32_e32 v101, v101
	s_nop 0
	v_pk_mul_f32 v[100:101], v[102:103], v[100:101]
	s_nop 0
	v_cvt_pk_bf16_f32 v107, v100, v101
	v_pk_mul_f32 v[100:101], v[96:97], s[30:31] op_sel_hi:[1,0]
	global_store_dwordx4 v[108:109], v[104:107], off offset:768
	v_exp_f32_e32 v100, v100
	v_exp_f32_e32 v101, v101
	s_nop 0
	v_pk_add_f32 v[100:101], s[2:3], v[100:101] op_sel_hi:[0,1]
	v_rcp_f32_e32 v100, v100
	v_rcp_f32_e32 v101, v101
	s_nop 0
	v_pk_mul_f32 v[96:97], v[96:97], v[100:101]
	v_pk_mul_f32 v[100:101], v[98:99], s[30:31] op_sel_hi:[1,0]
	v_cvt_pk_bf16_f32 v96, v96, v97
	v_exp_f32_e32 v100, v100
	v_exp_f32_e32 v101, v101
	s_nop 0
	v_pk_add_f32 v[100:101], s[2:3], v[100:101] op_sel_hi:[0,1]
	v_rcp_f32_e32 v100, v100
	v_rcp_f32_e32 v101, v101
	s_nop 0
	v_pk_mul_f32 v[98:99], v[98:99], v[100:101]
	s_nop 0
	v_cvt_pk_bf16_f32 v97, v98, v99
	v_pk_mul_f32 v[98:99], v[92:93], s[30:31] op_sel_hi:[1,0]
	s_nop 0
	v_exp_f32_e32 v98, v98
	v_exp_f32_e32 v99, v99
	s_nop 0
	v_pk_add_f32 v[98:99], s[2:3], v[98:99] op_sel_hi:[0,1]
	v_rcp_f32_e32 v98, v98
	v_rcp_f32_e32 v99, v99
	s_nop 0
	v_pk_mul_f32 v[92:93], v[92:93], v[98:99]
	s_nop 0
	v_cvt_pk_bf16_f32 v98, v92, v93
	v_pk_mul_f32 v[92:93], v[94:95], s[30:31] op_sel_hi:[1,0]
	s_nop 0
	v_exp_f32_e32 v92, v92
	v_exp_f32_e32 v93, v93
	s_nop 0
	v_pk_add_f32 v[92:93], s[2:3], v[92:93] op_sel_hi:[0,1]
	v_rcp_f32_e32 v92, v92
	v_rcp_f32_e32 v93, v93
	s_nop 0
	v_pk_mul_f32 v[92:93], v[94:95], v[92:93]
	v_pk_mul_f32 v[94:95], v[88:89], s[30:31] op_sel_hi:[1,0]
	v_cvt_pk_bf16_f32 v99, v92, v93
	v_exp_f32_e32 v94, v94
	v_exp_f32_e32 v95, v95
	v_add_co_u32_e32 v92, vcc, s70, v128
	v_pk_add_f32 v[94:95], s[2:3], v[94:95] op_sel_hi:[0,1]
	v_rcp_f32_e32 v94, v94
	v_rcp_f32_e32 v95, v95
	v_addc_co_u32_e32 v93, vcc, 0, v129, vcc
	global_store_dwordx4 v[92:93], v[96:99], off offset:512
	v_pk_mul_f32 v[88:89], v[88:89], v[94:95]
	v_pk_mul_f32 v[94:95], v[90:91], s[30:31] op_sel_hi:[1,0]
	v_cvt_pk_bf16_f32 v88, v88, v89
	v_exp_f32_e32 v94, v94
	v_exp_f32_e32 v95, v95
	s_nop 0
	v_pk_add_f32 v[94:95], s[2:3], v[94:95] op_sel_hi:[0,1]
	v_rcp_f32_e32 v94, v94
	v_rcp_f32_e32 v95, v95
	s_nop 0
	v_pk_mul_f32 v[90:91], v[90:91], v[94:95]
	s_nop 0
	v_cvt_pk_bf16_f32 v89, v90, v91
	v_pk_mul_f32 v[90:91], v[84:85], s[30:31] op_sel_hi:[1,0]
	s_nop 0
	v_exp_f32_e32 v90, v90
	v_exp_f32_e32 v91, v91
	s_nop 0
	v_pk_add_f32 v[90:91], s[2:3], v[90:91] op_sel_hi:[0,1]
	v_rcp_f32_e32 v90, v90
	v_rcp_f32_e32 v91, v91
	s_nop 0
	v_pk_mul_f32 v[84:85], v[84:85], v[90:91]
	s_nop 0
	v_cvt_pk_bf16_f32 v90, v84, v85
	v_pk_mul_f32 v[84:85], v[86:87], s[30:31] op_sel_hi:[1,0]
	s_nop 0
	v_exp_f32_e32 v84, v84
	v_exp_f32_e32 v85, v85
	s_nop 0
	v_pk_add_f32 v[84:85], s[2:3], v[84:85] op_sel_hi:[0,1]
	v_rcp_f32_e32 v84, v84
	v_rcp_f32_e32 v85, v85
	s_nop 0
	v_pk_mul_f32 v[84:85], v[86:87], v[84:85]
	s_nop 0
	v_cvt_pk_bf16_f32 v91, v84, v85
	v_pk_mul_f32 v[84:85], v[80:81], s[30:31] op_sel_hi:[1,0]
	global_store_dwordx4 v[92:93], v[88:91], off offset:768
	v_exp_f32_e32 v84, v84
	v_exp_f32_e32 v85, v85
	s_nop 0
	v_pk_add_f32 v[84:85], s[2:3], v[84:85] op_sel_hi:[0,1]
	v_rcp_f32_e32 v84, v84
	v_rcp_f32_e32 v85, v85
	s_nop 0
	v_pk_mul_f32 v[80:81], v[80:81], v[84:85]
	v_pk_mul_f32 v[84:85], v[82:83], s[30:31] op_sel_hi:[1,0]
	v_cvt_pk_bf16_f32 v80, v80, v81
	v_exp_f32_e32 v84, v84
	v_exp_f32_e32 v85, v85
	s_nop 0
	v_pk_add_f32 v[84:85], s[2:3], v[84:85] op_sel_hi:[0,1]
	v_rcp_f32_e32 v84, v84
	v_rcp_f32_e32 v85, v85
	s_nop 0
	v_pk_mul_f32 v[82:83], v[82:83], v[84:85]
	s_nop 0
	v_cvt_pk_bf16_f32 v81, v82, v83
	v_pk_mul_f32 v[82:83], v[76:77], s[30:31] op_sel_hi:[1,0]
	s_nop 0
	v_exp_f32_e32 v82, v82
	v_exp_f32_e32 v83, v83
	s_nop 0
	v_pk_add_f32 v[82:83], s[2:3], v[82:83] op_sel_hi:[0,1]
	v_rcp_f32_e32 v82, v82
	v_rcp_f32_e32 v83, v83
	s_nop 0
	v_pk_mul_f32 v[76:77], v[76:77], v[82:83]
	s_nop 0
	v_cvt_pk_bf16_f32 v82, v76, v77
	v_pk_mul_f32 v[76:77], v[78:79], s[30:31] op_sel_hi:[1,0]
	s_nop 0
	v_exp_f32_e32 v76, v76
	v_exp_f32_e32 v77, v77
	s_nop 0
	v_pk_add_f32 v[76:77], s[2:3], v[76:77] op_sel_hi:[0,1]
	v_rcp_f32_e32 v76, v76
	v_rcp_f32_e32 v77, v77
	s_nop 0
	v_pk_mul_f32 v[76:77], v[78:79], v[76:77]
	v_pk_mul_f32 v[78:79], v[72:73], s[30:31] op_sel_hi:[1,0]
	v_cvt_pk_bf16_f32 v83, v76, v77
	v_exp_f32_e32 v78, v78
	v_exp_f32_e32 v79, v79
	v_add_co_u32_e32 v76, vcc, s71, v128
	v_pk_add_f32 v[78:79], s[2:3], v[78:79] op_sel_hi:[0,1]
	v_rcp_f32_e32 v78, v78
	v_rcp_f32_e32 v79, v79
	v_addc_co_u32_e32 v77, vcc, 0, v129, vcc
	global_store_dwordx4 v[76:77], v[80:83], off offset:512
	v_pk_mul_f32 v[72:73], v[72:73], v[78:79]
	v_pk_mul_f32 v[78:79], v[74:75], s[30:31] op_sel_hi:[1,0]
	v_cvt_pk_bf16_f32 v72, v72, v73
	v_exp_f32_e32 v78, v78
	v_exp_f32_e32 v79, v79
	s_nop 0
	v_pk_add_f32 v[78:79], s[2:3], v[78:79] op_sel_hi:[0,1]
	v_rcp_f32_e32 v78, v78
	v_rcp_f32_e32 v79, v79
	s_nop 0
	v_pk_mul_f32 v[74:75], v[74:75], v[78:79]
	s_nop 0
	v_cvt_pk_bf16_f32 v73, v74, v75
	v_pk_mul_f32 v[74:75], v[68:69], s[30:31] op_sel_hi:[1,0]
	s_nop 0
	v_exp_f32_e32 v74, v74
	v_exp_f32_e32 v75, v75
	s_nop 0
	v_pk_add_f32 v[74:75], s[2:3], v[74:75] op_sel_hi:[0,1]
	v_rcp_f32_e32 v74, v74
	v_rcp_f32_e32 v75, v75
	s_nop 0
	v_pk_mul_f32 v[68:69], v[68:69], v[74:75]
	s_nop 0
	v_cvt_pk_bf16_f32 v74, v68, v69
	v_pk_mul_f32 v[68:69], v[70:71], s[30:31] op_sel_hi:[1,0]
	s_nop 0
; __device__ __forceinline__ unsigned cvt_pk_bf16(float lo, float hi) { const bf16x2_t r = __builtin_convertvector((f32x2_t){lo, hi}, bf16x2_t); return __builtin_bit_cast(unsigned, r); }
; __device__ __forceinline__ float kf(float x) { asm volatile("" : "+s"(x)); return x; }
; #define EP_FENCE() asm volatile("" ::: "memory")
;     __device__ __forceinline__ void operator()(const f32x4 (&acc)[2][2][4][2], const Unit& u, int wr, int wc, int fr, int fq, LAS unsigned char*, int) const {
;     ...
;         } else if (pn <= 4 || pn >= 11) {
;             bf16_t* dst = (pn <= 4) ? QH : GS;
;             const unsigned off0 = (unsigned)((row0 * 512 + (pn <= 4 ? (pn - 3) : (pn - 11)) * BM + wc * 32 + 8 * fq) * 2);
;             const float nl = kf(-1.4426950408889634f), on = kf(1.f); const f32x2_t nl2 = (f32x2_t){nl, nl}, one2 = (f32x2_t){on, on};
; #pragma unroll
;             for (int ai = 0; ai < 2; ++ai)
; #pragma unroll
;                 for (int m = 0; m < 4; ++m) {
; #pragma unroll
;                     for (int bj = 0; bj < 2; ++bj) {
;                         const f32x4 v0 = acc[ai][bj][m][0], v1 = acc[ai][bj][m][1];
;                         unsigned wq[4];
; #pragma unroll
;                         for (int q = 0; q < 4; ++q) {
;                             const f32x2_t x = q < 2 ? (f32x2_t){v0[2 * q], v0[2 * q + 1]} : (f32x2_t){v1[2 * q - 4], v1[2 * q - 3]};
;                             const f32x2_t t = x * nl2;
;                             const f32x2_t d = (f32x2_t){__builtin_amdgcn_exp2f(t.x), __builtin_amdgcn_exp2f(t.y)} + one2;
;                             const f32x2_t o = x * (f32x2_t){__builtin_amdgcn_rcpf(d.x), __builtin_amdgcn_rcpf(d.y)};
;                             wq[q] = cvt_pk_bf16(o.x, o.y);
;                         }
;                         *(u32x4*)((char*)dst + off0 + (unsigned)(((ai * HALF + m * 16) * 512 + bj * HALF) * 2)) = (u32x4){wq[0], wq[1], wq[2], wq[3]};
;                     }
;                     EP_FENCE();
;                 }
	v_exp_f32_e32 v68, v68
	v_exp_f32_e32 v69, v69
	s_nop 0
	v_pk_add_f32 v[68:69], s[2:3], v[68:69] op_sel_hi:[0,1]
	v_rcp_f32_e32 v68, v68
	v_rcp_f32_e32 v69, v69
	s_nop 0
	v_pk_mul_f32 v[68:69], v[70:71], v[68:69]
	s_nop 0
	v_cvt_pk_bf16_f32 v75, v68, v69
	v_pk_mul_f32 v[68:69], v[64:65], s[30:31] op_sel_hi:[1,0]
	global_store_dwordx4 v[76:77], v[72:75], off offset:768
	v_exp_f32_e32 v68, v68
	v_exp_f32_e32 v69, v69
	s_nop 0
	v_pk_add_f32 v[68:69], s[2:3], v[68:69] op_sel_hi:[0,1]
	v_rcp_f32_e32 v68, v68
	v_rcp_f32_e32 v69, v69
	s_nop 0
	v_pk_mul_f32 v[64:65], v[64:65], v[68:69]
	v_pk_mul_f32 v[68:69], v[66:67], s[30:31] op_sel_hi:[1,0]
	v_cvt_pk_bf16_f32 v64, v64, v65
	v_exp_f32_e32 v68, v68
	v_exp_f32_e32 v69, v69
	s_nop 0
	v_pk_add_f32 v[68:69], s[2:3], v[68:69] op_sel_hi:[0,1]
	v_rcp_f32_e32 v68, v68
	v_rcp_f32_e32 v69, v69
	s_nop 0
	v_pk_mul_f32 v[66:67], v[66:67], v[68:69]
	s_nop 0
	v_cvt_pk_bf16_f32 v65, v66, v67
	v_pk_mul_f32 v[66:67], v[60:61], s[30:31] op_sel_hi:[1,0]
	s_nop 0
	v_exp_f32_e32 v66, v66
	v_exp_f32_e32 v67, v67
	s_nop 0
	v_pk_add_f32 v[66:67], s[2:3], v[66:67] op_sel_hi:[0,1]
	v_rcp_f32_e32 v66, v66
	v_rcp_f32_e32 v67, v67
	s_nop 0
	v_pk_mul_f32 v[60:61], v[60:61], v[66:67]
	s_nop 0
	v_cvt_pk_bf16_f32 v66, v60, v61
	v_pk_mul_f32 v[60:61], v[62:63], s[30:31] op_sel_hi:[1,0]
	s_nop 0
	v_exp_f32_e32 v60, v60
	v_exp_f32_e32 v61, v61
	s_nop 0
	v_pk_add_f32 v[60:61], s[2:3], v[60:61] op_sel_hi:[0,1]
	v_rcp_f32_e32 v60, v60
	v_rcp_f32_e32 v61, v61
	s_nop 0
	v_pk_mul_f32 v[60:61], v[62:63], v[60:61]
	v_pk_mul_f32 v[62:63], v[56:57], s[30:31] op_sel_hi:[1,0]
	v_cvt_pk_bf16_f32 v67, v60, v61
	v_exp_f32_e32 v62, v62
	v_exp_f32_e32 v63, v63
	v_add_co_u32_e32 v60, vcc, s72, v128
	v_pk_add_f32 v[62:63], s[2:3], v[62:63] op_sel_hi:[0,1]
	v_rcp_f32_e32 v62, v62
	v_rcp_f32_e32 v63, v63
	v_addc_co_u32_e32 v61, vcc, 0, v129, vcc
	global_store_dwordx4 v[60:61], v[64:67], off offset:512
	v_pk_mul_f32 v[56:57], v[56:57], v[62:63]
	v_pk_mul_f32 v[62:63], v[58:59], s[30:31] op_sel_hi:[1,0]
	v_cvt_pk_bf16_f32 v56, v56, v57
	v_exp_f32_e32 v62, v62
	v_exp_f32_e32 v63, v63
	s_nop 0
	v_pk_add_f32 v[62:63], s[2:3], v[62:63] op_sel_hi:[0,1]
	v_rcp_f32_e32 v62, v62
	v_rcp_f32_e32 v63, v63
	s_nop 0
	v_pk_mul_f32 v[58:59], v[58:59], v[62:63]
	s_nop 0
	v_cvt_pk_bf16_f32 v57, v58, v59
	v_pk_mul_f32 v[58:59], v[52:53], s[30:31] op_sel_hi:[1,0]
	s_nop 0
	v_exp_f32_e32 v58, v58
	v_exp_f32_e32 v59, v59
	s_nop 0
	v_pk_add_f32 v[58:59], s[2:3], v[58:59] op_sel_hi:[0,1]
	v_rcp_f32_e32 v58, v58
	v_rcp_f32_e32 v59, v59
	s_nop 0
	v_pk_mul_f32 v[52:53], v[52:53], v[58:59]
	s_nop 0
	v_cvt_pk_bf16_f32 v58, v52, v53
	v_pk_mul_f32 v[52:53], v[54:55], s[30:31] op_sel_hi:[1,0]
	s_nop 0
	v_exp_f32_e32 v52, v52
	v_exp_f32_e32 v53, v53
	s_nop 0
	v_pk_add_f32 v[52:53], s[2:3], v[52:53] op_sel_hi:[0,1]
	v_rcp_f32_e32 v52, v52
	v_rcp_f32_e32 v53, v53
	s_nop 0
	v_pk_mul_f32 v[52:53], v[54:55], v[52:53]
	s_nop 0
	v_cvt_pk_bf16_f32 v59, v52, v53
	v_pk_mul_f32 v[52:53], v[48:49], s[30:31] op_sel_hi:[1,0]
	global_store_dwordx4 v[60:61], v[56:59], off offset:768
	v_exp_f32_e32 v52, v52
	v_exp_f32_e32 v53, v53
	s_nop 0
	v_pk_add_f32 v[52:53], s[2:3], v[52:53] op_sel_hi:[0,1]
	v_rcp_f32_e32 v52, v52
	v_rcp_f32_e32 v53, v53
	s_nop 0
	v_pk_mul_f32 v[48:49], v[48:49], v[52:53]
	v_pk_mul_f32 v[52:53], v[50:51], s[30:31] op_sel_hi:[1,0]
	v_cvt_pk_bf16_f32 v48, v48, v49
	v_exp_f32_e32 v52, v52
	v_exp_f32_e32 v53, v53
	s_nop 0
	v_pk_add_f32 v[52:53], s[2:3], v[52:53] op_sel_hi:[0,1]
	v_rcp_f32_e32 v52, v52
	v_rcp_f32_e32 v53, v53
	s_nop 0
	v_pk_mul_f32 v[50:51], v[50:51], v[52:53]
	s_nop 0
	v_cvt_pk_bf16_f32 v49, v50, v51
	v_pk_mul_f32 v[50:51], v[44:45], s[30:31] op_sel_hi:[1,0]
	s_nop 0
	v_exp_f32_e32 v50, v50
	v_exp_f32_e32 v51, v51
	s_nop 0
	v_pk_add_f32 v[50:51], s[2:3], v[50:51] op_sel_hi:[0,1]
	v_rcp_f32_e32 v50, v50
	v_rcp_f32_e32 v51, v51
	s_nop 0
	v_pk_mul_f32 v[44:45], v[44:45], v[50:51]
	s_nop 0
	v_cvt_pk_bf16_f32 v50, v44, v45
	v_pk_mul_f32 v[44:45], v[46:47], s[30:31] op_sel_hi:[1,0]
	s_nop 0
	v_exp_f32_e32 v44, v44
	v_exp_f32_e32 v45, v45
	s_nop 0
	v_pk_add_f32 v[44:45], s[2:3], v[44:45] op_sel_hi:[0,1]
	v_rcp_f32_e32 v44, v44
	v_rcp_f32_e32 v45, v45
	s_nop 0
	v_pk_mul_f32 v[44:45], v[46:47], v[44:45]
	v_pk_mul_f32 v[46:47], v[40:41], s[30:31] op_sel_hi:[1,0]
	v_cvt_pk_bf16_f32 v51, v44, v45
	v_exp_f32_e32 v46, v46
	v_exp_f32_e32 v47, v47
	v_add_co_u32_e32 v44, vcc, s73, v128
	v_pk_add_f32 v[46:47], s[2:3], v[46:47] op_sel_hi:[0,1]
	v_rcp_f32_e32 v46, v46
	v_rcp_f32_e32 v47, v47
	v_addc_co_u32_e32 v45, vcc, 0, v129, vcc
	global_store_dwordx4 v[44:45], v[48:51], off offset:512
	v_pk_mul_f32 v[40:41], v[40:41], v[46:47]
	v_pk_mul_f32 v[46:47], v[42:43], s[30:31] op_sel_hi:[1,0]
	v_cvt_pk_bf16_f32 v40, v40, v41
	v_exp_f32_e32 v46, v46
	v_exp_f32_e32 v47, v47
	s_nop 0
	v_pk_add_f32 v[46:47], s[2:3], v[46:47] op_sel_hi:[0,1]
	v_rcp_f32_e32 v46, v46
	v_rcp_f32_e32 v47, v47
	s_nop 0
	v_pk_mul_f32 v[42:43], v[42:43], v[46:47]
	s_nop 0
	v_cvt_pk_bf16_f32 v41, v42, v43
	v_pk_mul_f32 v[42:43], v[36:37], s[30:31] op_sel_hi:[1,0]
	s_nop 0
	v_exp_f32_e32 v42, v42
	v_exp_f32_e32 v43, v43
	s_nop 0
	v_pk_add_f32 v[42:43], s[2:3], v[42:43] op_sel_hi:[0,1]
	v_rcp_f32_e32 v42, v42
	v_rcp_f32_e32 v43, v43
	s_nop 0
	v_pk_mul_f32 v[36:37], v[36:37], v[42:43]
	s_nop 0
	v_cvt_pk_bf16_f32 v42, v36, v37
	v_pk_mul_f32 v[36:37], v[38:39], s[30:31] op_sel_hi:[1,0]
	s_nop 0
	v_exp_f32_e32 v36, v36
	v_exp_f32_e32 v37, v37
	s_nop 0
	v_pk_add_f32 v[36:37], s[2:3], v[36:37] op_sel_hi:[0,1]
	v_rcp_f32_e32 v36, v36
	v_rcp_f32_e32 v37, v37
	s_nop 0
	v_pk_mul_f32 v[36:37], v[38:39], v[36:37]
; __device__ __forceinline__ unsigned cvt_pk_bf16(float lo, float hi) { const bf16x2_t r = __builtin_convertvector((f32x2_t){lo, hi}, bf16x2_t); return __builtin_bit_cast(unsigned, r); }
; __device__ __forceinline__ float kf(float x) { asm volatile("" : "+s"(x)); return x; }
; #define EP_FENCE() asm volatile("" ::: "memory")
; template <class Epi, class Src>
; __device__ __forceinline__ void gemm_phase(LAS unsigned char* lds, const Src S, const Epi E) {
;     ...
;         { int tz = threadIdx.x; asm volatile("" : "+v"(tz));
;           const int wid2 = __builtin_amdgcn_readfirstlane(tz >> 6), lane2 = tz & 63;
;           E(acc, cur, wid2 >> 2, wid2 & 3, lane2 & 15, lane2 >> 4, lds, par); }
;         if (!has_next) break;
;     __device__ __forceinline__ void operator()(const f32x4 (&acc)[2][2][4][2], const Unit& u, int wr, int wc, int fr, int fq, LAS unsigned char*, int) const {
;     ...
;         } else if (pn <= 4 || pn >= 11) {
;             bf16_t* dst = (pn <= 4) ? QH : GS;
;             const unsigned off0 = (unsigned)((row0 * 512 + (pn <= 4 ? (pn - 3) : (pn - 11)) * BM + wc * 32 + 8 * fq) * 2);
;             const float nl = kf(-1.4426950408889634f), on = kf(1.f); const f32x2_t nl2 = (f32x2_t){nl, nl}, one2 = (f32x2_t){on, on};
; #pragma unroll
;             for (int ai = 0; ai < 2; ++ai)
; #pragma unroll
;                 for (int m = 0; m < 4; ++m) {
; #pragma unroll
;                     for (int bj = 0; bj < 2; ++bj) {
;                         const f32x4 v0 = acc[ai][bj][m][0], v1 = acc[ai][bj][m][1];
;                         unsigned wq[4];
; #pragma unroll
;                         for (int q = 0; q < 4; ++q) {
;                             const f32x2_t x = q < 2 ? (f32x2_t){v0[2 * q], v0[2 * q + 1]} : (f32x2_t){v1[2 * q - 4], v1[2 * q - 3]};
;                             const f32x2_t t = x * nl2;
;                             const f32x2_t d = (f32x2_t){__builtin_amdgcn_exp2f(t.x), __builtin_amdgcn_exp2f(t.y)} + one2;
;                             const f32x2_t o = x * (f32x2_t){__builtin_amdgcn_rcpf(d.x), __builtin_amdgcn_rcpf(d.y)};
;                             wq[q] = cvt_pk_bf16(o.x, o.y);
;                         }
;                         *(u32x4*)((char*)dst + off0 + (unsigned)(((ai * HALF + m * 16) * 512 + bj * HALF) * 2)) = (u32x4){wq[0], wq[1], wq[2], wq[3]};
;                     }
;                     EP_FENCE();
;                 }
	s_nop 0
	v_cvt_pk_bf16_f32 v43, v36, v37
	v_pk_mul_f32 v[36:37], v[30:31], s[30:31] op_sel_hi:[1,0]
	global_store_dwordx4 v[44:45], v[40:43], off offset:768
	v_exp_f32_e32 v36, v36
	v_exp_f32_e32 v37, v37
	s_nop 0
	v_pk_add_f32 v[36:37], s[2:3], v[36:37] op_sel_hi:[0,1]
	v_rcp_f32_e32 v36, v36
	v_rcp_f32_e32 v37, v37
	s_nop 0
	v_pk_mul_f32 v[30:31], v[30:31], v[36:37]
	v_pk_mul_f32 v[36:37], v[32:33], s[30:31] op_sel_hi:[1,0]
	v_cvt_pk_bf16_f32 v30, v30, v31
	v_exp_f32_e32 v36, v36
	v_exp_f32_e32 v37, v37
	s_nop 0
	v_pk_add_f32 v[36:37], s[2:3], v[36:37] op_sel_hi:[0,1]
	v_rcp_f32_e32 v36, v36
	v_rcp_f32_e32 v37, v37
	s_nop 0
	v_pk_mul_f32 v[32:33], v[32:33], v[36:37]
	s_nop 0
	v_cvt_pk_bf16_f32 v31, v32, v33
	v_pk_mul_f32 v[32:33], v[26:27], s[30:31] op_sel_hi:[1,0]
	s_nop 0
	v_exp_f32_e32 v32, v32
	v_exp_f32_e32 v33, v33
	s_nop 0
	v_pk_add_f32 v[32:33], s[2:3], v[32:33] op_sel_hi:[0,1]
	v_rcp_f32_e32 v32, v32
	v_rcp_f32_e32 v33, v33
	s_nop 0
	v_pk_mul_f32 v[26:27], v[26:27], v[32:33]
	s_nop 0
	v_cvt_pk_bf16_f32 v32, v26, v27
	v_pk_mul_f32 v[26:27], v[28:29], s[30:31] op_sel_hi:[1,0]
	s_nop 0
	v_exp_f32_e32 v26, v26
	v_exp_f32_e32 v27, v27
	s_nop 0
	v_pk_add_f32 v[26:27], s[2:3], v[26:27] op_sel_hi:[0,1]
	v_rcp_f32_e32 v26, v26
	v_rcp_f32_e32 v27, v27
	s_nop 0
	v_pk_mul_f32 v[26:27], v[28:29], v[26:27]
	v_pk_mul_f32 v[28:29], v[22:23], s[30:31] op_sel_hi:[1,0]
	v_cvt_pk_bf16_f32 v33, v26, v27
	v_exp_f32_e32 v28, v28
	v_exp_f32_e32 v29, v29
	v_add_co_u32_e32 v26, vcc, s74, v128
	v_pk_add_f32 v[28:29], s[2:3], v[28:29] op_sel_hi:[0,1]
	v_rcp_f32_e32 v28, v28
	v_rcp_f32_e32 v29, v29
	v_addc_co_u32_e32 v27, vcc, 0, v129, vcc
	global_store_dwordx4 v[26:27], v[30:33], off offset:512
	v_pk_mul_f32 v[22:23], v[22:23], v[28:29]
	v_pk_mul_f32 v[28:29], v[24:25], s[30:31] op_sel_hi:[1,0]
	v_cvt_pk_bf16_f32 v22, v22, v23
	v_exp_f32_e32 v28, v28
	v_exp_f32_e32 v29, v29
	s_nop 0
	v_pk_add_f32 v[28:29], s[2:3], v[28:29] op_sel_hi:[0,1]
	v_rcp_f32_e32 v28, v28
	v_rcp_f32_e32 v29, v29
	s_nop 0
	v_pk_mul_f32 v[24:25], v[24:25], v[28:29]
	s_nop 0
	v_cvt_pk_bf16_f32 v23, v24, v25
	v_pk_mul_f32 v[24:25], v[18:19], s[30:31] op_sel_hi:[1,0]
	s_nop 0
	v_exp_f32_e32 v24, v24
	v_exp_f32_e32 v25, v25
	s_nop 0
	v_pk_add_f32 v[24:25], s[2:3], v[24:25] op_sel_hi:[0,1]
	v_rcp_f32_e32 v24, v24
	v_rcp_f32_e32 v25, v25
	s_nop 0
	v_pk_mul_f32 v[18:19], v[18:19], v[24:25]
	s_nop 0
	v_cvt_pk_bf16_f32 v24, v18, v19
	v_pk_mul_f32 v[18:19], v[20:21], s[30:31] op_sel_hi:[1,0]
	s_nop 0
	v_exp_f32_e32 v18, v18
	v_exp_f32_e32 v19, v19
	s_nop 0
	v_pk_add_f32 v[18:19], s[2:3], v[18:19] op_sel_hi:[0,1]
	v_rcp_f32_e32 v18, v18
	v_rcp_f32_e32 v19, v19
	s_nop 0
	v_pk_mul_f32 v[18:19], v[20:21], v[18:19]
	s_nop 0
	v_cvt_pk_bf16_f32 v25, v18, v19
	v_pk_mul_f32 v[18:19], v[14:15], s[30:31] op_sel_hi:[1,0]
	global_store_dwordx4 v[26:27], v[22:25], off offset:768
	v_exp_f32_e32 v18, v18
	v_exp_f32_e32 v19, v19
	s_nop 0
	v_pk_add_f32 v[18:19], s[2:3], v[18:19] op_sel_hi:[0,1]
	v_rcp_f32_e32 v18, v18
	v_rcp_f32_e32 v19, v19
	s_nop 0
	v_pk_mul_f32 v[14:15], v[14:15], v[18:19]
	v_pk_mul_f32 v[18:19], v[16:17], s[30:31] op_sel_hi:[1,0]
	v_cvt_pk_bf16_f32 v14, v14, v15
	v_exp_f32_e32 v18, v18
	v_exp_f32_e32 v19, v19
	s_nop 0
	v_pk_add_f32 v[18:19], s[2:3], v[18:19] op_sel_hi:[0,1]
	v_rcp_f32_e32 v18, v18
	v_rcp_f32_e32 v19, v19
	s_nop 0
	v_pk_mul_f32 v[16:17], v[16:17], v[18:19]
	s_nop 0
	v_cvt_pk_bf16_f32 v15, v16, v17
	v_pk_mul_f32 v[16:17], v[10:11], s[30:31] op_sel_hi:[1,0]
	s_nop 0
	v_exp_f32_e32 v16, v16
	v_exp_f32_e32 v17, v17
	s_nop 0
	v_pk_add_f32 v[16:17], s[2:3], v[16:17] op_sel_hi:[0,1]
	v_rcp_f32_e32 v16, v16
	v_rcp_f32_e32 v17, v17
	s_nop 0
	v_pk_mul_f32 v[10:11], v[10:11], v[16:17]
	s_nop 0
	v_cvt_pk_bf16_f32 v16, v10, v11
	v_pk_mul_f32 v[10:11], v[12:13], s[30:31] op_sel_hi:[1,0]
	s_nop 0
	v_exp_f32_e32 v10, v10
	v_exp_f32_e32 v11, v11
	s_nop 0
	v_pk_add_f32 v[10:11], s[2:3], v[10:11] op_sel_hi:[0,1]
	v_rcp_f32_e32 v10, v10
	v_rcp_f32_e32 v11, v11
	s_nop 0
	v_pk_mul_f32 v[10:11], v[12:13], v[10:11]
	v_pk_mul_f32 v[12:13], v[6:7], s[30:31] op_sel_hi:[1,0]
	v_cvt_pk_bf16_f32 v17, v10, v11
	v_exp_f32_e32 v12, v12
	v_exp_f32_e32 v13, v13
	v_add_co_u32_e32 v10, vcc, s75, v128
	v_pk_add_f32 v[12:13], s[2:3], v[12:13] op_sel_hi:[0,1]
	v_rcp_f32_e32 v12, v12
	v_rcp_f32_e32 v13, v13
	v_addc_co_u32_e32 v11, vcc, 0, v129, vcc
	global_store_dwordx4 v[10:11], v[14:17], off offset:512
	v_pk_mul_f32 v[6:7], v[6:7], v[12:13]
	v_pk_mul_f32 v[12:13], v[8:9], s[30:31] op_sel_hi:[1,0]
	v_cvt_pk_bf16_f32 v6, v6, v7
	v_exp_f32_e32 v12, v12
	v_exp_f32_e32 v13, v13
	s_and_b64 vcc, exec, s[28:29]
	v_pk_add_f32 v[12:13], s[2:3], v[12:13] op_sel_hi:[0,1]
	v_rcp_f32_e32 v12, v12
	v_rcp_f32_e32 v13, v13
	s_nop 0
	v_pk_mul_f32 v[8:9], v[8:9], v[12:13]
	s_nop 0
	v_cvt_pk_bf16_f32 v7, v8, v9
	v_pk_mul_f32 v[8:9], v[2:3], s[30:31] op_sel_hi:[1,0]
	s_nop 0
	v_exp_f32_e32 v8, v8
	v_exp_f32_e32 v9, v9
	s_nop 0
	v_pk_add_f32 v[8:9], s[2:3], v[8:9] op_sel_hi:[0,1]
	v_rcp_f32_e32 v8, v8
	v_rcp_f32_e32 v9, v9
	s_nop 0
	v_pk_mul_f32 v[2:3], v[2:3], v[8:9]
	s_nop 0
	v_cvt_pk_bf16_f32 v8, v2, v3
	v_pk_mul_f32 v[2:3], v[4:5], s[30:31] op_sel_hi:[1,0]
	s_nop 0
	v_exp_f32_e32 v2, v2
	v_exp_f32_e32 v3, v3
	s_nop 0
	v_pk_add_f32 v[2:3], s[2:3], v[2:3] op_sel_hi:[0,1]
	v_rcp_f32_e32 v2, v2
	v_rcp_f32_e32 v3, v3
	s_mov_b64 s[2:3], s[0:1]
	v_pk_mul_f32 v[2:3], v[4:5], v[2:3]
	s_nop 0
	v_cvt_pk_bf16_f32 v9, v2, v3
	global_store_dwordx4 v[10:11], v[6:9], off offset:768
	s_cbranch_vccz .LBB0_720
	s_waitcnt vmcnt(0)
	s_cmpk_gt_u32 s37, 0xff
	s_cbranch_scc1 .LBB0_731
	s_barrier

; __device__ __forceinline__ int tid_hidden() { int t = threadIdx.x; asm volatile("" : "+v"(t)); return t; }
; #define lds lds_hidden(lds0)
; template <class Epi, class Src>
; __device__ __forceinline__ void gemm_phase(LAS unsigned char* lds, const Src S, const Epi E) {
;     ...
;         { const int tp = tid_hidden(); E.prefetch(cur, lds, par, tp, __builtin_amdgcn_readfirstlane(tp >> 6)); }
;         if (Src::GATHER && has_next) { const int tp = tid_hidden(); tab_fill(S, nxt, tp, __builtin_amdgcn_readfirstlane(tp >> 6), lds, par ^ 1); }
;         for (int t = 0; t < NKTR - 2; t += 2) {
;             const size_t k1 = (size_t)(t + 1) * kstep, k2 = (size_t)(t + 2) * kstep;
;             const char* b2 = cB + k2; const char* b3 = b2 + kstep;
;             G8_ITER(cA, par, k1, cA, par, k2, b2, b3);
;         }
.LBB0_1193:
	s_add_u32 s12, s14, s0
	s_addc_u32 s13, s15, s1
	s_add_u32 s54, s12, 0x100
	s_addc_u32 s55, s13, 0
	v_add_u32_e32 v132, s23, v156
	ds_read_b128 v[134:137], v132
	ds_read_b128 v[138:141], v132 offset:1024
	ds_read_b128 v[142:145], v132 offset:2048
	ds_read_b128 v[146:149], v132 offset:3072
	s_add_u32 s51, s2, s0
	s_addc_u32 s52, s3, s1
	s_add_u32 s56, s51, 0x40080
	s_addc_u32 s57, s52, 0
	s_add_u32 s58, s51, 0x60080
	s_addc_u32 s59, s52, 0
	s_add_i32 s50, s26, 0xc000
	ds_read_b128 v[150:153], v157
	ds_read_b128 v[158:161], v157 offset:1024
	ds_read_b128 v[162:165], v157 offset:2048
	ds_read_b128 v[166:169], v157 offset:3072
	ds_read_b128 v[170:173], v157 offset:4096
	ds_read_b128 v[174:177], v157 offset:5120
	ds_read_b128 v[178:181], v157 offset:6144
	ds_read_b128 v[182:185], v157 offset:7168
	s_mov_b32 m0, s50
	v_lshl_add_u64 v[154:155], s[56:57], 0, v[34:35]
	s_add_i32 s49, s26, 0xe000
	global_load_lds_dwordx4 v[154:155], off
	v_lshl_add_u64 v[154:155], s[58:59], 0, v[34:35]
	s_mov_b32 m0, s49
	s_nop 0
	global_load_lds_dwordx4 v[154:155], off
	s_waitcnt lgkmcnt(8)
	s_barrier
	s_waitcnt lgkmcnt(0)
	s_waitcnt lgkmcnt(0)
	v_mfma_f32_16x16x32_bf16 v[128:131], v[134:137], v[150:153], v[128:131]
	v_mfma_f32_16x16x32_bf16 v[124:127], v[142:145], v[150:153], v[124:127]
	v_mfma_f32_16x16x32_bf16 v[120:123], v[134:137], v[162:165], v[120:123]
	v_mfma_f32_16x16x32_bf16 v[116:119], v[142:145], v[162:165], v[116:119]
	v_mfma_f32_16x16x32_bf16 v[112:115], v[134:137], v[170:173], v[112:115]
	v_mfma_f32_16x16x32_bf16 v[108:111], v[142:145], v[170:173], v[108:111]
	v_mfma_f32_16x16x32_bf16 v[104:107], v[134:137], v[178:181], v[104:107]
	v_mfma_f32_16x16x32_bf16 v[100:103], v[142:145], v[178:181], v[100:103]
	v_mfma_f32_16x16x32_bf16 v[128:131], v[138:141], v[158:161], v[128:131]
	v_mfma_f32_16x16x32_bf16 v[124:127], v[146:149], v[158:161], v[124:127]
	v_mfma_f32_16x16x32_bf16 v[120:123], v[138:141], v[166:169], v[120:123]
	v_mfma_f32_16x16x32_bf16 v[116:119], v[146:149], v[166:169], v[116:119]
	v_mfma_f32_16x16x32_bf16 v[112:115], v[138:141], v[174:177], v[112:115]
	v_mfma_f32_16x16x32_bf16 v[108:111], v[146:149], v[174:177], v[108:111]
	v_mfma_f32_16x16x32_bf16 v[104:107], v[138:141], v[182:185], v[104:107]
	v_mfma_f32_16x16x32_bf16 v[100:103], v[146:149], v[182:185], v[100:103]
	s_barrier
	s_add_u32 s56, s12, 0x20100
	v_add_u32_e32 v133, s28, v156
	s_addc_u32 s57, s13, 0
	s_mov_b32 m0, s24
	ds_read_b128 v[186:189], v133
	ds_read_b128 v[190:193], v133 offset:1024
	ds_read_b128 v[194:197], v133 offset:2048
	ds_read_b128 v[198:201], v133 offset:3072
	s_nop 0
	v_lshl_add_u64 v[154:155], s[54:55], 0, v[34:35]
	global_load_lds_dwordx4 v[154:155], off
	v_lshl_add_u64 v[154:155], s[56:57], 0, v[34:35]
	s_mov_b32 m0, s25
	s_nop 0
	global_load_lds_dwordx4 v[154:155], off
	s_barrier
	s_waitcnt lgkmcnt(0)
	s_waitcnt lgkmcnt(0)
	v_mfma_f32_16x16x32_bf16 v[96:99], v[186:189], v[150:153], v[96:99]
	v_mfma_f32_16x16x32_bf16 v[92:95], v[194:197], v[150:153], v[92:95]
	v_mfma_f32_16x16x32_bf16 v[88:91], v[186:189], v[162:165], v[88:91]
	v_mfma_f32_16x16x32_bf16 v[84:87], v[194:197], v[162:165], v[84:87]
	v_mfma_f32_16x16x32_bf16 v[80:83], v[186:189], v[170:173], v[80:83]
	v_mfma_f32_16x16x32_bf16 v[76:79], v[194:197], v[170:173], v[76:79]
	v_mfma_f32_16x16x32_bf16 v[72:75], v[186:189], v[178:181], v[72:75]
	v_mfma_f32_16x16x32_bf16 v[68:71], v[194:197], v[178:181], v[68:71]
	v_mfma_f32_16x16x32_bf16 v[96:99], v[190:193], v[158:161], v[96:99]
	v_mfma_f32_16x16x32_bf16 v[92:95], v[198:201], v[158:161], v[92:95]
	v_mfma_f32_16x16x32_bf16 v[88:91], v[190:193], v[166:169], v[88:91]
	v_mfma_f32_16x16x32_bf16 v[84:87], v[198:201], v[166:169], v[84:87]
	v_mfma_f32_16x16x32_bf16 v[80:83], v[190:193], v[174:177], v[80:83]
	v_mfma_f32_16x16x32_bf16 v[76:79], v[198:201], v[174:177], v[76:79]
	v_mfma_f32_16x16x32_bf16 v[72:75], v[190:193], v[182:185], v[72:75]
	v_mfma_f32_16x16x32_bf16 v[68:71], v[198:201], v[182:185], v[68:71]
	s_barrier
	s_add_u32 s54, s51, 0x100
	s_addc_u32 s55, s52, 0
	s_add_u32 s56, s51, 0x20100
	s_addc_u32 s57, s52, 0
	s_mov_b32 m0, s26
	ds_read_b128 v[150:153], v157 offset:16384
	ds_read_b128 v[158:161], v157 offset:17408
	ds_read_b128 v[162:165], v157 offset:18432
	ds_read_b128 v[166:169], v157 offset:19456
	ds_read_b128 v[170:173], v157 offset:20480
	ds_read_b128 v[174:177], v157 offset:21504
	ds_read_b128 v[178:181], v157 offset:22528
	ds_read_b128 v[182:185], v157 offset:23552
	s_nop 0
	v_lshl_add_u64 v[154:155], s[54:55], 0, v[34:35]
	global_load_lds_dwordx4 v[154:155], off
	v_lshl_add_u64 v[154:155], s[56:57], 0, v[34:35]
	s_mov_b32 m0, s27
	s_nop 0
	global_load_lds_dwordx4 v[154:155], off
	s_barrier
	s_waitcnt lgkmcnt(0)
	s_waitcnt lgkmcnt(0)
	v_mfma_f32_16x16x32_bf16 v[64:67], v[134:137], v[150:153], v[64:67]
	v_mfma_f32_16x16x32_bf16 v[60:63], v[142:145], v[150:153], v[60:63]
	v_mfma_f32_16x16x32_bf16 v[56:59], v[134:137], v[162:165], v[56:59]
	v_mfma_f32_16x16x32_bf16 v[52:55], v[142:145], v[162:165], v[52:55]
	v_mfma_f32_16x16x32_bf16 v[48:51], v[134:137], v[170:173], v[48:51]
	v_mfma_f32_16x16x32_bf16 v[44:47], v[142:145], v[170:173], v[44:47]
	v_mfma_f32_16x16x32_bf16 v[40:43], v[134:137], v[178:181], v[40:43]
	v_mfma_f32_16x16x32_bf16 v[36:39], v[142:145], v[178:181], v[36:39]
	v_mfma_f32_16x16x32_bf16 v[64:67], v[138:141], v[158:161], v[64:67]
	v_mfma_f32_16x16x32_bf16 v[60:63], v[146:149], v[158:161], v[60:63]
	v_mfma_f32_16x16x32_bf16 v[56:59], v[138:141], v[166:169], v[56:59]
	v_mfma_f32_16x16x32_bf16 v[52:55], v[146:149], v[166:169], v[52:55]
	v_mfma_f32_16x16x32_bf16 v[48:51], v[138:141], v[174:177], v[48:51]
	v_mfma_f32_16x16x32_bf16 v[44:47], v[146:149], v[174:177], v[44:47]
	v_mfma_f32_16x16x32_bf16 v[40:43], v[138:141], v[182:185], v[40:43]
	v_mfma_f32_16x16x32_bf16 v[36:39], v[146:149], v[182:185], v[36:39]
	s_barrier
; __device__ __forceinline__ int tid_hidden() { int t = threadIdx.x; asm volatile("" : "+v"(t)); return t; }
; #define lds lds_hidden(lds0)
; template <class Epi, class Src>
; __device__ __forceinline__ void gemm_phase(LAS unsigned char* lds, const Src S, const Epi E) {
;     ...
;         { const int tp = tid_hidden(); E.prefetch(cur, lds, par, tp, __builtin_amdgcn_readfirstlane(tp >> 6)); }
;         if (Src::GATHER && has_next) { const int tp = tid_hidden(); tab_fill(S, nxt, tp, __builtin_amdgcn_readfirstlane(tp >> 6), lds, par ^ 1); }
;         for (int t = 0; t < NKTR - 2; t += 2) {
;             const size_t k1 = (size_t)(t + 1) * kstep, k2 = (size_t)(t + 2) * kstep;
;             const char* b2 = cB + k2; const char* b3 = b2 + kstep;
;             G8_ITER(cA, par, k1, cA, par, k2, b2, b3);
;         }
	s_add_u32 s54, s12, 0x40100
	s_addc_u32 s55, s13, 0
	s_add_u32 s56, s12, 0x60100
	s_addc_u32 s57, s13, 0
	s_mov_b32 m0, s29
	s_nop 0
	v_lshl_add_u64 v[134:135], s[54:55], 0, v[34:35]
	global_load_lds_dwordx4 v[134:135], off
	v_lshl_add_u64 v[134:135], s[56:57], 0, v[34:35]
	s_mov_b32 m0, s30
	s_nop 0
	global_load_lds_dwordx4 v[134:135], off
	s_waitcnt vmcnt(6)
	s_barrier
	v_mfma_f32_16x16x32_bf16 v[30:33], v[186:189], v[150:153], v[30:33]
	v_mfma_f32_16x16x32_bf16 v[26:29], v[194:197], v[150:153], v[26:29]
	v_mfma_f32_16x16x32_bf16 v[22:25], v[186:189], v[162:165], v[22:25]
	v_mfma_f32_16x16x32_bf16 v[18:21], v[194:197], v[162:165], v[18:21]
	v_mfma_f32_16x16x32_bf16 v[14:17], v[186:189], v[170:173], v[14:17]
	v_mfma_f32_16x16x32_bf16 v[10:13], v[194:197], v[170:173], v[10:13]
	v_mfma_f32_16x16x32_bf16 v[6:9], v[186:189], v[178:181], v[6:9]
	v_mfma_f32_16x16x32_bf16 v[2:5], v[194:197], v[178:181], v[2:5]
	v_mfma_f32_16x16x32_bf16 v[30:33], v[190:193], v[158:161], v[30:33]
	v_mfma_f32_16x16x32_bf16 v[26:29], v[198:201], v[158:161], v[26:29]
	v_mfma_f32_16x16x32_bf16 v[22:25], v[190:193], v[166:169], v[22:25]
	v_mfma_f32_16x16x32_bf16 v[18:21], v[198:201], v[166:169], v[18:21]
	v_mfma_f32_16x16x32_bf16 v[14:17], v[190:193], v[174:177], v[14:17]
	v_mfma_f32_16x16x32_bf16 v[10:13], v[198:201], v[174:177], v[10:13]
	v_mfma_f32_16x16x32_bf16 v[6:9], v[190:193], v[182:185], v[6:9]
	v_mfma_f32_16x16x32_bf16 v[2:5], v[198:201], v[182:185], v[2:5]
	s_barrier
	v_add_u32_e32 v134, s37, v156
	ds_read_b128 v[136:139], v134
	ds_read_b128 v[140:143], v134 offset:1024
	ds_read_b128 v[144:147], v134 offset:2048
	ds_read_b128 v[148:151], v134 offset:3072
	s_add_u32 s54, s51, 0x40100
	s_addc_u32 s55, s52, 0
	s_add_u32 s56, s51, 0x60100
	s_addc_u32 s57, s52, 0
	s_mov_b32 m0, s31
	ds_read_b128 v[152:155], v157 offset:32768
	ds_read_b128 v[158:161], v157 offset:33792
	ds_read_b128 v[162:165], v157 offset:34816
	ds_read_b128 v[166:169], v157 offset:35840
	ds_read_b128 v[170:173], v157 offset:36864
	ds_read_b128 v[174:177], v157 offset:37888
	ds_read_b128 v[178:181], v157 offset:38912
	ds_read_b128 v[182:185], v157 offset:39936
	s_nop 0
	v_lshl_add_u64 v[186:187], s[54:55], 0, v[34:35]
	global_load_lds_dwordx4 v[186:187], off
	v_lshl_add_u64 v[186:187], s[56:57], 0, v[34:35]
	s_mov_b32 m0, s34
	s_nop 0
	global_load_lds_dwordx4 v[186:187], off
	s_waitcnt lgkmcnt(8)
	s_barrier
	s_waitcnt lgkmcnt(0)
	s_waitcnt lgkmcnt(0)
	v_mfma_f32_16x16x32_bf16 v[128:131], v[136:139], v[152:155], v[128:131]
	v_mfma_f32_16x16x32_bf16 v[124:127], v[144:147], v[152:155], v[124:127]
	v_mfma_f32_16x16x32_bf16 v[120:123], v[136:139], v[162:165], v[120:123]
	v_mfma_f32_16x16x32_bf16 v[116:119], v[144:147], v[162:165], v[116:119]
	v_mfma_f32_16x16x32_bf16 v[112:115], v[136:139], v[170:173], v[112:115]
	v_mfma_f32_16x16x32_bf16 v[108:111], v[144:147], v[170:173], v[108:111]
	v_mfma_f32_16x16x32_bf16 v[104:107], v[136:139], v[178:181], v[104:107]
	v_mfma_f32_16x16x32_bf16 v[100:103], v[144:147], v[178:181], v[100:103]
	v_mfma_f32_16x16x32_bf16 v[128:131], v[140:143], v[158:161], v[128:131]
	v_mfma_f32_16x16x32_bf16 v[124:127], v[148:151], v[158:161], v[124:127]
	v_mfma_f32_16x16x32_bf16 v[120:123], v[140:143], v[166:169], v[120:123]
	v_mfma_f32_16x16x32_bf16 v[116:119], v[148:151], v[166:169], v[116:119]
	v_mfma_f32_16x16x32_bf16 v[112:115], v[140:143], v[174:177], v[112:115]
	v_mfma_f32_16x16x32_bf16 v[108:111], v[148:151], v[174:177], v[108:111]
	v_mfma_f32_16x16x32_bf16 v[104:107], v[140:143], v[182:185], v[104:107]
	v_mfma_f32_16x16x32_bf16 v[100:103], v[148:151], v[182:185], v[100:103]
	s_barrier
	s_add_u32 s54, s12, 0x180
	s_addc_u32 s55, s13, 0
	s_add_u32 s56, s12, 0x20180
	v_add_u32_e32 v135, s42, v156
	s_addc_u32 s57, s13, 0
	s_mov_b32 m0, s38
	ds_read_b128 v[186:189], v135
	ds_read_b128 v[190:193], v135 offset:1024
	ds_read_b128 v[194:197], v135 offset:2048
	ds_read_b128 v[198:201], v135 offset:3072
	s_nop 0
	v_lshl_add_u64 v[202:203], s[54:55], 0, v[34:35]
	global_load_lds_dwordx4 v[202:203], off
	v_lshl_add_u64 v[202:203], s[56:57], 0, v[34:35]
	s_mov_b32 m0, s39
	s_nop 0
	global_load_lds_dwordx4 v[202:203], off
	s_barrier
	s_waitcnt lgkmcnt(0)
	s_waitcnt lgkmcnt(0)
	v_mfma_f32_16x16x32_bf16 v[96:99], v[186:189], v[152:155], v[96:99]
	v_mfma_f32_16x16x32_bf16 v[92:95], v[194:197], v[152:155], v[92:95]
	v_mfma_f32_16x16x32_bf16 v[88:91], v[186:189], v[162:165], v[88:91]
	v_mfma_f32_16x16x32_bf16 v[84:87], v[194:197], v[162:165], v[84:87]
	v_mfma_f32_16x16x32_bf16 v[80:83], v[186:189], v[170:173], v[80:83]
	v_mfma_f32_16x16x32_bf16 v[76:79], v[194:197], v[170:173], v[76:79]
	v_mfma_f32_16x16x32_bf16 v[72:75], v[186:189], v[178:181], v[72:75]
	v_mfma_f32_16x16x32_bf16 v[68:71], v[194:197], v[178:181], v[68:71]
	v_mfma_f32_16x16x32_bf16 v[96:99], v[190:193], v[158:161], v[96:99]
	v_mfma_f32_16x16x32_bf16 v[92:95], v[198:201], v[158:161], v[92:95]
	v_mfma_f32_16x16x32_bf16 v[88:91], v[190:193], v[166:169], v[88:91]
	v_mfma_f32_16x16x32_bf16 v[84:87], v[198:201], v[166:169], v[84:87]
	v_mfma_f32_16x16x32_bf16 v[80:83], v[190:193], v[174:177], v[80:83]
	v_mfma_f32_16x16x32_bf16 v[76:79], v[198:201], v[174:177], v[76:79]
	v_mfma_f32_16x16x32_bf16 v[72:75], v[190:193], v[182:185], v[72:75]
	v_mfma_f32_16x16x32_bf16 v[68:71], v[198:201], v[182:185], v[68:71]
	s_barrier
; __device__ __forceinline__ int tid_hidden() { int t = threadIdx.x; asm volatile("" : "+v"(t)); return t; }
; #define lds lds_hidden(lds0)
; template <class Epi, class Src>
; __device__ __forceinline__ void gemm_phase(LAS unsigned char* lds, const Src S, const Epi E) {
;     ...
;         { const int tp = tid_hidden(); E.prefetch(cur, lds, par, tp, __builtin_amdgcn_readfirstlane(tp >> 6)); }
;         if (Src::GATHER && has_next) { const int tp = tid_hidden(); tab_fill(S, nxt, tp, __builtin_amdgcn_readfirstlane(tp >> 6), lds, par ^ 1); }
;         for (int t = 0; t < NKTR - 2; t += 2) {
;             const size_t k1 = (size_t)(t + 1) * kstep, k2 = (size_t)(t + 2) * kstep;
;             const char* b2 = cB + k2; const char* b3 = b2 + kstep;
;             G8_ITER(cA, par, k1, cA, par, k2, b2, b3);
;         }
;         {
;             const int par2 = has_next ? (par ^ 1) : par;
;             const char* b3 = nB + kstep;
;             G8_ITER(cA, par, (size_t)(NKTR - 1) * kstep, nA, par2, (size_t)0, nB, b3);
	s_add_u32 s54, s51, 0x180
	s_addc_u32 s55, s52, 0
	s_add_u32 s56, s51, 0x20180
	s_addc_u32 s57, s52, 0
	s_mov_b32 m0, s40
	ds_read_b128 v[152:155], v157 offset:49152
	ds_read_b128 v[158:161], v157 offset:50176
	ds_read_b128 v[162:165], v157 offset:51200
	ds_read_b128 v[166:169], v157 offset:52224
	ds_read_b128 v[170:173], v157 offset:53248
	ds_read_b128 v[174:177], v157 offset:54272
	ds_read_b128 v[178:181], v157 offset:55296
	ds_read_b128 v[182:185], v157 offset:56320
	s_nop 0
	v_lshl_add_u64 v[202:203], s[54:55], 0, v[34:35]
	global_load_lds_dwordx4 v[202:203], off
	v_lshl_add_u64 v[202:203], s[56:57], 0, v[34:35]
	s_mov_b32 m0, s41
	s_nop 0
	global_load_lds_dwordx4 v[202:203], off
	s_barrier
	s_waitcnt lgkmcnt(0)
	s_waitcnt lgkmcnt(0)
	v_mfma_f32_16x16x32_bf16 v[64:67], v[136:139], v[152:155], v[64:67]
	v_mfma_f32_16x16x32_bf16 v[60:63], v[144:147], v[152:155], v[60:63]
	v_mfma_f32_16x16x32_bf16 v[56:59], v[136:139], v[162:165], v[56:59]
	v_mfma_f32_16x16x32_bf16 v[52:55], v[144:147], v[162:165], v[52:55]
	v_mfma_f32_16x16x32_bf16 v[48:51], v[136:139], v[170:173], v[48:51]
	v_mfma_f32_16x16x32_bf16 v[44:47], v[144:147], v[170:173], v[44:47]
	v_mfma_f32_16x16x32_bf16 v[40:43], v[136:139], v[178:181], v[40:43]
	v_mfma_f32_16x16x32_bf16 v[36:39], v[144:147], v[178:181], v[36:39]
	v_mfma_f32_16x16x32_bf16 v[64:67], v[140:143], v[158:161], v[64:67]
	v_mfma_f32_16x16x32_bf16 v[60:63], v[148:151], v[158:161], v[60:63]
	v_mfma_f32_16x16x32_bf16 v[56:59], v[140:143], v[166:169], v[56:59]
	v_mfma_f32_16x16x32_bf16 v[52:55], v[148:151], v[166:169], v[52:55]
	v_mfma_f32_16x16x32_bf16 v[48:51], v[140:143], v[174:177], v[48:51]
	v_mfma_f32_16x16x32_bf16 v[44:47], v[148:151], v[174:177], v[44:47]
	v_mfma_f32_16x16x32_bf16 v[40:43], v[140:143], v[182:185], v[40:43]
	v_mfma_f32_16x16x32_bf16 v[36:39], v[148:151], v[182:185], v[36:39]
	s_barrier
	s_add_u32 s52, s12, 0x40180
	s_addc_u32 s53, s13, 0
	s_add_u32 s12, s12, 0x60180
	s_addc_u32 s13, s13, 0
	s_mov_b32 m0, s43
	s_nop 0
	v_lshl_add_u64 v[136:137], s[52:53], 0, v[34:35]
	global_load_lds_dwordx4 v[136:137], off
	v_lshl_add_u64 v[136:137], s[12:13], 0, v[34:35]
	s_mov_b32 m0, s44
	s_nop 0
	global_load_lds_dwordx4 v[136:137], off
	s_waitcnt vmcnt(6)
	s_barrier
	v_mfma_f32_16x16x32_bf16 v[30:33], v[186:189], v[152:155], v[30:33]
	v_mfma_f32_16x16x32_bf16 v[26:29], v[194:197], v[152:155], v[26:29]
	v_mfma_f32_16x16x32_bf16 v[22:25], v[186:189], v[162:165], v[22:25]
	v_mfma_f32_16x16x32_bf16 v[18:21], v[194:197], v[162:165], v[18:21]
	v_mfma_f32_16x16x32_bf16 v[14:17], v[186:189], v[170:173], v[14:17]
	v_mfma_f32_16x16x32_bf16 v[10:13], v[194:197], v[170:173], v[10:13]
	v_mfma_f32_16x16x32_bf16 v[6:9], v[186:189], v[178:181], v[6:9]
	v_mfma_f32_16x16x32_bf16 v[2:5], v[194:197], v[178:181], v[2:5]
	v_mfma_f32_16x16x32_bf16 v[30:33], v[190:193], v[158:161], v[30:33]
	v_mfma_f32_16x16x32_bf16 v[26:29], v[198:201], v[158:161], v[26:29]
	v_mfma_f32_16x16x32_bf16 v[22:25], v[190:193], v[166:169], v[22:25]
	v_mfma_f32_16x16x32_bf16 v[18:21], v[198:201], v[166:169], v[18:21]
	v_mfma_f32_16x16x32_bf16 v[14:17], v[190:193], v[174:177], v[14:17]
	v_mfma_f32_16x16x32_bf16 v[10:13], v[198:201], v[174:177], v[10:13]
	v_mfma_f32_16x16x32_bf16 v[6:9], v[190:193], v[182:185], v[6:9]
	v_mfma_f32_16x16x32_bf16 v[2:5], v[198:201], v[182:185], v[2:5]
	s_add_i32 s11, s11, 2
	s_add_u32 s0, s0, 0x100
	s_addc_u32 s1, s1, 0
	s_cmp_gt_u32 s11, 11
	s_barrier
	s_cbranch_scc0 .LBB0_1193
	s_lshl_b32 s12, s46, 8
	s_ashr_i32 s11, s10, 31
	s_ashr_i32 s13, s12, 31
	s_lshl_b64 s[0:1], s[10:11], 19
	s_lshl_b64 s[12:13], s[12:13], 11
	s_add_u32 s0, s21, s0
	s_addc_u32 s1, s22, s1
	s_add_u32 s12, s4, s12
	s_addc_u32 s13, s5, s13
	s_and_b64 s[16:17], s[16:17], exec
	s_cselect_b32 s17, s13, s3
	s_cselect_b32 s16, s12, s2
	ds_read_b128 v[136:139], v132
	ds_read_b128 v[140:143], v132 offset:1024
	ds_read_b128 v[144:147], v132 offset:2048
	ds_read_b128 v[148:151], v132 offset:3072
	s_cselect_b32 s15, s1, s15
	s_cselect_b32 s14, s0, s14
	s_mov_b32 m0, s50
	s_add_u32 s50, s2, 0x40780
	s_addc_u32 s51, s3, 0
	s_add_u32 s2, s2, 0x60780
	s_addc_u32 s3, s3, 0
	ds_read_b128 v[152:155], v157
	ds_read_b128 v[158:161], v157 offset:1024
	ds_read_b128 v[162:165], v157 offset:2048
	ds_read_b128 v[166:169], v157 offset:3072
	ds_read_b128 v[170:173], v157 offset:4096
	ds_read_b128 v[174:177], v157 offset:5120
	ds_read_b128 v[178:181], v157 offset:6144
	ds_read_b128 v[182:185], v157 offset:7168
	s_nop 0
	v_lshl_add_u64 v[186:187], s[50:51], 0, v[34:35]
	global_load_lds_dwordx4 v[186:187], off
	v_lshl_add_u64 v[186:187], s[2:3], 0, v[34:35]
	s_mov_b32 m0, s49
	s_nop 0
	global_load_lds_dwordx4 v[186:187], off
	s_waitcnt lgkmcnt(8)
	s_barrier
	s_waitcnt lgkmcnt(0)
	s_waitcnt lgkmcnt(0)
	v_mfma_f32_16x16x32_bf16 v[128:131], v[136:139], v[152:155], v[128:131]
	v_mfma_f32_16x16x32_bf16 v[124:127], v[144:147], v[152:155], v[124:127]
	v_mfma_f32_16x16x32_bf16 v[120:123], v[136:139], v[162:165], v[120:123]
	v_mfma_f32_16x16x32_bf16 v[116:119], v[144:147], v[162:165], v[116:119]
	v_mfma_f32_16x16x32_bf16 v[112:115], v[136:139], v[170:173], v[112:115]
	v_mfma_f32_16x16x32_bf16 v[108:111], v[144:147], v[170:173], v[108:111]
	v_mfma_f32_16x16x32_bf16 v[104:107], v[136:139], v[178:181], v[104:107]
	v_mfma_f32_16x16x32_bf16 v[100:103], v[144:147], v[178:181], v[100:103]
	v_mfma_f32_16x16x32_bf16 v[128:131], v[140:143], v[158:161], v[128:131]
	v_mfma_f32_16x16x32_bf16 v[124:127], v[148:151], v[158:161], v[124:127]
	v_mfma_f32_16x16x32_bf16 v[120:123], v[140:143], v[166:169], v[120:123]
	v_mfma_f32_16x16x32_bf16 v[116:119], v[148:151], v[166:169], v[116:119]
	v_mfma_f32_16x16x32_bf16 v[112:115], v[140:143], v[174:177], v[112:115]
	v_mfma_f32_16x16x32_bf16 v[108:111], v[148:151], v[174:177], v[108:111]
	v_mfma_f32_16x16x32_bf16 v[186:189], v[140:143], v[182:185], v[104:107]
	v_mfma_f32_16x16x32_bf16 v[190:193], v[148:151], v[182:185], v[100:103]
	s_barrier
; __device__ __forceinline__ int tid_hidden() { int t = threadIdx.x; asm volatile("" : "+v"(t)); return t; }
; #define lds lds_hidden(lds0)
; template <class Epi, class Src>
; __device__ __forceinline__ void gemm_phase(LAS unsigned char* lds, const Src S, const Epi E) {
;     ...
;         { const int tp = tid_hidden(); E.prefetch(cur, lds, par, tp, __builtin_amdgcn_readfirstlane(tp >> 6)); }
;         if (Src::GATHER && has_next) { const int tp = tid_hidden(); tab_fill(S, nxt, tp, __builtin_amdgcn_readfirstlane(tp >> 6), lds, par ^ 1); }
;         for (int t = 0; t < NKTR - 2; t += 2) {
;             const size_t k1 = (size_t)(t + 1) * kstep, k2 = (size_t)(t + 2) * kstep;
;             const char* b2 = cB + k2; const char* b3 = b2 + kstep;
;             G8_ITER(cA, par, k1, cA, par, k2, b2, b3);
;         }
;         {
;             const int par2 = has_next ? (par ^ 1) : par;
;             const char* b3 = nB + kstep;
;             G8_ITER(cA, par, (size_t)(NKTR - 1) * kstep, nA, par2, (size_t)0, nB, b3);
	s_add_u32 s2, s14, 0x20000
	s_addc_u32 s3, s15, 0
	s_mov_b64 s[50:51], s[14:15]
	s_mov_b32 m0, s24
	ds_read_b128 v[100:103], v133
	ds_read_b128 v[104:107], v133 offset:1024
	ds_read_b128 v[194:197], v133 offset:2048
	ds_read_b128 v[198:201], v133 offset:3072
	s_nop 0
	v_lshl_add_u64 v[132:133], s[50:51], 0, v[34:35]
	global_load_lds_dwordx4 v[132:133], off
	v_lshl_add_u64 v[132:133], s[2:3], 0, v[34:35]
	s_mov_b32 m0, s25
	s_nop 0
	global_load_lds_dwordx4 v[132:133], off
	s_barrier
	s_waitcnt lgkmcnt(0)
	s_waitcnt lgkmcnt(0)
	v_mfma_f32_16x16x32_bf16 v[96:99], v[100:103], v[152:155], v[96:99]
	v_mfma_f32_16x16x32_bf16 v[92:95], v[194:197], v[152:155], v[92:95]
	v_mfma_f32_16x16x32_bf16 v[88:91], v[100:103], v[162:165], v[88:91]
	v_mfma_f32_16x16x32_bf16 v[84:87], v[194:197], v[162:165], v[84:87]
	v_mfma_f32_16x16x32_bf16 v[80:83], v[100:103], v[170:173], v[80:83]
	v_mfma_f32_16x16x32_bf16 v[76:79], v[194:197], v[170:173], v[76:79]
	v_mfma_f32_16x16x32_bf16 v[72:75], v[100:103], v[178:181], v[72:75]
	v_mfma_f32_16x16x32_bf16 v[68:71], v[194:197], v[178:181], v[68:71]
	v_mfma_f32_16x16x32_bf16 v[96:99], v[104:107], v[158:161], v[96:99]
	v_mfma_f32_16x16x32_bf16 v[92:95], v[198:201], v[158:161], v[92:95]
	v_mfma_f32_16x16x32_bf16 v[152:155], v[104:107], v[166:169], v[88:91]
	v_mfma_f32_16x16x32_bf16 v[158:161], v[198:201], v[166:169], v[84:87]
	v_mfma_f32_16x16x32_bf16 v[80:83], v[104:107], v[174:177], v[80:83]
	v_mfma_f32_16x16x32_bf16 v[76:79], v[198:201], v[174:177], v[76:79]
	v_mfma_f32_16x16x32_bf16 v[72:75], v[104:107], v[182:185], v[72:75]
	v_mfma_f32_16x16x32_bf16 v[68:71], v[198:201], v[182:185], v[68:71]
	s_barrier
	s_add_u32 s2, s16, 0x20000
	s_addc_u32 s3, s17, 0
	s_mov_b64 s[50:51], s[16:17]
	s_mov_b32 m0, s26
	ds_read_b128 v[84:87], v157 offset:16384
	ds_read_b128 v[88:91], v157 offset:17408
	ds_read_b128 v[162:165], v157 offset:18432
	ds_read_b128 v[166:169], v157 offset:19456
	ds_read_b128 v[170:173], v157 offset:20480
	ds_read_b128 v[174:177], v157 offset:21504
	ds_read_b128 v[178:181], v157 offset:22528
	ds_read_b128 v[182:185], v157 offset:23552
	s_nop 0
	v_lshl_add_u64 v[132:133], s[50:51], 0, v[34:35]
	global_load_lds_dwordx4 v[132:133], off
	v_lshl_add_u64 v[132:133], s[2:3], 0, v[34:35]
	s_mov_b32 m0, s27
	s_nop 0
	global_load_lds_dwordx4 v[132:133], off
	s_barrier
	s_waitcnt lgkmcnt(0)
	s_waitcnt lgkmcnt(0)
	v_mfma_f32_16x16x32_bf16 v[64:67], v[136:139], v[84:87], v[64:67]
	v_mfma_f32_16x16x32_bf16 v[60:63], v[144:147], v[84:87], v[60:63]
	v_mfma_f32_16x16x32_bf16 v[56:59], v[136:139], v[162:165], v[56:59]
	v_mfma_f32_16x16x32_bf16 v[52:55], v[144:147], v[162:165], v[52:55]
	v_mfma_f32_16x16x32_bf16 v[48:51], v[136:139], v[170:173], v[48:51]
	v_mfma_f32_16x16x32_bf16 v[44:47], v[144:147], v[170:173], v[44:47]
	v_mfma_f32_16x16x32_bf16 v[40:43], v[136:139], v[178:181], v[40:43]
	v_mfma_f32_16x16x32_bf16 v[36:39], v[144:147], v[178:181], v[36:39]
	v_mfma_f32_16x16x32_bf16 v[64:67], v[140:143], v[88:91], v[64:67]
	v_mfma_f32_16x16x32_bf16 v[60:63], v[148:151], v[88:91], v[60:63]
	v_mfma_f32_16x16x32_bf16 v[56:59], v[140:143], v[166:169], v[56:59]
	v_mfma_f32_16x16x32_bf16 v[202:205], v[148:151], v[166:169], v[52:55]
	v_mfma_f32_16x16x32_bf16 v[48:51], v[140:143], v[174:177], v[48:51]
	v_mfma_f32_16x16x32_bf16 v[206:209], v[148:151], v[174:177], v[44:47]
	v_mfma_f32_16x16x32_bf16 v[40:43], v[140:143], v[182:185], v[40:43]
	v_mfma_f32_16x16x32_bf16 v[36:39], v[148:151], v[182:185], v[36:39]
	s_barrier
	s_add_u32 s2, s14, 0x40000
	s_addc_u32 s3, s15, 0
	s_add_u32 s50, s14, 0x60000
	s_addc_u32 s51, s15, 0
	s_mov_b32 m0, s29
	s_nop 0
	v_lshl_add_u64 v[44:45], s[2:3], 0, v[34:35]
	global_load_lds_dwordx4 v[44:45], off
	v_lshl_add_u64 v[44:45], s[50:51], 0, v[34:35]
	s_mov_b32 m0, s30
	s_nop 0
	global_load_lds_dwordx4 v[44:45], off
	s_waitcnt vmcnt(6)
	s_barrier
	v_mfma_f32_16x16x32_bf16 v[30:33], v[100:103], v[84:87], v[30:33]
	v_mfma_f32_16x16x32_bf16 v[26:29], v[194:197], v[84:87], v[26:29]
	v_mfma_f32_16x16x32_bf16 v[22:25], v[100:103], v[162:165], v[22:25]
	v_mfma_f32_16x16x32_bf16 v[18:21], v[194:197], v[162:165], v[18:21]
	v_mfma_f32_16x16x32_bf16 v[14:17], v[100:103], v[170:173], v[14:17]
	v_mfma_f32_16x16x32_bf16 v[10:13], v[194:197], v[170:173], v[10:13]
	v_mfma_f32_16x16x32_bf16 v[6:9], v[100:103], v[178:181], v[6:9]
	v_mfma_f32_16x16x32_bf16 v[2:5], v[194:197], v[178:181], v[2:5]
	v_mfma_f32_16x16x32_bf16 v[30:33], v[104:107], v[88:91], v[30:33]
	v_mfma_f32_16x16x32_bf16 v[26:29], v[198:201], v[88:91], v[26:29]
	v_mfma_f32_16x16x32_bf16 v[140:143], v[104:107], v[166:169], v[22:25]
	v_mfma_f32_16x16x32_bf16 v[144:147], v[198:201], v[166:169], v[18:21]
	v_mfma_f32_16x16x32_bf16 v[14:17], v[104:107], v[174:177], v[14:17]
	v_mfma_f32_16x16x32_bf16 v[10:13], v[198:201], v[174:177], v[10:13]
	v_mfma_f32_16x16x32_bf16 v[6:9], v[104:107], v[182:185], v[6:9]
	v_mfma_f32_16x16x32_bf16 v[2:5], v[198:201], v[182:185], v[2:5]
	s_barrier
	ds_read_b128 v[18:21], v134
	ds_read_b128 v[22:25], v134 offset:1024
	ds_read_b128 v[148:151], v134 offset:2048
	ds_read_b128 v[162:165], v134 offset:3072
	s_add_u32 s2, s16, 0x40000
	s_addc_u32 s3, s17, 0
	s_add_u32 s50, s16, 0x60000
	s_addc_u32 s51, s17, 0
	s_mov_b32 m0, s31
	ds_read_b128 v[44:47], v157 offset:32768
	ds_read_b128 v[52:55], v157 offset:33792
	ds_read_b128 v[136:139], v157 offset:34816
	ds_read_b128 v[166:169], v157 offset:35840
	ds_read_b128 v[170:173], v157 offset:36864
	ds_read_b128 v[174:177], v157 offset:37888
	ds_read_b128 v[178:181], v157 offset:38912
	ds_read_b128 v[182:185], v157 offset:39936
	s_nop 0
	v_lshl_add_u64 v[84:85], s[2:3], 0, v[34:35]
	global_load_lds_dwordx4 v[84:85], off
	v_lshl_add_u64 v[84:85], s[50:51], 0, v[34:35]
	s_mov_b32 m0, s34
	s_nop 0
	global_load_lds_dwordx4 v[84:85], off
	s_waitcnt lgkmcnt(8)
	s_barrier
; __device__ __forceinline__ int tid_hidden() { int t = threadIdx.x; asm volatile("" : "+v"(t)); return t; }
; #define lds lds_hidden(lds0)
; template <class Epi, class Src>
; __device__ __forceinline__ void gemm_phase(LAS unsigned char* lds, const Src S, const Epi E) {
;     ...
;         { const int tp = tid_hidden(); E.prefetch(cur, lds, par, tp, __builtin_amdgcn_readfirstlane(tp >> 6)); }
;         if (Src::GATHER && has_next) { const int tp = tid_hidden(); tab_fill(S, nxt, tp, __builtin_amdgcn_readfirstlane(tp >> 6), lds, par ^ 1); }
;         for (int t = 0; t < NKTR - 2; t += 2) {
;             const size_t k1 = (size_t)(t + 1) * kstep, k2 = (size_t)(t + 2) * kstep;
;             const char* b2 = cB + k2; const char* b3 = b2 + kstep;
;             G8_ITER(cA, par, k1, cA, par, k2, b2, b3);
;         }
;         {
;             const int par2 = has_next ? (par ^ 1) : par;
;             const char* b3 = nB + kstep;
;             G8_ITER(cA, par, (size_t)(NKTR - 1) * kstep, nA, par2, (size_t)0, nB, b3);
	s_waitcnt lgkmcnt(0)
	s_waitcnt lgkmcnt(0)
	v_mfma_f32_16x16x32_bf16 v[84:87], v[18:21], v[44:47], v[128:131]
	v_mfma_f32_16x16x32_bf16 v[194:197], v[22:25], v[52:55], v[84:87]
	v_mfma_f32_16x16x32_bf16 v[84:87], v[148:151], v[44:47], v[124:127]
	v_mfma_f32_16x16x32_bf16 v[198:201], v[162:165], v[52:55], v[84:87]
	v_mfma_f32_16x16x32_bf16 v[84:87], v[18:21], v[136:139], v[120:123]
	v_mfma_f32_16x16x32_bf16 v[124:127], v[22:25], v[166:169], v[84:87]
	v_mfma_f32_16x16x32_bf16 v[84:87], v[148:151], v[136:139], v[116:119]
	v_mfma_f32_16x16x32_bf16 v[128:131], v[162:165], v[166:169], v[84:87]
	v_mfma_f32_16x16x32_bf16 v[84:87], v[18:21], v[170:173], v[112:115]
	v_mfma_f32_16x16x32_bf16 v[100:103], v[22:25], v[174:177], v[84:87]
	v_mfma_f32_16x16x32_bf16 v[84:87], v[148:151], v[170:173], v[108:111]
	v_mfma_f32_16x16x32_bf16 v[104:107], v[162:165], v[174:177], v[84:87]
	v_mfma_f32_16x16x32_bf16 v[84:87], v[18:21], v[178:181], v[186:189]
	v_mfma_f32_16x16x32_bf16 v[88:91], v[148:151], v[178:181], v[190:193]
	v_mfma_f32_16x16x32_bf16 v[84:87], v[22:25], v[182:185], v[84:87]
	v_mfma_f32_16x16x32_bf16 v[88:91], v[162:165], v[182:185], v[88:91]
	s_barrier
	s_add_u32 s2, s14, 0x80
	s_addc_u32 s3, s15, 0
	s_add_u32 s50, s14, 0x20080
	s_addc_u32 s51, s15, 0
	s_mov_b32 m0, s38
	ds_read_b128 v[116:119], v135
	ds_read_b128 v[120:123], v135 offset:1024
	ds_read_b128 v[186:189], v135 offset:2048
	ds_read_b128 v[190:193], v135 offset:3072
	s_nop 0
	v_lshl_add_u64 v[108:109], s[2:3], 0, v[34:35]
	global_load_lds_dwordx4 v[108:109], off
	v_lshl_add_u64 v[108:109], s[50:51], 0, v[34:35]
	s_mov_b32 m0, s39
	s_nop 0
	global_load_lds_dwordx4 v[108:109], off
	s_barrier
	s_waitcnt lgkmcnt(0)
	s_waitcnt lgkmcnt(0)
	v_mfma_f32_16x16x32_bf16 v[96:99], v[116:119], v[44:47], v[96:99]
	v_mfma_f32_16x16x32_bf16 v[44:47], v[186:189], v[44:47], v[92:95]
	v_mfma_f32_16x16x32_bf16 v[214:217], v[190:193], v[52:55], v[44:47]
	v_mfma_f32_16x16x32_bf16 v[44:47], v[116:119], v[136:139], v[152:155]
	v_mfma_f32_16x16x32_bf16 v[132:135], v[120:123], v[166:169], v[44:47]
	v_mfma_f32_16x16x32_bf16 v[44:47], v[186:189], v[136:139], v[158:161]
	v_mfma_f32_16x16x32_bf16 v[136:139], v[190:193], v[166:169], v[44:47]
	v_mfma_f32_16x16x32_bf16 v[44:47], v[116:119], v[170:173], v[80:83]
	v_mfma_f32_16x16x32_bf16 v[108:111], v[120:123], v[174:177], v[44:47]
	v_mfma_f32_16x16x32_bf16 v[44:47], v[186:189], v[170:173], v[76:79]
	v_mfma_f32_16x16x32_bf16 v[112:115], v[190:193], v[174:177], v[44:47]
	v_mfma_f32_16x16x32_bf16 v[44:47], v[116:119], v[178:181], v[72:75]
	v_mfma_f32_16x16x32_bf16 v[92:95], v[120:123], v[182:185], v[44:47]
	v_mfma_f32_16x16x32_bf16 v[44:47], v[186:189], v[178:181], v[68:71]
	v_mfma_f32_16x16x32_bf16 v[210:213], v[120:123], v[52:55], v[96:99]
	v_mfma_f32_16x16x32_bf16 v[96:99], v[190:193], v[182:185], v[44:47]
	s_barrier
	s_add_u32 s2, s16, 0x80
	s_addc_u32 s3, s17, 0
	s_add_u32 s16, s16, 0x20080
	s_addc_u32 s17, s17, 0
	s_mov_b32 m0, s40
	ds_read_b128 v[80:83], v157 offset:49152
	ds_read_b128 v[152:155], v157 offset:50176
	ds_read_b128 v[158:161], v157 offset:51200
	ds_read_b128 v[166:169], v157 offset:52224
	ds_read_b128 v[170:173], v157 offset:53248
	ds_read_b128 v[174:177], v157 offset:54272
	ds_read_b128 v[178:181], v157 offset:55296
	ds_read_b128 v[182:185], v157 offset:56320
	s_nop 0
	v_lshl_add_u64 v[44:45], s[2:3], 0, v[34:35]
	global_load_lds_dwordx4 v[44:45], off
	v_lshl_add_u64 v[44:45], s[16:17], 0, v[34:35]
	s_mov_b32 m0, s41
	s_nop 0
	global_load_lds_dwordx4 v[44:45], off
	s_barrier
	s_waitcnt lgkmcnt(0)
	s_waitcnt lgkmcnt(0)
	v_mfma_f32_16x16x32_bf16 v[44:47], v[18:21], v[80:83], v[64:67]
	v_mfma_f32_16x16x32_bf16 v[68:71], v[22:25], v[152:155], v[44:47]
	v_mfma_f32_16x16x32_bf16 v[44:47], v[148:151], v[80:83], v[60:63]
	v_mfma_f32_16x16x32_bf16 v[72:75], v[162:165], v[152:155], v[44:47]
	v_mfma_f32_16x16x32_bf16 v[44:47], v[18:21], v[158:161], v[56:59]
	v_mfma_f32_16x16x32_bf16 v[52:55], v[22:25], v[166:169], v[44:47]
	v_mfma_f32_16x16x32_bf16 v[44:47], v[148:151], v[158:161], v[202:205]
	v_mfma_f32_16x16x32_bf16 v[56:59], v[162:165], v[166:169], v[44:47]
	v_mfma_f32_16x16x32_bf16 v[44:47], v[18:21], v[170:173], v[48:51]
	v_mfma_f32_16x16x32_bf16 v[18:21], v[18:21], v[178:181], v[40:43]
	v_mfma_f32_16x16x32_bf16 v[44:47], v[22:25], v[174:177], v[44:47]
	v_mfma_f32_16x16x32_bf16 v[48:51], v[148:151], v[170:173], v[206:209]
	v_mfma_f32_16x16x32_bf16 v[18:21], v[22:25], v[182:185], v[18:21]
	v_mfma_f32_16x16x32_bf16 v[22:25], v[148:151], v[178:181], v[36:39]
	v_mfma_f32_16x16x32_bf16 v[48:51], v[162:165], v[174:177], v[48:51]
	v_mfma_f32_16x16x32_bf16 v[22:25], v[162:165], v[182:185], v[22:25]
	s_barrier
	s_add_u32 s2, s14, 0x40080
	s_addc_u32 s3, s15, 0
	s_add_u32 s14, s14, 0x60080
	s_addc_u32 s15, s15, 0
	s_mov_b32 m0, s43
	s_nop 0
	v_lshl_add_u64 v[36:37], s[2:3], 0, v[34:35]
	global_load_lds_dwordx4 v[36:37], off
	v_lshl_add_u64 v[36:37], s[14:15], 0, v[34:35]
	s_mov_b32 m0, s44
	s_nop 0
	global_load_lds_dwordx4 v[36:37], off
	s_waitcnt vmcnt(6)
	s_barrier
	v_mfma_f32_16x16x32_bf16 v[26:29], v[186:189], v[80:83], v[26:29]
	v_mfma_f32_16x16x32_bf16 v[30:33], v[116:119], v[80:83], v[30:33]
	v_mfma_f32_16x16x32_bf16 v[80:83], v[190:193], v[152:155], v[26:29]
	v_mfma_f32_16x16x32_bf16 v[26:29], v[116:119], v[158:161], v[140:143]
	v_mfma_f32_16x16x32_bf16 v[60:63], v[120:123], v[166:169], v[26:29]
	v_mfma_f32_16x16x32_bf16 v[26:29], v[186:189], v[158:161], v[144:147]
	v_mfma_f32_16x16x32_bf16 v[14:17], v[116:119], v[170:173], v[14:17]
	v_mfma_f32_16x16x32_bf16 v[10:13], v[186:189], v[170:173], v[10:13]
	v_mfma_f32_16x16x32_bf16 v[6:9], v[116:119], v[178:181], v[6:9]
	v_mfma_f32_16x16x32_bf16 v[2:5], v[186:189], v[178:181], v[2:5]
	v_mfma_f32_16x16x32_bf16 v[76:79], v[120:123], v[152:155], v[30:33]
	v_mfma_f32_16x16x32_bf16 v[64:67], v[190:193], v[166:169], v[26:29]
	v_mfma_f32_16x16x32_bf16 v[40:43], v[120:123], v[174:177], v[14:17]
	v_mfma_f32_16x16x32_bf16 v[36:39], v[190:193], v[174:177], v[10:13]
	v_mfma_f32_16x16x32_bf16 v[6:9], v[120:123], v[182:185], v[6:9]
	v_mfma_f32_16x16x32_bf16 v[2:5], v[190:193], v[182:185], v[2:5]
	v_mov_b32_e32 v118, v0
	s_ashr_i32 s2, s47, 31
	s_barrier
; #define LAS __attribute__((address_space(3)))
;     __device__ __forceinline__ void operator()(const f32x4 (&acc)[2][2][4][2], const Unit& u, int wr, int wc, int fr, int fq, LAS unsigned char*, int) const {
;         const int b = (u.rt * BM) / SEQ;
;         const int col0 = u.pn * BM + wc * 32 + 8 * fq;
;         f32x4 g[2][2];
; #pragma unroll
;         for (int bj = 0; bj < 2; ++bj)
; #pragma unroll
;             for (int n = 0; n < 2; ++n) g[bj][n] = *(const f32x4*)(gate + (size_t)b * 6 * D + col0 + bj * HALF + n * 4);
;         u32x4 xn[2];
;         { const bf16_t* pi = X + (size_t)(u.rt * BM + wr * 64 + fr) * D + col0;
; #pragma unroll
;           for (int bj = 0; bj < 2; ++bj) xn[bj] = *(const u32x4*)(pi + bj * HALF); }
; #pragma unroll
;         for (int g8i = 0; g8i < 8; ++g8i) {
;             const int ai = g8i >> 2, m = g8i & 3;
;             const size_t po = (size_t)(u.rt * BM + ai * HALF + wr * 64 + m * 16 + fr) * D + col0;
;             u32x4 xv[2];
; #pragma unroll
;             for (int bj = 0; bj < 2; ++bj) xv[bj] = xn[bj];
;             if (g8i < 7) { const int ai2 = (g8i + 1) >> 2, m2 = (g8i + 1) & 3; const bf16_t* pi = X + (size_t)(u.rt * BM + ai2 * HALF + wr * 64 + m2 * 16 + fr) * D + col0;
; #pragma unroll
;                 for (int bj = 0; bj < 2; ++bj) xn[bj] = *(const u32x4*)(pi + bj * HALF); }
;             bf16_t* p = X + po;
; #pragma unroll
;             for (int bj = 0; bj < 2; ++bj) {
;                 const u32x4 xw = xv[bj];
;                 const f32x4 x0 = (f32x4){__uint_as_float(xw.x << 16), __uint_as_float(xw.x & 0xffff0000u), __uint_as_float(xw.y << 16), __uint_as_float(xw.y & 0xffff0000u)};
;                 const f32x4 x1 = (f32x4){__uint_as_float(xw.z << 16), __uint_as_float(xw.z & 0xffff0000u), __uint_as_float(xw.w << 16), __uint_as_float(xw.w & 0xffff0000u)};
;                 const f32x4 r0 = x0 + g[bj][0] * acc[ai][bj][m][0], r1 = x1 + g[bj][1] * acc[ai][bj][m][1];
;                 u32x4 w; w.x = cvt_pk_bf16(r0[0], r0[1]); w.y = cvt_pk_bf16(r0[2], r0[3]); w.z = cvt_pk_bf16(r1[0], r1[1]); w.w = cvt_pk_bf16(r1[2], r1[3]);
;                 *(u32x4*)(p + bj * HALF) = w;
;             }
;             asm volatile("" ::: "memory");
;         }
;     }
	s_lshr_b32 s2, s2, 29
	v_readfirstlane_b32 s11, v118
	s_add_i32 s2, s47, s2
	s_lshr_b32 s14, s11, 1
	s_ashr_i32 s2, s2, 3
	s_lshl_b32 s3, s48, 8
	s_and_b32 s14, s14, 0x60
	s_or_b32 s3, s14, s3
	v_lshrrev_b32_e32 v10, 1, v118
	s_mul_i32 s2, s2, 6
	v_and_or_b32 v116, v10, 24, s3
	s_ashr_i32 s3, s2, 31
	s_lshl_b64 s[2:3], s[2:3], 12
	s_add_u32 s2, s35, s2
	s_addc_u32 s3, s36, s3
	v_ashrrev_i32_e32 v117, 31, v116
	v_lshl_add_u64 v[14:15], v[116:117], 2, s[2:3]
	s_ashr_i32 s3, s11, 2
	s_lshl_b32 s2, s47, 8
	s_andn2_b32 s3, s3, 63
	s_add_i32 s3, s3, s2
	v_and_or_b32 v150, v118, 15, s3
	v_ashrrev_i32_e32 v151, 31, v150
	v_lshlrev_b64 v[152:153], 11, v[150:151]
	v_lshl_add_u64 v[118:119], s[6:7], 0, v[152:153]
	v_lshlrev_b64 v[140:141], 1, v[116:117]
	v_lshl_add_u64 v[120:121], v[118:119], 0, v[140:141]
	global_load_dwordx4 v[26:29], v[14:15], off offset:16
	global_load_dwordx4 v[30:33], v[14:15], off
	global_load_dwordx4 v[10:13], v[14:15], off offset:528
	s_nop 0
	global_load_dwordx4 v[14:17], v[14:15], off offset:512
	s_nop 0
	global_load_dwordx4 v[116:119], v[120:121], off
	s_nop 0
	global_load_dwordx4 v[120:123], v[120:121], off offset:256
	v_lshl_add_u64 v[148:149], s[6:7], 0, v[140:141]
	v_or_b32_e32 v140, 16, v150
	v_ashrrev_i32_e32 v141, 31, v140
	v_lshlrev_b64 v[140:141], 11, v[140:141]
	v_lshl_add_u64 v[154:155], v[148:149], 0, v[140:141]
	global_load_dwordx4 v[140:143], v[154:155], off offset:256
	global_load_dwordx4 v[144:147], v[154:155], off
	v_lshl_add_u64 v[152:153], v[148:149], 0, v[152:153]
	s_and_b64 vcc, exec, s[8:9]
	s_mov_b32 s47, s46
	s_mov_b32 s48, s10
	s_mov_b64 s[2:3], s[12:13]
	s_mov_b64 s[14:15], s[0:1]
	s_waitcnt vmcnt(0)
	v_lshlrev_b32_e32 v158, 16, v116
	v_and_b32_e32 v159, 0xffff0000, v116
	v_lshlrev_b32_e32 v116, 16, v117
	v_and_b32_e32 v117, 0xffff0000, v117
	v_lshlrev_b32_e32 v160, 16, v118
	v_and_b32_e32 v161, 0xffff0000, v118
	v_lshlrev_b32_e32 v118, 16, v119
	v_and_b32_e32 v119, 0xffff0000, v119
	v_pk_fma_f32 v[162:163], v[196:197], v[32:33], v[116:117]
	v_pk_fma_f32 v[116:117], v[194:195], v[30:31], v[158:159]
	v_pk_fma_f32 v[158:159], v[200:201], v[28:29], v[118:119]
	v_pk_fma_f32 v[118:119], v[198:199], v[26:27], v[160:161]
	v_cvt_pk_bf16_f32 v116, v116, v117
	v_cvt_pk_bf16_f32 v117, v162, v163
	v_cvt_pk_bf16_f32 v118, v118, v119
	v_cvt_pk_bf16_f32 v119, v158, v159
	global_store_dwordx4 v[152:153], v[116:119], off
	v_lshlrev_b32_e32 v158, 16, v144
	v_and_b32_e32 v159, 0xffff0000, v144
	v_lshlrev_b32_e32 v116, 16, v120
	v_and_b32_e32 v117, 0xffff0000, v120
	v_lshlrev_b32_e32 v118, 16, v121
	v_and_b32_e32 v119, 0xffff0000, v121
	v_lshlrev_b32_e32 v120, 16, v122
	v_and_b32_e32 v121, 0xffff0000, v122
	v_lshlrev_b32_e32 v122, 16, v123
	v_and_b32_e32 v123, 0xffff0000, v123
	v_pk_fma_f32 v[118:119], v[212:213], v[16:17], v[118:119]
	v_pk_fma_f32 v[116:117], v[210:211], v[14:15], v[116:117]
	v_pk_fma_f32 v[122:123], v[216:217], v[12:13], v[122:123]
	v_pk_fma_f32 v[120:121], v[214:215], v[10:11], v[120:121]
	v_cvt_pk_bf16_f32 v116, v116, v117
	v_cvt_pk_bf16_f32 v117, v118, v119
	v_cvt_pk_bf16_f32 v118, v120, v121
	v_cvt_pk_bf16_f32 v119, v122, v123
	global_store_dwordx4 v[152:153], v[116:119], off offset:256
	v_lshlrev_b32_e32 v144, 16, v145
	v_and_b32_e32 v145, 0xffff0000, v145
	v_or_b32_e32 v116, 32, v150
	v_ashrrev_i32_e32 v117, 31, v116
	v_lshlrev_b32_e32 v160, 16, v146
	v_and_b32_e32 v161, 0xffff0000, v146
	v_lshlrev_b32_e32 v146, 16, v147
	v_and_b32_e32 v147, 0xffff0000, v147
	v_lshlrev_b64 v[116:117], 11, v[116:117]
	v_pk_fma_f32 v[126:127], v[126:127], v[32:33], v[144:145]
	v_pk_fma_f32 v[124:125], v[124:125], v[30:31], v[158:159]
	v_pk_fma_f32 v[130:131], v[130:131], v[28:29], v[146:147]
	v_pk_fma_f32 v[128:129], v[128:129], v[26:27], v[160:161]
	v_lshl_add_u64 v[152:153], v[148:149], 0, v[116:117]
	v_cvt_pk_bf16_f32 v124, v124, v125
	v_cvt_pk_bf16_f32 v125, v126, v127
	v_cvt_pk_bf16_f32 v126, v128, v129
	v_cvt_pk_bf16_f32 v127, v130, v131
	global_load_dwordx4 v[116:119], v[152:153], off offset:256
	global_load_dwordx4 v[120:123], v[152:153], off
	v_lshlrev_b32_e32 v128, 16, v142
	global_store_dwordx4 v[154:155], v[124:127], off
	v_and_b32_e32 v129, 0xffff0000, v142
	v_lshlrev_b32_e32 v130, 16, v143
	v_lshlrev_b32_e32 v124, 16, v140
	v_and_b32_e32 v125, 0xffff0000, v140
	v_lshlrev_b32_e32 v126, 16, v141
	v_and_b32_e32 v127, 0xffff0000, v141
	v_and_b32_e32 v131, 0xffff0000, v143
	v_pk_fma_f32 v[126:127], v[134:135], v[16:17], v[126:127]
	v_pk_fma_f32 v[124:125], v[132:133], v[14:15], v[124:125]
	v_pk_fma_f32 v[130:131], v[138:139], v[12:13], v[130:131]
	v_pk_fma_f32 v[128:129], v[136:137], v[10:11], v[128:129]
	v_cvt_pk_bf16_f32 v124, v124, v125
	v_cvt_pk_bf16_f32 v125, v126, v127
	v_cvt_pk_bf16_f32 v126, v128, v129
	v_cvt_pk_bf16_f32 v127, v130, v131
	global_store_dwordx4 v[154:155], v[124:127], off offset:256
	s_waitcnt vmcnt(0)
; __device__ __forceinline__ unsigned cvt_pk_bf16(float lo, float hi) { const bf16x2_t r = __builtin_convertvector((f32x2_t){lo, hi}, bf16x2_t); return __builtin_bit_cast(unsigned, r); }
;     __device__ __forceinline__ void operator()(const f32x4 (&acc)[2][2][4][2], const Unit& u, int wr, int wc, int fr, int fq, LAS unsigned char*, int) const {
;     ...
;         { const bf16_t* pi = X + (size_t)(u.rt * BM + wr * 64 + fr) * D + col0;
; #pragma unroll
;           for (int bj = 0; bj < 2; ++bj) xn[bj] = *(const u32x4*)(pi + bj * HALF); }
; #pragma unroll
;         for (int g8i = 0; g8i < 8; ++g8i) {
;             const int ai = g8i >> 2, m = g8i & 3;
;             const size_t po = (size_t)(u.rt * BM + ai * HALF + wr * 64 + m * 16 + fr) * D + col0;
;             u32x4 xv[2];
; #pragma unroll
;             for (int bj = 0; bj < 2; ++bj) xv[bj] = xn[bj];
;             if (g8i < 7) { const int ai2 = (g8i + 1) >> 2, m2 = (g8i + 1) & 3; const bf16_t* pi = X + (size_t)(u.rt * BM + ai2 * HALF + wr * 64 + m2 * 16 + fr) * D + col0;
; #pragma unroll
;                 for (int bj = 0; bj < 2; ++bj) xn[bj] = *(const u32x4*)(pi + bj * HALF); }
;             bf16_t* p = X + po;
; #pragma unroll
;             for (int bj = 0; bj < 2; ++bj) {
;                 const u32x4 xw = xv[bj];
;                 const f32x4 x0 = (f32x4){__uint_as_float(xw.x << 16), __uint_as_float(xw.x & 0xffff0000u), __uint_as_float(xw.y << 16), __uint_as_float(xw.y & 0xffff0000u)};
;                 const f32x4 x1 = (f32x4){__uint_as_float(xw.z << 16), __uint_as_float(xw.z & 0xffff0000u), __uint_as_float(xw.w << 16), __uint_as_float(xw.w & 0xffff0000u)};
;                 const f32x4 r0 = x0 + g[bj][0] * acc[ai][bj][m][0], r1 = x1 + g[bj][1] * acc[ai][bj][m][1];
;                 u32x4 w; w.x = cvt_pk_bf16(r0[0], r0[1]); w.y = cvt_pk_bf16(r0[2], r0[3]); w.z = cvt_pk_bf16(r1[0], r1[1]); w.w = cvt_pk_bf16(r1[2], r1[3]);
;                 *(u32x4*)(p + bj * HALF) = w;
;             }
;             asm volatile("" ::: "memory");
;         }
	v_lshlrev_b32_e32 v134, 16, v120
	v_or_b32_e32 v124, 48, v150
	v_ashrrev_i32_e32 v125, 31, v124
	v_lshlrev_b64 v[124:125], 11, v[124:125]
	v_lshl_add_u64 v[128:129], v[148:149], 0, v[124:125]
	global_load_dwordx4 v[124:127], v[128:129], off offset:256
	global_load_dwordx4 v[130:133], v[128:129], off
	v_and_b32_e32 v135, 0xffff0000, v120
	v_lshlrev_b32_e32 v120, 16, v121
	v_and_b32_e32 v121, 0xffff0000, v121
	v_lshlrev_b32_e32 v136, 16, v122
	v_and_b32_e32 v137, 0xffff0000, v122
	v_lshlrev_b32_e32 v122, 16, v123
	v_and_b32_e32 v123, 0xffff0000, v123
	v_pk_fma_f32 v[102:103], v[102:103], v[32:33], v[120:121]
	v_pk_fma_f32 v[100:101], v[100:101], v[30:31], v[134:135]
	v_pk_fma_f32 v[106:107], v[106:107], v[28:29], v[122:123]
	v_pk_fma_f32 v[104:105], v[104:105], v[26:27], v[136:137]
	v_cvt_pk_bf16_f32 v100, v100, v101
	v_cvt_pk_bf16_f32 v101, v102, v103
	v_cvt_pk_bf16_f32 v102, v104, v105
	v_cvt_pk_bf16_f32 v103, v106, v107
	global_store_dwordx4 v[152:153], v[100:103], off
	v_lshlrev_b32_e32 v104, 16, v118
	v_and_b32_e32 v105, 0xffff0000, v118
	v_lshlrev_b32_e32 v100, 16, v116
	v_and_b32_e32 v101, 0xffff0000, v116
	v_lshlrev_b32_e32 v102, 16, v117
	v_and_b32_e32 v103, 0xffff0000, v117
	v_lshlrev_b32_e32 v106, 16, v119
	v_and_b32_e32 v107, 0xffff0000, v119
	v_pk_fma_f32 v[102:103], v[110:111], v[16:17], v[102:103]
	v_pk_fma_f32 v[100:101], v[108:109], v[14:15], v[100:101]
	v_pk_fma_f32 v[106:107], v[114:115], v[12:13], v[106:107]
	v_pk_fma_f32 v[104:105], v[112:113], v[10:11], v[104:105]
	v_cvt_pk_bf16_f32 v100, v100, v101
	v_cvt_pk_bf16_f32 v101, v102, v103
	v_cvt_pk_bf16_f32 v102, v104, v105
	v_cvt_pk_bf16_f32 v103, v106, v107
	global_store_dwordx4 v[152:153], v[100:103], off offset:256
	s_waitcnt vmcnt(0)
	v_lshlrev_b32_e32 v110, 16, v130
	v_add_u32_e32 v100, 0x80, v150
	v_ashrrev_i32_e32 v101, 31, v100
	v_and_b32_e32 v111, 0xffff0000, v130
	v_lshlrev_b32_e32 v112, 16, v131
	v_and_b32_e32 v113, 0xffff0000, v131
	v_lshlrev_b32_e32 v114, 16, v132
	v_and_b32_e32 v115, 0xffff0000, v132
	v_lshlrev_b32_e32 v116, 16, v133
	v_and_b32_e32 v117, 0xffff0000, v133
	v_lshlrev_b64 v[100:101], 11, v[100:101]
	v_pk_fma_f32 v[86:87], v[86:87], v[32:33], v[112:113]
	v_pk_fma_f32 v[84:85], v[84:85], v[30:31], v[110:111]
	v_pk_fma_f32 v[90:91], v[90:91], v[28:29], v[116:117]
	v_pk_fma_f32 v[88:89], v[88:89], v[26:27], v[114:115]
	v_lshl_add_u64 v[108:109], v[148:149], 0, v[100:101]
	v_cvt_pk_bf16_f32 v84, v84, v85
	v_cvt_pk_bf16_f32 v85, v86, v87
	v_cvt_pk_bf16_f32 v86, v88, v89
	v_cvt_pk_bf16_f32 v87, v90, v91
	global_load_dwordx4 v[100:103], v[108:109], off offset:256
	global_load_dwordx4 v[104:107], v[108:109], off
	v_lshlrev_b32_e32 v88, 16, v126
	global_store_dwordx4 v[128:129], v[84:87], off
	v_and_b32_e32 v89, 0xffff0000, v126
	v_lshlrev_b32_e32 v90, 16, v127
	v_lshlrev_b32_e32 v84, 16, v124
	v_and_b32_e32 v85, 0xffff0000, v124
	v_lshlrev_b32_e32 v86, 16, v125
	v_and_b32_e32 v87, 0xffff0000, v125
	v_and_b32_e32 v91, 0xffff0000, v127
	v_pk_fma_f32 v[86:87], v[94:95], v[16:17], v[86:87]
	v_pk_fma_f32 v[84:85], v[92:93], v[14:15], v[84:85]
	v_pk_fma_f32 v[90:91], v[98:99], v[12:13], v[90:91]
	v_pk_fma_f32 v[88:89], v[96:97], v[10:11], v[88:89]
	v_cvt_pk_bf16_f32 v84, v84, v85
	v_cvt_pk_bf16_f32 v85, v86, v87
	v_cvt_pk_bf16_f32 v86, v88, v89
	v_cvt_pk_bf16_f32 v87, v90, v91
	global_store_dwordx4 v[128:129], v[84:87], off offset:256
	s_waitcnt vmcnt(0)
	v_lshlrev_b32_e32 v94, 16, v104
	v_add_u32_e32 v84, 0x90, v150
	v_ashrrev_i32_e32 v85, 31, v84
	v_lshlrev_b64 v[84:85], 11, v[84:85]
	v_lshl_add_u64 v[88:89], v[148:149], 0, v[84:85]
	global_load_dwordx4 v[84:87], v[88:89], off offset:256
	global_load_dwordx4 v[90:93], v[88:89], off
	v_and_b32_e32 v95, 0xffff0000, v104
	v_lshlrev_b32_e32 v96, 16, v105
	v_and_b32_e32 v97, 0xffff0000, v105
	v_lshlrev_b32_e32 v98, 16, v106
	v_and_b32_e32 v99, 0xffff0000, v106
	v_lshlrev_b32_e32 v104, 16, v107
	v_and_b32_e32 v105, 0xffff0000, v107
	v_pk_fma_f32 v[70:71], v[70:71], v[32:33], v[96:97]
	v_pk_fma_f32 v[68:69], v[68:69], v[30:31], v[94:95]
	v_pk_fma_f32 v[74:75], v[74:75], v[28:29], v[104:105]
	v_pk_fma_f32 v[72:73], v[72:73], v[26:27], v[98:99]
	v_cvt_pk_bf16_f32 v68, v68, v69
	v_cvt_pk_bf16_f32 v69, v70, v71
	v_cvt_pk_bf16_f32 v70, v72, v73
	v_cvt_pk_bf16_f32 v71, v74, v75
	global_store_dwordx4 v[108:109], v[68:71], off
	v_lshlrev_b32_e32 v72, 16, v102
	v_and_b32_e32 v73, 0xffff0000, v102
	v_lshlrev_b32_e32 v68, 16, v100
	v_and_b32_e32 v69, 0xffff0000, v100
	v_lshlrev_b32_e32 v70, 16, v101
	v_and_b32_e32 v71, 0xffff0000, v101
	v_lshlrev_b32_e32 v74, 16, v103
	v_and_b32_e32 v75, 0xffff0000, v103
	v_pk_fma_f32 v[70:71], v[78:79], v[16:17], v[70:71]
	v_pk_fma_f32 v[68:69], v[76:77], v[14:15], v[68:69]
	v_pk_fma_f32 v[74:75], v[82:83], v[12:13], v[74:75]
	v_pk_fma_f32 v[72:73], v[80:81], v[10:11], v[72:73]
	v_cvt_pk_bf16_f32 v68, v68, v69
	v_cvt_pk_bf16_f32 v69, v70, v71
	v_cvt_pk_bf16_f32 v70, v72, v73
	v_cvt_pk_bf16_f32 v71, v74, v75
	global_store_dwordx4 v[108:109], v[68:71], off offset:256
	s_waitcnt vmcnt(0)
; __device__ __forceinline__ unsigned cvt_pk_bf16(float lo, float hi) { const bf16x2_t r = __builtin_convertvector((f32x2_t){lo, hi}, bf16x2_t); return __builtin_bit_cast(unsigned, r); }
; template <class Epi, class Src>
; __device__ __forceinline__ void gemm_phase(LAS unsigned char* lds, const Src S, const Epi E) {
;     ...
;         if (!has_next) break;
;     __device__ __forceinline__ void operator()(const f32x4 (&acc)[2][2][4][2], const Unit& u, int wr, int wc, int fr, int fq, LAS unsigned char*, int) const {
;     ...
;         { const bf16_t* pi = X + (size_t)(u.rt * BM + wr * 64 + fr) * D + col0;
; #pragma unroll
;           for (int bj = 0; bj < 2; ++bj) xn[bj] = *(const u32x4*)(pi + bj * HALF); }
; #pragma unroll
;         for (int g8i = 0; g8i < 8; ++g8i) {
;             const int ai = g8i >> 2, m = g8i & 3;
;             const size_t po = (size_t)(u.rt * BM + ai * HALF + wr * 64 + m * 16 + fr) * D + col0;
;             u32x4 xv[2];
; #pragma unroll
;             for (int bj = 0; bj < 2; ++bj) xv[bj] = xn[bj];
;             if (g8i < 7) { const int ai2 = (g8i + 1) >> 2, m2 = (g8i + 1) & 3; const bf16_t* pi = X + (size_t)(u.rt * BM + ai2 * HALF + wr * 64 + m2 * 16 + fr) * D + col0;
; #pragma unroll
;                 for (int bj = 0; bj < 2; ++bj) xn[bj] = *(const u32x4*)(pi + bj * HALF); }
;             bf16_t* p = X + po;
; #pragma unroll
;             for (int bj = 0; bj < 2; ++bj) {
;                 const u32x4 xw = xv[bj];
;                 const f32x4 x0 = (f32x4){__uint_as_float(xw.x << 16), __uint_as_float(xw.x & 0xffff0000u), __uint_as_float(xw.y << 16), __uint_as_float(xw.y & 0xffff0000u)};
;                 const f32x4 x1 = (f32x4){__uint_as_float(xw.z << 16), __uint_as_float(xw.z & 0xffff0000u), __uint_as_float(xw.w << 16), __uint_as_float(xw.w & 0xffff0000u)};
;                 const f32x4 r0 = x0 + g[bj][0] * acc[ai][bj][m][0], r1 = x1 + g[bj][1] * acc[ai][bj][m][1];
;                 u32x4 w; w.x = cvt_pk_bf16(r0[0], r0[1]); w.y = cvt_pk_bf16(r0[2], r0[3]); w.z = cvt_pk_bf16(r1[0], r1[1]); w.w = cvt_pk_bf16(r1[2], r1[3]);
;                 *(u32x4*)(p + bj * HALF) = w;
;             }
;             asm volatile("" ::: "memory");
;         }
	v_lshlrev_b32_e32 v78, 16, v90
	v_add_u32_e32 v68, 0xa0, v150
	v_ashrrev_i32_e32 v69, 31, v68
	v_and_b32_e32 v79, 0xffff0000, v90
	v_lshlrev_b32_e32 v80, 16, v91
	v_and_b32_e32 v81, 0xffff0000, v91
	v_lshlrev_b32_e32 v82, 16, v92
	v_and_b32_e32 v83, 0xffff0000, v92
	v_lshlrev_b32_e32 v90, 16, v93
	v_and_b32_e32 v91, 0xffff0000, v93
	v_lshlrev_b64 v[68:69], 11, v[68:69]
	v_pk_fma_f32 v[54:55], v[54:55], v[32:33], v[80:81]
	v_pk_fma_f32 v[52:53], v[52:53], v[30:31], v[78:79]
	v_pk_fma_f32 v[58:59], v[58:59], v[28:29], v[90:91]
	v_pk_fma_f32 v[56:57], v[56:57], v[26:27], v[82:83]
	v_lshl_add_u64 v[76:77], v[148:149], 0, v[68:69]
	v_cvt_pk_bf16_f32 v52, v52, v53
	v_cvt_pk_bf16_f32 v53, v54, v55
	v_cvt_pk_bf16_f32 v54, v56, v57
	v_cvt_pk_bf16_f32 v55, v58, v59
	global_load_dwordx4 v[68:71], v[76:77], off offset:256
	global_load_dwordx4 v[72:75], v[76:77], off
	v_lshlrev_b32_e32 v56, 16, v86
	global_store_dwordx4 v[88:89], v[52:55], off
	v_and_b32_e32 v57, 0xffff0000, v86
	v_lshlrev_b32_e32 v58, 16, v87
	v_lshlrev_b32_e32 v52, 16, v84
	v_and_b32_e32 v53, 0xffff0000, v84
	v_lshlrev_b32_e32 v54, 16, v85
	v_and_b32_e32 v55, 0xffff0000, v85
	v_and_b32_e32 v59, 0xffff0000, v87
	v_pk_fma_f32 v[54:55], v[62:63], v[16:17], v[54:55]
	v_pk_fma_f32 v[52:53], v[60:61], v[14:15], v[52:53]
	v_pk_fma_f32 v[58:59], v[66:67], v[12:13], v[58:59]
	v_pk_fma_f32 v[56:57], v[64:65], v[10:11], v[56:57]
	v_cvt_pk_bf16_f32 v52, v52, v53
	v_cvt_pk_bf16_f32 v53, v54, v55
	v_cvt_pk_bf16_f32 v54, v56, v57
	v_cvt_pk_bf16_f32 v55, v58, v59
	global_store_dwordx4 v[88:89], v[52:55], off offset:256
	s_waitcnt vmcnt(0)
	v_lshlrev_b32_e32 v62, 16, v72
	v_add_u32_e32 v52, 0xb0, v150
	v_ashrrev_i32_e32 v53, 31, v52
	v_lshlrev_b64 v[52:53], 11, v[52:53]
	v_lshl_add_u64 v[56:57], v[148:149], 0, v[52:53]
	global_load_dwordx4 v[52:55], v[56:57], off offset:256
	global_load_dwordx4 v[58:61], v[56:57], off
	v_and_b32_e32 v63, 0xffff0000, v72
	v_lshlrev_b32_e32 v64, 16, v73
	v_and_b32_e32 v65, 0xffff0000, v73
	v_lshlrev_b32_e32 v66, 16, v74
	v_and_b32_e32 v67, 0xffff0000, v74
	v_lshlrev_b32_e32 v72, 16, v75
	v_and_b32_e32 v73, 0xffff0000, v75
	v_pk_fma_f32 v[46:47], v[46:47], v[32:33], v[64:65]
	v_pk_fma_f32 v[44:45], v[44:45], v[30:31], v[62:63]
	v_pk_fma_f32 v[50:51], v[50:51], v[28:29], v[72:73]
	v_pk_fma_f32 v[48:49], v[48:49], v[26:27], v[66:67]
	v_cvt_pk_bf16_f32 v44, v44, v45
	v_cvt_pk_bf16_f32 v45, v46, v47
	v_cvt_pk_bf16_f32 v46, v48, v49
	v_cvt_pk_bf16_f32 v47, v50, v51
	global_store_dwordx4 v[76:77], v[44:47], off
	v_lshlrev_b32_e32 v48, 16, v70
	v_and_b32_e32 v49, 0xffff0000, v70
	v_lshlrev_b32_e32 v44, 16, v68
	v_and_b32_e32 v45, 0xffff0000, v68
	v_lshlrev_b32_e32 v46, 16, v69
	v_and_b32_e32 v47, 0xffff0000, v69
	v_lshlrev_b32_e32 v50, 16, v71
	v_and_b32_e32 v51, 0xffff0000, v71
	v_pk_fma_f32 v[42:43], v[42:43], v[16:17], v[46:47]
	v_pk_fma_f32 v[40:41], v[40:41], v[14:15], v[44:45]
	v_pk_fma_f32 v[44:45], v[38:39], v[12:13], v[50:51]
	v_pk_fma_f32 v[38:39], v[36:37], v[10:11], v[48:49]
	v_cvt_pk_bf16_f32 v36, v40, v41
	v_cvt_pk_bf16_f32 v37, v42, v43
	v_cvt_pk_bf16_f32 v38, v38, v39
	v_cvt_pk_bf16_f32 v39, v44, v45
	global_store_dwordx4 v[76:77], v[36:39], off offset:256
	s_waitcnt vmcnt(0)
	v_lshlrev_b32_e32 v40, 16, v60
	v_lshlrev_b32_e32 v36, 16, v58
	v_and_b32_e32 v37, 0xffff0000, v58
	v_lshlrev_b32_e32 v38, 16, v59
	v_and_b32_e32 v39, 0xffff0000, v59
	v_and_b32_e32 v41, 0xffff0000, v60
	v_lshlrev_b32_e32 v42, 16, v61
	v_and_b32_e32 v43, 0xffff0000, v61
	v_pk_fma_f32 v[20:21], v[20:21], v[32:33], v[38:39]
	v_pk_fma_f32 v[18:19], v[18:19], v[30:31], v[36:37]
	v_pk_fma_f32 v[24:25], v[24:25], v[28:29], v[42:43]
	v_pk_fma_f32 v[22:23], v[22:23], v[26:27], v[40:41]
	v_cvt_pk_bf16_f32 v18, v18, v19
	v_cvt_pk_bf16_f32 v19, v20, v21
	v_cvt_pk_bf16_f32 v20, v22, v23
	v_cvt_pk_bf16_f32 v21, v24, v25
	global_store_dwordx4 v[56:57], v[18:21], off
	v_lshlrev_b32_e32 v22, 16, v54
	v_and_b32_e32 v23, 0xffff0000, v54
	v_lshlrev_b32_e32 v18, 16, v52
	v_and_b32_e32 v19, 0xffff0000, v52
	v_lshlrev_b32_e32 v20, 16, v53
	v_and_b32_e32 v21, 0xffff0000, v53
	v_lshlrev_b32_e32 v24, 16, v55
	v_and_b32_e32 v25, 0xffff0000, v55
	v_pk_fma_f32 v[8:9], v[8:9], v[16:17], v[20:21]
	v_pk_fma_f32 v[6:7], v[6:7], v[14:15], v[18:19]
	v_pk_fma_f32 v[12:13], v[4:5], v[12:13], v[24:25]
	v_pk_fma_f32 v[4:5], v[2:3], v[10:11], v[22:23]
	v_cvt_pk_bf16_f32 v2, v6, v7
	v_cvt_pk_bf16_f32 v3, v8, v9
	v_cvt_pk_bf16_f32 v4, v4, v5
	v_cvt_pk_bf16_f32 v5, v12, v13
	global_store_dwordx4 v[56:57], v[2:5], off offset:256
	s_cbranch_vccz .LBB0_1186
	s_waitcnt vmcnt(0)
	s_cmpk_gt_u32 s20, 0xff
	s_cbranch_scc1 .LBB0_1197
	s_barrier

;     __device__ __forceinline__ const char* bptr(const Unit& u) const { return (const char*)Bt + ((size_t)u.e * NTN * BM + (size_t)u.pn * BM) * RB; }
;     __device__ __forceinline__ const char* bptr(const Unit& u) const { return (const char*)Bt + (size_t)u.pn * BM * KD * 2; }
; template <class Epi, class Src>
; __device__ __forceinline__ void gemm_phase(LAS unsigned char* lds, const Src S, const Epi E) {
;     ...
;         const char* nB = has_next ? S.bptr(nxt) : cB;
;         const char* nA = has_next ? Ab + (size_t)(nxt.rowbase + nxt.rt * BM) * RB : cA;
.LBB0_1369:
	s_ashr_i32 s27, s26, 31
	s_lshl_b64 s[0:1], s[26:27], 18
	s_lshl_b64 s[2:3], s[22:23], 21
	s_add_u32 s2, s40, s2
	s_addc_u32 s3, s41, s3
	s_add_u32 s28, s2, s0
	v_lshl_add_u32 v134, s68, 10, v156
	s_addc_u32 s29, s3, s1
	s_and_b64 s[0:1], s[24:25], exec
	s_cselect_b32 s1, s29, s21
	s_cselect_b32 s0, s28, s20
	s_add_u32 s2, s20, 0x100
	s_addc_u32 s3, s21, 0
	v_add_u32_e32 v132, s43, v157
	s_mov_b64 s[94:95], 0x80
	s_add_i32 s23, s47, 0xc000
	s_add_i32 s17, s47, 0xe000
	ds_read_b128 v[136:139], v132
	ds_read_b128 v[140:143], v132 offset:1024
	ds_read_b128 v[160:163], v132 offset:2048
	ds_read_b128 v[164:167], v132 offset:3072
	ds_read_b128 v[168:171], v158
	ds_read_b128 v[172:175], v158 offset:1024
	ds_read_b128 v[176:179], v158 offset:2048
	ds_read_b128 v[180:183], v158 offset:3072
	ds_read_b128 v[184:187], v158 offset:4096
	ds_read_b128 v[188:191], v158 offset:5120
	ds_read_b128 v[192:195], v158 offset:6144
	ds_read_b128 v[196:199], v158 offset:7168
	s_add_u32 s94, s8, 0x80
	s_addc_u32 s95, s9, 0
	v_and_b32_e32 v34, 0xffff, v255
	v_lshl_add_u32 v34, v34, 10, v155
	s_mov_b32 m0, s23
	s_nop 0
	global_load_lds_dwordx4 v34, s[94:95]
	v_lshrrev_b32_e32 v34, 16, v255
	v_lshl_add_u32 v34, v34, 10, v155
	s_mov_b32 m0, s17
	s_nop 0
	global_load_lds_dwordx4 v34, s[94:95]
	s_waitcnt lgkmcnt(8)
	s_barrier
	s_waitcnt lgkmcnt(0)
	s_waitcnt lgkmcnt(0)
	v_mfma_scale_f32_16x16x128_f8f6f4 v[150:153], v[136:143], v[168:175], 0, v154, v154 op_sel_hi:[0,0,0]
	v_mfma_scale_f32_16x16x128_f8f6f4 v[208:211], v[160:167], v[168:175], 0, v154, v154 op_sel_hi:[0,0,0]
	v_mfma_scale_f32_16x16x128_f8f6f4 v[212:215], v[136:143], v[176:183], 0, v154, v154 op_sel_hi:[0,0,0]
	v_mfma_scale_f32_16x16x128_f8f6f4 v[216:219], v[160:167], v[176:183], 0, v154, v154 op_sel_hi:[0,0,0]
	v_mfma_scale_f32_16x16x128_f8f6f4 v[220:223], v[136:143], v[184:191], 0, v154, v154 op_sel_hi:[0,0,0]
	v_mfma_scale_f32_16x16x128_f8f6f4 v[224:227], v[160:167], v[184:191], 0, v154, v154 op_sel_hi:[0,0,0]
	v_mfma_scale_f32_16x16x128_f8f6f4 v[228:231], v[136:143], v[192:199], 0, v154, v154 op_sel_hi:[0,0,0]
	v_mfma_scale_f32_16x16x128_f8f6f4 v[232:235], v[160:167], v[192:199], 0, v154, v154 op_sel_hi:[0,0,0]
	s_barrier
	s_add_u32 s74, s20, 0x10100
	v_add_u32_e32 v133, s49, v157
	s_addc_u32 s75, s21, 0
	s_mov_b32 m0, s44
	ds_read_b128 v[124:127], v133
	ds_read_b128 v[128:131], v133 offset:1024
	ds_read_b128 v[200:203], v133 offset:2048
	ds_read_b128 v[204:207], v133 offset:3072
	s_nop 0
	v_lshl_add_u64 v[68:69], s[2:3], 0, v[252:253]
	global_load_lds_dwordx4 v[68:69], off
	v_lshl_add_u64 v[68:69], s[74:75], 0, v[252:253]
	s_mov_b32 m0, s45
	s_nop 0
	global_load_lds_dwordx4 v[68:69], off
	s_barrier
	s_waitcnt lgkmcnt(0)
	s_waitcnt lgkmcnt(0)
	v_mfma_scale_f32_16x16x128_f8f6f4 v[96:99], v[124:131], v[168:175], 0, v154, v154 op_sel_hi:[0,0,0]
	v_mfma_scale_f32_16x16x128_f8f6f4 v[92:95], v[200:207], v[168:175], 0, v154, v154 op_sel_hi:[0,0,0]
	v_mfma_scale_f32_16x16x128_f8f6f4 v[88:91], v[124:131], v[176:183], 0, v154, v154 op_sel_hi:[0,0,0]
	v_mfma_scale_f32_16x16x128_f8f6f4 v[84:87], v[200:207], v[176:183], 0, v154, v154 op_sel_hi:[0,0,0]
	v_mfma_scale_f32_16x16x128_f8f6f4 v[80:83], v[124:131], v[184:191], 0, v154, v154 op_sel_hi:[0,0,0]
	v_mfma_scale_f32_16x16x128_f8f6f4 v[76:79], v[200:207], v[184:191], 0, v154, v154 op_sel_hi:[0,0,0]
	v_mfma_scale_f32_16x16x128_f8f6f4 v[72:75], v[124:131], v[192:199], 0, v154, v154 op_sel_hi:[0,0,0]
	v_mfma_scale_f32_16x16x128_f8f6f4 v[68:71], v[200:207], v[192:199], 0, v154, v154 op_sel_hi:[0,0,0]
	s_barrier
	s_nop 0
	s_mov_b64 s[76:77], 0x100
	ds_read_b128 v[104:107], v158 offset:16384
	ds_read_b128 v[108:111], v158 offset:17408
	ds_read_b128 v[112:115], v158 offset:18432
	ds_read_b128 v[116:119], v158 offset:19456
	ds_read_b128 v[168:171], v158 offset:20480
	ds_read_b128 v[172:175], v158 offset:21504
	ds_read_b128 v[176:179], v158 offset:22528
	ds_read_b128 v[180:183], v158 offset:23552
	s_add_u32 s94, s8, 0x100
	s_addc_u32 s95, s9, 0
	v_and_b32_e32 v34, 0xffff, v159
	v_lshl_add_u32 v34, v34, 10, v155
	s_mov_b32 m0, s47
	s_nop 0
	global_load_lds_dwordx4 v34, s[94:95]
	v_lshrrev_b32_e32 v34, 16, v159
	v_lshl_add_u32 v34, v34, 10, v155
	s_mov_b32 m0, s48
	s_nop 0
	global_load_lds_dwordx4 v34, s[94:95]
	s_barrier
	s_waitcnt lgkmcnt(0)
	s_waitcnt lgkmcnt(0)
	v_mfma_scale_f32_16x16x128_f8f6f4 v[64:67], v[136:143], v[104:111], 0, v154, v154 op_sel_hi:[0,0,0]
	v_mfma_scale_f32_16x16x128_f8f6f4 v[60:63], v[160:167], v[104:111], 0, v154, v154 op_sel_hi:[0,0,0]
	v_mfma_scale_f32_16x16x128_f8f6f4 v[56:59], v[136:143], v[112:119], 0, v154, v154 op_sel_hi:[0,0,0]
	v_mfma_scale_f32_16x16x128_f8f6f4 v[52:55], v[160:167], v[112:119], 0, v154, v154 op_sel_hi:[0,0,0]
	v_mfma_scale_f32_16x16x128_f8f6f4 v[48:51], v[136:143], v[168:175], 0, v154, v154 op_sel_hi:[0,0,0]
	v_mfma_scale_f32_16x16x128_f8f6f4 v[44:47], v[160:167], v[168:175], 0, v154, v154 op_sel_hi:[0,0,0]
	v_mfma_scale_f32_16x16x128_f8f6f4 v[40:43], v[136:143], v[176:183], 0, v154, v154 op_sel_hi:[0,0,0]
	v_mfma_scale_f32_16x16x128_f8f6f4 v[36:39], v[160:167], v[176:183], 0, v154, v154 op_sel_hi:[0,0,0]
	s_barrier
	s_add_u32 s2, s20, 0x20100
	s_addc_u32 s3, s21, 0
	s_add_u32 s74, s20, 0x30100
	s_addc_u32 s75, s21, 0
	s_mov_b32 m0, s50
	s_nop 0
	v_lshl_add_u64 v[6:7], s[2:3], 0, v[252:253]
	global_load_lds_dwordx4 v[6:7], off
	v_lshl_add_u64 v[6:7], s[74:75], 0, v[252:253]
	s_mov_b32 m0, s51
	s_nop 0
	global_load_lds_dwordx4 v[6:7], off
	s_waitcnt vmcnt(6)
	s_barrier
	v_mfma_scale_f32_16x16x128_f8f6f4 v[100:103], v[124:131], v[104:111], 0, v154, v154 op_sel_hi:[0,0,0]
	v_mfma_scale_f32_16x16x128_f8f6f4 v[104:107], v[200:207], v[104:111], 0, v154, v154 op_sel_hi:[0,0,0]
	v_mfma_scale_f32_16x16x128_f8f6f4 v[108:111], v[124:131], v[112:119], 0, v154, v154 op_sel_hi:[0,0,0]
	v_mfma_scale_f32_16x16x128_f8f6f4 v[112:115], v[200:207], v[112:119], 0, v154, v154 op_sel_hi:[0,0,0]
	v_mfma_scale_f32_16x16x128_f8f6f4 v[116:119], v[124:131], v[168:175], 0, v154, v154 op_sel_hi:[0,0,0]
	v_mfma_scale_f32_16x16x128_f8f6f4 v[120:123], v[200:207], v[168:175], 0, v154, v154 op_sel_hi:[0,0,0]
	v_mfma_scale_f32_16x16x128_f8f6f4 v[124:127], v[124:131], v[176:183], 0, v154, v154 op_sel_hi:[0,0,0]
	v_mfma_scale_f32_16x16x128_f8f6f4 v[128:131], v[200:207], v[176:183], 0, v154, v154 op_sel_hi:[0,0,0]
	s_barrier
	s_nop 4
	v_add_u32_e32 v135, s58, v157
	ds_read_b128 v[138:141], v135
	ds_read_b128 v[142:145], v135 offset:1024
	ds_read_b128 v[160:163], v135 offset:2048
	ds_read_b128 v[164:167], v135 offset:3072
	ds_read_b128 v[168:171], v158 offset:32768
	ds_read_b128 v[172:175], v158 offset:33792
	ds_read_b128 v[176:179], v158 offset:34816
	ds_read_b128 v[180:183], v158 offset:35840
	ds_read_b128 v[184:187], v158 offset:36864
	ds_read_b128 v[188:191], v158 offset:37888
	ds_read_b128 v[192:195], v158 offset:38912
	ds_read_b128 v[196:199], v158 offset:39936
	s_add_u32 s94, s8, 0x100
	s_addc_u32 s95, s9, 0
	v_and_b32_e32 v34, 0xffff, v255
	v_lshl_add_u32 v34, v34, 10, v155
	s_mov_b32 m0, s52
	s_nop 0
	global_load_lds_dwordx4 v34, s[94:95]
	v_lshrrev_b32_e32 v34, 16, v255
	v_lshl_add_u32 v34, v34, 10, v155
	s_mov_b32 m0, s53
	s_nop 0
	global_load_lds_dwordx4 v34, s[94:95]
	s_waitcnt lgkmcnt(8)
	s_barrier
	s_waitcnt lgkmcnt(0)
	s_waitcnt lgkmcnt(0)
	v_mfma_scale_f32_16x16x128_f8f6f4 v[2:5], v[138:145], v[168:175], v[150:153], v154, v154 op_sel_hi:[0,0,0]
	v_mfma_scale_f32_16x16x128_f8f6f4 v[6:9], v[160:167], v[168:175], v[208:211], v154, v154 op_sel_hi:[0,0,0]
	v_mfma_scale_f32_16x16x128_f8f6f4 v[10:13], v[138:145], v[176:183], v[212:215], v154, v154 op_sel_hi:[0,0,0]
	v_mfma_scale_f32_16x16x128_f8f6f4 v[14:17], v[160:167], v[176:183], v[216:219], v154, v154 op_sel_hi:[0,0,0]
	v_mfma_scale_f32_16x16x128_f8f6f4 v[18:21], v[138:145], v[184:191], v[220:223], v154, v154 op_sel_hi:[0,0,0]
	v_mfma_scale_f32_16x16x128_f8f6f4 v[22:25], v[160:167], v[184:191], v[224:227], v154, v154 op_sel_hi:[0,0,0]
	v_mfma_scale_f32_16x16x128_f8f6f4 v[26:29], v[138:145], v[192:199], v[228:231], v154, v154 op_sel_hi:[0,0,0]
	v_mfma_scale_f32_16x16x128_f8f6f4 v[30:33], v[160:167], v[192:199], v[232:235], v154, v154 op_sel_hi:[0,0,0]
	s_barrier
	s_add_u32 s2, s20, 0x180
	s_addc_u32 s3, s21, 0
	s_add_u32 s74, s20, 0x10180
	v_add_u32_e32 v136, s63, v157
	s_addc_u32 s75, s21, 0
	s_mov_b32 m0, s59
	ds_read_b128 v[200:203], v136
	ds_read_b128 v[204:207], v136 offset:1024
	ds_read_b128 v[208:211], v136 offset:2048
	ds_read_b128 v[212:215], v136 offset:3072
	s_nop 0
	v_lshl_add_u64 v[146:147], s[2:3], 0, v[252:253]
	global_load_lds_dwordx4 v[146:147], off
	v_lshl_add_u64 v[146:147], s[74:75], 0, v[252:253]
	s_mov_b32 m0, s60
	s_nop 0
	global_load_lds_dwordx4 v[146:147], off
	s_barrier
	s_waitcnt lgkmcnt(0)
	s_waitcnt lgkmcnt(0)
	v_mfma_scale_f32_16x16x128_f8f6f4 v[96:99], v[200:207], v[168:175], v[96:99], v154, v154 op_sel_hi:[0,0,0]
	v_mfma_scale_f32_16x16x128_f8f6f4 v[92:95], v[208:215], v[168:175], v[92:95], v154, v154 op_sel_hi:[0,0,0]
	v_mfma_scale_f32_16x16x128_f8f6f4 v[88:91], v[200:207], v[176:183], v[88:91], v154, v154 op_sel_hi:[0,0,0]
	v_mfma_scale_f32_16x16x128_f8f6f4 v[84:87], v[208:215], v[176:183], v[84:87], v154, v154 op_sel_hi:[0,0,0]
	v_mfma_scale_f32_16x16x128_f8f6f4 v[80:83], v[200:207], v[184:191], v[80:83], v154, v154 op_sel_hi:[0,0,0]
	v_mfma_scale_f32_16x16x128_f8f6f4 v[76:79], v[208:215], v[184:191], v[76:79], v154, v154 op_sel_hi:[0,0,0]
	v_mfma_scale_f32_16x16x128_f8f6f4 v[72:75], v[200:207], v[192:199], v[72:75], v154, v154 op_sel_hi:[0,0,0]
	v_mfma_scale_f32_16x16x128_f8f6f4 v[68:71], v[208:215], v[192:199], v[68:71], v154, v154 op_sel_hi:[0,0,0]
	s_barrier
	s_mov_b64 s[76:77], 0x180
	ds_read_b128 v[168:171], v158 offset:49152
	ds_read_b128 v[172:175], v158 offset:50176
	ds_read_b128 v[176:179], v158 offset:51200
	ds_read_b128 v[180:183], v158 offset:52224
	ds_read_b128 v[184:187], v158 offset:53248
	ds_read_b128 v[188:191], v158 offset:54272
	ds_read_b128 v[192:195], v158 offset:55296
	ds_read_b128 v[196:199], v158 offset:56320
	s_add_u32 s94, s8, 0x180
	s_addc_u32 s95, s9, 0
	v_and_b32_e32 v34, 0xffff, v159
	v_lshl_add_u32 v34, v34, 10, v155
	s_mov_b32 m0, s61
	s_nop 0
	global_load_lds_dwordx4 v34, s[94:95]
	v_lshrrev_b32_e32 v34, 16, v159
	v_lshl_add_u32 v34, v34, 10, v155
	s_mov_b32 m0, s62
	s_nop 0
	global_load_lds_dwordx4 v34, s[94:95]
	s_barrier
	s_waitcnt lgkmcnt(0)
	s_waitcnt lgkmcnt(0)
	v_mfma_scale_f32_16x16x128_f8f6f4 v[64:67], v[138:145], v[168:175], v[64:67], v154, v154 op_sel_hi:[0,0,0]
	v_mfma_scale_f32_16x16x128_f8f6f4 v[60:63], v[160:167], v[168:175], v[60:63], v154, v154 op_sel_hi:[0,0,0]
	v_mfma_scale_f32_16x16x128_f8f6f4 v[56:59], v[138:145], v[176:183], v[56:59], v154, v154 op_sel_hi:[0,0,0]
	v_mfma_scale_f32_16x16x128_f8f6f4 v[52:55], v[160:167], v[176:183], v[52:55], v154, v154 op_sel_hi:[0,0,0]
	v_mfma_scale_f32_16x16x128_f8f6f4 v[48:51], v[138:145], v[184:191], v[48:51], v154, v154 op_sel_hi:[0,0,0]
	v_mfma_scale_f32_16x16x128_f8f6f4 v[44:47], v[160:167], v[184:191], v[44:47], v154, v154 op_sel_hi:[0,0,0]
	v_mfma_scale_f32_16x16x128_f8f6f4 v[40:43], v[138:145], v[192:199], v[40:43], v154, v154 op_sel_hi:[0,0,0]
	v_mfma_scale_f32_16x16x128_f8f6f4 v[36:39], v[160:167], v[192:199], v[36:39], v154, v154 op_sel_hi:[0,0,0]
	s_barrier
	s_add_u32 s2, s20, 0x20180
	s_addc_u32 s3, s21, 0
	s_add_u32 s74, s20, 0x30180
	s_addc_u32 s75, s21, 0
	s_mov_b32 m0, s64
	s_nop 0
	v_lshl_add_u64 v[138:139], s[2:3], 0, v[252:253]
	global_load_lds_dwordx4 v[138:139], off
	v_lshl_add_u64 v[138:139], s[74:75], 0, v[252:253]
	s_mov_b32 m0, s65
	s_nop 0
	global_load_lds_dwordx4 v[138:139], off
	s_waitcnt vmcnt(6)
	s_barrier
	v_mfma_scale_f32_16x16x128_f8f6f4 v[108:111], v[200:207], v[176:183], v[108:111], v154, v154 op_sel_hi:[0,0,0]
	v_mfma_scale_f32_16x16x128_f8f6f4 v[112:115], v[208:215], v[176:183], v[112:115], v154, v154 op_sel_hi:[0,0,0]
	v_mfma_scale_f32_16x16x128_f8f6f4 v[116:119], v[200:207], v[184:191], v[116:119], v154, v154 op_sel_hi:[0,0,0]
	v_mfma_scale_f32_16x16x128_f8f6f4 v[120:123], v[208:215], v[184:191], v[120:123], v154, v154 op_sel_hi:[0,0,0]
	v_mfma_scale_f32_16x16x128_f8f6f4 v[124:127], v[200:207], v[192:199], v[124:127], v154, v154 op_sel_hi:[0,0,0]
	v_mfma_scale_f32_16x16x128_f8f6f4 v[128:131], v[208:215], v[192:199], v[128:131], v154, v154 op_sel_hi:[0,0,0]
	v_mfma_scale_f32_16x16x128_f8f6f4 v[100:103], v[200:207], v[168:175], v[100:103], v154, v154 op_sel_hi:[0,0,0]
	v_mfma_scale_f32_16x16x128_f8f6f4 v[104:107], v[208:215], v[168:175], v[104:107], v154, v154 op_sel_hi:[0,0,0]
	s_barrier
	s_add_u32 s2, s20, 0x200
	s_addc_u32 s3, s21, 0
	ds_read_b128 v[138:141], v132
	ds_read_b128 v[142:145], v132 offset:1024
	ds_read_b128 v[160:163], v132 offset:2048
	ds_read_b128 v[164:167], v132 offset:3072
	ds_read_b128 v[168:171], v158
	ds_read_b128 v[172:175], v158 offset:1024
	ds_read_b128 v[176:179], v158 offset:2048
	ds_read_b128 v[180:183], v158 offset:3072
	ds_read_b128 v[184:187], v158 offset:4096
	ds_read_b128 v[188:191], v158 offset:5120
	ds_read_b128 v[192:195], v158 offset:6144
	ds_read_b128 v[196:199], v158 offset:7168
	s_add_u32 s94, s8, 0x180
	s_addc_u32 s95, s9, 0
	v_and_b32_e32 v34, 0xffff, v255
	v_lshl_add_u32 v34, v34, 10, v155
	s_mov_b32 m0, s23
	s_nop 0
	global_load_lds_dwordx4 v34, s[94:95]
	v_lshrrev_b32_e32 v34, 16, v255
	v_lshl_add_u32 v34, v34, 10, v155
	s_mov_b32 m0, s17
	s_nop 0
	global_load_lds_dwordx4 v34, s[94:95]
	s_waitcnt lgkmcnt(8)
	s_barrier
	s_waitcnt lgkmcnt(0)
	s_waitcnt lgkmcnt(0)
	v_mfma_scale_f32_16x16x128_f8f6f4 v[204:207], v[138:145], v[176:183], v[10:13], v154, v154 op_sel_hi:[0,0,0]
	v_mfma_scale_f32_16x16x128_f8f6f4 v[150:153], v[138:145], v[168:175], v[2:5], v154, v154 op_sel_hi:[0,0,0]
	v_mfma_scale_f32_16x16x128_f8f6f4 v[200:203], v[160:167], v[168:175], v[6:9], v154, v154 op_sel_hi:[0,0,0]
	v_mfma_scale_f32_16x16x128_f8f6f4 v[208:211], v[160:167], v[176:183], v[14:17], v154, v154 op_sel_hi:[0,0,0]
	v_mfma_scale_f32_16x16x128_f8f6f4 v[212:215], v[138:145], v[184:191], v[18:21], v154, v154 op_sel_hi:[0,0,0]
	v_mfma_scale_f32_16x16x128_f8f6f4 v[216:219], v[160:167], v[184:191], v[22:25], v154, v154 op_sel_hi:[0,0,0]
	v_mfma_scale_f32_16x16x128_f8f6f4 v[220:223], v[138:145], v[192:199], v[26:29], v154, v154 op_sel_hi:[0,0,0]
	v_mfma_scale_f32_16x16x128_f8f6f4 v[224:227], v[160:167], v[192:199], v[30:33], v154, v154 op_sel_hi:[0,0,0]
	s_barrier
	s_add_u32 s74, s20, 0x10200
	s_addc_u32 s75, s21, 0
	s_mov_b32 m0, s44
	ds_read_b128 v[2:5], v133
	ds_read_b128 v[6:9], v133 offset:1024
	ds_read_b128 v[10:13], v133 offset:2048
	ds_read_b128 v[14:17], v133 offset:3072
	s_nop 0
	v_lshl_add_u64 v[18:19], s[2:3], 0, v[252:253]
	global_load_lds_dwordx4 v[18:19], off
	v_lshl_add_u64 v[18:19], s[74:75], 0, v[252:253]
	s_mov_b32 m0, s45
	s_nop 0
	global_load_lds_dwordx4 v[18:19], off
	s_barrier
	s_waitcnt lgkmcnt(0)
	s_waitcnt lgkmcnt(0)
	v_mfma_scale_f32_16x16x128_f8f6f4 v[88:91], v[2:9], v[176:183], v[88:91], v154, v154 op_sel_hi:[0,0,0]
	v_mfma_scale_f32_16x16x128_f8f6f4 v[84:87], v[10:17], v[176:183], v[84:87], v154, v154 op_sel_hi:[0,0,0]
	v_mfma_scale_f32_16x16x128_f8f6f4 v[228:231], v[2:9], v[168:175], v[96:99], v154, v154 op_sel_hi:[0,0,0]
	v_mfma_scale_f32_16x16x128_f8f6f4 v[168:171], v[10:17], v[168:175], v[92:95], v154, v154 op_sel_hi:[0,0,0]
	v_mfma_scale_f32_16x16x128_f8f6f4 v[172:175], v[2:9], v[184:191], v[80:83], v154, v154 op_sel_hi:[0,0,0]
	v_mfma_scale_f32_16x16x128_f8f6f4 v[176:179], v[10:17], v[184:191], v[76:79], v154, v154 op_sel_hi:[0,0,0]
	v_mfma_scale_f32_16x16x128_f8f6f4 v[180:183], v[2:9], v[192:199], v[72:75], v154, v154 op_sel_hi:[0,0,0]
	v_mfma_scale_f32_16x16x128_f8f6f4 v[184:187], v[10:17], v[192:199], v[68:71], v154, v154 op_sel_hi:[0,0,0]
	s_barrier
	s_nop 0
	s_mov_b64 s[76:77], 0x200
	ds_read_b128 v[18:21], v158 offset:16384
	ds_read_b128 v[22:25], v158 offset:17408
	ds_read_b128 v[26:29], v158 offset:18432
	ds_read_b128 v[30:33], v158 offset:19456
	ds_read_b128 v[68:71], v158 offset:20480
	ds_read_b128 v[72:75], v158 offset:21504
	ds_read_b128 v[76:79], v158 offset:22528
	ds_read_b128 v[80:83], v158 offset:23552
	s_add_u32 s94, s8, 0x200
	s_addc_u32 s95, s9, 0
	v_and_b32_e32 v34, 0xffff, v159
	v_lshl_add_u32 v34, v34, 10, v155
	s_mov_b32 m0, s47
	s_nop 0
	global_load_lds_dwordx4 v34, s[94:95]
	v_lshrrev_b32_e32 v34, 16, v159
	v_lshl_add_u32 v34, v34, 10, v155
	s_mov_b32 m0, s48
	s_nop 0
	global_load_lds_dwordx4 v34, s[94:95]
	s_barrier
	s_waitcnt lgkmcnt(0)
	s_waitcnt lgkmcnt(0)
	v_mfma_scale_f32_16x16x128_f8f6f4 v[236:239], v[138:145], v[68:75], v[48:51], v154, v154 op_sel_hi:[0,0,0]
	v_mfma_scale_f32_16x16x128_f8f6f4 v[240:243], v[160:167], v[68:75], v[44:47], v154, v154 op_sel_hi:[0,0,0]
	v_mfma_scale_f32_16x16x128_f8f6f4 v[244:247], v[138:145], v[76:83], v[40:43], v154, v154 op_sel_hi:[0,0,0]
	v_mfma_scale_f32_16x16x128_f8f6f4 v[248:251], v[160:167], v[76:83], v[36:39], v154, v154 op_sel_hi:[0,0,0]
	v_mfma_scale_f32_16x16x128_f8f6f4 v[188:191], v[138:145], v[18:25], v[64:67], v154, v154 op_sel_hi:[0,0,0]
	v_mfma_scale_f32_16x16x128_f8f6f4 v[192:195], v[160:167], v[18:25], v[60:63], v154, v154 op_sel_hi:[0,0,0]
	v_mfma_scale_f32_16x16x128_f8f6f4 v[196:199], v[138:145], v[26:33], v[56:59], v154, v154 op_sel_hi:[0,0,0]
	v_mfma_scale_f32_16x16x128_f8f6f4 v[232:235], v[160:167], v[26:33], v[52:55], v154, v154 op_sel_hi:[0,0,0]
	s_barrier
	s_add_u32 s2, s20, 0x20200
	s_addc_u32 s3, s21, 0
	s_add_u32 s74, s20, 0x30200
	s_addc_u32 s75, s21, 0
	s_mov_b32 m0, s50
	s_nop 0
	v_lshl_add_u64 v[36:37], s[2:3], 0, v[252:253]
	global_load_lds_dwordx4 v[36:37], off
	v_lshl_add_u64 v[36:37], s[74:75], 0, v[252:253]
	s_mov_b32 m0, s51
	s_nop 0
	global_load_lds_dwordx4 v[36:37], off
	s_waitcnt vmcnt(6)
	s_barrier
	v_mfma_scale_f32_16x16x128_f8f6f4 v[146:149], v[2:9], v[18:25], v[100:103], v154, v154 op_sel_hi:[0,0,0]
	v_mfma_scale_f32_16x16x128_f8f6f4 v[18:21], v[10:17], v[18:25], v[104:107], v154, v154 op_sel_hi:[0,0,0]
	v_mfma_scale_f32_16x16x128_f8f6f4 v[22:25], v[2:9], v[26:33], v[108:111], v154, v154 op_sel_hi:[0,0,0]
	v_mfma_scale_f32_16x16x128_f8f6f4 v[26:29], v[10:17], v[26:33], v[112:115], v154, v154 op_sel_hi:[0,0,0]
	v_mfma_scale_f32_16x16x128_f8f6f4 v[30:33], v[2:9], v[68:75], v[116:119], v154, v154 op_sel_hi:[0,0,0]
	v_mfma_scale_f32_16x16x128_f8f6f4 v[36:39], v[10:17], v[68:75], v[120:123], v154, v154 op_sel_hi:[0,0,0]
	v_mfma_scale_f32_16x16x128_f8f6f4 v[72:75], v[2:9], v[76:83], v[124:127], v154, v154 op_sel_hi:[0,0,0]
	v_mfma_scale_f32_16x16x128_f8f6f4 v[76:79], v[10:17], v[76:83], v[128:131], v154, v154 op_sel_hi:[0,0,0]
	s_barrier
	ds_read_b128 v[92:95], v135
	ds_read_b128 v[96:99], v135 offset:1024
	ds_read_b128 v[100:103], v135 offset:2048
	ds_read_b128 v[104:107], v135 offset:3072
	ds_read_b128 v[40:43], v158 offset:32768
	ds_read_b128 v[44:47], v158 offset:33792
	ds_read_b128 v[48:51], v158 offset:34816
	ds_read_b128 v[52:55], v158 offset:35840
	ds_read_b128 v[56:59], v158 offset:36864
	ds_read_b128 v[60:63], v158 offset:37888
	ds_read_b128 v[64:67], v158 offset:38912
	ds_read_b128 v[68:71], v158 offset:39936
	s_add_u32 s94, s8, 0x200
	s_addc_u32 s95, s9, 0
	v_and_b32_e32 v34, 0xffff, v255
	v_lshl_add_u32 v34, v34, 10, v155
	s_mov_b32 m0, s52
	s_nop 0
	global_load_lds_dwordx4 v34, s[94:95]
	v_lshrrev_b32_e32 v34, 16, v255
	v_lshl_add_u32 v34, v34, 10, v155
	s_mov_b32 m0, s53
	s_nop 0
	global_load_lds_dwordx4 v34, s[94:95]
	s_waitcnt lgkmcnt(8)
	s_barrier
	s_waitcnt lgkmcnt(0)
	s_waitcnt lgkmcnt(0)
	v_mfma_scale_f32_16x16x128_f8f6f4 v[2:5], v[92:99], v[40:47], v[150:153], v154, v154 op_sel_hi:[0,0,0]
	v_mfma_scale_f32_16x16x128_f8f6f4 v[6:9], v[100:107], v[40:47], v[200:203], v154, v154 op_sel_hi:[0,0,0]
	v_mfma_scale_f32_16x16x128_f8f6f4 v[10:13], v[92:99], v[48:55], v[204:207], v154, v154 op_sel_hi:[0,0,0]
	v_mfma_scale_f32_16x16x128_f8f6f4 v[14:17], v[100:107], v[48:55], v[208:211], v154, v154 op_sel_hi:[0,0,0]
	v_mfma_scale_f32_16x16x128_f8f6f4 v[204:207], v[92:99], v[64:71], v[220:223], v154, v154 op_sel_hi:[0,0,0]
	v_mfma_scale_f32_16x16x128_f8f6f4 v[150:153], v[92:99], v[56:63], v[212:215], v154, v154 op_sel_hi:[0,0,0]
	v_mfma_scale_f32_16x16x128_f8f6f4 v[200:203], v[100:107], v[56:63], v[216:219], v154, v154 op_sel_hi:[0,0,0]
	v_mfma_scale_f32_16x16x128_f8f6f4 v[208:211], v[100:107], v[64:71], v[224:227], v154, v154 op_sel_hi:[0,0,0]
	s_barrier
	s_add_u32 s2, s20, 0x280
	s_addc_u32 s3, s21, 0
	s_add_u32 s74, s20, 0x10280
	s_addc_u32 s75, s21, 0
	s_mov_b32 m0, s59
	ds_read_b128 v[124:127], v136
	ds_read_b128 v[128:131], v136 offset:1024
	ds_read_b128 v[138:141], v136 offset:2048
	ds_read_b128 v[142:145], v136 offset:3072
	s_nop 0
	v_lshl_add_u64 v[80:81], s[2:3], 0, v[252:253]
	global_load_lds_dwordx4 v[80:81], off
	v_lshl_add_u64 v[80:81], s[74:75], 0, v[252:253]
	s_mov_b32 m0, s60
	s_nop 0
	global_load_lds_dwordx4 v[80:81], off
	s_barrier
	s_waitcnt lgkmcnt(0)
	s_waitcnt lgkmcnt(0)
	v_mfma_scale_f32_16x16x128_f8f6f4 v[212:215], v[124:131], v[40:47], v[228:231], v154, v154 op_sel_hi:[0,0,0]
	v_mfma_scale_f32_16x16x128_f8f6f4 v[40:43], v[138:145], v[40:47], v[168:171], v154, v154 op_sel_hi:[0,0,0]
	v_mfma_scale_f32_16x16x128_f8f6f4 v[44:47], v[124:131], v[48:55], v[88:91], v154, v154 op_sel_hi:[0,0,0]
	v_mfma_scale_f32_16x16x128_f8f6f4 v[48:51], v[138:145], v[48:55], v[84:87], v154, v154 op_sel_hi:[0,0,0]
	v_mfma_scale_f32_16x16x128_f8f6f4 v[52:55], v[124:131], v[56:63], v[172:175], v154, v154 op_sel_hi:[0,0,0]
	v_mfma_scale_f32_16x16x128_f8f6f4 v[56:59], v[138:145], v[56:63], v[176:179], v154, v154 op_sel_hi:[0,0,0]
	v_mfma_scale_f32_16x16x128_f8f6f4 v[60:63], v[124:131], v[64:71], v[180:183], v154, v154 op_sel_hi:[0,0,0]
	v_mfma_scale_f32_16x16x128_f8f6f4 v[64:67], v[138:145], v[64:71], v[184:187], v154, v154 op_sel_hi:[0,0,0]
	s_barrier
	s_mov_b64 s[76:77], 0x280
	ds_read_b128 v[108:111], v158 offset:49152
	ds_read_b128 v[112:115], v158 offset:50176
	ds_read_b128 v[116:119], v158 offset:51200
	ds_read_b128 v[120:123], v158 offset:52224
	ds_read_b128 v[160:163], v158 offset:53248
	ds_read_b128 v[164:167], v158 offset:54272
	ds_read_b128 v[168:171], v158 offset:55296
	ds_read_b128 v[172:175], v158 offset:56320
	s_add_u32 s94, s8, 0x280
	s_addc_u32 s95, s9, 0
	v_and_b32_e32 v34, 0xffff, v159
	v_lshl_add_u32 v34, v34, 10, v155
	s_mov_b32 m0, s61
	s_nop 0
	global_load_lds_dwordx4 v34, s[94:95]
	v_lshrrev_b32_e32 v34, 16, v159
	v_lshl_add_u32 v34, v34, 10, v155
	s_mov_b32 m0, s62
	s_nop 0
	global_load_lds_dwordx4 v34, s[94:95]
	s_barrier
	s_waitcnt lgkmcnt(0)
	s_waitcnt lgkmcnt(0)
	v_mfma_scale_f32_16x16x128_f8f6f4 v[68:71], v[92:99], v[108:115], v[188:191], v154, v154 op_sel_hi:[0,0,0]
	v_mfma_scale_f32_16x16x128_f8f6f4 v[220:223], v[92:99], v[116:123], v[196:199], v154, v154 op_sel_hi:[0,0,0]
	v_mfma_scale_f32_16x16x128_f8f6f4 v[80:83], v[100:107], v[116:123], v[232:235], v154, v154 op_sel_hi:[0,0,0]
	v_mfma_scale_f32_16x16x128_f8f6f4 v[84:87], v[92:99], v[160:167], v[236:239], v154, v154 op_sel_hi:[0,0,0]
	v_mfma_scale_f32_16x16x128_f8f6f4 v[88:91], v[100:107], v[160:167], v[240:243], v154, v154 op_sel_hi:[0,0,0]
	v_mfma_scale_f32_16x16x128_f8f6f4 v[92:95], v[92:99], v[168:175], v[244:247], v154, v154 op_sel_hi:[0,0,0]
	v_mfma_scale_f32_16x16x128_f8f6f4 v[96:99], v[100:107], v[168:175], v[248:251], v154, v154 op_sel_hi:[0,0,0]
	v_mfma_scale_f32_16x16x128_f8f6f4 v[216:219], v[100:107], v[108:115], v[192:195], v154, v154 op_sel_hi:[0,0,0]
	s_barrier
	s_add_u32 s2, s20, 0x20280
	s_addc_u32 s3, s21, 0
	s_add_u32 s74, s20, 0x30280
	s_addc_u32 s75, s21, 0
	s_mov_b32 m0, s64
	s_nop 0
	v_lshl_add_u64 v[100:101], s[2:3], 0, v[252:253]
	global_load_lds_dwordx4 v[100:101], off
	v_lshl_add_u64 v[100:101], s[74:75], 0, v[252:253]
	s_mov_b32 m0, s65
	s_nop 0
	global_load_lds_dwordx4 v[100:101], off
	s_waitcnt vmcnt(6)
	s_barrier
	v_mfma_scale_f32_16x16x128_f8f6f4 v[100:103], v[124:131], v[108:115], v[146:149], v154, v154 op_sel_hi:[0,0,0]
	v_mfma_scale_f32_16x16x128_f8f6f4 v[104:107], v[138:145], v[108:115], v[18:21], v154, v154 op_sel_hi:[0,0,0]
	v_mfma_scale_f32_16x16x128_f8f6f4 v[108:111], v[124:131], v[116:123], v[22:25], v154, v154 op_sel_hi:[0,0,0]
	v_mfma_scale_f32_16x16x128_f8f6f4 v[112:115], v[138:145], v[116:123], v[26:29], v154, v154 op_sel_hi:[0,0,0]
	v_mfma_scale_f32_16x16x128_f8f6f4 v[116:119], v[124:131], v[160:167], v[30:33], v154, v154 op_sel_hi:[0,0,0]
	v_mfma_scale_f32_16x16x128_f8f6f4 v[120:123], v[138:145], v[160:167], v[36:39], v154, v154 op_sel_hi:[0,0,0]
	v_mfma_scale_f32_16x16x128_f8f6f4 v[124:127], v[124:131], v[168:175], v[72:75], v154, v154 op_sel_hi:[0,0,0]
	v_mfma_scale_f32_16x16x128_f8f6f4 v[128:131], v[138:145], v[168:175], v[76:79], v154, v154 op_sel_hi:[0,0,0]
	s_barrier
	s_add_u32 s2, s20, 0x300
	s_addc_u32 s3, s21, 0
	ds_read_b128 v[138:141], v132
	ds_read_b128 v[142:145], v132 offset:1024
	ds_read_b128 v[160:163], v132 offset:2048
	ds_read_b128 v[164:167], v132 offset:3072
	ds_read_b128 v[168:171], v158
	ds_read_b128 v[172:175], v158 offset:1024
	ds_read_b128 v[176:179], v158 offset:2048
	ds_read_b128 v[180:183], v158 offset:3072
	ds_read_b128 v[184:187], v158 offset:4096
	ds_read_b128 v[188:191], v158 offset:5120
	ds_read_b128 v[192:195], v158 offset:6144
	ds_read_b128 v[196:199], v158 offset:7168
	s_add_u32 s94, s8, 0x280
	s_addc_u32 s95, s9, 0
	v_and_b32_e32 v34, 0xffff, v255
	v_lshl_add_u32 v34, v34, 10, v155
	s_mov_b32 m0, s23
	s_nop 0
	global_load_lds_dwordx4 v34, s[94:95]
	v_lshrrev_b32_e32 v34, 16, v255
	v_lshl_add_u32 v34, v34, 10, v155
	s_mov_b32 m0, s17
	s_nop 0
	global_load_lds_dwordx4 v34, s[94:95]
	s_waitcnt lgkmcnt(8)
	s_barrier
	s_waitcnt lgkmcnt(0)
	s_waitcnt lgkmcnt(0)
	v_mfma_scale_f32_16x16x128_f8f6f4 v[204:207], v[138:145], v[192:199], v[204:207], v154, v154 op_sel_hi:[0,0,0]
	v_mfma_scale_f32_16x16x128_f8f6f4 v[146:149], v[138:145], v[168:175], v[2:5], v154, v154 op_sel_hi:[0,0,0]
	v_mfma_scale_f32_16x16x128_f8f6f4 v[224:227], v[160:167], v[168:175], v[6:9], v154, v154 op_sel_hi:[0,0,0]
	v_mfma_scale_f32_16x16x128_f8f6f4 v[228:231], v[138:145], v[176:183], v[10:13], v154, v154 op_sel_hi:[0,0,0]
	v_mfma_scale_f32_16x16x128_f8f6f4 v[232:235], v[160:167], v[176:183], v[14:17], v154, v154 op_sel_hi:[0,0,0]
	v_mfma_scale_f32_16x16x128_f8f6f4 v[150:153], v[138:145], v[184:191], v[150:153], v154, v154 op_sel_hi:[0,0,0]
	v_mfma_scale_f32_16x16x128_f8f6f4 v[200:203], v[160:167], v[184:191], v[200:203], v154, v154 op_sel_hi:[0,0,0]
	v_mfma_scale_f32_16x16x128_f8f6f4 v[208:211], v[160:167], v[192:199], v[208:211], v154, v154 op_sel_hi:[0,0,0]
	s_barrier
	s_add_u32 s74, s20, 0x10300
	s_addc_u32 s75, s21, 0
	s_mov_b32 m0, s44
	ds_read_b128 v[2:5], v133
	ds_read_b128 v[6:9], v133 offset:1024
	ds_read_b128 v[10:13], v133 offset:2048
	ds_read_b128 v[14:17], v133 offset:3072
	s_nop 0
	v_lshl_add_u64 v[18:19], s[2:3], 0, v[252:253]
	global_load_lds_dwordx4 v[18:19], off
	v_lshl_add_u64 v[18:19], s[74:75], 0, v[252:253]
	s_mov_b32 m0, s45
	s_nop 0
	global_load_lds_dwordx4 v[18:19], off
	s_barrier
	s_waitcnt lgkmcnt(0)
	s_waitcnt lgkmcnt(0)
	v_mfma_scale_f32_16x16x128_f8f6f4 v[64:67], v[10:17], v[192:199], v[64:67], v154, v154 op_sel_hi:[0,0,0]
	v_mfma_scale_f32_16x16x128_f8f6f4 v[212:215], v[2:9], v[168:175], v[212:215], v154, v154 op_sel_hi:[0,0,0]
	v_mfma_scale_f32_16x16x128_f8f6f4 v[168:171], v[10:17], v[168:175], v[40:43], v154, v154 op_sel_hi:[0,0,0]
	v_mfma_scale_f32_16x16x128_f8f6f4 v[172:175], v[2:9], v[176:183], v[44:47], v154, v154 op_sel_hi:[0,0,0]
	v_mfma_scale_f32_16x16x128_f8f6f4 v[176:179], v[10:17], v[176:183], v[48:51], v154, v154 op_sel_hi:[0,0,0]
	v_mfma_scale_f32_16x16x128_f8f6f4 v[180:183], v[2:9], v[184:191], v[52:55], v154, v154 op_sel_hi:[0,0,0]
	v_mfma_scale_f32_16x16x128_f8f6f4 v[184:187], v[10:17], v[184:191], v[56:59], v154, v154 op_sel_hi:[0,0,0]
	v_mfma_scale_f32_16x16x128_f8f6f4 v[188:191], v[2:9], v[192:199], v[60:63], v154, v154 op_sel_hi:[0,0,0]
	s_barrier
	s_nop 2
	s_mov_b64 s[76:77], 0x300
	ds_read_b128 v[18:21], v158 offset:16384
	ds_read_b128 v[22:25], v158 offset:17408
	ds_read_b128 v[26:29], v158 offset:18432
	ds_read_b128 v[30:33], v158 offset:19456
	ds_read_b128 v[36:39], v158 offset:20480
	ds_read_b128 v[40:43], v158 offset:21504
	ds_read_b128 v[44:47], v158 offset:22528
	ds_read_b128 v[48:51], v158 offset:23552
	s_add_u32 s94, s8, 0x300
	s_addc_u32 s95, s9, 0
	v_and_b32_e32 v34, 0xffff, v159
	v_lshl_add_u32 v34, v34, 10, v155
	s_mov_b32 m0, s47
	s_nop 0
	global_load_lds_dwordx4 v34, s[94:95]
	v_lshrrev_b32_e32 v34, 16, v159
	v_lshl_add_u32 v34, v34, 10, v155
	s_mov_b32 m0, s48
	s_nop 0
	global_load_lds_dwordx4 v34, s[94:95]
	s_barrier
	s_waitcnt lgkmcnt(0)
	s_waitcnt lgkmcnt(0)
	v_mfma_scale_f32_16x16x128_f8f6f4 v[236:239], v[138:145], v[36:43], v[84:87], v154, v154 op_sel_hi:[0,0,0]
	v_mfma_scale_f32_16x16x128_f8f6f4 v[240:243], v[160:167], v[36:43], v[88:91], v154, v154 op_sel_hi:[0,0,0]
	v_mfma_scale_f32_16x16x128_f8f6f4 v[192:195], v[138:145], v[18:25], v[68:71], v154, v154 op_sel_hi:[0,0,0]
	v_mfma_scale_f32_16x16x128_f8f6f4 v[196:199], v[160:167], v[18:25], v[216:219], v154, v154 op_sel_hi:[0,0,0]
	v_mfma_scale_f32_16x16x128_f8f6f4 v[216:219], v[138:145], v[26:33], v[220:223], v154, v154 op_sel_hi:[0,0,0]
	v_mfma_scale_f32_16x16x128_f8f6f4 v[220:223], v[160:167], v[26:33], v[80:83], v154, v154 op_sel_hi:[0,0,0]
	v_mfma_scale_f32_16x16x128_f8f6f4 v[138:141], v[138:145], v[44:51], v[92:95], v154, v154 op_sel_hi:[0,0,0]
	v_mfma_scale_f32_16x16x128_f8f6f4 v[142:145], v[160:167], v[44:51], v[96:99], v154, v154 op_sel_hi:[0,0,0]
	s_barrier
	s_add_u32 s2, s20, 0x20300
	s_addc_u32 s3, s21, 0
	s_add_u32 s74, s20, 0x30300
	s_addc_u32 s75, s21, 0
	s_mov_b32 m0, s50
	s_nop 0
	v_lshl_add_u64 v[52:53], s[2:3], 0, v[252:253]
	global_load_lds_dwordx4 v[52:53], off
	v_lshl_add_u64 v[52:53], s[74:75], 0, v[252:253]
	s_mov_b32 m0, s51
	s_nop 0
	global_load_lds_dwordx4 v[52:53], off
	s_waitcnt vmcnt(6)
	s_barrier
	v_mfma_scale_f32_16x16x128_f8f6f4 v[160:163], v[2:9], v[18:25], v[100:103], v154, v154 op_sel_hi:[0,0,0]
	v_mfma_scale_f32_16x16x128_f8f6f4 v[164:167], v[10:17], v[18:25], v[104:107], v154, v154 op_sel_hi:[0,0,0]
	v_mfma_scale_f32_16x16x128_f8f6f4 v[244:247], v[2:9], v[26:33], v[108:111], v154, v154 op_sel_hi:[0,0,0]
	v_mfma_scale_f32_16x16x128_f8f6f4 v[248:251], v[10:17], v[26:33], v[112:115], v154, v154 op_sel_hi:[0,0,0]
	v_mfma_scale_f32_16x16x128_f8f6f4 v[18:21], v[2:9], v[36:43], v[116:119], v154, v154 op_sel_hi:[0,0,0]
	v_mfma_scale_f32_16x16x128_f8f6f4 v[22:25], v[10:17], v[36:43], v[120:123], v154, v154 op_sel_hi:[0,0,0]
	v_mfma_scale_f32_16x16x128_f8f6f4 v[6:9], v[2:9], v[44:51], v[124:127], v154, v154 op_sel_hi:[0,0,0]
	v_mfma_scale_f32_16x16x128_f8f6f4 v[10:13], v[10:17], v[44:51], v[128:131], v154, v154 op_sel_hi:[0,0,0]
	s_barrier
	ds_read_b128 v[68:71], v135
	ds_read_b128 v[72:75], v135 offset:1024
	ds_read_b128 v[76:79], v135 offset:2048
	ds_read_b128 v[80:83], v135 offset:3072
	ds_read_b128 v[40:43], v158 offset:32768
	ds_read_b128 v[44:47], v158 offset:33792
	ds_read_b128 v[48:51], v158 offset:34816
	ds_read_b128 v[52:55], v158 offset:35840
	ds_read_b128 v[56:59], v158 offset:36864
	ds_read_b128 v[60:63], v158 offset:37888
	ds_read_b128 v[84:87], v158 offset:38912
	ds_read_b128 v[88:91], v158 offset:39936
	s_add_u32 s94, s8, 0x300
	s_addc_u32 s95, s9, 0
	v_and_b32_e32 v34, 0xffff, v255
	v_lshl_add_u32 v34, v34, 10, v155
	s_mov_b32 m0, s52
	s_nop 0
	global_load_lds_dwordx4 v34, s[94:95]
	v_lshrrev_b32_e32 v34, 16, v255
	v_lshl_add_u32 v34, v34, 10, v155
	s_mov_b32 m0, s53
	s_nop 0
	global_load_lds_dwordx4 v34, s[94:95]
	s_waitcnt lgkmcnt(8)
	s_barrier
	s_waitcnt lgkmcnt(0)
	s_waitcnt lgkmcnt(0)
	v_mfma_scale_f32_16x16x128_f8f6f4 v[2:5], v[68:75], v[40:47], v[146:149], v154, v154 op_sel_hi:[0,0,0]
	v_mfma_scale_f32_16x16x128_f8f6f4 v[14:17], v[76:83], v[48:55], v[232:235], v154, v154 op_sel_hi:[0,0,0]
	v_mfma_scale_f32_16x16x128_f8f6f4 v[26:29], v[68:75], v[84:91], v[204:207], v154, v154 op_sel_hi:[0,0,0]
	v_mfma_scale_f32_16x16x128_f8f6f4 v[30:33], v[76:83], v[84:91], v[208:211], v154, v154 op_sel_hi:[0,0,0]
	v_mfma_scale_f32_16x16x128_f8f6f4 v[224:227], v[76:83], v[40:47], v[224:227], v154, v154 op_sel_hi:[0,0,0]
	v_mfma_scale_f32_16x16x128_f8f6f4 v[228:231], v[68:75], v[48:55], v[228:231], v154, v154 op_sel_hi:[0,0,0]
	v_mfma_scale_f32_16x16x128_f8f6f4 v[146:149], v[68:75], v[56:63], v[150:153], v154, v154 op_sel_hi:[0,0,0]
	v_mfma_scale_f32_16x16x128_f8f6f4 v[150:153], v[76:83], v[56:63], v[200:203], v154, v154 op_sel_hi:[0,0,0]
	s_barrier
	s_add_u32 s2, s20, 0x380
	s_addc_u32 s3, s21, 0
	s_add_u32 s74, s20, 0x10380
	s_addc_u32 s75, s21, 0
	s_mov_b32 m0, s59
	ds_read_b128 v[92:95], v136
	ds_read_b128 v[96:99], v136 offset:1024
	ds_read_b128 v[100:103], v136 offset:2048
	ds_read_b128 v[104:107], v136 offset:3072
	s_nop 0
	v_lshl_add_u64 v[36:37], s[2:3], 0, v[252:253]
	global_load_lds_dwordx4 v[36:37], off
	v_lshl_add_u64 v[36:37], s[74:75], 0, v[252:253]
	s_mov_b32 m0, s60
	s_nop 0
	global_load_lds_dwordx4 v[36:37], off
	s_barrier
	s_waitcnt lgkmcnt(0)
	s_waitcnt lgkmcnt(0)
	v_mfma_scale_f32_16x16x128_f8f6f4 v[36:39], v[92:99], v[40:47], v[212:215], v154, v154 op_sel_hi:[0,0,0]
	v_mfma_scale_f32_16x16x128_f8f6f4 v[40:43], v[100:107], v[40:47], v[168:171], v154, v154 op_sel_hi:[0,0,0]
	v_mfma_scale_f32_16x16x128_f8f6f4 v[44:47], v[92:99], v[48:55], v[172:175], v154, v154 op_sel_hi:[0,0,0]
	v_mfma_scale_f32_16x16x128_f8f6f4 v[48:51], v[100:107], v[48:55], v[176:179], v154, v154 op_sel_hi:[0,0,0]
	v_mfma_scale_f32_16x16x128_f8f6f4 v[52:55], v[92:99], v[56:63], v[180:183], v154, v154 op_sel_hi:[0,0,0]
	v_mfma_scale_f32_16x16x128_f8f6f4 v[56:59], v[100:107], v[56:63], v[184:187], v154, v154 op_sel_hi:[0,0,0]
	v_mfma_scale_f32_16x16x128_f8f6f4 v[60:63], v[92:99], v[84:91], v[188:191], v154, v154 op_sel_hi:[0,0,0]
	v_mfma_scale_f32_16x16x128_f8f6f4 v[64:67], v[100:107], v[84:91], v[64:67], v154, v154 op_sel_hi:[0,0,0]
	s_barrier
	s_mov_b64 s[76:77], 0x380
	ds_read_b128 v[84:87], v158 offset:49152
	ds_read_b128 v[88:91], v158 offset:50176
	ds_read_b128 v[108:111], v158 offset:51200
	ds_read_b128 v[112:115], v158 offset:52224
	ds_read_b128 v[116:119], v158 offset:53248
	ds_read_b128 v[120:123], v158 offset:54272
	ds_read_b128 v[124:127], v158 offset:55296
	ds_read_b128 v[128:131], v158 offset:56320
	s_add_u32 s94, s8, 0x380
	s_addc_u32 s95, s9, 0
	v_and_b32_e32 v34, 0xffff, v159
	v_lshl_add_u32 v34, v34, 10, v155
	s_mov_b32 m0, s61
	s_nop 0
	global_load_lds_dwordx4 v34, s[94:95]
	v_lshrrev_b32_e32 v34, 16, v159
	v_lshl_add_u32 v34, v34, 10, v155
	s_mov_b32 m0, s62
	s_nop 0
	global_load_lds_dwordx4 v34, s[94:95]
	s_barrier
	s_waitcnt lgkmcnt(0)
	s_waitcnt lgkmcnt(0)
	v_mfma_scale_f32_16x16x128_f8f6f4 v[168:171], v[68:75], v[84:91], v[192:195], v154, v154 op_sel_hi:[0,0,0]
	v_mfma_scale_f32_16x16x128_f8f6f4 v[172:175], v[76:83], v[84:91], v[196:199], v154, v154 op_sel_hi:[0,0,0]
	v_mfma_scale_f32_16x16x128_f8f6f4 v[176:179], v[68:75], v[108:115], v[216:219], v154, v154 op_sel_hi:[0,0,0]
	v_mfma_scale_f32_16x16x128_f8f6f4 v[180:183], v[76:83], v[108:115], v[220:223], v154, v154 op_sel_hi:[0,0,0]
	v_mfma_scale_f32_16x16x128_f8f6f4 v[184:187], v[68:75], v[116:123], v[236:239], v154, v154 op_sel_hi:[0,0,0]
	v_mfma_scale_f32_16x16x128_f8f6f4 v[188:191], v[76:83], v[116:123], v[240:243], v154, v154 op_sel_hi:[0,0,0]
	v_mfma_scale_f32_16x16x128_f8f6f4 v[138:141], v[68:75], v[124:131], v[138:141], v154, v154 op_sel_hi:[0,0,0]
	v_mfma_scale_f32_16x16x128_f8f6f4 v[142:145], v[76:83], v[124:131], v[142:145], v154, v154 op_sel_hi:[0,0,0]
	s_barrier
; template <class Epi, class Src>
; __device__ __forceinline__ void gemm_phase(LAS unsigned char* lds, const Src S, const Epi E) {
;     ...
;         {
;             const int par2 = has_next ? (par ^ 1) : par;
;             const char* b3 = nB + kstep;
;             G8_ITER(cA, par, (size_t)(NKTR - 1) * kstep, nA, par2, (size_t)0, nB, b3);
;         }
	s_add_u32 s2, s20, 0x20380
	s_addc_u32 s3, s21, 0
	s_add_u32 s74, s20, 0x30380
	s_addc_u32 s75, s21, 0
	s_mov_b32 m0, s64
	s_nop 0
	v_lshl_add_u64 v[68:69], s[2:3], 0, v[252:253]
	global_load_lds_dwordx4 v[68:69], off
	v_lshl_add_u64 v[68:69], s[74:75], 0, v[252:253]
	s_mov_b32 m0, s65
	s_nop 0
	global_load_lds_dwordx4 v[68:69], off
	s_waitcnt vmcnt(6)
	s_barrier
	v_mfma_scale_f32_16x16x128_f8f6f4 v[200:203], v[92:99], v[116:123], v[18:21], v154, v154 op_sel_hi:[0,0,0]
	v_mfma_scale_f32_16x16x128_f8f6f4 v[116:119], v[100:107], v[116:123], v[22:25], v154, v154 op_sel_hi:[0,0,0]
	v_mfma_scale_f32_16x16x128_f8f6f4 v[120:123], v[92:99], v[124:131], v[6:9], v154, v154 op_sel_hi:[0,0,0]
	v_mfma_scale_f32_16x16x128_f8f6f4 v[124:127], v[100:107], v[124:131], v[10:13], v154, v154 op_sel_hi:[0,0,0]
	v_mfma_scale_f32_16x16x128_f8f6f4 v[160:163], v[92:99], v[84:91], v[160:163], v154, v154 op_sel_hi:[0,0,0]
	v_mfma_scale_f32_16x16x128_f8f6f4 v[164:167], v[100:107], v[84:91], v[164:167], v154, v154 op_sel_hi:[0,0,0]
	v_mfma_scale_f32_16x16x128_f8f6f4 v[192:195], v[92:99], v[108:115], v[244:247], v154, v154 op_sel_hi:[0,0,0]
	v_mfma_scale_f32_16x16x128_f8f6f4 v[196:199], v[100:107], v[108:115], v[248:251], v154, v154 op_sel_hi:[0,0,0]
	s_barrier
	s_xor_b32 s3, s68, 1
	s_and_b64 s[74:75], s[24:25], exec
	s_cselect_b32 s2, s3, s68
	ds_read_b128 v[68:71], v132
	ds_read_b128 v[72:75], v132 offset:1024
	ds_read_b128 v[76:79], v132 offset:2048
	ds_read_b128 v[80:83], v132 offset:3072
	ds_read_b128 v[84:87], v158
	ds_read_b128 v[88:91], v158 offset:1024
	ds_read_b128 v[92:95], v158 offset:2048
	ds_read_b128 v[96:99], v158 offset:3072
	ds_read_b128 v[100:103], v158 offset:4096
	ds_read_b128 v[104:107], v158 offset:5120
	ds_read_b128 v[108:111], v158 offset:6144
	ds_read_b128 v[112:115], v158 offset:7168
	s_add_u32 s94, s8, 0x380
	s_addc_u32 s95, s9, 0
	v_and_b32_e32 v34, 0xffff, v255
	v_lshl_add_u32 v34, v34, 10, v155
	s_mov_b32 m0, s23
	s_nop 0
	global_load_lds_dwordx4 v34, s[94:95]
	v_lshrrev_b32_e32 v34, 16, v255
	v_lshl_add_u32 v34, v34, 10, v155
	s_mov_b32 m0, s17
	s_nop 0
	global_load_lds_dwordx4 v34, s[94:95]
	s_waitcnt lgkmcnt(8)
	s_barrier
	s_waitcnt lgkmcnt(0)
	s_waitcnt lgkmcnt(0)
	v_mfma_scale_f32_16x16x128_f8f6f4 v[128:131], v[68:75], v[84:91], v[2:5], v154, v154 op_sel_hi:[0,0,0]
	v_mfma_scale_f32_16x16x128_f8f6f4 v[204:207], v[76:83], v[84:91], v[224:227], v154, v154 op_sel_hi:[0,0,0]
	v_mfma_scale_f32_16x16x128_f8f6f4 v[208:211], v[68:75], v[92:99], v[228:231], v154, v154 op_sel_hi:[0,0,0]
	v_mfma_scale_f32_16x16x128_f8f6f4 v[212:215], v[76:83], v[92:99], v[14:17], v154, v154 op_sel_hi:[0,0,0]
	v_mfma_scale_f32_16x16x128_f8f6f4 v[146:149], v[68:75], v[100:107], v[146:149], v154, v154 op_sel_hi:[0,0,0]
	v_mfma_scale_f32_16x16x128_f8f6f4 v[150:153], v[76:83], v[100:107], v[150:153], v154, v154 op_sel_hi:[0,0,0]
	v_mfma_scale_f32_16x16x128_f8f6f4 v[216:219], v[68:75], v[108:115], v[26:29], v154, v154 op_sel_hi:[0,0,0]
	v_mfma_scale_f32_16x16x128_f8f6f4 v[220:223], v[76:83], v[108:115], v[30:33], v154, v154 op_sel_hi:[0,0,0]
	s_barrier
	s_add_u32 s74, s0, 0x10000
	s_addc_u32 s75, s1, 0
	s_mov_b64 s[76:77], s[0:1]
	s_mov_b32 m0, s44
	ds_read_b128 v[2:5], v133
	ds_read_b128 v[6:9], v133 offset:1024
	ds_read_b128 v[10:13], v133 offset:2048
	ds_read_b128 v[14:17], v133 offset:3072
	s_nop 0
	v_lshl_add_u64 v[18:19], s[76:77], 0, v[252:253]
	global_load_lds_dwordx4 v[18:19], off
	v_lshl_add_u64 v[18:19], s[74:75], 0, v[252:253]
	s_mov_b32 m0, s45
	s_nop 0
	global_load_lds_dwordx4 v[18:19], off
	s_barrier
	s_waitcnt lgkmcnt(0)
	s_waitcnt lgkmcnt(0)
	v_mfma_scale_f32_16x16x128_f8f6f4 v[224:227], v[2:9], v[84:91], v[36:39], v154, v154 op_sel_hi:[0,0,0]
	v_mfma_scale_f32_16x16x128_f8f6f4 v[84:87], v[10:17], v[84:91], v[40:43], v154, v154 op_sel_hi:[0,0,0]
	v_mfma_scale_f32_16x16x128_f8f6f4 v[88:91], v[2:9], v[92:99], v[44:47], v154, v154 op_sel_hi:[0,0,0]
	v_mfma_scale_f32_16x16x128_f8f6f4 v[52:55], v[2:9], v[100:107], v[52:55], v154, v154 op_sel_hi:[0,0,0]
	v_mfma_scale_f32_16x16x128_f8f6f4 v[56:59], v[10:17], v[100:107], v[56:59], v154, v154 op_sel_hi:[0,0,0]
	v_mfma_scale_f32_16x16x128_f8f6f4 v[60:63], v[2:9], v[108:115], v[60:63], v154, v154 op_sel_hi:[0,0,0]
	v_mfma_scale_f32_16x16x128_f8f6f4 v[64:67], v[10:17], v[108:115], v[64:67], v154, v154 op_sel_hi:[0,0,0]
	v_mfma_scale_f32_16x16x128_f8f6f4 v[228:231], v[10:17], v[92:99], v[48:51], v154, v154 op_sel_hi:[0,0,0]
	v_lshl_add_u32 v34, s2, 10, v156
	s_barrier
	ds_read2st64_b32 v[92:93], v34 offset1:1
	ds_read_b128 v[18:21], v158 offset:16384
	ds_read_b128 v[22:25], v158 offset:17408
	ds_read_b128 v[26:29], v158 offset:18432
	ds_read_b128 v[30:33], v158 offset:19456
	ds_read_b128 v[36:39], v158 offset:20480
	ds_read_b128 v[40:43], v158 offset:21504
	ds_read_b128 v[44:47], v158 offset:22528
	ds_read_b128 v[48:51], v158 offset:23552
	s_mov_b32 m0, s47
	s_waitcnt lgkmcnt(8)
	v_lshl_or_b32 v159, v93, 16, v92
	v_lshl_add_u32 v92, v92, 10, v155
	global_load_lds_dwordx4 v92, s[8:9]
	v_lshl_add_u32 v92, v93, 10, v155
	s_mov_b32 m0, s48
	s_nop 0
	global_load_lds_dwordx4 v92, s[8:9]
	s_barrier
	s_waitcnt lgkmcnt(0)
	s_waitcnt lgkmcnt(0)
	v_mfma_scale_f32_16x16x128_f8f6f4 v[236:239], v[76:83], v[18:25], v[172:175], v154, v154 op_sel_hi:[0,0,0]
	v_mfma_scale_f32_16x16x128_f8f6f4 v[240:243], v[68:75], v[26:33], v[176:179], v154, v154 op_sel_hi:[0,0,0]
	v_mfma_scale_f32_16x16x128_f8f6f4 v[244:247], v[76:83], v[26:33], v[180:183], v154, v154 op_sel_hi:[0,0,0]
	v_mfma_scale_f32_16x16x128_f8f6f4 v[248:251], v[68:75], v[36:43], v[184:187], v154, v154 op_sel_hi:[0,0,0]
	v_mfma_scale_f32_16x16x128_f8f6f4 v[92:95], v[76:83], v[36:43], v[188:191], v154, v154 op_sel_hi:[0,0,0]
	v_mfma_scale_f32_16x16x128_f8f6f4 v[232:235], v[68:75], v[18:25], v[168:171], v154, v154 op_sel_hi:[0,0,0]
	v_mfma_scale_f32_16x16x128_f8f6f4 v[72:75], v[68:75], v[44:51], v[138:141], v154, v154 op_sel_hi:[0,0,0]
	v_mfma_scale_f32_16x16x128_f8f6f4 v[76:79], v[76:83], v[44:51], v[142:145], v154, v154 op_sel_hi:[0,0,0]
	s_barrier
	s_add_u32 s74, s0, 0x20000
	s_addc_u32 s75, s1, 0
	s_add_u32 s76, s0, 0x30000
	s_addc_u32 s77, s1, 0
	s_mov_b32 m0, s50
	s_nop 0
	v_lshl_add_u64 v[68:69], s[74:75], 0, v[252:253]
	global_load_lds_dwordx4 v[68:69], off
	v_lshl_add_u64 v[68:69], s[76:77], 0, v[252:253]
	s_mov_b32 m0, s51
	s_nop 0
	global_load_lds_dwordx4 v[68:69], off
	s_waitcnt vmcnt(6)
	s_barrier
	v_mfma_scale_f32_16x16x128_f8f6f4 v[80:83], v[2:9], v[18:25], v[160:163], v154, v154 op_sel_hi:[0,0,0]
	v_mfma_scale_f32_16x16x128_f8f6f4 v[96:99], v[10:17], v[36:43], v[116:119], v154, v154 op_sel_hi:[0,0,0]
	v_mfma_scale_f32_16x16x128_f8f6f4 v[68:71], v[10:17], v[18:25], v[164:167], v154, v154 op_sel_hi:[0,0,0]
	v_mfma_scale_f32_16x16x128_f8f6f4 v[192:195], v[2:9], v[26:33], v[192:195], v154, v154 op_sel_hi:[0,0,0]
	v_mfma_scale_f32_16x16x128_f8f6f4 v[196:199], v[10:17], v[26:33], v[196:199], v154, v154 op_sel_hi:[0,0,0]
	v_mfma_scale_f32_16x16x128_f8f6f4 v[200:203], v[2:9], v[36:43], v[200:203], v154, v154 op_sel_hi:[0,0,0]
	v_mfma_scale_f32_16x16x128_f8f6f4 v[100:103], v[2:9], v[44:51], v[120:123], v154, v154 op_sel_hi:[0,0,0]
	v_mfma_scale_f32_16x16x128_f8f6f4 v[104:107], v[10:17], v[44:51], v[124:127], v154, v154 op_sel_hi:[0,0,0]
	s_barrier
	ds_read2st64_b32 v[108:109], v34 offset0:2 offset1:3
	ds_read_b128 v[2:5], v135
	ds_read_b128 v[6:9], v135 offset:1024
	ds_read_b128 v[10:13], v135 offset:2048
	ds_read_b128 v[14:17], v135 offset:3072
	ds_read_b128 v[18:21], v158 offset:32768
	ds_read_b128 v[22:25], v158 offset:33792
	ds_read_b128 v[26:29], v158 offset:34816
	ds_read_b128 v[30:33], v158 offset:35840
	ds_read_b128 v[36:39], v158 offset:36864
	ds_read_b128 v[40:43], v158 offset:37888
	ds_read_b128 v[44:47], v158 offset:38912
	ds_read_b128 v[48:51], v158 offset:39936
	s_mov_b32 m0, s52
	s_waitcnt lgkmcnt(12)
	v_lshl_or_b32 v255, v109, 16, v108
	v_lshl_add_u32 v108, v108, 10, v155
	global_load_lds_dwordx4 v108, s[8:9]
	v_lshl_add_u32 v108, v109, 10, v155
	s_mov_b32 m0, s53
	s_nop 0
	global_load_lds_dwordx4 v108, s[8:9]
	s_waitcnt lgkmcnt(8)
	s_barrier
	s_waitcnt lgkmcnt(0)
	s_waitcnt lgkmcnt(0)
	v_mfma_scale_f32_16x16x128_f8f6f4 v[128:131], v[2:9], v[18:25], v[128:131], v154, v154 op_sel_hi:[0,0,0]
	v_mfma_scale_f32_16x16x128_f8f6f4 v[124:127], v[10:17], v[18:25], v[204:207], v154, v154 op_sel_hi:[0,0,0]
	v_mfma_scale_f32_16x16x128_f8f6f4 v[120:123], v[2:9], v[26:33], v[208:211], v154, v154 op_sel_hi:[0,0,0]
	v_mfma_scale_f32_16x16x128_f8f6f4 v[116:119], v[10:17], v[26:33], v[212:215], v154, v154 op_sel_hi:[0,0,0]
	v_mfma_scale_f32_16x16x128_f8f6f4 v[112:115], v[2:9], v[36:43], v[146:149], v154, v154 op_sel_hi:[0,0,0]
	v_mfma_scale_f32_16x16x128_f8f6f4 v[108:111], v[10:17], v[36:43], v[150:153], v154, v154 op_sel_hi:[0,0,0]
	v_mfma_scale_f32_16x16x128_f8f6f4 v[204:207], v[2:9], v[44:51], v[216:219], v154, v154 op_sel_hi:[0,0,0]
	v_mfma_scale_f32_16x16x128_f8f6f4 v[208:211], v[10:17], v[44:51], v[220:223], v154, v154 op_sel_hi:[0,0,0]
	s_barrier
	s_add_u32 s74, s0, 0x80
	s_addc_u32 s75, s1, 0
	s_add_u32 s76, s0, 0x10080
	s_addc_u32 s77, s1, 0
	s_mov_b32 m0, s59
	ds_read_b128 v[138:141], v136
	ds_read_b128 v[142:145], v136 offset:1024
	ds_read_b128 v[160:163], v136 offset:2048
	ds_read_b128 v[164:167], v136 offset:3072
	s_nop 0
	v_lshl_add_u64 v[132:133], s[74:75], 0, v[252:253]
	global_load_lds_dwordx4 v[132:133], off
	v_lshl_add_u64 v[132:133], s[76:77], 0, v[252:253]
	s_mov_b32 m0, s60
	s_nop 0
	global_load_lds_dwordx4 v[132:133], off
	s_barrier
	s_waitcnt lgkmcnt(0)
	s_waitcnt lgkmcnt(0)
	v_mfma_scale_f32_16x16x128_f8f6f4 v[84:87], v[160:167], v[18:25], v[84:87], v154, v154 op_sel_hi:[0,0,0]
	v_mfma_scale_f32_16x16x128_f8f6f4 v[88:91], v[138:145], v[26:33], v[88:91], v154, v154 op_sel_hi:[0,0,0]
	v_mfma_scale_f32_16x16x128_f8f6f4 v[26:29], v[160:167], v[26:33], v[228:231], v154, v154 op_sel_hi:[0,0,0]
	v_mfma_scale_f32_16x16x128_f8f6f4 v[52:55], v[138:145], v[36:43], v[52:55], v154, v154 op_sel_hi:[0,0,0]
	v_mfma_scale_f32_16x16x128_f8f6f4 v[36:39], v[160:167], v[36:43], v[56:59], v154, v154 op_sel_hi:[0,0,0]
	v_mfma_scale_f32_16x16x128_f8f6f4 v[30:33], v[138:145], v[44:51], v[60:63], v154, v154 op_sel_hi:[0,0,0]
	v_mfma_scale_f32_16x16x128_f8f6f4 v[40:43], v[160:167], v[44:51], v[64:67], v154, v154 op_sel_hi:[0,0,0]
	v_mfma_scale_f32_16x16x128_f8f6f4 v[132:135], v[138:145], v[18:25], v[224:227], v154, v154 op_sel_hi:[0,0,0]
	s_barrier
	ds_read_b128 v[18:21], v158 offset:49152
	ds_read_b128 v[22:25], v158 offset:50176
	ds_read_b128 v[168:171], v158 offset:51200
	ds_read_b128 v[172:175], v158 offset:52224
	ds_read_b128 v[176:179], v158 offset:53248
	ds_read_b128 v[180:183], v158 offset:54272
	ds_read_b128 v[184:187], v158 offset:55296
	ds_read_b128 v[188:191], v158 offset:56320
	s_add_u32 s94, s8, 0x80
	s_addc_u32 s95, s9, 0
	v_and_b32_e32 v34, 0xffff, v159
	v_lshl_add_u32 v34, v34, 10, v155
	s_mov_b32 m0, s61
	s_nop 0
	global_load_lds_dwordx4 v34, s[94:95]
	v_lshrrev_b32_e32 v34, 16, v159
	v_lshl_add_u32 v34, v34, 10, v155
	s_mov_b32 m0, s62
	s_nop 0
	global_load_lds_dwordx4 v34, s[94:95]
	s_barrier
	s_waitcnt lgkmcnt(0)
	s_waitcnt lgkmcnt(0)
	v_mfma_scale_f32_16x16x128_f8f6f4 v[64:67], v[2:9], v[18:25], v[232:235], v154, v154 op_sel_hi:[0,0,0]
	v_mfma_scale_f32_16x16x128_f8f6f4 v[60:63], v[10:17], v[18:25], v[236:239], v154, v154 op_sel_hi:[0,0,0]
	v_mfma_scale_f32_16x16x128_f8f6f4 v[56:59], v[2:9], v[168:175], v[240:243], v154, v154 op_sel_hi:[0,0,0]
	v_mfma_scale_f32_16x16x128_f8f6f4 v[236:239], v[10:17], v[168:175], v[244:247], v154, v154 op_sel_hi:[0,0,0]
	v_mfma_scale_f32_16x16x128_f8f6f4 v[48:51], v[2:9], v[176:183], v[248:251], v154, v154 op_sel_hi:[0,0,0]
	v_mfma_scale_f32_16x16x128_f8f6f4 v[44:47], v[10:17], v[176:183], v[92:95], v154, v154 op_sel_hi:[0,0,0]
	v_mfma_scale_f32_16x16x128_f8f6f4 v[6:9], v[2:9], v[184:191], v[72:75], v154, v154 op_sel_hi:[0,0,0]
	v_mfma_scale_f32_16x16x128_f8f6f4 v[244:247], v[10:17], v[184:191], v[76:79], v154, v154 op_sel_hi:[0,0,0]
	s_barrier
; #define LAS __attribute__((address_space(3)))
; #define lds lds_hidden(lds0)
;     __device__ __forceinline__ void operator()(const f32x4 (&acc)[2][2][4][2], const Unit& u, int wr, int wc, int fr, int fq, LAS unsigned char* lds, int par) const {
;         LAS const float* tb = (LAS const float*)(lds + EPI_OFF + par * 2048);
;         const int colu = wc * 32 + 8 * fq, col = u.pn * 128 + colu;
;         const f32x4 bg0 = *(LAS const f32x4*)(tb + colu), bg1 = *(LAS const f32x4*)(tb + colu + 4), bl0 = *(LAS const f32x4*)(tb + 128 + colu), bl1 = *(LAS const f32x4*)(tb + 128 + colu + 4);
;         const float sc = kf(1.f / (W8_SCALE * H28_SCALE * MX_SCALE)), lim = kf(7.f), ke = kf(-1.702f * 1.4426950408889634f), one = kf(1.f), as = kf(ACT8_SCALE);
;         const f32x2_t sc2 = (f32x2_t){sc, sc}, ke2 = (f32x2_t){ke, ke}, one2 = (f32x2_t){one, one}, as2 = (f32x2_t){as, as};
; #pragma unroll
;         for (int ai = 0; ai < 2; ++ai)
; #pragma unroll
;             for (int m = 0; m < 4; ++m) {
;                 const int r = u.rt * BM + ai * HALF + wr * 64 + m * 16 + fr;
;                 f32x2_t o[4];
; #pragma unroll
;                 for (int n = 0; n < 2; ++n)
; #pragma unroll
;                     for (int h = 0; h < 2; ++h) {
;                         const f32x4 bgv = n ? bg1 : bg0, blv = n ? bl1 : bl0;
;                         f32x2_t glu = (f32x2_t){acc[ai][0][m][n][2 * h], acc[ai][0][m][n][2 * h + 1]} * sc2 + (f32x2_t){bgv[2 * h], bgv[2 * h + 1]};
;                         f32x2_t lin = (f32x2_t){acc[ai][1][m][n][2 * h], acc[ai][1][m][n][2 * h + 1]} * sc2 + (f32x2_t){blv[2 * h], blv[2 * h + 1]};
;                         glu.x = fminf(glu.x, lim); glu.y = fminf(glu.y, lim);
;                         lin.x = __builtin_amdgcn_fmed3f(lin.x, -lim, lim); lin.y = __builtin_amdgcn_fmed3f(lin.y, -lim, lim);
;                         const f32x2_t t = glu * ke2;
;                         const f32x2_t d = (f32x2_t){__builtin_amdgcn_exp2f(t.x), __builtin_amdgcn_exp2f(t.y)} + one2;
;                         const f32x2_t rc = (f32x2_t){__builtin_amdgcn_rcpf(d.x), __builtin_amdgcn_rcpf(d.y)};
;                         o[n * 2 + h] = (glu * rc) * (lin * as2 + as2);
;                     }
;                 const int ro = u.rowbase + r;
;                 u32x2 w; w.x = cvt_pk4_fp8(o[0].x, o[0].y, o[1].x, o[1].y); w.y = cvt_pk4_fp8(o[2].x, o[2].y, o[3].x, o[3].y);
	s_add_u32 s74, s0, 0x20080
	s_addc_u32 s75, s1, 0
	s_add_u32 s0, s0, 0x30080
	s_addc_u32 s1, s1, 0
	s_mov_b32 m0, s64
	s_nop 0
	v_lshl_add_u64 v[2:3], s[74:75], 0, v[252:253]
	global_load_lds_dwordx4 v[2:3], off
	v_lshl_add_u64 v[2:3], s[0:1], 0, v[252:253]
	s_mov_b32 m0, s65
	s_nop 0
	global_load_lds_dwordx4 v[2:3], off
	s_waitcnt vmcnt(6)
	s_barrier
	v_mfma_scale_f32_16x16x128_f8f6f4 v[240:243], v[138:145], v[18:25], v[80:83], v154, v154 op_sel_hi:[0,0,0]
	v_mfma_scale_f32_16x16x128_f8f6f4 v[248:251], v[160:167], v[18:25], v[68:71], v154, v154 op_sel_hi:[0,0,0]
	v_mfma_scale_f32_16x16x128_f8f6f4 v[22:25], v[138:145], v[168:175], v[192:195], v154, v154 op_sel_hi:[0,0,0]
	v_mfma_scale_f32_16x16x128_f8f6f4 v[18:21], v[160:167], v[168:175], v[196:199], v154, v154 op_sel_hi:[0,0,0]
	v_mfma_scale_f32_16x16x128_f8f6f4 v[14:17], v[138:145], v[176:183], v[200:203], v154, v154 op_sel_hi:[0,0,0]
	v_mfma_scale_f32_16x16x128_f8f6f4 v[10:13], v[160:167], v[176:183], v[96:99], v154, v154 op_sel_hi:[0,0,0]
	v_mfma_scale_f32_16x16x128_f8f6f4 v[92:95], v[138:145], v[184:191], v[100:103], v154, v154 op_sel_hi:[0,0,0]
	s_nop 5
	v_mov_b64_e32 v[96:97], v[132:133]
	v_mov_b64_e32 v[98:99], v[134:135]
	v_mfma_scale_f32_16x16x128_f8f6f4 v[2:5], v[160:167], v[184:191], v[104:107], v154, v154 op_sel_hi:[0,0,0]
	v_mov_b32_e32 v34, v0
	s_barrier
	s_lshl_b32 s0, s68, 11
	v_readfirstlane_b32 s17, v34
	s_lshr_b32 s1, s17, 1
	s_and_b32 s1, s1, 0x60
	v_lshrrev_b32_e32 v68, 1, v34
	s_add_i32 s0, s67, s0
	v_and_or_b32 v69, v68, 24, s1
	v_lshl_or_b32 v68, s18, 7, v69
	v_lshl_add_u32 v69, v69, 2, s0
	ds_read_b128 v[140:143], v69
	ds_read_b128 v[132:135], v69 offset:16
	ds_read_b128 v[144:147], v69 offset:512
	ds_read_b128 v[136:139], v69 offset:528
	s_ashr_i32 s17, s17, 2
	s_mov_b32 s34, 0x3b000000
	s_mov_b32 s1, 0x40e00000
	s_andn2_b32 s17, s17, 63
	v_ashrrev_i32_e32 v69, 31, v68
	v_and_or_b32 v80, v34, 15, s17
	v_lshl_add_u64 v[150:151], s[14:15], 0, v[68:69]
	s_waitcnt lgkmcnt(0)
	v_pk_fma_f32 v[68:69], v[128:129], s[34:35], v[140:141] op_sel_hi:[1,0,1]
	v_max_f32_e64 v34, s1, s1
	s_mov_b32 s30, 0xc01d265f
	v_min_f32_e32 v68, v68, v34
	v_min_f32_e32 v69, v69, v34
	s_mov_b32 s2, 1.0
	v_pk_mul_f32 v[72:73], s[30:31], v[68:69] op_sel_hi:[0,1]
	v_exp_f32_e32 v72, v72
	v_exp_f32_e32 v73, v73
	v_pk_fma_f32 v[70:71], v[96:97], s[34:35], v[144:145] op_sel_hi:[1,0,1]
	s_mov_b32 s0, 4.0
	v_pk_add_f32 v[72:73], s[2:3], v[72:73] op_sel_hi:[0,1]
	v_rcp_f32_e32 v72, v72
	v_rcp_f32_e32 v73, v73
	v_med3_f32 v70, v70, -s1, s1
	v_med3_f32 v71, v71, -s1, s1
	v_pk_mul_f32 v[68:69], v[68:69], v[72:73]
	v_pk_fma_f32 v[70:71], s[0:1], v[70:71], s[0:1] op_sel_hi:[0,1,0]
	v_pk_mul_f32 v[68:69], v[70:71], v[68:69]
	v_pk_fma_f32 v[70:71], v[130:131], s[34:35], v[142:143] op_sel_hi:[1,0,1]
	v_pk_fma_f32 v[72:73], v[98:99], s[34:35], v[146:147] op_sel_hi:[1,0,1]
	v_min_f32_e32 v70, v70, v34
	v_min_f32_e32 v71, v71, v34
	v_pk_mul_f32 v[74:75], s[30:31], v[70:71] op_sel_hi:[0,1]
	v_exp_f32_e32 v74, v74
	v_exp_f32_e32 v75, v75
	v_med3_f32 v72, v72, -s1, s1
	v_med3_f32 v73, v73, -s1, s1
	v_pk_fma_f32 v[72:73], s[0:1], v[72:73], s[0:1] op_sel_hi:[0,1,0]
	v_pk_add_f32 v[74:75], s[2:3], v[74:75] op_sel_hi:[0,1]
	v_rcp_f32_e32 v74, v74
	v_rcp_f32_e32 v75, v75
	s_lshl_b32 s17, s38, 8
	s_add_i32 s17, s17, s39
	v_add_u32_e32 v152, s17, v80
	v_pk_mul_f32 v[70:71], v[70:71], v[74:75]
	v_pk_fma_f32 v[74:75], v[84:85], s[34:35], v[136:137] op_sel_hi:[1,0,1]
	v_pk_mul_f32 v[70:71], v[72:73], v[70:71]
	v_pk_fma_f32 v[72:73], v[124:125], s[34:35], v[132:133] op_sel_hi:[1,0,1]
	v_med3_f32 v74, v74, -s1, s1
	v_min_f32_e32 v72, v72, v34
	v_min_f32_e32 v73, v73, v34
	v_pk_mul_f32 v[76:77], s[30:31], v[72:73] op_sel_hi:[0,1]
	v_exp_f32_e32 v76, v76
	v_exp_f32_e32 v77, v77
	v_med3_f32 v75, v75, -s1, s1
	v_pk_fma_f32 v[74:75], s[0:1], v[74:75], s[0:1] op_sel_hi:[0,1,0]
	v_ashrrev_i32_e32 v153, 31, v152
	v_pk_add_f32 v[76:77], s[2:3], v[76:77] op_sel_hi:[0,1]
	v_rcp_f32_e32 v76, v76
	v_rcp_f32_e32 v77, v77
	v_mov_b64_e32 v[80:81], v[208:209]
	v_mov_b64_e32 v[82:83], v[210:211]
	s_and_b64 vcc, exec, s[4:5]
	v_pk_mul_f32 v[72:73], v[72:73], v[76:77]
	v_pk_fma_f32 v[76:77], v[86:87], s[34:35], v[138:139] op_sel_hi:[1,0,1]
	v_pk_mul_f32 v[72:73], v[74:75], v[72:73]
	v_pk_fma_f32 v[74:75], v[126:127], s[34:35], v[134:135] op_sel_hi:[1,0,1]
	v_med3_f32 v76, v76, -s1, s1
	v_min_f32_e32 v74, v74, v34
	v_min_f32_e32 v75, v75, v34
	v_pk_mul_f32 v[78:79], s[30:31], v[74:75] op_sel_hi:[0,1]
	v_exp_f32_e32 v78, v78
	v_exp_f32_e32 v79, v79
	v_med3_f32 v77, v77, -s1, s1
	v_pk_fma_f32 v[76:77], s[0:1], v[76:77], s[0:1] op_sel_hi:[0,1,0]
	v_pk_add_f32 v[78:79], s[2:3], v[78:79] op_sel_hi:[0,1]
	v_rcp_f32_e32 v78, v78
	v_rcp_f32_e32 v79, v79
	s_nop 0
	v_pk_mul_f32 v[74:75], v[74:75], v[78:79]
	s_nop 0
	v_pk_mul_f32 v[74:75], v[76:77], v[74:75]
	v_mov_b32_e32 v76, v35
	v_mov_b32_e32 v77, v35
	v_cvt_pk_fp8_f32 v76, v68, v69
	v_cvt_pk_fp8_f32 v77, v72, v73
	v_lshlrev_b64 v[68:69], 10, v[152:153]
	v_lshl_add_u64 v[68:69], v[150:151], 0, v[68:69]
	v_cvt_pk_fp8_f32 v76, v70, v71 op_sel:[0,0,1]
	v_cvt_pk_fp8_f32 v77, v74, v75 op_sel:[0,0,1]
	v_pk_fma_f32 v[70:71], v[88:89], s[34:35], v[144:145] op_sel_hi:[1,0,1]
	global_store_dwordx2 v[68:69], v[76:77], off sc1
	v_pk_fma_f32 v[68:69], v[120:121], s[34:35], v[140:141] op_sel_hi:[1,0,1]
	v_med3_f32 v70, v70, -s1, s1
	v_min_f32_e32 v68, v68, v34
	v_min_f32_e32 v69, v69, v34
	v_pk_mul_f32 v[72:73], s[30:31], v[68:69] op_sel_hi:[0,1]
	v_exp_f32_e32 v72, v72
	v_exp_f32_e32 v73, v73
	v_med3_f32 v71, v71, -s1, s1
	v_pk_fma_f32 v[70:71], s[0:1], v[70:71], s[0:1] op_sel_hi:[0,1,0]
; __device__ __forceinline__ unsigned cvt_pk4_fp8(float a, float b, float c, float d) { int w = 0; w = __builtin_amdgcn_cvt_pk_fp8_f32(a, b, w, false); w = __builtin_amdgcn_cvt_pk_fp8_f32(c, d, w, true); return (unsigned)w; }
; #define GAS __attribute__((address_space(1)))
;     __device__ __forceinline__ void operator()(const f32x4 (&acc)[2][2][4][2], const Unit& u, int wr, int wc, int fr, int fq, LAS unsigned char* lds, int par) const {
;     ...
;         for (int ai = 0; ai < 2; ++ai)
; #pragma unroll
;             for (int m = 0; m < 4; ++m) {
;                 const int r = u.rt * BM + ai * HALF + wr * 64 + m * 16 + fr;
;                 f32x2_t o[4];
; #pragma unroll
;                 for (int n = 0; n < 2; ++n)
; #pragma unroll
;                     for (int h = 0; h < 2; ++h) {
;                         const f32x4 bgv = n ? bg1 : bg0, blv = n ? bl1 : bl0;
;                         f32x2_t glu = (f32x2_t){acc[ai][0][m][n][2 * h], acc[ai][0][m][n][2 * h + 1]} * sc2 + (f32x2_t){bgv[2 * h], bgv[2 * h + 1]};
;                         f32x2_t lin = (f32x2_t){acc[ai][1][m][n][2 * h], acc[ai][1][m][n][2 * h + 1]} * sc2 + (f32x2_t){blv[2 * h], blv[2 * h + 1]};
;                         glu.x = fminf(glu.x, lim); glu.y = fminf(glu.y, lim);
;                         lin.x = __builtin_amdgcn_fmed3f(lin.x, -lim, lim); lin.y = __builtin_amdgcn_fmed3f(lin.y, -lim, lim);
;                         const f32x2_t t = glu * ke2;
;                         const f32x2_t d = (f32x2_t){__builtin_amdgcn_exp2f(t.x), __builtin_amdgcn_exp2f(t.y)} + one2;
;                         const f32x2_t rc = (f32x2_t){__builtin_amdgcn_rcpf(d.x), __builtin_amdgcn_rcpf(d.y)};
;                         o[n * 2 + h] = (glu * rc) * (lin * as2 + as2);
;                     }
;                 const int ro = u.rowbase + r;
;                 u32x2 w; w.x = cvt_pk4_fp8(o[0].x, o[0].y, o[1].x, o[1].y); w.y = cvt_pk4_fp8(o[2].x, o[2].y, o[3].x, o[3].y);
;                 __hip_atomic_store((unsigned long long GAS*)(act + (size_t)ro * DFF + col), ((unsigned long long)w.y << 32) | w.x, __ATOMIC_RELAXED, __HIP_MEMORY_SCOPE_AGENT);
	v_pk_add_f32 v[72:73], s[2:3], v[72:73] op_sel_hi:[0,1]
	v_rcp_f32_e32 v72, v72
	v_rcp_f32_e32 v73, v73
	s_nop 0
	v_pk_mul_f32 v[68:69], v[68:69], v[72:73]
	s_nop 0
	v_pk_mul_f32 v[68:69], v[70:71], v[68:69]
	v_pk_fma_f32 v[70:71], v[122:123], s[34:35], v[142:143] op_sel_hi:[1,0,1]
	v_pk_fma_f32 v[72:73], v[90:91], s[34:35], v[146:147] op_sel_hi:[1,0,1]
	v_min_f32_e32 v70, v70, v34
	v_min_f32_e32 v71, v71, v34
	v_pk_mul_f32 v[74:75], s[30:31], v[70:71] op_sel_hi:[0,1]
	v_exp_f32_e32 v74, v74
	v_exp_f32_e32 v75, v75
	v_med3_f32 v72, v72, -s1, s1
	v_med3_f32 v73, v73, -s1, s1
	v_pk_fma_f32 v[72:73], s[0:1], v[72:73], s[0:1] op_sel_hi:[0,1,0]
	v_pk_add_f32 v[74:75], s[2:3], v[74:75] op_sel_hi:[0,1]
	v_rcp_f32_e32 v74, v74
	v_rcp_f32_e32 v75, v75
	s_nop 0
	v_pk_mul_f32 v[70:71], v[70:71], v[74:75]
	s_nop 0
	v_pk_mul_f32 v[70:71], v[72:73], v[70:71]
	v_pk_fma_f32 v[72:73], v[116:117], s[34:35], v[132:133] op_sel_hi:[1,0,1]
	v_pk_fma_f32 v[74:75], v[26:27], s[34:35], v[136:137] op_sel_hi:[1,0,1]
	v_min_f32_e32 v72, v72, v34
	v_min_f32_e32 v73, v73, v34
	v_pk_mul_f32 v[76:77], s[30:31], v[72:73] op_sel_hi:[0,1]
	v_exp_f32_e32 v76, v76
	v_exp_f32_e32 v77, v77
	v_med3_f32 v74, v74, -s1, s1
	v_med3_f32 v75, v75, -s1, s1
	v_pk_fma_f32 v[74:75], s[0:1], v[74:75], s[0:1] op_sel_hi:[0,1,0]
	v_pk_add_f32 v[76:77], s[2:3], v[76:77] op_sel_hi:[0,1]
	v_rcp_f32_e32 v76, v76
	v_rcp_f32_e32 v77, v77
	s_nop 0
	v_pk_mul_f32 v[72:73], v[72:73], v[76:77]
	s_nop 0
	v_pk_mul_f32 v[72:73], v[74:75], v[72:73]
	v_pk_fma_f32 v[74:75], v[118:119], s[34:35], v[134:135] op_sel_hi:[1,0,1]
	v_pk_fma_f32 v[76:77], v[28:29], s[34:35], v[138:139] op_sel_hi:[1,0,1]
	v_min_f32_e32 v74, v74, v34
	v_min_f32_e32 v75, v75, v34
	v_pk_mul_f32 v[78:79], s[30:31], v[74:75] op_sel_hi:[0,1]
	v_exp_f32_e32 v78, v78
	v_exp_f32_e32 v79, v79
	v_med3_f32 v76, v76, -s1, s1
	v_med3_f32 v77, v77, -s1, s1
	v_pk_fma_f32 v[76:77], s[0:1], v[76:77], s[0:1] op_sel_hi:[0,1,0]
	v_pk_add_f32 v[78:79], s[2:3], v[78:79] op_sel_hi:[0,1]
	v_rcp_f32_e32 v78, v78
	v_rcp_f32_e32 v79, v79
	s_nop 0
	v_pk_mul_f32 v[74:75], v[74:75], v[78:79]
	v_mov_b32_e32 v78, v35
	v_mov_b32_e32 v79, v35
	v_cvt_pk_fp8_f32 v78, v68, v69
	v_cvt_pk_fp8_f32 v79, v72, v73
	v_pk_mul_f32 v[74:75], v[76:77], v[74:75]
	v_add_u32_e32 v76, 16, v152
	v_cvt_pk_fp8_f32 v78, v70, v71 op_sel:[0,0,1]
	v_cvt_pk_fp8_f32 v79, v74, v75 op_sel:[0,0,1]
	v_ashrrev_i32_e32 v77, 31, v76
	v_lshlrev_b64 v[68:69], 10, v[76:77]
	v_lshl_add_u64 v[68:69], v[150:151], 0, v[68:69]
	global_store_dwordx2 v[68:69], v[78:79], off sc1
	v_pk_fma_f32 v[68:69], v[112:113], s[34:35], v[140:141] op_sel_hi:[1,0,1]
	v_pk_fma_f32 v[70:71], v[52:53], s[34:35], v[144:145] op_sel_hi:[1,0,1]
	v_min_f32_e32 v68, v68, v34
	v_min_f32_e32 v69, v69, v34
	v_pk_mul_f32 v[72:73], s[30:31], v[68:69] op_sel_hi:[0,1]
	v_exp_f32_e32 v72, v72
	v_exp_f32_e32 v73, v73
	v_med3_f32 v70, v70, -s1, s1
	v_med3_f32 v71, v71, -s1, s1
	v_pk_fma_f32 v[70:71], s[0:1], v[70:71], s[0:1] op_sel_hi:[0,1,0]
	v_pk_add_f32 v[72:73], s[2:3], v[72:73] op_sel_hi:[0,1]
	v_rcp_f32_e32 v72, v72
	v_rcp_f32_e32 v73, v73
	s_nop 0
	v_pk_mul_f32 v[68:69], v[68:69], v[72:73]
	s_nop 0
	v_pk_mul_f32 v[68:69], v[70:71], v[68:69]
	v_pk_fma_f32 v[70:71], v[114:115], s[34:35], v[142:143] op_sel_hi:[1,0,1]
	v_pk_fma_f32 v[72:73], v[54:55], s[34:35], v[146:147] op_sel_hi:[1,0,1]
	v_min_f32_e32 v70, v70, v34
	v_min_f32_e32 v71, v71, v34
	v_pk_mul_f32 v[74:75], s[30:31], v[70:71] op_sel_hi:[0,1]
	v_exp_f32_e32 v74, v74
	v_exp_f32_e32 v75, v75
	v_med3_f32 v72, v72, -s1, s1
	v_med3_f32 v73, v73, -s1, s1
	v_pk_fma_f32 v[72:73], s[0:1], v[72:73], s[0:1] op_sel_hi:[0,1,0]
	v_pk_add_f32 v[74:75], s[2:3], v[74:75] op_sel_hi:[0,1]
	v_rcp_f32_e32 v74, v74
	v_rcp_f32_e32 v75, v75
	s_nop 0
	v_pk_mul_f32 v[70:71], v[70:71], v[74:75]
	s_nop 0
	v_pk_mul_f32 v[70:71], v[72:73], v[70:71]
	v_pk_fma_f32 v[72:73], v[108:109], s[34:35], v[132:133] op_sel_hi:[1,0,1]
	v_pk_fma_f32 v[74:75], v[36:37], s[34:35], v[136:137] op_sel_hi:[1,0,1]
	v_min_f32_e32 v72, v72, v34
	v_min_f32_e32 v73, v73, v34
	v_pk_mul_f32 v[76:77], s[30:31], v[72:73] op_sel_hi:[0,1]
	v_exp_f32_e32 v76, v76
	v_exp_f32_e32 v77, v77
	v_med3_f32 v74, v74, -s1, s1
	v_med3_f32 v75, v75, -s1, s1
	v_pk_fma_f32 v[74:75], s[0:1], v[74:75], s[0:1] op_sel_hi:[0,1,0]
	v_pk_add_f32 v[76:77], s[2:3], v[76:77] op_sel_hi:[0,1]
	v_rcp_f32_e32 v76, v76
	v_rcp_f32_e32 v77, v77
	s_nop 0
	v_pk_mul_f32 v[72:73], v[72:73], v[76:77]
	s_nop 0
	v_pk_mul_f32 v[72:73], v[74:75], v[72:73]
	v_pk_fma_f32 v[74:75], v[110:111], s[34:35], v[134:135] op_sel_hi:[1,0,1]
	v_pk_fma_f32 v[76:77], v[38:39], s[34:35], v[138:139] op_sel_hi:[1,0,1]
	v_min_f32_e32 v74, v74, v34
	v_min_f32_e32 v75, v75, v34
	v_pk_mul_f32 v[78:79], s[30:31], v[74:75] op_sel_hi:[0,1]
	v_exp_f32_e32 v78, v78
	v_exp_f32_e32 v79, v79
	v_med3_f32 v76, v76, -s1, s1
	v_med3_f32 v77, v77, -s1, s1
	v_pk_fma_f32 v[76:77], s[0:1], v[76:77], s[0:1] op_sel_hi:[0,1,0]
	v_pk_add_f32 v[78:79], s[2:3], v[78:79] op_sel_hi:[0,1]
	v_rcp_f32_e32 v78, v78
	v_rcp_f32_e32 v79, v79
	s_nop 0
	v_pk_mul_f32 v[74:75], v[74:75], v[78:79]
	v_mov_b32_e32 v78, v35
	v_mov_b32_e32 v79, v35
	v_cvt_pk_fp8_f32 v78, v68, v69
	v_cvt_pk_fp8_f32 v79, v72, v73
	v_pk_mul_f32 v[74:75], v[76:77], v[74:75]
	v_add_u32_e32 v76, 32, v152
	v_cvt_pk_fp8_f32 v78, v70, v71 op_sel:[0,0,1]
	v_cvt_pk_fp8_f32 v79, v74, v75 op_sel:[0,0,1]
	v_ashrrev_i32_e32 v77, 31, v76
	v_lshlrev_b64 v[68:69], 10, v[76:77]
	v_lshl_add_u64 v[68:69], v[150:151], 0, v[68:69]
	global_store_dwordx2 v[68:69], v[78:79], off sc1
	v_pk_fma_f32 v[68:69], v[204:205], s[34:35], v[140:141] op_sel_hi:[1,0,1]
; __device__ __forceinline__ unsigned cvt_pk4_fp8(float a, float b, float c, float d) { int w = 0; w = __builtin_amdgcn_cvt_pk_fp8_f32(a, b, w, false); w = __builtin_amdgcn_cvt_pk_fp8_f32(c, d, w, true); return (unsigned)w; }
; #define GAS __attribute__((address_space(1)))
;     __device__ __forceinline__ void operator()(const f32x4 (&acc)[2][2][4][2], const Unit& u, int wr, int wc, int fr, int fq, LAS unsigned char* lds, int par) const {
;     ...
;         for (int ai = 0; ai < 2; ++ai)
; #pragma unroll
;             for (int m = 0; m < 4; ++m) {
;                 const int r = u.rt * BM + ai * HALF + wr * 64 + m * 16 + fr;
;                 f32x2_t o[4];
; #pragma unroll
;                 for (int n = 0; n < 2; ++n)
; #pragma unroll
;                     for (int h = 0; h < 2; ++h) {
;                         const f32x4 bgv = n ? bg1 : bg0, blv = n ? bl1 : bl0;
;                         f32x2_t glu = (f32x2_t){acc[ai][0][m][n][2 * h], acc[ai][0][m][n][2 * h + 1]} * sc2 + (f32x2_t){bgv[2 * h], bgv[2 * h + 1]};
;                         f32x2_t lin = (f32x2_t){acc[ai][1][m][n][2 * h], acc[ai][1][m][n][2 * h + 1]} * sc2 + (f32x2_t){blv[2 * h], blv[2 * h + 1]};
;                         glu.x = fminf(glu.x, lim); glu.y = fminf(glu.y, lim);
;                         lin.x = __builtin_amdgcn_fmed3f(lin.x, -lim, lim); lin.y = __builtin_amdgcn_fmed3f(lin.y, -lim, lim);
;                         const f32x2_t t = glu * ke2;
;                         const f32x2_t d = (f32x2_t){__builtin_amdgcn_exp2f(t.x), __builtin_amdgcn_exp2f(t.y)} + one2;
;                         const f32x2_t rc = (f32x2_t){__builtin_amdgcn_rcpf(d.x), __builtin_amdgcn_rcpf(d.y)};
;                         o[n * 2 + h] = (glu * rc) * (lin * as2 + as2);
;                     }
;                 const int ro = u.rowbase + r;
;                 u32x2 w; w.x = cvt_pk4_fp8(o[0].x, o[0].y, o[1].x, o[1].y); w.y = cvt_pk4_fp8(o[2].x, o[2].y, o[3].x, o[3].y);
;                 __hip_atomic_store((unsigned long long GAS*)(act + (size_t)ro * DFF + col), ((unsigned long long)w.y << 32) | w.x, __ATOMIC_RELAXED, __HIP_MEMORY_SCOPE_AGENT);
	v_pk_fma_f32 v[70:71], v[30:31], s[34:35], v[144:145] op_sel_hi:[1,0,1]
	v_min_f32_e32 v68, v68, v34
	v_min_f32_e32 v69, v69, v34
	v_pk_mul_f32 v[72:73], s[30:31], v[68:69] op_sel_hi:[0,1]
	v_exp_f32_e32 v72, v72
	v_exp_f32_e32 v73, v73
	v_med3_f32 v70, v70, -s1, s1
	v_med3_f32 v71, v71, -s1, s1
	v_pk_fma_f32 v[70:71], s[0:1], v[70:71], s[0:1] op_sel_hi:[0,1,0]
	v_pk_add_f32 v[72:73], s[2:3], v[72:73] op_sel_hi:[0,1]
	v_rcp_f32_e32 v72, v72
	v_rcp_f32_e32 v73, v73
	s_nop 0
	v_pk_mul_f32 v[68:69], v[68:69], v[72:73]
	s_nop 0
	v_pk_mul_f32 v[68:69], v[70:71], v[68:69]
	v_pk_fma_f32 v[70:71], v[206:207], s[34:35], v[142:143] op_sel_hi:[1,0,1]
	v_pk_fma_f32 v[72:73], v[32:33], s[34:35], v[146:147] op_sel_hi:[1,0,1]
	v_min_f32_e32 v70, v70, v34
	v_min_f32_e32 v71, v71, v34
	v_pk_mul_f32 v[74:75], s[30:31], v[70:71] op_sel_hi:[0,1]
	v_exp_f32_e32 v74, v74
	v_exp_f32_e32 v75, v75
	v_med3_f32 v72, v72, -s1, s1
	v_med3_f32 v73, v73, -s1, s1
	v_pk_fma_f32 v[72:73], s[0:1], v[72:73], s[0:1] op_sel_hi:[0,1,0]
	v_pk_add_f32 v[74:75], s[2:3], v[74:75] op_sel_hi:[0,1]
	v_rcp_f32_e32 v74, v74
	v_rcp_f32_e32 v75, v75
	s_nop 0
	v_pk_mul_f32 v[70:71], v[70:71], v[74:75]
	s_nop 0
	v_pk_mul_f32 v[70:71], v[72:73], v[70:71]
	v_pk_fma_f32 v[72:73], v[80:81], s[34:35], v[132:133] op_sel_hi:[1,0,1]
	v_pk_fma_f32 v[74:75], v[40:41], s[34:35], v[136:137] op_sel_hi:[1,0,1]
	v_min_f32_e32 v72, v72, v34
	v_min_f32_e32 v73, v73, v34
	v_pk_mul_f32 v[76:77], s[30:31], v[72:73] op_sel_hi:[0,1]
	v_exp_f32_e32 v76, v76
	v_exp_f32_e32 v77, v77
	v_med3_f32 v74, v74, -s1, s1
	v_med3_f32 v75, v75, -s1, s1
	v_pk_fma_f32 v[74:75], s[0:1], v[74:75], s[0:1] op_sel_hi:[0,1,0]
	v_pk_add_f32 v[76:77], s[2:3], v[76:77] op_sel_hi:[0,1]
	v_rcp_f32_e32 v76, v76
	v_rcp_f32_e32 v77, v77
	s_nop 0
	v_pk_mul_f32 v[72:73], v[72:73], v[76:77]
	s_nop 0
	v_pk_mul_f32 v[72:73], v[74:75], v[72:73]
	v_pk_fma_f32 v[74:75], v[82:83], s[34:35], v[134:135] op_sel_hi:[1,0,1]
	v_pk_fma_f32 v[76:77], v[42:43], s[34:35], v[138:139] op_sel_hi:[1,0,1]
	v_min_f32_e32 v74, v74, v34
	v_min_f32_e32 v75, v75, v34
	v_pk_mul_f32 v[78:79], s[30:31], v[74:75] op_sel_hi:[0,1]
	v_exp_f32_e32 v78, v78
	v_exp_f32_e32 v79, v79
	v_med3_f32 v76, v76, -s1, s1
	v_med3_f32 v77, v77, -s1, s1
	v_pk_fma_f32 v[76:77], s[0:1], v[76:77], s[0:1] op_sel_hi:[0,1,0]
	v_pk_add_f32 v[78:79], s[2:3], v[78:79] op_sel_hi:[0,1]
	v_rcp_f32_e32 v78, v78
	v_rcp_f32_e32 v79, v79
	s_nop 0
	v_pk_mul_f32 v[74:75], v[74:75], v[78:79]
	v_mov_b32_e32 v78, v35
	v_mov_b32_e32 v79, v35
	v_cvt_pk_fp8_f32 v78, v68, v69
	v_cvt_pk_fp8_f32 v79, v72, v73
	v_pk_mul_f32 v[74:75], v[76:77], v[74:75]
	v_add_u32_e32 v76, 48, v152
	v_cvt_pk_fp8_f32 v78, v70, v71 op_sel:[0,0,1]
	v_cvt_pk_fp8_f32 v79, v74, v75 op_sel:[0,0,1]
	v_ashrrev_i32_e32 v77, 31, v76
	v_lshlrev_b64 v[68:69], 10, v[76:77]
	v_lshl_add_u64 v[68:69], v[150:151], 0, v[68:69]
	global_store_dwordx2 v[68:69], v[78:79], off sc1
	v_pk_fma_f32 v[68:69], v[64:65], s[34:35], v[140:141] op_sel_hi:[1,0,1]
	v_pk_fma_f32 v[70:71], v[240:241], s[34:35], v[144:145] op_sel_hi:[1,0,1]
	v_min_f32_e32 v68, v68, v34
	v_min_f32_e32 v69, v69, v34
	v_pk_mul_f32 v[72:73], s[30:31], v[68:69] op_sel_hi:[0,1]
	v_exp_f32_e32 v72, v72
	v_exp_f32_e32 v73, v73
	v_med3_f32 v70, v70, -s1, s1
	v_med3_f32 v71, v71, -s1, s1
	v_pk_fma_f32 v[70:71], s[0:1], v[70:71], s[0:1] op_sel_hi:[0,1,0]
	v_pk_add_f32 v[72:73], s[2:3], v[72:73] op_sel_hi:[0,1]
	v_rcp_f32_e32 v72, v72
	v_rcp_f32_e32 v73, v73
	s_nop 0
	v_pk_mul_f32 v[68:69], v[68:69], v[72:73]
	s_nop 0
	v_pk_mul_f32 v[68:69], v[70:71], v[68:69]
	v_pk_fma_f32 v[70:71], v[66:67], s[34:35], v[142:143] op_sel_hi:[1,0,1]
	v_pk_fma_f32 v[72:73], v[242:243], s[34:35], v[146:147] op_sel_hi:[1,0,1]
	v_min_f32_e32 v70, v70, v34
	v_min_f32_e32 v71, v71, v34
	v_pk_mul_f32 v[74:75], s[30:31], v[70:71] op_sel_hi:[0,1]
	v_exp_f32_e32 v74, v74
	v_exp_f32_e32 v75, v75
	v_med3_f32 v72, v72, -s1, s1
	v_med3_f32 v73, v73, -s1, s1
	v_pk_fma_f32 v[72:73], s[0:1], v[72:73], s[0:1] op_sel_hi:[0,1,0]
	v_pk_add_f32 v[74:75], s[2:3], v[74:75] op_sel_hi:[0,1]
	v_rcp_f32_e32 v74, v74
	v_rcp_f32_e32 v75, v75
	s_nop 0
	v_pk_mul_f32 v[70:71], v[70:71], v[74:75]
	s_nop 0
	v_pk_mul_f32 v[70:71], v[72:73], v[70:71]
	v_pk_fma_f32 v[72:73], v[60:61], s[34:35], v[132:133] op_sel_hi:[1,0,1]
	v_pk_fma_f32 v[74:75], v[248:249], s[34:35], v[136:137] op_sel_hi:[1,0,1]
	v_min_f32_e32 v72, v72, v34
	v_min_f32_e32 v73, v73, v34
	v_pk_mul_f32 v[76:77], s[30:31], v[72:73] op_sel_hi:[0,1]
	v_exp_f32_e32 v76, v76
	v_exp_f32_e32 v77, v77
	v_med3_f32 v74, v74, -s1, s1
	v_med3_f32 v75, v75, -s1, s1
	v_pk_fma_f32 v[74:75], s[0:1], v[74:75], s[0:1] op_sel_hi:[0,1,0]
	v_pk_add_f32 v[76:77], s[2:3], v[76:77] op_sel_hi:[0,1]
	v_rcp_f32_e32 v76, v76
	v_rcp_f32_e32 v77, v77
	s_nop 0
	v_pk_mul_f32 v[72:73], v[72:73], v[76:77]
	s_nop 0
	v_pk_mul_f32 v[72:73], v[74:75], v[72:73]
	v_pk_fma_f32 v[74:75], v[62:63], s[34:35], v[134:135] op_sel_hi:[1,0,1]
	v_pk_fma_f32 v[76:77], v[250:251], s[34:35], v[138:139] op_sel_hi:[1,0,1]
	v_min_f32_e32 v74, v74, v34
	v_min_f32_e32 v75, v75, v34
	v_pk_mul_f32 v[78:79], s[30:31], v[74:75] op_sel_hi:[0,1]
	v_exp_f32_e32 v78, v78
	v_exp_f32_e32 v79, v79
	v_med3_f32 v76, v76, -s1, s1
	v_med3_f32 v77, v77, -s1, s1
	v_pk_fma_f32 v[76:77], s[0:1], v[76:77], s[0:1] op_sel_hi:[0,1,0]
	v_pk_add_f32 v[78:79], s[2:3], v[78:79] op_sel_hi:[0,1]
	v_rcp_f32_e32 v78, v78
	v_rcp_f32_e32 v79, v79
	s_nop 0
	v_pk_mul_f32 v[74:75], v[74:75], v[78:79]
	v_mov_b32_e32 v78, v35
	v_mov_b32_e32 v79, v35
	v_cvt_pk_fp8_f32 v78, v68, v69
	v_cvt_pk_fp8_f32 v79, v72, v73
	v_pk_mul_f32 v[74:75], v[76:77], v[74:75]
	v_add_u32_e32 v76, 0x80, v152
; __device__ __forceinline__ unsigned cvt_pk4_fp8(float a, float b, float c, float d) { int w = 0; w = __builtin_amdgcn_cvt_pk_fp8_f32(a, b, w, false); w = __builtin_amdgcn_cvt_pk_fp8_f32(c, d, w, true); return (unsigned)w; }
; #define GAS __attribute__((address_space(1)))
;     __device__ __forceinline__ void operator()(const f32x4 (&acc)[2][2][4][2], const Unit& u, int wr, int wc, int fr, int fq, LAS unsigned char* lds, int par) const {
;     ...
;         for (int ai = 0; ai < 2; ++ai)
; #pragma unroll
;             for (int m = 0; m < 4; ++m) {
;                 const int r = u.rt * BM + ai * HALF + wr * 64 + m * 16 + fr;
;                 f32x2_t o[4];
; #pragma unroll
;                 for (int n = 0; n < 2; ++n)
; #pragma unroll
;                     for (int h = 0; h < 2; ++h) {
;                         const f32x4 bgv = n ? bg1 : bg0, blv = n ? bl1 : bl0;
;                         f32x2_t glu = (f32x2_t){acc[ai][0][m][n][2 * h], acc[ai][0][m][n][2 * h + 1]} * sc2 + (f32x2_t){bgv[2 * h], bgv[2 * h + 1]};
;                         f32x2_t lin = (f32x2_t){acc[ai][1][m][n][2 * h], acc[ai][1][m][n][2 * h + 1]} * sc2 + (f32x2_t){blv[2 * h], blv[2 * h + 1]};
;                         glu.x = fminf(glu.x, lim); glu.y = fminf(glu.y, lim);
;                         lin.x = __builtin_amdgcn_fmed3f(lin.x, -lim, lim); lin.y = __builtin_amdgcn_fmed3f(lin.y, -lim, lim);
;                         const f32x2_t t = glu * ke2;
;                         const f32x2_t d = (f32x2_t){__builtin_amdgcn_exp2f(t.x), __builtin_amdgcn_exp2f(t.y)} + one2;
;                         const f32x2_t rc = (f32x2_t){__builtin_amdgcn_rcpf(d.x), __builtin_amdgcn_rcpf(d.y)};
;                         o[n * 2 + h] = (glu * rc) * (lin * as2 + as2);
;                     }
;                 const int ro = u.rowbase + r;
;                 u32x2 w; w.x = cvt_pk4_fp8(o[0].x, o[0].y, o[1].x, o[1].y); w.y = cvt_pk4_fp8(o[2].x, o[2].y, o[3].x, o[3].y);
;                 __hip_atomic_store((unsigned long long GAS*)(act + (size_t)ro * DFF + col), ((unsigned long long)w.y << 32) | w.x, __ATOMIC_RELAXED, __HIP_MEMORY_SCOPE_AGENT);
	v_cvt_pk_fp8_f32 v78, v70, v71 op_sel:[0,0,1]
	v_cvt_pk_fp8_f32 v79, v74, v75 op_sel:[0,0,1]
	v_ashrrev_i32_e32 v77, 31, v76
	v_lshlrev_b64 v[68:69], 10, v[76:77]
	v_lshl_add_u64 v[68:69], v[150:151], 0, v[68:69]
	global_store_dwordx2 v[68:69], v[78:79], off sc1
	v_pk_fma_f32 v[68:69], v[56:57], s[34:35], v[140:141] op_sel_hi:[1,0,1]
	v_pk_fma_f32 v[70:71], v[22:23], s[34:35], v[144:145] op_sel_hi:[1,0,1]
	v_min_f32_e32 v68, v68, v34
	v_min_f32_e32 v69, v69, v34
	v_pk_mul_f32 v[72:73], s[30:31], v[68:69] op_sel_hi:[0,1]
	v_exp_f32_e32 v72, v72
	v_exp_f32_e32 v73, v73
	v_med3_f32 v70, v70, -s1, s1
	v_med3_f32 v71, v71, -s1, s1
	v_pk_fma_f32 v[70:71], s[0:1], v[70:71], s[0:1] op_sel_hi:[0,1,0]
	v_pk_add_f32 v[72:73], s[2:3], v[72:73] op_sel_hi:[0,1]
	v_rcp_f32_e32 v72, v72
	v_rcp_f32_e32 v73, v73
	s_nop 0
	v_pk_mul_f32 v[68:69], v[68:69], v[72:73]
	s_nop 0
	v_pk_mul_f32 v[68:69], v[70:71], v[68:69]
	v_pk_fma_f32 v[70:71], v[58:59], s[34:35], v[142:143] op_sel_hi:[1,0,1]
	v_pk_fma_f32 v[72:73], v[24:25], s[34:35], v[146:147] op_sel_hi:[1,0,1]
	v_min_f32_e32 v70, v70, v34
	v_min_f32_e32 v71, v71, v34
	v_pk_mul_f32 v[74:75], s[30:31], v[70:71] op_sel_hi:[0,1]
	v_exp_f32_e32 v74, v74
	v_exp_f32_e32 v75, v75
	v_med3_f32 v72, v72, -s1, s1
	v_med3_f32 v73, v73, -s1, s1
	v_pk_fma_f32 v[72:73], s[0:1], v[72:73], s[0:1] op_sel_hi:[0,1,0]
	v_pk_add_f32 v[74:75], s[2:3], v[74:75] op_sel_hi:[0,1]
	v_rcp_f32_e32 v74, v74
	v_rcp_f32_e32 v75, v75
	s_nop 0
	v_pk_mul_f32 v[70:71], v[70:71], v[74:75]
	s_nop 0
	v_pk_mul_f32 v[70:71], v[72:73], v[70:71]
	v_pk_fma_f32 v[72:73], v[236:237], s[34:35], v[132:133] op_sel_hi:[1,0,1]
	v_pk_fma_f32 v[74:75], v[18:19], s[34:35], v[136:137] op_sel_hi:[1,0,1]
	v_min_f32_e32 v72, v72, v34
	v_min_f32_e32 v73, v73, v34
	v_pk_mul_f32 v[76:77], s[30:31], v[72:73] op_sel_hi:[0,1]
	v_exp_f32_e32 v76, v76
	v_exp_f32_e32 v77, v77
	v_med3_f32 v74, v74, -s1, s1
	v_med3_f32 v75, v75, -s1, s1
	v_pk_fma_f32 v[74:75], s[0:1], v[74:75], s[0:1] op_sel_hi:[0,1,0]
	v_pk_add_f32 v[76:77], s[2:3], v[76:77] op_sel_hi:[0,1]
	v_rcp_f32_e32 v76, v76
	v_rcp_f32_e32 v77, v77
	s_nop 0
	v_pk_mul_f32 v[72:73], v[72:73], v[76:77]
	s_nop 0
	v_pk_mul_f32 v[72:73], v[74:75], v[72:73]
	v_pk_fma_f32 v[74:75], v[238:239], s[34:35], v[134:135] op_sel_hi:[1,0,1]
	v_pk_fma_f32 v[76:77], v[20:21], s[34:35], v[138:139] op_sel_hi:[1,0,1]
	v_min_f32_e32 v74, v74, v34
	v_min_f32_e32 v75, v75, v34
	v_pk_mul_f32 v[78:79], s[30:31], v[74:75] op_sel_hi:[0,1]
	v_exp_f32_e32 v78, v78
	v_exp_f32_e32 v79, v79
	v_med3_f32 v76, v76, -s1, s1
	v_med3_f32 v77, v77, -s1, s1
	v_pk_fma_f32 v[76:77], s[0:1], v[76:77], s[0:1] op_sel_hi:[0,1,0]
	v_pk_add_f32 v[78:79], s[2:3], v[78:79] op_sel_hi:[0,1]
	v_rcp_f32_e32 v78, v78
	v_rcp_f32_e32 v79, v79
	s_nop 0
	v_pk_mul_f32 v[74:75], v[74:75], v[78:79]
	v_mov_b32_e32 v78, v35
	v_mov_b32_e32 v79, v35
	v_cvt_pk_fp8_f32 v78, v68, v69
	v_cvt_pk_fp8_f32 v79, v72, v73
	v_pk_mul_f32 v[74:75], v[76:77], v[74:75]
	v_add_u32_e32 v76, 0x90, v152
	v_cvt_pk_fp8_f32 v78, v70, v71 op_sel:[0,0,1]
	v_cvt_pk_fp8_f32 v79, v74, v75 op_sel:[0,0,1]
	v_ashrrev_i32_e32 v77, 31, v76
	v_lshlrev_b64 v[68:69], 10, v[76:77]
	v_lshl_add_u64 v[68:69], v[150:151], 0, v[68:69]
	global_store_dwordx2 v[68:69], v[78:79], off sc1
	v_pk_fma_f32 v[68:69], v[48:49], s[34:35], v[140:141] op_sel_hi:[1,0,1]
	v_pk_fma_f32 v[70:71], v[14:15], s[34:35], v[144:145] op_sel_hi:[1,0,1]
	v_min_f32_e32 v68, v68, v34
	v_min_f32_e32 v69, v69, v34
	v_pk_mul_f32 v[72:73], s[30:31], v[68:69] op_sel_hi:[0,1]
	v_exp_f32_e32 v72, v72
	v_exp_f32_e32 v73, v73
	v_med3_f32 v70, v70, -s1, s1
	v_med3_f32 v71, v71, -s1, s1
	v_pk_fma_f32 v[70:71], s[0:1], v[70:71], s[0:1] op_sel_hi:[0,1,0]
	v_pk_add_f32 v[72:73], s[2:3], v[72:73] op_sel_hi:[0,1]
	v_rcp_f32_e32 v72, v72
	v_rcp_f32_e32 v73, v73
	s_nop 0
	v_pk_mul_f32 v[68:69], v[68:69], v[72:73]
	s_nop 0
	v_pk_mul_f32 v[68:69], v[70:71], v[68:69]
	v_pk_fma_f32 v[70:71], v[50:51], s[34:35], v[142:143] op_sel_hi:[1,0,1]
	v_pk_fma_f32 v[72:73], v[16:17], s[34:35], v[146:147] op_sel_hi:[1,0,1]
	v_min_f32_e32 v70, v70, v34
	v_min_f32_e32 v71, v71, v34
	v_pk_mul_f32 v[74:75], s[30:31], v[70:71] op_sel_hi:[0,1]
	v_exp_f32_e32 v74, v74
	v_exp_f32_e32 v75, v75
	v_med3_f32 v72, v72, -s1, s1
	v_med3_f32 v73, v73, -s1, s1
	v_pk_fma_f32 v[72:73], s[0:1], v[72:73], s[0:1] op_sel_hi:[0,1,0]
	v_pk_add_f32 v[74:75], s[2:3], v[74:75] op_sel_hi:[0,1]
	v_rcp_f32_e32 v74, v74
	v_rcp_f32_e32 v75, v75
	s_nop 0
	v_pk_mul_f32 v[70:71], v[70:71], v[74:75]
	s_nop 0
	v_pk_mul_f32 v[70:71], v[72:73], v[70:71]
	v_pk_fma_f32 v[72:73], v[44:45], s[34:35], v[132:133] op_sel_hi:[1,0,1]
	v_pk_fma_f32 v[74:75], v[10:11], s[34:35], v[136:137] op_sel_hi:[1,0,1]
	v_min_f32_e32 v72, v72, v34
	v_min_f32_e32 v73, v73, v34
; #define GAS __attribute__((address_space(1)))
; template <class Epi, class Src>
; __device__ __forceinline__ void gemm_phase(LAS unsigned char* lds, const Src S, const Epi E) {
;     ...
;         if (!has_next) break;
; #pragma unroll
;         for (int a = 0; a < 2; ++a)
; #pragma unroll
;             for (int b = 0; b < 2; ++b)
; #pragma unroll
;                 for (int m = 0; m < 4; ++m)
; #pragma unroll
;                     for (int n = 0; n < 2; ++n) acc[a][b][m][n] = (f32x4){0.f, 0.f, 0.f, 0.f};
;         cur = nxt; cB = nB; cA = nA; ++ui; par ^= 1;
;     __device__ __forceinline__ void operator()(const f32x4 (&acc)[2][2][4][2], const Unit& u, int wr, int wc, int fr, int fq, LAS unsigned char* lds, int par) const {
;     ...
;         for (int ai = 0; ai < 2; ++ai)
; #pragma unroll
;             for (int m = 0; m < 4; ++m) {
;                 const int r = u.rt * BM + ai * HALF + wr * 64 + m * 16 + fr;
;                 f32x2_t o[4];
; #pragma unroll
;                 for (int n = 0; n < 2; ++n)
; #pragma unroll
;                     for (int h = 0; h < 2; ++h) {
;                         const f32x4 bgv = n ? bg1 : bg0, blv = n ? bl1 : bl0;
;                         f32x2_t glu = (f32x2_t){acc[ai][0][m][n][2 * h], acc[ai][0][m][n][2 * h + 1]} * sc2 + (f32x2_t){bgv[2 * h], bgv[2 * h + 1]};
;                         f32x2_t lin = (f32x2_t){acc[ai][1][m][n][2 * h], acc[ai][1][m][n][2 * h + 1]} * sc2 + (f32x2_t){blv[2 * h], blv[2 * h + 1]};
;                         glu.x = fminf(glu.x, lim); glu.y = fminf(glu.y, lim);
;                         lin.x = __builtin_amdgcn_fmed3f(lin.x, -lim, lim); lin.y = __builtin_amdgcn_fmed3f(lin.y, -lim, lim);
;                         const f32x2_t t = glu * ke2;
;                         const f32x2_t d = (f32x2_t){__builtin_amdgcn_exp2f(t.x), __builtin_amdgcn_exp2f(t.y)} + one2;
;                         const f32x2_t rc = (f32x2_t){__builtin_amdgcn_rcpf(d.x), __builtin_amdgcn_rcpf(d.y)};
;                         o[n * 2 + h] = (glu * rc) * (lin * as2 + as2);
;                     }
;                 const int ro = u.rowbase + r;
;                 u32x2 w; w.x = cvt_pk4_fp8(o[0].x, o[0].y, o[1].x, o[1].y); w.y = cvt_pk4_fp8(o[2].x, o[2].y, o[3].x, o[3].y);
;                 __hip_atomic_store((unsigned long long GAS*)(act + (size_t)ro * DFF + col), ((unsigned long long)w.y << 32) | w.x, __ATOMIC_RELAXED, __HIP_MEMORY_SCOPE_AGENT);
	v_pk_mul_f32 v[76:77], s[30:31], v[72:73] op_sel_hi:[0,1]
	v_exp_f32_e32 v76, v76
	v_exp_f32_e32 v77, v77
	v_med3_f32 v74, v74, -s1, s1
	v_med3_f32 v75, v75, -s1, s1
	v_pk_fma_f32 v[74:75], s[0:1], v[74:75], s[0:1] op_sel_hi:[0,1,0]
	v_pk_add_f32 v[76:77], s[2:3], v[76:77] op_sel_hi:[0,1]
	v_rcp_f32_e32 v76, v76
	v_rcp_f32_e32 v77, v77
	s_nop 0
	v_pk_mul_f32 v[72:73], v[72:73], v[76:77]
	s_nop 0
	v_pk_mul_f32 v[72:73], v[74:75], v[72:73]
	v_pk_fma_f32 v[74:75], v[46:47], s[34:35], v[134:135] op_sel_hi:[1,0,1]
	v_pk_fma_f32 v[76:77], v[12:13], s[34:35], v[138:139] op_sel_hi:[1,0,1]
	v_min_f32_e32 v74, v74, v34
	v_min_f32_e32 v75, v75, v34
	v_pk_mul_f32 v[78:79], s[30:31], v[74:75] op_sel_hi:[0,1]
	v_exp_f32_e32 v78, v78
	v_exp_f32_e32 v79, v79
	v_med3_f32 v76, v76, -s1, s1
	v_med3_f32 v77, v77, -s1, s1
	v_pk_fma_f32 v[76:77], s[0:1], v[76:77], s[0:1] op_sel_hi:[0,1,0]
	v_pk_add_f32 v[78:79], s[2:3], v[78:79] op_sel_hi:[0,1]
	v_rcp_f32_e32 v78, v78
	v_rcp_f32_e32 v79, v79
	s_nop 0
	v_pk_mul_f32 v[74:75], v[74:75], v[78:79]
	v_mov_b32_e32 v78, v35
	v_mov_b32_e32 v79, v35
	v_cvt_pk_fp8_f32 v78, v68, v69
	v_cvt_pk_fp8_f32 v79, v72, v73
	v_pk_mul_f32 v[74:75], v[76:77], v[74:75]
	v_add_u32_e32 v76, 0xa0, v152
	v_cvt_pk_fp8_f32 v78, v70, v71 op_sel:[0,0,1]
	v_cvt_pk_fp8_f32 v79, v74, v75 op_sel:[0,0,1]
	v_ashrrev_i32_e32 v77, 31, v76
	v_lshlrev_b64 v[68:69], 10, v[76:77]
	v_lshl_add_u64 v[68:69], v[150:151], 0, v[68:69]
	global_store_dwordx2 v[68:69], v[78:79], off sc1
	v_pk_fma_f32 v[68:69], v[6:7], s[34:35], v[140:141] op_sel_hi:[1,0,1]
	v_pk_fma_f32 v[70:71], v[92:93], s[34:35], v[144:145] op_sel_hi:[1,0,1]
	v_min_f32_e32 v68, v68, v34
	v_min_f32_e32 v69, v69, v34
	v_pk_mul_f32 v[72:73], s[30:31], v[68:69] op_sel_hi:[0,1]
	v_exp_f32_e32 v72, v72
	v_exp_f32_e32 v73, v73
	v_med3_f32 v70, v70, -s1, s1
	v_med3_f32 v71, v71, -s1, s1
	v_pk_fma_f32 v[70:71], s[0:1], v[70:71], s[0:1] op_sel_hi:[0,1,0]
	v_pk_add_f32 v[72:73], s[2:3], v[72:73] op_sel_hi:[0,1]
	v_rcp_f32_e32 v72, v72
	v_rcp_f32_e32 v73, v73
	s_nop 0
	v_pk_mul_f32 v[68:69], v[68:69], v[72:73]
	s_nop 0
	v_pk_mul_f32 v[68:69], v[70:71], v[68:69]
	v_pk_fma_f32 v[70:71], v[8:9], s[34:35], v[142:143] op_sel_hi:[1,0,1]
	v_pk_fma_f32 v[72:73], v[94:95], s[34:35], v[146:147] op_sel_hi:[1,0,1]
	v_min_f32_e32 v70, v70, v34
	v_min_f32_e32 v71, v71, v34
	v_pk_mul_f32 v[74:75], s[30:31], v[70:71] op_sel_hi:[0,1]
	v_exp_f32_e32 v74, v74
	v_exp_f32_e32 v75, v75
	v_med3_f32 v72, v72, -s1, s1
	v_med3_f32 v73, v73, -s1, s1
	v_pk_fma_f32 v[72:73], s[0:1], v[72:73], s[0:1] op_sel_hi:[0,1,0]
	v_pk_add_f32 v[74:75], s[2:3], v[74:75] op_sel_hi:[0,1]
	v_rcp_f32_e32 v74, v74
	v_rcp_f32_e32 v75, v75
	s_nop 0
	v_pk_mul_f32 v[70:71], v[70:71], v[74:75]
	s_nop 0
	v_pk_mul_f32 v[70:71], v[72:73], v[70:71]
	v_pk_fma_f32 v[72:73], v[244:245], s[34:35], v[132:133] op_sel_hi:[1,0,1]
	v_pk_fma_f32 v[74:75], v[2:3], s[34:35], v[136:137] op_sel_hi:[1,0,1]
	v_min_f32_e32 v72, v72, v34
	v_min_f32_e32 v73, v73, v34
	v_pk_mul_f32 v[76:77], s[30:31], v[72:73] op_sel_hi:[0,1]
	v_exp_f32_e32 v76, v76
	v_exp_f32_e32 v77, v77
	v_med3_f32 v74, v74, -s1, s1
	v_med3_f32 v75, v75, -s1, s1
	v_pk_fma_f32 v[74:75], s[0:1], v[74:75], s[0:1] op_sel_hi:[0,1,0]
	v_pk_add_f32 v[76:77], s[2:3], v[76:77] op_sel_hi:[0,1]
	v_rcp_f32_e32 v76, v76
	v_rcp_f32_e32 v77, v77
	s_nop 0
	v_pk_mul_f32 v[72:73], v[72:73], v[76:77]
	s_nop 0
	v_pk_mul_f32 v[72:73], v[74:75], v[72:73]
	v_pk_fma_f32 v[74:75], v[246:247], s[34:35], v[134:135] op_sel_hi:[1,0,1]
	v_pk_fma_f32 v[76:77], v[4:5], s[34:35], v[138:139] op_sel_hi:[1,0,1]
	v_min_f32_e32 v74, v74, v34
	v_min_f32_e32 v75, v75, v34
	v_pk_mul_f32 v[78:79], s[30:31], v[74:75] op_sel_hi:[0,1]
	v_exp_f32_e32 v78, v78
	v_exp_f32_e32 v79, v79
	v_med3_f32 v76, v76, -s1, s1
	v_med3_f32 v77, v77, -s1, s1
	v_pk_fma_f32 v[76:77], s[0:1], v[76:77], s[0:1] op_sel_hi:[0,1,0]
	v_pk_add_f32 v[78:79], s[2:3], v[78:79] op_sel_hi:[0,1]
	v_rcp_f32_e32 v78, v78
	v_rcp_f32_e32 v79, v79
	s_nop 0
	v_pk_mul_f32 v[74:75], v[74:75], v[78:79]
	v_mov_b32_e32 v78, v35
	v_mov_b32_e32 v79, v35
	v_cvt_pk_fp8_f32 v78, v68, v69
	v_cvt_pk_fp8_f32 v79, v72, v73
	v_pk_mul_f32 v[74:75], v[76:77], v[74:75]
	v_add_u32_e32 v76, 0xb0, v152
	v_cvt_pk_fp8_f32 v78, v70, v71 op_sel:[0,0,1]
	v_cvt_pk_fp8_f32 v79, v74, v75 op_sel:[0,0,1]
	v_ashrrev_i32_e32 v77, 31, v76
	v_lshlrev_b64 v[68:69], 10, v[76:77]
	v_lshl_add_u64 v[68:69], v[150:151], 0, v[68:69]
	global_store_dwordx2 v[68:69], v[78:79], off sc1
	s_cbranch_vccnz .LBB0_1371
	s_mov_b32 s39, s71
	s_mov_b32 s18, s26
	s_mov_b32 s38, s70
	s_mov_b32 s16, s22
	s_mov_b32 s68, s3
	s_mov_b64 s[20:21], s[28:29]
	s_mov_b32 s57, s72
	s_xor_b64 s[0:1], s[24:25], -1
	s_andn2_b64 vcc, exec, s[0:1]
	s_cbranch_vccnz .LBB0_1372
	s_branch .LBB0_1373

;     __device__ __forceinline__ const char* bptr(const Unit& u) const { return (const char*)Bt + ((size_t)u.e * NTN * BM + (size_t)u.pn * BM) * RB; }
;     __device__ __forceinline__ const char* bptr(const Unit& u) const { return (const char*)Bt + (size_t)u.pn * BM * KD * 2; }
; template <class Epi, class Src>
; __device__ __forceinline__ void gemm_phase(LAS unsigned char* lds, const Src S, const Epi E) {
;     ...
;         const char* nB = has_next ? S.bptr(nxt) : cB;
;         const char* nA = has_next ? Ab + (size_t)(nxt.rowbase + nxt.rt * BM) * RB : cA;
.LBB0_1401:
	s_lshl_b32 s22, s66, 8
	s_add_i32 s22, s22, s67
	s_ashr_i32 s23, s22, 31
	s_lshl_b64 s[22:23], s[22:23], 10
	s_add_u32 s22, s4, s22
	s_addc_u32 s23, s5, s23
	s_and_b64 s[24:25], s[28:29], exec
	s_cselect_b32 s25, s23, s1
	s_cselect_b32 s24, s22, s0
	s_add_u32 s26, s2, 0x100
	s_addc_u32 s27, s3, 0
	v_add_u32_e32 v34, s40, v167
	ds_read_b128 v[92:95], v34
	ds_read_b128 v[96:99], v34 offset:1024
	ds_read_b128 v[100:103], v34 offset:2048
	ds_read_b128 v[104:107], v34 offset:3072
	s_add_u32 s28, s0, 0x20080
	s_addc_u32 s29, s1, 0
	s_add_u32 s70, s0, 0x30080
	s_addc_u32 s71, s1, 0
	ds_read_b128 v[40:43], v168
	ds_read_b128 v[44:47], v168 offset:1024
	ds_read_b128 v[48:51], v168 offset:2048
	ds_read_b128 v[52:55], v168 offset:3072
	ds_read_b128 v[56:59], v168 offset:4096
	ds_read_b128 v[60:63], v168 offset:5120
	ds_read_b128 v[64:67], v168 offset:6144
	ds_read_b128 v[68:71], v168 offset:7168
	s_nop 0
	v_lshl_add_u64 v[2:3], s[28:29], 0, v[164:165]
	s_add_i32 s29, s43, 0xc000
	s_mov_b32 m0, s29
	s_add_i32 s28, s43, 0xe000
	global_load_lds_dwordx4 v[2:3], off
	v_lshl_add_u64 v[2:3], s[70:71], 0, v[164:165]
	s_mov_b32 m0, s28
	s_nop 0
	global_load_lds_dwordx4 v[2:3], off
	s_waitcnt lgkmcnt(8)
	s_barrier
	s_waitcnt lgkmcnt(0)
	s_waitcnt lgkmcnt(0)
	v_mfma_scale_f32_16x16x128_f8f6f4 v[2:5], v[92:99], v[40:47], 0, v166, v166 op_sel_hi:[0,0,0]
	v_mfma_scale_f32_16x16x128_f8f6f4 v[6:9], v[100:107], v[40:47], 0, v166, v166 op_sel_hi:[0,0,0]
	v_mfma_scale_f32_16x16x128_f8f6f4 v[10:13], v[92:99], v[48:55], 0, v166, v166 op_sel_hi:[0,0,0]
	v_mfma_scale_f32_16x16x128_f8f6f4 v[14:17], v[100:107], v[48:55], 0, v166, v166 op_sel_hi:[0,0,0]
	v_mfma_scale_f32_16x16x128_f8f6f4 v[18:21], v[92:99], v[56:63], 0, v166, v166 op_sel_hi:[0,0,0]
	v_mfma_scale_f32_16x16x128_f8f6f4 v[22:25], v[100:107], v[56:63], 0, v166, v166 op_sel_hi:[0,0,0]
	v_mfma_scale_f32_16x16x128_f8f6f4 v[26:29], v[92:99], v[64:71], 0, v166, v166 op_sel_hi:[0,0,0]
	v_mfma_scale_f32_16x16x128_f8f6f4 v[30:33], v[100:107], v[64:71], 0, v166, v166 op_sel_hi:[0,0,0]
	s_barrier
	s_add_u32 s70, s2, 0x10100
	v_add_u32_e32 v169, s45, v167
	s_addc_u32 s71, s3, 0
	s_mov_b32 m0, s41
	ds_read_b128 v[124:127], v169
	ds_read_b128 v[128:131], v169 offset:1024
	ds_read_b128 v[132:135], v169 offset:2048
	ds_read_b128 v[136:139], v169 offset:3072
	s_nop 0
	v_lshl_add_u64 v[36:37], s[26:27], 0, v[164:165]
	global_load_lds_dwordx4 v[36:37], off
	v_lshl_add_u64 v[36:37], s[70:71], 0, v[164:165]
	s_mov_b32 m0, s42
	s_nop 0
	global_load_lds_dwordx4 v[36:37], off
	s_barrier
	s_waitcnt lgkmcnt(0)
	s_waitcnt lgkmcnt(0)
	v_mfma_scale_f32_16x16x128_f8f6f4 v[36:39], v[124:131], v[40:47], 0, v166, v166 op_sel_hi:[0,0,0]
	v_mfma_scale_f32_16x16x128_f8f6f4 v[40:43], v[132:139], v[40:47], 0, v166, v166 op_sel_hi:[0,0,0]
	v_mfma_scale_f32_16x16x128_f8f6f4 v[44:47], v[124:131], v[48:55], 0, v166, v166 op_sel_hi:[0,0,0]
	v_mfma_scale_f32_16x16x128_f8f6f4 v[48:51], v[132:139], v[48:55], 0, v166, v166 op_sel_hi:[0,0,0]
	v_mfma_scale_f32_16x16x128_f8f6f4 v[52:55], v[124:131], v[56:63], 0, v166, v166 op_sel_hi:[0,0,0]
	v_mfma_scale_f32_16x16x128_f8f6f4 v[56:59], v[132:139], v[56:63], 0, v166, v166 op_sel_hi:[0,0,0]
	v_mfma_scale_f32_16x16x128_f8f6f4 v[60:63], v[124:131], v[64:71], 0, v166, v166 op_sel_hi:[0,0,0]
	v_mfma_scale_f32_16x16x128_f8f6f4 v[64:67], v[132:139], v[64:71], 0, v166, v166 op_sel_hi:[0,0,0]
	s_barrier
	s_add_u32 s26, s0, 0x100
	s_addc_u32 s27, s1, 0
	s_add_u32 s70, s0, 0x10100
	s_addc_u32 s71, s1, 0
	s_mov_b32 m0, s43
	ds_read_b128 v[108:111], v168 offset:16384
	ds_read_b128 v[112:115], v168 offset:17408
	ds_read_b128 v[116:119], v168 offset:18432
	ds_read_b128 v[120:123], v168 offset:19456
	ds_read_b128 v[140:143], v168 offset:20480
	ds_read_b128 v[144:147], v168 offset:21504
	ds_read_b128 v[148:151], v168 offset:22528
	ds_read_b128 v[152:155], v168 offset:23552
	s_nop 0
	v_lshl_add_u64 v[68:69], s[26:27], 0, v[164:165]
	global_load_lds_dwordx4 v[68:69], off
	v_lshl_add_u64 v[68:69], s[70:71], 0, v[164:165]
	s_mov_b32 m0, s44
	s_nop 0
	global_load_lds_dwordx4 v[68:69], off
	s_barrier
	s_waitcnt lgkmcnt(0)
	s_waitcnt lgkmcnt(0)
	v_mfma_scale_f32_16x16x128_f8f6f4 v[68:71], v[92:99], v[108:115], 0, v166, v166 op_sel_hi:[0,0,0]
	v_mfma_scale_f32_16x16x128_f8f6f4 v[72:75], v[100:107], v[108:115], 0, v166, v166 op_sel_hi:[0,0,0]
	v_mfma_scale_f32_16x16x128_f8f6f4 v[76:79], v[92:99], v[116:123], 0, v166, v166 op_sel_hi:[0,0,0]
	v_mfma_scale_f32_16x16x128_f8f6f4 v[80:83], v[100:107], v[116:123], 0, v166, v166 op_sel_hi:[0,0,0]
	v_mfma_scale_f32_16x16x128_f8f6f4 v[84:87], v[92:99], v[140:147], 0, v166, v166 op_sel_hi:[0,0,0]
	v_mfma_scale_f32_16x16x128_f8f6f4 v[88:91], v[100:107], v[140:147], 0, v166, v166 op_sel_hi:[0,0,0]
	v_mfma_scale_f32_16x16x128_f8f6f4 v[92:95], v[92:99], v[148:155], 0, v166, v166 op_sel_hi:[0,0,0]
	v_mfma_scale_f32_16x16x128_f8f6f4 v[96:99], v[100:107], v[148:155], 0, v166, v166 op_sel_hi:[0,0,0]
	s_barrier
	s_add_u32 s26, s2, 0x20100
	s_addc_u32 s27, s3, 0
	s_add_u32 s70, s2, 0x30100
	s_addc_u32 s71, s3, 0
	s_mov_b32 m0, s46
	s_nop 0
	v_lshl_add_u64 v[100:101], s[26:27], 0, v[164:165]
	global_load_lds_dwordx4 v[100:101], off
	v_lshl_add_u64 v[100:101], s[70:71], 0, v[164:165]
	s_mov_b32 m0, s47
	s_nop 0
	global_load_lds_dwordx4 v[100:101], off
	s_waitcnt vmcnt(6)
	s_barrier
	v_mfma_scale_f32_16x16x128_f8f6f4 v[100:103], v[124:131], v[108:115], 0, v166, v166 op_sel_hi:[0,0,0]
	v_mfma_scale_f32_16x16x128_f8f6f4 v[104:107], v[132:139], v[108:115], 0, v166, v166 op_sel_hi:[0,0,0]
	v_mfma_scale_f32_16x16x128_f8f6f4 v[108:111], v[124:131], v[116:123], 0, v166, v166 op_sel_hi:[0,0,0]
	v_mfma_scale_f32_16x16x128_f8f6f4 v[112:115], v[132:139], v[116:123], 0, v166, v166 op_sel_hi:[0,0,0]
	v_mfma_scale_f32_16x16x128_f8f6f4 v[116:119], v[124:131], v[140:147], 0, v166, v166 op_sel_hi:[0,0,0]
	v_mfma_scale_f32_16x16x128_f8f6f4 v[120:123], v[132:139], v[140:147], 0, v166, v166 op_sel_hi:[0,0,0]
	v_mfma_scale_f32_16x16x128_f8f6f4 v[124:127], v[124:131], v[148:155], 0, v166, v166 op_sel_hi:[0,0,0]
	v_mfma_scale_f32_16x16x128_f8f6f4 v[128:131], v[132:139], v[148:155], 0, v166, v166 op_sel_hi:[0,0,0]
	s_barrier
	v_add_u32_e32 v170, s52, v167
	ds_read_b128 v[132:135], v170
	ds_read_b128 v[136:139], v170 offset:1024
	ds_read_b128 v[140:143], v170 offset:2048
	ds_read_b128 v[144:147], v170 offset:3072
	s_add_u32 s26, s0, 0x20100
	s_addc_u32 s27, s1, 0
	s_add_u32 s70, s0, 0x30100
	s_addc_u32 s71, s1, 0
	s_mov_b32 m0, s48
	ds_read_b128 v[148:151], v168 offset:32768
	ds_read_b128 v[152:155], v168 offset:33792
	ds_read_b128 v[156:159], v168 offset:34816
	ds_read_b128 v[160:163], v168 offset:35840
	ds_read_b128 v[172:175], v168 offset:36864
	ds_read_b128 v[176:179], v168 offset:37888
	ds_read_b128 v[180:183], v168 offset:38912
	ds_read_b128 v[184:187], v168 offset:39936
	s_nop 0
	v_lshl_add_u64 v[188:189], s[26:27], 0, v[164:165]
	global_load_lds_dwordx4 v[188:189], off
	v_lshl_add_u64 v[188:189], s[70:71], 0, v[164:165]
	s_mov_b32 m0, s49
	s_nop 0
	global_load_lds_dwordx4 v[188:189], off
	s_waitcnt lgkmcnt(8)
	s_barrier
	s_waitcnt lgkmcnt(0)
	s_waitcnt lgkmcnt(0)
	v_mfma_scale_f32_16x16x128_f8f6f4 v[2:5], v[132:139], v[148:155], v[2:5], v166, v166 op_sel_hi:[0,0,0]
	v_mfma_scale_f32_16x16x128_f8f6f4 v[6:9], v[140:147], v[148:155], v[6:9], v166, v166 op_sel_hi:[0,0,0]
	v_mfma_scale_f32_16x16x128_f8f6f4 v[10:13], v[132:139], v[156:163], v[10:13], v166, v166 op_sel_hi:[0,0,0]
	v_mfma_scale_f32_16x16x128_f8f6f4 v[14:17], v[140:147], v[156:163], v[14:17], v166, v166 op_sel_hi:[0,0,0]
	v_mfma_scale_f32_16x16x128_f8f6f4 v[18:21], v[132:139], v[172:179], v[18:21], v166, v166 op_sel_hi:[0,0,0]
	v_mfma_scale_f32_16x16x128_f8f6f4 v[22:25], v[140:147], v[172:179], v[22:25], v166, v166 op_sel_hi:[0,0,0]
	v_mfma_scale_f32_16x16x128_f8f6f4 v[26:29], v[132:139], v[180:187], v[26:29], v166, v166 op_sel_hi:[0,0,0]
	v_mfma_scale_f32_16x16x128_f8f6f4 v[30:33], v[140:147], v[180:187], v[30:33], v166, v166 op_sel_hi:[0,0,0]
	s_barrier
	s_add_u32 s26, s2, 0x180
	s_addc_u32 s27, s3, 0
	s_add_u32 s70, s2, 0x10180
	v_add_u32_e32 v171, s57, v167
	s_addc_u32 s71, s3, 0
	s_mov_b32 m0, s53
	ds_read_b128 v[188:191], v171
	ds_read_b128 v[192:195], v171 offset:1024
	ds_read_b128 v[196:199], v171 offset:2048
	ds_read_b128 v[200:203], v171 offset:3072
	s_nop 0
	v_lshl_add_u64 v[204:205], s[26:27], 0, v[164:165]
	global_load_lds_dwordx4 v[204:205], off
	v_lshl_add_u64 v[204:205], s[70:71], 0, v[164:165]
	s_mov_b32 m0, s54
	s_nop 0
	global_load_lds_dwordx4 v[204:205], off
	s_barrier
	s_waitcnt lgkmcnt(0)
	s_waitcnt lgkmcnt(0)
	v_mfma_scale_f32_16x16x128_f8f6f4 v[36:39], v[188:195], v[148:155], v[36:39], v166, v166 op_sel_hi:[0,0,0]
	v_mfma_scale_f32_16x16x128_f8f6f4 v[40:43], v[196:203], v[148:155], v[40:43], v166, v166 op_sel_hi:[0,0,0]
	v_mfma_scale_f32_16x16x128_f8f6f4 v[44:47], v[188:195], v[156:163], v[44:47], v166, v166 op_sel_hi:[0,0,0]
	v_mfma_scale_f32_16x16x128_f8f6f4 v[48:51], v[196:203], v[156:163], v[48:51], v166, v166 op_sel_hi:[0,0,0]
	v_mfma_scale_f32_16x16x128_f8f6f4 v[52:55], v[188:195], v[172:179], v[52:55], v166, v166 op_sel_hi:[0,0,0]
	v_mfma_scale_f32_16x16x128_f8f6f4 v[56:59], v[196:203], v[172:179], v[56:59], v166, v166 op_sel_hi:[0,0,0]
	v_mfma_scale_f32_16x16x128_f8f6f4 v[60:63], v[188:195], v[180:187], v[60:63], v166, v166 op_sel_hi:[0,0,0]
	v_mfma_scale_f32_16x16x128_f8f6f4 v[64:67], v[196:203], v[180:187], v[64:67], v166, v166 op_sel_hi:[0,0,0]
	s_barrier
	s_add_u32 s26, s0, 0x180
	s_addc_u32 s27, s1, 0
	s_add_u32 s70, s0, 0x10180
	s_addc_u32 s71, s1, 0
	s_mov_b32 m0, s55
	ds_read_b128 v[148:151], v168 offset:49152
	ds_read_b128 v[152:155], v168 offset:50176
	ds_read_b128 v[156:159], v168 offset:51200
	ds_read_b128 v[160:163], v168 offset:52224
	ds_read_b128 v[172:175], v168 offset:53248
	ds_read_b128 v[176:179], v168 offset:54272
	ds_read_b128 v[180:183], v168 offset:55296
	ds_read_b128 v[184:187], v168 offset:56320
	s_nop 0
	v_lshl_add_u64 v[204:205], s[26:27], 0, v[164:165]
	global_load_lds_dwordx4 v[204:205], off
	v_lshl_add_u64 v[204:205], s[70:71], 0, v[164:165]
	s_mov_b32 m0, s56
	s_nop 0
	global_load_lds_dwordx4 v[204:205], off
	s_barrier
	s_waitcnt lgkmcnt(0)
	s_waitcnt lgkmcnt(0)
	v_mfma_scale_f32_16x16x128_f8f6f4 v[68:71], v[132:139], v[148:155], v[68:71], v166, v166 op_sel_hi:[0,0,0]
	v_mfma_scale_f32_16x16x128_f8f6f4 v[72:75], v[140:147], v[148:155], v[72:75], v166, v166 op_sel_hi:[0,0,0]
	v_mfma_scale_f32_16x16x128_f8f6f4 v[76:79], v[132:139], v[156:163], v[76:79], v166, v166 op_sel_hi:[0,0,0]
	v_mfma_scale_f32_16x16x128_f8f6f4 v[80:83], v[140:147], v[156:163], v[80:83], v166, v166 op_sel_hi:[0,0,0]
	v_mfma_scale_f32_16x16x128_f8f6f4 v[84:87], v[132:139], v[172:179], v[84:87], v166, v166 op_sel_hi:[0,0,0]
	v_mfma_scale_f32_16x16x128_f8f6f4 v[88:91], v[140:147], v[172:179], v[88:91], v166, v166 op_sel_hi:[0,0,0]
	v_mfma_scale_f32_16x16x128_f8f6f4 v[92:95], v[132:139], v[180:187], v[92:95], v166, v166 op_sel_hi:[0,0,0]
	v_mfma_scale_f32_16x16x128_f8f6f4 v[96:99], v[140:147], v[180:187], v[96:99], v166, v166 op_sel_hi:[0,0,0]
	s_barrier
	s_add_u32 s26, s2, 0x20180
	s_addc_u32 s27, s3, 0
	s_add_u32 s70, s2, 0x30180
	s_addc_u32 s71, s3, 0
	s_mov_b32 m0, s58
	s_nop 0
	v_lshl_add_u64 v[132:133], s[26:27], 0, v[164:165]
	global_load_lds_dwordx4 v[132:133], off
	v_lshl_add_u64 v[132:133], s[70:71], 0, v[164:165]
	s_mov_b32 m0, s59
	s_nop 0
	global_load_lds_dwordx4 v[132:133], off
	s_waitcnt vmcnt(6)
	s_barrier
	v_mfma_scale_f32_16x16x128_f8f6f4 v[100:103], v[188:195], v[148:155], v[100:103], v166, v166 op_sel_hi:[0,0,0]
	v_mfma_scale_f32_16x16x128_f8f6f4 v[104:107], v[196:203], v[148:155], v[104:107], v166, v166 op_sel_hi:[0,0,0]
	v_mfma_scale_f32_16x16x128_f8f6f4 v[108:111], v[188:195], v[156:163], v[108:111], v166, v166 op_sel_hi:[0,0,0]
	v_mfma_scale_f32_16x16x128_f8f6f4 v[112:115], v[196:203], v[156:163], v[112:115], v166, v166 op_sel_hi:[0,0,0]
	v_mfma_scale_f32_16x16x128_f8f6f4 v[116:119], v[188:195], v[172:179], v[116:119], v166, v166 op_sel_hi:[0,0,0]
	v_mfma_scale_f32_16x16x128_f8f6f4 v[120:123], v[196:203], v[172:179], v[120:123], v166, v166 op_sel_hi:[0,0,0]
	v_mfma_scale_f32_16x16x128_f8f6f4 v[124:127], v[188:195], v[180:187], v[124:127], v166, v166 op_sel_hi:[0,0,0]
	v_mfma_scale_f32_16x16x128_f8f6f4 v[128:131], v[196:203], v[180:187], v[128:131], v166, v166 op_sel_hi:[0,0,0]
	s_add_u32 s26, s2, 0x200
	s_barrier
	s_addc_u32 s27, s3, 0
	ds_read_b128 v[132:135], v34
	ds_read_b128 v[136:139], v34 offset:1024
	ds_read_b128 v[140:143], v34 offset:2048
	ds_read_b128 v[144:147], v34 offset:3072
	s_add_u32 s70, s0, 0x20180
	s_addc_u32 s71, s1, 0
	s_add_u32 s72, s0, 0x30180
	s_addc_u32 s73, s1, 0
	s_mov_b32 m0, s29
	ds_read_b128 v[148:151], v168
	ds_read_b128 v[152:155], v168 offset:1024
	ds_read_b128 v[156:159], v168 offset:2048
	ds_read_b128 v[160:163], v168 offset:3072
	ds_read_b128 v[172:175], v168 offset:4096
	ds_read_b128 v[176:179], v168 offset:5120
	ds_read_b128 v[180:183], v168 offset:6144
	ds_read_b128 v[184:187], v168 offset:7168
	s_nop 0
	v_lshl_add_u64 v[188:189], s[70:71], 0, v[164:165]
	global_load_lds_dwordx4 v[188:189], off
	v_lshl_add_u64 v[188:189], s[72:73], 0, v[164:165]
	s_mov_b32 m0, s28
	s_nop 0
	global_load_lds_dwordx4 v[188:189], off
	s_waitcnt lgkmcnt(8)
	s_barrier
	s_waitcnt lgkmcnt(0)
	s_waitcnt lgkmcnt(0)
	v_mfma_scale_f32_16x16x128_f8f6f4 v[2:5], v[132:139], v[148:155], v[2:5], v166, v166 op_sel_hi:[0,0,0]
	v_mfma_scale_f32_16x16x128_f8f6f4 v[6:9], v[140:147], v[148:155], v[6:9], v166, v166 op_sel_hi:[0,0,0]
	v_mfma_scale_f32_16x16x128_f8f6f4 v[10:13], v[132:139], v[156:163], v[10:13], v166, v166 op_sel_hi:[0,0,0]
	v_mfma_scale_f32_16x16x128_f8f6f4 v[14:17], v[140:147], v[156:163], v[14:17], v166, v166 op_sel_hi:[0,0,0]
	v_mfma_scale_f32_16x16x128_f8f6f4 v[18:21], v[132:139], v[172:179], v[18:21], v166, v166 op_sel_hi:[0,0,0]
	v_mfma_scale_f32_16x16x128_f8f6f4 v[22:25], v[140:147], v[172:179], v[22:25], v166, v166 op_sel_hi:[0,0,0]
	v_mfma_scale_f32_16x16x128_f8f6f4 v[26:29], v[132:139], v[180:187], v[26:29], v166, v166 op_sel_hi:[0,0,0]
	v_mfma_scale_f32_16x16x128_f8f6f4 v[30:33], v[140:147], v[180:187], v[30:33], v166, v166 op_sel_hi:[0,0,0]
	s_barrier
	s_add_u32 s70, s2, 0x10200
	s_addc_u32 s71, s3, 0
	s_mov_b32 m0, s41
	ds_read_b128 v[188:191], v169
	ds_read_b128 v[192:195], v169 offset:1024
	ds_read_b128 v[196:199], v169 offset:2048
	ds_read_b128 v[200:203], v169 offset:3072
	s_nop 0
	v_lshl_add_u64 v[204:205], s[26:27], 0, v[164:165]
	global_load_lds_dwordx4 v[204:205], off
	v_lshl_add_u64 v[204:205], s[70:71], 0, v[164:165]
	s_mov_b32 m0, s42
	s_nop 0
	global_load_lds_dwordx4 v[204:205], off
	s_barrier
	s_waitcnt lgkmcnt(0)
	s_waitcnt lgkmcnt(0)
	v_mfma_scale_f32_16x16x128_f8f6f4 v[36:39], v[188:195], v[148:155], v[36:39], v166, v166 op_sel_hi:[0,0,0]
	v_mfma_scale_f32_16x16x128_f8f6f4 v[40:43], v[196:203], v[148:155], v[40:43], v166, v166 op_sel_hi:[0,0,0]
	v_mfma_scale_f32_16x16x128_f8f6f4 v[44:47], v[188:195], v[156:163], v[44:47], v166, v166 op_sel_hi:[0,0,0]
	v_mfma_scale_f32_16x16x128_f8f6f4 v[48:51], v[196:203], v[156:163], v[48:51], v166, v166 op_sel_hi:[0,0,0]
	v_mfma_scale_f32_16x16x128_f8f6f4 v[52:55], v[188:195], v[172:179], v[52:55], v166, v166 op_sel_hi:[0,0,0]
	v_mfma_scale_f32_16x16x128_f8f6f4 v[56:59], v[196:203], v[172:179], v[56:59], v166, v166 op_sel_hi:[0,0,0]
	v_mfma_scale_f32_16x16x128_f8f6f4 v[60:63], v[188:195], v[180:187], v[60:63], v166, v166 op_sel_hi:[0,0,0]
	v_mfma_scale_f32_16x16x128_f8f6f4 v[64:67], v[196:203], v[180:187], v[64:67], v166, v166 op_sel_hi:[0,0,0]
	s_barrier
	s_add_u32 s26, s0, 0x200
	s_addc_u32 s27, s1, 0
	s_add_u32 s70, s0, 0x10200
	s_addc_u32 s71, s1, 0
	s_mov_b32 m0, s43
	ds_read_b128 v[148:151], v168 offset:16384
	ds_read_b128 v[152:155], v168 offset:17408
	ds_read_b128 v[156:159], v168 offset:18432
	ds_read_b128 v[160:163], v168 offset:19456
	ds_read_b128 v[172:175], v168 offset:20480
	ds_read_b128 v[176:179], v168 offset:21504
	ds_read_b128 v[180:183], v168 offset:22528
	ds_read_b128 v[184:187], v168 offset:23552
	s_nop 0
	v_lshl_add_u64 v[204:205], s[26:27], 0, v[164:165]
	global_load_lds_dwordx4 v[204:205], off
	v_lshl_add_u64 v[204:205], s[70:71], 0, v[164:165]
	s_mov_b32 m0, s44
	s_nop 0
	global_load_lds_dwordx4 v[204:205], off
	s_barrier
	s_waitcnt lgkmcnt(0)
	s_waitcnt lgkmcnt(0)
	v_mfma_scale_f32_16x16x128_f8f6f4 v[68:71], v[132:139], v[148:155], v[68:71], v166, v166 op_sel_hi:[0,0,0]
	v_mfma_scale_f32_16x16x128_f8f6f4 v[72:75], v[140:147], v[148:155], v[72:75], v166, v166 op_sel_hi:[0,0,0]
	v_mfma_scale_f32_16x16x128_f8f6f4 v[76:79], v[132:139], v[156:163], v[76:79], v166, v166 op_sel_hi:[0,0,0]
	v_mfma_scale_f32_16x16x128_f8f6f4 v[80:83], v[140:147], v[156:163], v[80:83], v166, v166 op_sel_hi:[0,0,0]
	v_mfma_scale_f32_16x16x128_f8f6f4 v[84:87], v[132:139], v[172:179], v[84:87], v166, v166 op_sel_hi:[0,0,0]
	v_mfma_scale_f32_16x16x128_f8f6f4 v[88:91], v[140:147], v[172:179], v[88:91], v166, v166 op_sel_hi:[0,0,0]
	v_mfma_scale_f32_16x16x128_f8f6f4 v[92:95], v[132:139], v[180:187], v[92:95], v166, v166 op_sel_hi:[0,0,0]
	v_mfma_scale_f32_16x16x128_f8f6f4 v[96:99], v[140:147], v[180:187], v[96:99], v166, v166 op_sel_hi:[0,0,0]
	s_barrier
	s_add_u32 s26, s2, 0x20200
	s_addc_u32 s27, s3, 0
	s_add_u32 s70, s2, 0x30200
	s_addc_u32 s71, s3, 0
	s_mov_b32 m0, s46
	s_nop 0
	v_lshl_add_u64 v[132:133], s[26:27], 0, v[164:165]
	global_load_lds_dwordx4 v[132:133], off
	v_lshl_add_u64 v[132:133], s[70:71], 0, v[164:165]
	s_mov_b32 m0, s47
	s_nop 0
	global_load_lds_dwordx4 v[132:133], off
	s_waitcnt vmcnt(6)
	s_barrier
	v_mfma_scale_f32_16x16x128_f8f6f4 v[100:103], v[188:195], v[148:155], v[100:103], v166, v166 op_sel_hi:[0,0,0]
	v_mfma_scale_f32_16x16x128_f8f6f4 v[104:107], v[196:203], v[148:155], v[104:107], v166, v166 op_sel_hi:[0,0,0]
	v_mfma_scale_f32_16x16x128_f8f6f4 v[108:111], v[188:195], v[156:163], v[108:111], v166, v166 op_sel_hi:[0,0,0]
	v_mfma_scale_f32_16x16x128_f8f6f4 v[112:115], v[196:203], v[156:163], v[112:115], v166, v166 op_sel_hi:[0,0,0]
	v_mfma_scale_f32_16x16x128_f8f6f4 v[116:119], v[188:195], v[172:179], v[116:119], v166, v166 op_sel_hi:[0,0,0]
	v_mfma_scale_f32_16x16x128_f8f6f4 v[120:123], v[196:203], v[172:179], v[120:123], v166, v166 op_sel_hi:[0,0,0]
	v_mfma_scale_f32_16x16x128_f8f6f4 v[124:127], v[188:195], v[180:187], v[124:127], v166, v166 op_sel_hi:[0,0,0]
	v_mfma_scale_f32_16x16x128_f8f6f4 v[128:131], v[196:203], v[180:187], v[128:131], v166, v166 op_sel_hi:[0,0,0]
	s_barrier
	ds_read_b128 v[132:135], v170
	ds_read_b128 v[136:139], v170 offset:1024
	ds_read_b128 v[140:143], v170 offset:2048
	ds_read_b128 v[144:147], v170 offset:3072
	s_add_u32 s26, s0, 0x20200
	s_addc_u32 s27, s1, 0
	s_add_u32 s70, s0, 0x30200
	s_addc_u32 s71, s1, 0
	s_mov_b32 m0, s48
	ds_read_b128 v[148:151], v168 offset:32768
	ds_read_b128 v[152:155], v168 offset:33792
	ds_read_b128 v[156:159], v168 offset:34816
	ds_read_b128 v[160:163], v168 offset:35840
	ds_read_b128 v[172:175], v168 offset:36864
	ds_read_b128 v[176:179], v168 offset:37888
	ds_read_b128 v[180:183], v168 offset:38912
	ds_read_b128 v[184:187], v168 offset:39936
	s_nop 0
	v_lshl_add_u64 v[188:189], s[26:27], 0, v[164:165]
	global_load_lds_dwordx4 v[188:189], off
	v_lshl_add_u64 v[188:189], s[70:71], 0, v[164:165]
	s_mov_b32 m0, s49
	s_nop 0
	global_load_lds_dwordx4 v[188:189], off
	s_waitcnt lgkmcnt(8)
	s_barrier
	s_waitcnt lgkmcnt(0)
	s_waitcnt lgkmcnt(0)
	v_mfma_scale_f32_16x16x128_f8f6f4 v[2:5], v[132:139], v[148:155], v[2:5], v166, v166 op_sel_hi:[0,0,0]
	v_mfma_scale_f32_16x16x128_f8f6f4 v[6:9], v[140:147], v[148:155], v[6:9], v166, v166 op_sel_hi:[0,0,0]
	v_mfma_scale_f32_16x16x128_f8f6f4 v[10:13], v[132:139], v[156:163], v[10:13], v166, v166 op_sel_hi:[0,0,0]
	v_mfma_scale_f32_16x16x128_f8f6f4 v[14:17], v[140:147], v[156:163], v[14:17], v166, v166 op_sel_hi:[0,0,0]
	v_mfma_scale_f32_16x16x128_f8f6f4 v[18:21], v[132:139], v[172:179], v[18:21], v166, v166 op_sel_hi:[0,0,0]
	v_mfma_scale_f32_16x16x128_f8f6f4 v[22:25], v[140:147], v[172:179], v[22:25], v166, v166 op_sel_hi:[0,0,0]
	v_mfma_scale_f32_16x16x128_f8f6f4 v[26:29], v[132:139], v[180:187], v[26:29], v166, v166 op_sel_hi:[0,0,0]
	v_mfma_scale_f32_16x16x128_f8f6f4 v[30:33], v[140:147], v[180:187], v[30:33], v166, v166 op_sel_hi:[0,0,0]
	s_barrier
	s_add_u32 s26, s2, 0x280
	s_addc_u32 s27, s3, 0
	s_add_u32 s70, s2, 0x10280
	s_addc_u32 s71, s3, 0
	s_mov_b32 m0, s53
	ds_read_b128 v[188:191], v171
	ds_read_b128 v[192:195], v171 offset:1024
	ds_read_b128 v[196:199], v171 offset:2048
	ds_read_b128 v[200:203], v171 offset:3072
	s_nop 0
	v_lshl_add_u64 v[204:205], s[26:27], 0, v[164:165]
	global_load_lds_dwordx4 v[204:205], off
	v_lshl_add_u64 v[204:205], s[70:71], 0, v[164:165]
	s_mov_b32 m0, s54
	s_nop 0
	global_load_lds_dwordx4 v[204:205], off
	s_barrier
	s_waitcnt lgkmcnt(0)
	s_waitcnt lgkmcnt(0)
	v_mfma_scale_f32_16x16x128_f8f6f4 v[36:39], v[188:195], v[148:155], v[36:39], v166, v166 op_sel_hi:[0,0,0]
	v_mfma_scale_f32_16x16x128_f8f6f4 v[40:43], v[196:203], v[148:155], v[40:43], v166, v166 op_sel_hi:[0,0,0]
	v_mfma_scale_f32_16x16x128_f8f6f4 v[44:47], v[188:195], v[156:163], v[44:47], v166, v166 op_sel_hi:[0,0,0]
	v_mfma_scale_f32_16x16x128_f8f6f4 v[48:51], v[196:203], v[156:163], v[48:51], v166, v166 op_sel_hi:[0,0,0]
	v_mfma_scale_f32_16x16x128_f8f6f4 v[52:55], v[188:195], v[172:179], v[52:55], v166, v166 op_sel_hi:[0,0,0]
	v_mfma_scale_f32_16x16x128_f8f6f4 v[56:59], v[196:203], v[172:179], v[56:59], v166, v166 op_sel_hi:[0,0,0]
	v_mfma_scale_f32_16x16x128_f8f6f4 v[60:63], v[188:195], v[180:187], v[60:63], v166, v166 op_sel_hi:[0,0,0]
	v_mfma_scale_f32_16x16x128_f8f6f4 v[64:67], v[196:203], v[180:187], v[64:67], v166, v166 op_sel_hi:[0,0,0]
	s_barrier
	s_add_u32 s26, s0, 0x280
	s_addc_u32 s27, s1, 0
	s_add_u32 s70, s0, 0x10280
	s_addc_u32 s71, s1, 0
	s_mov_b32 m0, s55
	ds_read_b128 v[148:151], v168 offset:49152
	ds_read_b128 v[152:155], v168 offset:50176
	ds_read_b128 v[156:159], v168 offset:51200
	ds_read_b128 v[160:163], v168 offset:52224
	ds_read_b128 v[172:175], v168 offset:53248
	ds_read_b128 v[176:179], v168 offset:54272
	ds_read_b128 v[180:183], v168 offset:55296
	ds_read_b128 v[184:187], v168 offset:56320
	s_nop 0
	v_lshl_add_u64 v[204:205], s[26:27], 0, v[164:165]
	global_load_lds_dwordx4 v[204:205], off
	v_lshl_add_u64 v[204:205], s[70:71], 0, v[164:165]
	s_mov_b32 m0, s56
	s_nop 0
	global_load_lds_dwordx4 v[204:205], off
	s_barrier
	s_waitcnt lgkmcnt(0)
	s_waitcnt lgkmcnt(0)
	v_mfma_scale_f32_16x16x128_f8f6f4 v[68:71], v[132:139], v[148:155], v[68:71], v166, v166 op_sel_hi:[0,0,0]
	v_mfma_scale_f32_16x16x128_f8f6f4 v[72:75], v[140:147], v[148:155], v[72:75], v166, v166 op_sel_hi:[0,0,0]
	v_mfma_scale_f32_16x16x128_f8f6f4 v[76:79], v[132:139], v[156:163], v[76:79], v166, v166 op_sel_hi:[0,0,0]
	v_mfma_scale_f32_16x16x128_f8f6f4 v[80:83], v[140:147], v[156:163], v[80:83], v166, v166 op_sel_hi:[0,0,0]
	v_mfma_scale_f32_16x16x128_f8f6f4 v[84:87], v[132:139], v[172:179], v[84:87], v166, v166 op_sel_hi:[0,0,0]
	v_mfma_scale_f32_16x16x128_f8f6f4 v[88:91], v[140:147], v[172:179], v[88:91], v166, v166 op_sel_hi:[0,0,0]
	v_mfma_scale_f32_16x16x128_f8f6f4 v[92:95], v[132:139], v[180:187], v[92:95], v166, v166 op_sel_hi:[0,0,0]
	v_mfma_scale_f32_16x16x128_f8f6f4 v[96:99], v[140:147], v[180:187], v[96:99], v166, v166 op_sel_hi:[0,0,0]
	s_barrier
	s_add_u32 s26, s2, 0x20280
	s_addc_u32 s27, s3, 0
	s_add_u32 s70, s2, 0x30280
	s_addc_u32 s71, s3, 0
	s_mov_b32 m0, s58
	s_nop 0
	v_lshl_add_u64 v[132:133], s[26:27], 0, v[164:165]
	global_load_lds_dwordx4 v[132:133], off
	v_lshl_add_u64 v[132:133], s[70:71], 0, v[164:165]
	s_mov_b32 m0, s59
	s_nop 0
	global_load_lds_dwordx4 v[132:133], off
	s_waitcnt vmcnt(6)
	s_barrier
	v_mfma_scale_f32_16x16x128_f8f6f4 v[100:103], v[188:195], v[148:155], v[100:103], v166, v166 op_sel_hi:[0,0,0]
	v_mfma_scale_f32_16x16x128_f8f6f4 v[104:107], v[196:203], v[148:155], v[104:107], v166, v166 op_sel_hi:[0,0,0]
	v_mfma_scale_f32_16x16x128_f8f6f4 v[108:111], v[188:195], v[156:163], v[108:111], v166, v166 op_sel_hi:[0,0,0]
	v_mfma_scale_f32_16x16x128_f8f6f4 v[112:115], v[196:203], v[156:163], v[112:115], v166, v166 op_sel_hi:[0,0,0]
	v_mfma_scale_f32_16x16x128_f8f6f4 v[116:119], v[188:195], v[172:179], v[116:119], v166, v166 op_sel_hi:[0,0,0]
	v_mfma_scale_f32_16x16x128_f8f6f4 v[120:123], v[196:203], v[172:179], v[120:123], v166, v166 op_sel_hi:[0,0,0]
	v_mfma_scale_f32_16x16x128_f8f6f4 v[124:127], v[188:195], v[180:187], v[124:127], v166, v166 op_sel_hi:[0,0,0]
	v_mfma_scale_f32_16x16x128_f8f6f4 v[128:131], v[196:203], v[180:187], v[128:131], v166, v166 op_sel_hi:[0,0,0]
	s_add_u32 s26, s2, 0x300
	s_barrier
	s_addc_u32 s27, s3, 0
	ds_read_b128 v[172:175], v34
	ds_read_b128 v[176:179], v34 offset:1024
	ds_read_b128 v[180:183], v34 offset:2048
	ds_read_b128 v[184:187], v34 offset:3072
	s_add_u32 s70, s0, 0x20280
	s_addc_u32 s71, s1, 0
	s_add_u32 s72, s0, 0x30280
	s_addc_u32 s73, s1, 0
	s_mov_b32 m0, s29
	ds_read_b128 v[188:191], v168
	ds_read_b128 v[192:195], v168 offset:1024
	ds_read_b128 v[196:199], v168 offset:2048
	ds_read_b128 v[200:203], v168 offset:3072
	ds_read_b128 v[204:207], v168 offset:4096
	ds_read_b128 v[208:211], v168 offset:5120
	ds_read_b128 v[212:215], v168 offset:6144
	ds_read_b128 v[216:219], v168 offset:7168
	s_nop 0
	v_lshl_add_u64 v[132:133], s[70:71], 0, v[164:165]
	global_load_lds_dwordx4 v[132:133], off
	v_lshl_add_u64 v[132:133], s[72:73], 0, v[164:165]
	s_mov_b32 m0, s28
	s_nop 0
	global_load_lds_dwordx4 v[132:133], off
	s_waitcnt lgkmcnt(8)
	s_barrier
	s_waitcnt lgkmcnt(0)
	s_waitcnt lgkmcnt(0)
	v_mfma_scale_f32_16x16x128_f8f6f4 v[132:135], v[172:179], v[188:195], v[2:5], v166, v166 op_sel_hi:[0,0,0]
	v_mfma_scale_f32_16x16x128_f8f6f4 v[136:139], v[180:187], v[188:195], v[6:9], v166, v166 op_sel_hi:[0,0,0]
	v_mfma_scale_f32_16x16x128_f8f6f4 v[140:143], v[172:179], v[196:203], v[10:13], v166, v166 op_sel_hi:[0,0,0]
	v_mfma_scale_f32_16x16x128_f8f6f4 v[144:147], v[180:187], v[196:203], v[14:17], v166, v166 op_sel_hi:[0,0,0]
	v_mfma_scale_f32_16x16x128_f8f6f4 v[148:151], v[172:179], v[204:211], v[18:21], v166, v166 op_sel_hi:[0,0,0]
	v_mfma_scale_f32_16x16x128_f8f6f4 v[152:155], v[180:187], v[204:211], v[22:25], v166, v166 op_sel_hi:[0,0,0]
	v_mfma_scale_f32_16x16x128_f8f6f4 v[156:159], v[172:179], v[212:219], v[26:29], v166, v166 op_sel_hi:[0,0,0]
	v_mfma_scale_f32_16x16x128_f8f6f4 v[160:163], v[180:187], v[212:219], v[30:33], v166, v166 op_sel_hi:[0,0,0]
	s_barrier
	s_add_u32 s70, s2, 0x10300
	s_addc_u32 s71, s3, 0
	s_mov_b32 m0, s41
	ds_read_b128 v[220:223], v169
	ds_read_b128 v[224:227], v169 offset:1024
	ds_read_b128 v[228:231], v169 offset:2048
	ds_read_b128 v[232:235], v169 offset:3072
	s_nop 0
	v_lshl_add_u64 v[2:3], s[26:27], 0, v[164:165]
	global_load_lds_dwordx4 v[2:3], off
	v_lshl_add_u64 v[2:3], s[70:71], 0, v[164:165]
	s_mov_b32 m0, s42
	s_nop 0
	global_load_lds_dwordx4 v[2:3], off
	s_barrier
	s_waitcnt lgkmcnt(0)
	s_waitcnt lgkmcnt(0)
	v_mfma_scale_f32_16x16x128_f8f6f4 v[2:5], v[220:227], v[188:195], v[36:39], v166, v166 op_sel_hi:[0,0,0]
	v_mfma_scale_f32_16x16x128_f8f6f4 v[6:9], v[228:235], v[188:195], v[40:43], v166, v166 op_sel_hi:[0,0,0]
	v_mfma_scale_f32_16x16x128_f8f6f4 v[10:13], v[220:227], v[196:203], v[44:47], v166, v166 op_sel_hi:[0,0,0]
	v_mfma_scale_f32_16x16x128_f8f6f4 v[14:17], v[228:235], v[196:203], v[48:51], v166, v166 op_sel_hi:[0,0,0]
	v_mfma_scale_f32_16x16x128_f8f6f4 v[18:21], v[220:227], v[204:211], v[52:55], v166, v166 op_sel_hi:[0,0,0]
	v_mfma_scale_f32_16x16x128_f8f6f4 v[22:25], v[228:235], v[204:211], v[56:59], v166, v166 op_sel_hi:[0,0,0]
	v_mfma_scale_f32_16x16x128_f8f6f4 v[26:29], v[220:227], v[212:219], v[60:63], v166, v166 op_sel_hi:[0,0,0]
	v_mfma_scale_f32_16x16x128_f8f6f4 v[30:33], v[228:235], v[212:219], v[64:67], v166, v166 op_sel_hi:[0,0,0]
	s_barrier
	s_add_u32 s26, s0, 0x300
	s_addc_u32 s27, s1, 0
	s_add_u32 s70, s0, 0x10300
	s_addc_u32 s71, s1, 0
	s_mov_b32 m0, s43
	ds_read_b128 v[188:191], v168 offset:16384
	ds_read_b128 v[192:195], v168 offset:17408
	ds_read_b128 v[196:199], v168 offset:18432
	ds_read_b128 v[200:203], v168 offset:19456
	ds_read_b128 v[204:207], v168 offset:20480
	ds_read_b128 v[208:211], v168 offset:21504
	ds_read_b128 v[212:215], v168 offset:22528
	ds_read_b128 v[216:219], v168 offset:23552
	s_nop 0
	v_lshl_add_u64 v[36:37], s[26:27], 0, v[164:165]
	global_load_lds_dwordx4 v[36:37], off
	v_lshl_add_u64 v[36:37], s[70:71], 0, v[164:165]
	s_mov_b32 m0, s44
	s_nop 0
	global_load_lds_dwordx4 v[36:37], off
	s_barrier
	s_waitcnt lgkmcnt(0)
	s_waitcnt lgkmcnt(0)
	v_mfma_scale_f32_16x16x128_f8f6f4 v[36:39], v[172:179], v[188:195], v[68:71], v166, v166 op_sel_hi:[0,0,0]
	v_mfma_scale_f32_16x16x128_f8f6f4 v[40:43], v[180:187], v[188:195], v[72:75], v166, v166 op_sel_hi:[0,0,0]
	v_mfma_scale_f32_16x16x128_f8f6f4 v[44:47], v[172:179], v[196:203], v[76:79], v166, v166 op_sel_hi:[0,0,0]
	v_mfma_scale_f32_16x16x128_f8f6f4 v[48:51], v[180:187], v[196:203], v[80:83], v166, v166 op_sel_hi:[0,0,0]
	v_mfma_scale_f32_16x16x128_f8f6f4 v[52:55], v[172:179], v[204:211], v[84:87], v166, v166 op_sel_hi:[0,0,0]
	v_mfma_scale_f32_16x16x128_f8f6f4 v[56:59], v[180:187], v[204:211], v[88:91], v166, v166 op_sel_hi:[0,0,0]
	v_mfma_scale_f32_16x16x128_f8f6f4 v[60:63], v[172:179], v[212:219], v[92:95], v166, v166 op_sel_hi:[0,0,0]
	v_mfma_scale_f32_16x16x128_f8f6f4 v[64:67], v[180:187], v[212:219], v[96:99], v166, v166 op_sel_hi:[0,0,0]
	s_barrier
	s_add_u32 s26, s2, 0x20300
	s_addc_u32 s27, s3, 0
	s_add_u32 s70, s2, 0x30300
	s_addc_u32 s71, s3, 0
	s_mov_b32 m0, s46
	s_nop 0
	v_lshl_add_u64 v[68:69], s[26:27], 0, v[164:165]
	global_load_lds_dwordx4 v[68:69], off
	v_lshl_add_u64 v[68:69], s[70:71], 0, v[164:165]
	s_mov_b32 m0, s47
	s_nop 0
	global_load_lds_dwordx4 v[68:69], off
	s_waitcnt vmcnt(6)
	s_barrier
	v_mfma_scale_f32_16x16x128_f8f6f4 v[68:71], v[220:227], v[188:195], v[100:103], v166, v166 op_sel_hi:[0,0,0]
	v_mfma_scale_f32_16x16x128_f8f6f4 v[72:75], v[228:235], v[188:195], v[104:107], v166, v166 op_sel_hi:[0,0,0]
	v_mfma_scale_f32_16x16x128_f8f6f4 v[76:79], v[220:227], v[196:203], v[108:111], v166, v166 op_sel_hi:[0,0,0]
	v_mfma_scale_f32_16x16x128_f8f6f4 v[80:83], v[228:235], v[196:203], v[112:115], v166, v166 op_sel_hi:[0,0,0]
	v_mfma_scale_f32_16x16x128_f8f6f4 v[84:87], v[220:227], v[204:211], v[116:119], v166, v166 op_sel_hi:[0,0,0]
	v_mfma_scale_f32_16x16x128_f8f6f4 v[88:91], v[228:235], v[204:211], v[120:123], v166, v166 op_sel_hi:[0,0,0]
	v_mfma_scale_f32_16x16x128_f8f6f4 v[92:95], v[220:227], v[212:219], v[124:127], v166, v166 op_sel_hi:[0,0,0]
	v_mfma_scale_f32_16x16x128_f8f6f4 v[96:99], v[228:235], v[212:219], v[128:131], v166, v166 op_sel_hi:[0,0,0]
	s_barrier
	ds_read_b128 v[172:175], v170
	ds_read_b128 v[176:179], v170 offset:1024
	ds_read_b128 v[180:183], v170 offset:2048
	ds_read_b128 v[184:187], v170 offset:3072
	s_add_u32 s26, s0, 0x20300
	s_addc_u32 s27, s1, 0
	s_add_u32 s70, s0, 0x30300
	s_addc_u32 s71, s1, 0
	s_mov_b32 m0, s48
	ds_read_b128 v[188:191], v168 offset:32768
	ds_read_b128 v[192:195], v168 offset:33792
	ds_read_b128 v[196:199], v168 offset:34816
	ds_read_b128 v[200:203], v168 offset:35840
	ds_read_b128 v[204:207], v168 offset:36864
	ds_read_b128 v[208:211], v168 offset:37888
	ds_read_b128 v[212:215], v168 offset:38912
	ds_read_b128 v[216:219], v168 offset:39936
	s_nop 0
	v_lshl_add_u64 v[100:101], s[26:27], 0, v[164:165]
	global_load_lds_dwordx4 v[100:101], off
	v_lshl_add_u64 v[100:101], s[70:71], 0, v[164:165]
	s_mov_b32 m0, s49
	s_nop 0
	global_load_lds_dwordx4 v[100:101], off
	s_waitcnt lgkmcnt(8)
	s_barrier
	s_waitcnt lgkmcnt(0)
	s_waitcnt lgkmcnt(0)
	v_mfma_scale_f32_16x16x128_f8f6f4 v[100:103], v[172:179], v[188:195], v[132:135], v166, v166 op_sel_hi:[0,0,0]
	v_mfma_scale_f32_16x16x128_f8f6f4 v[104:107], v[180:187], v[188:195], v[136:139], v166, v166 op_sel_hi:[0,0,0]
	v_mfma_scale_f32_16x16x128_f8f6f4 v[108:111], v[172:179], v[196:203], v[140:143], v166, v166 op_sel_hi:[0,0,0]
	v_mfma_scale_f32_16x16x128_f8f6f4 v[112:115], v[180:187], v[196:203], v[144:147], v166, v166 op_sel_hi:[0,0,0]
	v_mfma_scale_f32_16x16x128_f8f6f4 v[116:119], v[172:179], v[204:211], v[148:151], v166, v166 op_sel_hi:[0,0,0]
	v_mfma_scale_f32_16x16x128_f8f6f4 v[120:123], v[180:187], v[204:211], v[152:155], v166, v166 op_sel_hi:[0,0,0]
	v_mfma_scale_f32_16x16x128_f8f6f4 v[124:127], v[172:179], v[212:219], v[156:159], v166, v166 op_sel_hi:[0,0,0]
	v_mfma_scale_f32_16x16x128_f8f6f4 v[128:131], v[180:187], v[212:219], v[160:163], v166, v166 op_sel_hi:[0,0,0]
	s_barrier
; template <class Epi, class Src>
; __device__ __forceinline__ void gemm_phase(LAS unsigned char* lds, const Src S, const Epi E) {
;     ...
;         {
;             const int par2 = has_next ? (par ^ 1) : par;
;             const char* b3 = nB + kstep;
;             G8_ITER(cA, par, (size_t)(NKTR - 1) * kstep, nA, par2, (size_t)0, nB, b3);
;         }
	s_add_u32 s26, s2, 0x380
	s_addc_u32 s27, s3, 0
	s_add_u32 s70, s2, 0x10380
	s_addc_u32 s71, s3, 0
	s_mov_b32 m0, s53
	ds_read_b128 v[132:135], v171
	ds_read_b128 v[136:139], v171 offset:1024
	ds_read_b128 v[140:143], v171 offset:2048
	ds_read_b128 v[144:147], v171 offset:3072
	s_nop 0
	v_lshl_add_u64 v[148:149], s[26:27], 0, v[164:165]
	global_load_lds_dwordx4 v[148:149], off
	v_lshl_add_u64 v[148:149], s[70:71], 0, v[164:165]
	s_mov_b32 m0, s54
	s_nop 0
	global_load_lds_dwordx4 v[148:149], off
	s_barrier
	s_waitcnt lgkmcnt(0)
	s_waitcnt lgkmcnt(0)
	v_mfma_scale_f32_16x16x128_f8f6f4 v[2:5], v[132:139], v[188:195], v[2:5], v166, v166 op_sel_hi:[0,0,0]
	v_mfma_scale_f32_16x16x128_f8f6f4 v[6:9], v[140:147], v[188:195], v[6:9], v166, v166 op_sel_hi:[0,0,0]
	v_mfma_scale_f32_16x16x128_f8f6f4 v[10:13], v[132:139], v[196:203], v[10:13], v166, v166 op_sel_hi:[0,0,0]
	v_mfma_scale_f32_16x16x128_f8f6f4 v[14:17], v[140:147], v[196:203], v[14:17], v166, v166 op_sel_hi:[0,0,0]
	v_mfma_scale_f32_16x16x128_f8f6f4 v[18:21], v[132:139], v[204:211], v[18:21], v166, v166 op_sel_hi:[0,0,0]
	v_mfma_scale_f32_16x16x128_f8f6f4 v[22:25], v[140:147], v[204:211], v[22:25], v166, v166 op_sel_hi:[0,0,0]
	v_mfma_scale_f32_16x16x128_f8f6f4 v[26:29], v[132:139], v[212:219], v[26:29], v166, v166 op_sel_hi:[0,0,0]
	v_mfma_scale_f32_16x16x128_f8f6f4 v[30:33], v[140:147], v[212:219], v[30:33], v166, v166 op_sel_hi:[0,0,0]
	s_barrier
	s_add_u32 s26, s0, 0x380
	s_addc_u32 s27, s1, 0
	s_add_u32 s70, s0, 0x10380
	s_addc_u32 s71, s1, 0
	s_mov_b32 m0, s55
	ds_read_b128 v[148:151], v168 offset:49152
	ds_read_b128 v[152:155], v168 offset:50176
	ds_read_b128 v[156:159], v168 offset:51200
	ds_read_b128 v[160:163], v168 offset:52224
	ds_read_b128 v[188:191], v168 offset:53248
	ds_read_b128 v[192:195], v168 offset:54272
	ds_read_b128 v[196:199], v168 offset:55296
	ds_read_b128 v[200:203], v168 offset:56320
	s_nop 0
	v_lshl_add_u64 v[204:205], s[26:27], 0, v[164:165]
	global_load_lds_dwordx4 v[204:205], off
	v_lshl_add_u64 v[204:205], s[70:71], 0, v[164:165]
	s_mov_b32 m0, s56
	s_nop 0
	global_load_lds_dwordx4 v[204:205], off
	s_barrier
	s_waitcnt lgkmcnt(0)
	s_waitcnt lgkmcnt(0)
	v_mfma_scale_f32_16x16x128_f8f6f4 v[204:207], v[172:179], v[148:155], v[36:39], v166, v166 op_sel_hi:[0,0,0]
	v_mfma_scale_f32_16x16x128_f8f6f4 v[208:211], v[180:187], v[148:155], v[40:43], v166, v166 op_sel_hi:[0,0,0]
	v_mfma_scale_f32_16x16x128_f8f6f4 v[212:215], v[172:179], v[156:163], v[44:47], v166, v166 op_sel_hi:[0,0,0]
	v_mfma_scale_f32_16x16x128_f8f6f4 v[216:219], v[180:187], v[156:163], v[48:51], v166, v166 op_sel_hi:[0,0,0]
	v_mfma_scale_f32_16x16x128_f8f6f4 v[220:223], v[172:179], v[188:195], v[52:55], v166, v166 op_sel_hi:[0,0,0]
	v_mfma_scale_f32_16x16x128_f8f6f4 v[224:227], v[180:187], v[188:195], v[56:59], v166, v166 op_sel_hi:[0,0,0]
	v_mfma_scale_f32_16x16x128_f8f6f4 v[172:175], v[172:179], v[196:203], v[60:63], v166, v166 op_sel_hi:[0,0,0]
	v_mfma_scale_f32_16x16x128_f8f6f4 v[176:179], v[180:187], v[196:203], v[64:67], v166, v166 op_sel_hi:[0,0,0]
	s_barrier
	s_add_u32 s26, s2, 0x20380
	s_addc_u32 s27, s3, 0
	s_add_u32 s2, s2, 0x30380
	s_addc_u32 s3, s3, 0
	s_mov_b32 m0, s58
	s_nop 0
	v_lshl_add_u64 v[36:37], s[26:27], 0, v[164:165]
	global_load_lds_dwordx4 v[36:37], off
	v_lshl_add_u64 v[36:37], s[2:3], 0, v[164:165]
	s_mov_b32 m0, s59
	s_nop 0
	global_load_lds_dwordx4 v[36:37], off
	s_waitcnt vmcnt(6)
	s_barrier
	v_mfma_scale_f32_16x16x128_f8f6f4 v[180:183], v[132:139], v[148:155], v[68:71], v166, v166 op_sel_hi:[0,0,0]
	v_mfma_scale_f32_16x16x128_f8f6f4 v[152:155], v[140:147], v[148:155], v[72:75], v166, v166 op_sel_hi:[0,0,0]
	v_mfma_scale_f32_16x16x128_f8f6f4 v[184:187], v[132:139], v[156:163], v[76:79], v166, v166 op_sel_hi:[0,0,0]
	v_mfma_scale_f32_16x16x128_f8f6f4 v[156:159], v[140:147], v[156:163], v[80:83], v166, v166 op_sel_hi:[0,0,0]
	v_mfma_scale_f32_16x16x128_f8f6f4 v[160:163], v[132:139], v[188:195], v[84:87], v166, v166 op_sel_hi:[0,0,0]
	v_mfma_scale_f32_16x16x128_f8f6f4 v[188:191], v[140:147], v[188:195], v[88:91], v166, v166 op_sel_hi:[0,0,0]
	v_mfma_scale_f32_16x16x128_f8f6f4 v[192:195], v[132:139], v[196:203], v[92:95], v166, v166 op_sel_hi:[0,0,0]
	v_mfma_scale_f32_16x16x128_f8f6f4 v[196:199], v[140:147], v[196:203], v[96:99], v166, v166 op_sel_hi:[0,0,0]
	s_barrier
	ds_read_b128 v[36:39], v34
	ds_read_b128 v[40:43], v34 offset:1024
	ds_read_b128 v[44:47], v34 offset:2048
	ds_read_b128 v[48:51], v34 offset:3072
	s_add_u32 s2, s0, 0x20380
	s_addc_u32 s3, s1, 0
	s_add_u32 s0, s0, 0x30380
	s_addc_u32 s1, s1, 0
	s_mov_b32 m0, s29
	ds_read_b128 v[56:59], v168
	ds_read_b128 v[60:63], v168 offset:1024
	ds_read_b128 v[64:67], v168 offset:2048
	ds_read_b128 v[68:71], v168 offset:3072
	ds_read_b128 v[72:75], v168 offset:4096
	ds_read_b128 v[76:79], v168 offset:5120
	ds_read_b128 v[80:83], v168 offset:6144
	ds_read_b128 v[84:87], v168 offset:7168
	s_nop 0
	v_lshl_add_u64 v[52:53], s[2:3], 0, v[164:165]
	global_load_lds_dwordx4 v[52:53], off
	v_lshl_add_u64 v[52:53], s[0:1], 0, v[164:165]
	s_mov_b32 m0, s28
	s_nop 0
	global_load_lds_dwordx4 v[52:53], off
	s_waitcnt lgkmcnt(8)
	s_barrier
	s_waitcnt lgkmcnt(0)
	s_waitcnt lgkmcnt(0)
	v_mfma_scale_f32_16x16x128_f8f6f4 v[200:203], v[36:43], v[56:63], v[100:103], v166, v166 op_sel_hi:[0,0,0]
	v_mfma_scale_f32_16x16x128_f8f6f4 v[228:231], v[44:51], v[56:63], v[104:107], v166, v166 op_sel_hi:[0,0,0]
	v_mfma_scale_f32_16x16x128_f8f6f4 v[232:235], v[36:43], v[64:71], v[108:111], v166, v166 op_sel_hi:[0,0,0]
	v_mfma_scale_f32_16x16x128_f8f6f4 v[236:239], v[44:51], v[64:71], v[112:115], v166, v166 op_sel_hi:[0,0,0]
	v_mfma_scale_f32_16x16x128_f8f6f4 v[240:243], v[36:43], v[72:79], v[116:119], v166, v166 op_sel_hi:[0,0,0]
	v_mfma_scale_f32_16x16x128_f8f6f4 v[244:247], v[44:51], v[72:79], v[120:123], v166, v166 op_sel_hi:[0,0,0]
	v_mfma_scale_f32_16x16x128_f8f6f4 v[248:251], v[36:43], v[80:87], v[124:127], v166, v166 op_sel_hi:[0,0,0]
	v_mfma_scale_f32_16x16x128_f8f6f4 v[88:91], v[44:51], v[80:87], v[128:131], v166, v166 op_sel_hi:[0,0,0]
	s_barrier
; template <class Epi, class Src>
; __device__ __forceinline__ void gemm_phase(LAS unsigned char* lds, const Src S, const Epi E) {
;     ...
;         {
;             const int par2 = has_next ? (par ^ 1) : par;
;             const char* b3 = nB + kstep;
;             G8_ITER(cA, par, (size_t)(NKTR - 1) * kstep, nA, par2, (size_t)0, nB, b3);
;         }
	s_add_u32 s0, s18, 0x10000
	s_addc_u32 s1, s19, 0
	s_mov_b64 s[2:3], s[18:19]
	s_mov_b32 m0, s41
	ds_read_b128 v[120:123], v169
	ds_read_b128 v[124:127], v169 offset:1024
	ds_read_b128 v[128:131], v169 offset:2048
	ds_read_b128 v[132:135], v169 offset:3072
	s_nop 0
	v_lshl_add_u64 v[52:53], s[2:3], 0, v[164:165]
	global_load_lds_dwordx4 v[52:53], off
	v_lshl_add_u64 v[52:53], s[0:1], 0, v[164:165]
	s_mov_b32 m0, s42
	s_nop 0
	global_load_lds_dwordx4 v[52:53], off
	s_barrier
	s_waitcnt lgkmcnt(0)
	s_waitcnt lgkmcnt(0)
	v_mfma_scale_f32_16x16x128_f8f6f4 v[52:55], v[120:127], v[56:63], v[2:5], v166, v166 op_sel_hi:[0,0,0]
	v_mfma_scale_f32_16x16x128_f8f6f4 v[56:59], v[128:135], v[56:63], v[6:9], v166, v166 op_sel_hi:[0,0,0]
	v_mfma_scale_f32_16x16x128_f8f6f4 v[60:63], v[120:127], v[64:71], v[10:13], v166, v166 op_sel_hi:[0,0,0]
	v_mfma_scale_f32_16x16x128_f8f6f4 v[64:67], v[128:135], v[64:71], v[14:17], v166, v166 op_sel_hi:[0,0,0]
	v_mfma_scale_f32_16x16x128_f8f6f4 v[68:71], v[120:127], v[72:79], v[18:21], v166, v166 op_sel_hi:[0,0,0]
	v_mfma_scale_f32_16x16x128_f8f6f4 v[92:95], v[128:135], v[72:79], v[22:25], v166, v166 op_sel_hi:[0,0,0]
	v_mfma_scale_f32_16x16x128_f8f6f4 v[26:29], v[120:127], v[80:87], v[26:29], v166, v166 op_sel_hi:[0,0,0]
	v_mfma_scale_f32_16x16x128_f8f6f4 v[30:33], v[128:135], v[80:87], v[30:33], v166, v166 op_sel_hi:[0,0,0]
	s_barrier
	s_add_u32 s0, s24, 0x10000
	s_addc_u32 s1, s25, 0
	s_mov_b64 s[2:3], s[24:25]
	s_mov_b32 m0, s43
	ds_read_b128 v[72:75], v168 offset:16384
	ds_read_b128 v[76:79], v168 offset:17408
	ds_read_b128 v[108:111], v168 offset:18432
	ds_read_b128 v[112:115], v168 offset:19456
	ds_read_b128 v[136:139], v168 offset:20480
	ds_read_b128 v[140:143], v168 offset:21504
	ds_read_b128 v[144:147], v168 offset:22528
	ds_read_b128 v[148:151], v168 offset:23552
	s_nop 0
	v_lshl_add_u64 v[2:3], s[2:3], 0, v[164:165]
	global_load_lds_dwordx4 v[2:3], off
	v_lshl_add_u64 v[2:3], s[0:1], 0, v[164:165]
	s_mov_b32 m0, s44
	s_nop 0
	global_load_lds_dwordx4 v[2:3], off
	s_barrier
	s_waitcnt lgkmcnt(0)
	s_waitcnt lgkmcnt(0)
	v_mfma_scale_f32_16x16x128_f8f6f4 v[2:5], v[36:43], v[72:79], v[204:207], v166, v166 op_sel_hi:[0,0,0]
	v_mfma_scale_f32_16x16x128_f8f6f4 v[6:9], v[44:51], v[72:79], v[208:211], v166, v166 op_sel_hi:[0,0,0]
	v_mfma_scale_f32_16x16x128_f8f6f4 v[10:13], v[36:43], v[108:115], v[212:215], v166, v166 op_sel_hi:[0,0,0]
	v_mfma_scale_f32_16x16x128_f8f6f4 v[14:17], v[44:51], v[108:115], v[216:219], v166, v166 op_sel_hi:[0,0,0]
	v_mfma_scale_f32_16x16x128_f8f6f4 v[18:21], v[36:43], v[136:143], v[220:223], v166, v166 op_sel_hi:[0,0,0]
	v_mfma_scale_f32_16x16x128_f8f6f4 v[22:25], v[44:51], v[136:143], v[224:227], v166, v166 op_sel_hi:[0,0,0]
	v_mfma_scale_f32_16x16x128_f8f6f4 v[84:87], v[36:43], v[144:151], v[172:175], v166, v166 op_sel_hi:[0,0,0]
	v_mfma_scale_f32_16x16x128_f8f6f4 v[204:207], v[44:51], v[144:151], v[176:179], v166, v166 op_sel_hi:[0,0,0]
	s_barrier
	s_add_u32 s0, s18, 0x20000
	s_addc_u32 s1, s19, 0
	s_add_u32 s2, s18, 0x30000
	s_addc_u32 s3, s19, 0
	s_mov_b32 m0, s46
	s_nop 0
	v_lshl_add_u64 v[36:37], s[0:1], 0, v[164:165]
	global_load_lds_dwordx4 v[36:37], off
	v_lshl_add_u64 v[36:37], s[2:3], 0, v[164:165]
	s_mov_b32 m0, s47
	s_nop 0
	global_load_lds_dwordx4 v[36:37], off
	s_waitcnt vmcnt(6)
	s_barrier
	v_mfma_scale_f32_16x16x128_f8f6f4 v[96:99], v[120:127], v[72:79], v[180:183], v166, v166 op_sel_hi:[0,0,0]
	v_mfma_scale_f32_16x16x128_f8f6f4 v[100:103], v[128:135], v[72:79], v[152:155], v166, v166 op_sel_hi:[0,0,0]
	v_mfma_scale_f32_16x16x128_f8f6f4 v[104:107], v[120:127], v[108:115], v[184:187], v166, v166 op_sel_hi:[0,0,0]
	v_mfma_scale_f32_16x16x128_f8f6f4 v[108:111], v[128:135], v[108:115], v[156:159], v166, v166 op_sel_hi:[0,0,0]
	v_mfma_scale_f32_16x16x128_f8f6f4 v[112:115], v[120:127], v[136:143], v[160:163], v166, v166 op_sel_hi:[0,0,0]
	v_mfma_scale_f32_16x16x128_f8f6f4 v[116:119], v[128:135], v[136:143], v[188:191], v166, v166 op_sel_hi:[0,0,0]
	v_mfma_scale_f32_16x16x128_f8f6f4 v[120:123], v[120:127], v[144:151], v[192:195], v166, v166 op_sel_hi:[0,0,0]
	v_mfma_scale_f32_16x16x128_f8f6f4 v[124:127], v[128:135], v[144:151], v[196:199], v166, v166 op_sel_hi:[0,0,0]
	s_barrier
	ds_read_b128 v[132:135], v170
	ds_read_b128 v[136:139], v170 offset:1024
	ds_read_b128 v[140:143], v170 offset:2048
	ds_read_b128 v[144:147], v170 offset:3072
	s_add_u32 s0, s24, 0x20000
	s_addc_u32 s1, s25, 0
	s_add_u32 s2, s24, 0x30000
	s_addc_u32 s3, s25, 0
	s_mov_b32 m0, s48
	ds_read_b128 v[148:151], v168 offset:32768
	ds_read_b128 v[152:155], v168 offset:33792
	ds_read_b128 v[156:159], v168 offset:34816
	ds_read_b128 v[160:163], v168 offset:35840
	ds_read_b128 v[172:175], v168 offset:36864
	ds_read_b128 v[176:179], v168 offset:37888
	ds_read_b128 v[180:183], v168 offset:38912
	ds_read_b128 v[184:187], v168 offset:39936
	s_nop 0
	v_lshl_add_u64 v[36:37], s[0:1], 0, v[164:165]
	global_load_lds_dwordx4 v[36:37], off
	v_lshl_add_u64 v[36:37], s[2:3], 0, v[164:165]
	s_mov_b32 m0, s49
	s_nop 0
	global_load_lds_dwordx4 v[36:37], off
	s_waitcnt lgkmcnt(8)
	s_barrier
	s_waitcnt lgkmcnt(0)
	s_waitcnt lgkmcnt(0)
	v_mfma_scale_f32_16x16x128_f8f6f4 v[208:211], v[132:139], v[148:155], v[200:203], v166, v166 op_sel_hi:[0,0,0]
	v_mfma_scale_f32_16x16x128_f8f6f4 v[212:215], v[140:147], v[148:155], v[228:231], v166, v166 op_sel_hi:[0,0,0]
	v_mfma_scale_f32_16x16x128_f8f6f4 v[80:83], v[132:139], v[156:163], v[232:235], v166, v166 op_sel_hi:[0,0,0]
	v_mfma_scale_f32_16x16x128_f8f6f4 v[72:75], v[140:147], v[156:163], v[236:239], v166, v166 op_sel_hi:[0,0,0]
	v_mfma_scale_f32_16x16x128_f8f6f4 v[48:51], v[132:139], v[172:179], v[240:243], v166, v166 op_sel_hi:[0,0,0]
	v_mfma_scale_f32_16x16x128_f8f6f4 v[44:47], v[140:147], v[172:179], v[244:247], v166, v166 op_sel_hi:[0,0,0]
	v_mfma_scale_f32_16x16x128_f8f6f4 v[40:43], v[132:139], v[180:187], v[248:251], v166, v166 op_sel_hi:[0,0,0]
	v_mfma_scale_f32_16x16x128_f8f6f4 v[36:39], v[140:147], v[180:187], v[88:91], v166, v166 op_sel_hi:[0,0,0]
	s_barrier
	s_add_u32 s0, s18, 0x80
	s_addc_u32 s1, s19, 0
	s_add_u32 s2, s18, 0x10080
	s_addc_u32 s3, s19, 0
	s_mov_b32 m0, s53
	ds_read_b128 v[188:191], v171
	ds_read_b128 v[192:195], v171 offset:1024
	ds_read_b128 v[196:199], v171 offset:2048
	ds_read_b128 v[200:203], v171 offset:3072
	s_nop 0
	v_lshl_add_u64 v[76:77], s[0:1], 0, v[164:165]
	global_load_lds_dwordx4 v[76:77], off
	v_lshl_add_u64 v[76:77], s[2:3], 0, v[164:165]
	s_mov_b32 m0, s54
	s_nop 0
	global_load_lds_dwordx4 v[76:77], off
	s_barrier
	s_waitcnt lgkmcnt(0)
	s_waitcnt lgkmcnt(0)
	v_mfma_scale_f32_16x16x128_f8f6f4 v[216:219], v[188:195], v[148:155], v[52:55], v166, v166 op_sel_hi:[0,0,0]
	v_mfma_scale_f32_16x16x128_f8f6f4 v[220:223], v[196:203], v[148:155], v[56:59], v166, v166 op_sel_hi:[0,0,0]
	v_mfma_scale_f32_16x16x128_f8f6f4 v[224:227], v[188:195], v[156:163], v[60:63], v166, v166 op_sel_hi:[0,0,0]
	v_mfma_scale_f32_16x16x128_f8f6f4 v[228:231], v[196:203], v[156:163], v[64:67], v166, v166 op_sel_hi:[0,0,0]
	v_mfma_scale_f32_16x16x128_f8f6f4 v[76:79], v[188:195], v[172:179], v[68:71], v166, v166 op_sel_hi:[0,0,0]
	v_mfma_scale_f32_16x16x128_f8f6f4 v[68:71], v[196:203], v[172:179], v[92:95], v166, v166 op_sel_hi:[0,0,0]
	v_mfma_scale_f32_16x16x128_f8f6f4 v[56:59], v[188:195], v[180:187], v[26:29], v166, v166 op_sel_hi:[0,0,0]
	v_mfma_scale_f32_16x16x128_f8f6f4 v[52:55], v[196:203], v[180:187], v[30:33], v166, v166 op_sel_hi:[0,0,0]
	s_barrier
	s_add_u32 s0, s24, 0x80
	s_addc_u32 s1, s25, 0
	s_add_u32 s2, s24, 0x10080
	s_addc_u32 s3, s25, 0
	s_mov_b32 m0, s55
	ds_read_b128 v[148:151], v168 offset:49152
	ds_read_b128 v[152:155], v168 offset:50176
	ds_read_b128 v[156:159], v168 offset:51200
	ds_read_b128 v[160:163], v168 offset:52224
	ds_read_b128 v[170:173], v168 offset:53248
	ds_read_b128 v[174:177], v168 offset:54272
	ds_read_b128 v[178:181], v168 offset:55296
	ds_read_b128 v[182:185], v168 offset:56320
	s_nop 0
	v_lshl_add_u64 v[26:27], s[0:1], 0, v[164:165]
	global_load_lds_dwordx4 v[26:27], off
	v_lshl_add_u64 v[26:27], s[2:3], 0, v[164:165]
	s_mov_b32 m0, s56
	s_nop 0
	global_load_lds_dwordx4 v[26:27], off
	s_barrier
	s_waitcnt lgkmcnt(0)
	s_waitcnt lgkmcnt(0)
	v_mfma_scale_f32_16x16x128_f8f6f4 v[128:131], v[132:139], v[148:155], v[2:5], v166, v166 op_sel_hi:[0,0,0]
	v_mfma_scale_f32_16x16x128_f8f6f4 v[92:95], v[140:147], v[148:155], v[6:9], v166, v166 op_sel_hi:[0,0,0]
	v_mfma_scale_f32_16x16x128_f8f6f4 v[64:67], v[132:139], v[156:163], v[10:13], v166, v166 op_sel_hi:[0,0,0]
	v_mfma_scale_f32_16x16x128_f8f6f4 v[60:63], v[140:147], v[156:163], v[14:17], v166, v166 op_sel_hi:[0,0,0]
	v_mfma_scale_f32_16x16x128_f8f6f4 v[30:33], v[132:139], v[170:177], v[18:21], v166, v166 op_sel_hi:[0,0,0]
	v_mfma_scale_f32_16x16x128_f8f6f4 v[26:29], v[140:147], v[170:177], v[22:25], v166, v166 op_sel_hi:[0,0,0]
	v_mfma_scale_f32_16x16x128_f8f6f4 v[14:17], v[132:139], v[178:185], v[84:87], v166, v166 op_sel_hi:[0,0,0]
	v_mfma_scale_f32_16x16x128_f8f6f4 v[10:13], v[140:147], v[178:185], v[204:207], v166, v166 op_sel_hi:[0,0,0]
	s_barrier
	s_add_u32 s0, s18, 0x20080
	s_addc_u32 s1, s19, 0
	s_add_u32 s2, s18, 0x30080
	s_addc_u32 s3, s19, 0
	s_mov_b32 m0, s58
	s_nop 0
	v_lshl_add_u64 v[2:3], s[0:1], 0, v[164:165]
	global_load_lds_dwordx4 v[2:3], off
	v_lshl_add_u64 v[2:3], s[2:3], 0, v[164:165]
	s_mov_b32 m0, s59
	s_nop 0
	global_load_lds_dwordx4 v[2:3], off
	s_waitcnt vmcnt(6)
	s_barrier
	v_mfma_scale_f32_16x16x128_f8f6f4 v[132:135], v[188:195], v[148:155], v[96:99], v166, v166 op_sel_hi:[0,0,0]
	v_mfma_scale_f32_16x16x128_f8f6f4 v[98:101], v[196:203], v[148:155], v[100:103], v166, v166 op_sel_hi:[0,0,0]
	v_mfma_scale_f32_16x16x128_f8f6f4 v[88:91], v[188:195], v[156:163], v[104:107], v166, v166 op_sel_hi:[0,0,0]
	v_mfma_scale_f32_16x16x128_f8f6f4 v[84:87], v[196:203], v[156:163], v[108:111], v166, v166 op_sel_hi:[0,0,0]
	v_mfma_scale_f32_16x16x128_f8f6f4 v[22:25], v[188:195], v[170:177], v[112:115], v166, v166 op_sel_hi:[0,0,0]
	v_mfma_scale_f32_16x16x128_f8f6f4 v[18:21], v[196:203], v[170:177], v[116:119], v166, v166 op_sel_hi:[0,0,0]
	v_mfma_scale_f32_16x16x128_f8f6f4 v[6:9], v[188:195], v[178:185], v[120:123], v166, v166 op_sel_hi:[0,0,0]
	v_mfma_scale_f32_16x16x128_f8f6f4 v[2:5], v[196:203], v[178:185], v[124:127], v166, v166 op_sel_hi:[0,0,0]
	v_mov_b32_e32 v34, v0
	s_barrier
; #define LAS __attribute__((address_space(3)))
; __device__ __forceinline__ unsigned cvt_pk4_fp8(float a, float b, float c, float d) { int w = 0; w = __builtin_amdgcn_cvt_pk_fp8_f32(a, b, w, false); w = __builtin_amdgcn_cvt_pk_fp8_f32(c, d, w, true); return (unsigned)w; }
; #define lds lds_hidden(lds0)
;     __device__ __forceinline__ void operator()(const f32x4 (&acc)[2][2][4][2], const Unit& u, int wr, int wc, int fr, int fq, LAS unsigned char* lds, int par) const {
;         LAS const float* tb = (LAS const float*)(lds + EPI_OFF + par * 2048);
; #pragma unroll
;         for (int ai = 0; ai < 2; ++ai)
; #pragma unroll
;             for (int mp = 0; mp < 2; ++mp) {
;                 u32x2 wv[2][2];
; #pragma unroll
;                 for (int mm = 0; mm < 2; ++mm) {
;                     const int ru = ai * HALF + wr * 64 + (mp * 2 + mm) * 16 + fr;
;                     const float g = tb[256 + ru] * Y8_SCALE;
; #pragma unroll
;                     for (int bj = 0; bj < 2; ++bj) {
;                         const int colu = bj * HALF + wc * 32 + 8 * fq;
;                         const f32x4 bd0 = *(LAS const f32x4*)(tb + colu), bd1 = *(LAS const f32x4*)(tb + colu + 4);
;                         const f32x4 v0 = (acc[ai][bj][mp * 2 + mm][0] * (1.f / (W8_SCALE * ACT8_SCALE * MX_SCALE)) + bd0) * g;
;                         const f32x4 v1 = (acc[ai][bj][mp * 2 + mm][1] * (1.f / (W8_SCALE * ACT8_SCALE * MX_SCALE)) + bd1) * g;
;                         wv[mm][bj].x = cvt_pk4_fp8(v0[0], v0[1], v0[2], v0[3]); wv[mm][bj].y = cvt_pk4_fp8(v1[0], v1[1], v1[2], v1[3]);
	s_add_i32 s2, s62, s15
	v_readfirstlane_b32 s0, v34
	s_and_b32 s3, s0, 0xffffff00
	s_bfe_u32 s1, s0, 0x20006
	v_and_b32_e32 v97, 15, v34
	s_add_i32 s3, s2, s3
	v_lshl_add_u32 v102, v97, 2, s3
	s_lshl_b32 s3, s1, 7
	v_lshlrev_b32_e32 v96, 1, v34
	s_add_i32 s2, s2, s3
	v_and_b32_e32 v96, 0x60, v96
	s_ashr_i32 s0, s0, 2
	v_add_u32_e32 v140, 0x400, v102
	v_add_u32_e32 v96, s2, v96
	s_andn2_b32 s0, s0, 63
	v_and_b32_e32 v103, 16, v34
	ds_read2_b32 v[112:113], v140 offset1:16
	v_or3_b32 v97, s0, v103, v97
	ds_read_b128 v[102:105], v96
	ds_read_b128 v[106:109], v96 offset:16
	s_mov_b32 s2, 0x3b800000
	s_add_i32 s0, s7, s68
	s_waitcnt lgkmcnt(0)
	v_mul_f32_e32 v112, 0x41800000, v112
	v_pk_fma_f32 v[110:111], v[210:211], s[2:3], v[104:105] op_sel_hi:[1,0,1]
	v_pk_fma_f32 v[114:115], v[208:209], s[2:3], v[102:103] op_sel_hi:[1,0,1]
	v_pk_mul_f32 v[116:117], v[110:111], v[112:113] op_sel_hi:[1,0]
	v_pk_fma_f32 v[110:111], v[214:215], s[2:3], v[108:109] op_sel_hi:[1,0,1]
	v_pk_mul_f32 v[114:115], v[114:115], v[112:113] op_sel_hi:[1,0]
	v_pk_mul_f32 v[120:121], v[112:113], v[110:111] op_sel_hi:[0,1]
	v_mov_b32_e32 v110, v35
	v_cvt_pk_fp8_f32 v110, v114, v115
	v_pk_fma_f32 v[118:119], v[212:213], s[2:3], v[106:107] op_sel_hi:[1,0,1]
	v_mov_b32_e32 v111, v35
	v_pk_mul_f32 v[118:119], v[112:113], v[118:119] op_sel_hi:[0,1]
	v_cvt_pk_fp8_f32 v110, v116, v117 op_sel:[0,0,1]
	ds_read_b128 v[114:117], v96 offset:512
	v_cvt_pk_fp8_f32 v111, v118, v119
	v_pk_fma_f32 v[80:81], v[80:81], s[2:3], v[102:103] op_sel_hi:[1,0,1]
	v_pk_fma_f32 v[72:73], v[72:73], s[2:3], v[106:107] op_sel_hi:[1,0,1]
	v_pk_fma_f32 v[82:83], v[82:83], s[2:3], v[104:105] op_sel_hi:[1,0,1]
	v_cvt_pk_fp8_f32 v111, v120, v121 op_sel:[0,0,1]
	s_waitcnt lgkmcnt(0)
	v_pk_fma_f32 v[118:119], v[218:219], s[2:3], v[116:117] op_sel_hi:[1,0,1]
	v_pk_fma_f32 v[120:121], v[216:217], s[2:3], v[114:115] op_sel_hi:[1,0,1]
	v_pk_mul_f32 v[124:125], v[112:113], v[118:119] op_sel_hi:[0,1]
	v_pk_mul_f32 v[126:127], v[112:113], v[120:121] op_sel_hi:[0,1]
	ds_read_b128 v[118:121], v96 offset:528
	v_pk_fma_f32 v[74:75], v[74:75], s[2:3], v[108:109] op_sel_hi:[1,0,1]
	s_lshl_b32 s90, s1, 5
	v_lshrrev_b32_e32 v34, 1, v34
	v_and_b32_e32 v34, 16, v34
	s_waitcnt lgkmcnt(0)
	v_pk_fma_f32 v[122:123], v[222:223], s[2:3], v[120:121] op_sel_hi:[1,0,1]
	v_pk_fma_f32 v[136:137], v[220:221], s[2:3], v[118:119] op_sel_hi:[1,0,1]
	v_pk_mul_f32 v[138:139], v[112:113], v[122:123] op_sel_hi:[0,1]
	v_mov_b32_e32 v122, v35
	v_cvt_pk_fp8_f32 v122, v126, v127
	v_pk_mul_f32 v[136:137], v[112:113], v[136:137] op_sel_hi:[0,1]
	v_mov_b32_e32 v112, v35
	v_mov_b32_e32 v123, v35
	v_cvt_pk_fp8_f32 v122, v124, v125 op_sel:[0,0,1]
	v_mul_f32_e32 v124, 0x41800000, v113
	v_pk_mul_f32 v[80:81], v[80:81], v[124:125] op_sel_hi:[1,0]
	v_pk_mul_f32 v[72:73], v[72:73], v[124:125] op_sel_hi:[1,0]
	v_mov_b32_e32 v113, v35
	v_cvt_pk_fp8_f32 v112, v80, v81
	v_cvt_pk_fp8_f32 v113, v72, v73
	v_pk_mul_f32 v[82:83], v[82:83], v[124:125] op_sel_hi:[1,0]
	v_pk_mul_f32 v[74:75], v[74:75], v[124:125] op_sel_hi:[1,0]
	v_cvt_pk_fp8_f32 v112, v82, v83 op_sel:[0,0,1]
	v_cvt_pk_fp8_f32 v113, v74, v75 op_sel:[0,0,1]
	v_pk_fma_f32 v[72:73], v[226:227], s[2:3], v[116:117] op_sel_hi:[1,0,1]
	v_pk_fma_f32 v[74:75], v[224:225], s[2:3], v[114:115] op_sel_hi:[1,0,1]
	v_pk_fma_f32 v[80:81], v[230:231], s[2:3], v[120:121] op_sel_hi:[1,0,1]
	v_pk_fma_f32 v[82:83], v[228:229], s[2:3], v[118:119] op_sel_hi:[1,0,1]
	v_pk_mul_f32 v[72:73], v[72:73], v[124:125] op_sel_hi:[1,0]
	v_pk_mul_f32 v[74:75], v[74:75], v[124:125] op_sel_hi:[1,0]
	v_pk_mul_f32 v[80:81], v[80:81], v[124:125] op_sel_hi:[1,0]
	v_pk_mul_f32 v[82:83], v[82:83], v[124:125] op_sel_hi:[1,0]
	v_mov_b32_e32 v124, v35
	v_cvt_pk_fp8_f32 v124, v74, v75
	v_mov_b32_e32 v125, v35
	v_cvt_pk_fp8_f32 v123, v136, v137
	v_cvt_pk_fp8_f32 v125, v82, v83
	v_cvt_pk_fp8_f32 v124, v72, v73 op_sel:[0,0,1]
	v_add_u32_e32 v72, s0, v97
	v_ashrrev_i32_e32 v73, 31, v72
	v_cvt_pk_fp8_f32 v123, v138, v139 op_sel:[0,0,1]
	v_cvt_pk_fp8_f32 v125, v80, v81 op_sel:[0,0,1]
	v_lshlrev_b64 v[74:75], 10, v[72:73]
	v_lshl_add_u64 v[74:75], s[10:11], 0, v[74:75]
	v_lshl_add_u64 v[74:75], v[74:75], 0, s[20:21]
	v_lshl_add_u64 v[74:75], v[74:75], 0, s[90:91]
	v_permlane16_swap_b32_e32 v110, v112
	v_permlane16_swap_b32_e32 v111, v113
	v_lshl_add_u64 v[74:75], v[74:75], 0, v[34:35]
	v_permlane16_swap_b32_e32 v122, v124
	v_permlane16_swap_b32_e32 v123, v125
	global_store_dwordx4 v[74:75], v[110:113], off
	global_store_dwordx4 v[74:75], v[122:125], off offset:128
	ds_read2_b32 v[74:75], v140 offset0:32 offset1:48
	v_pk_fma_f32 v[48:49], v[48:49], s[2:3], v[102:103] op_sel_hi:[1,0,1]
	v_pk_fma_f32 v[44:45], v[44:45], s[2:3], v[106:107] op_sel_hi:[1,0,1]
	v_pk_fma_f32 v[50:51], v[50:51], s[2:3], v[104:105] op_sel_hi:[1,0,1]
	v_pk_fma_f32 v[46:47], v[46:47], s[2:3], v[108:109] op_sel_hi:[1,0,1]
	s_waitcnt lgkmcnt(0)
; #define LAS __attribute__((address_space(3)))
; __device__ __forceinline__ unsigned cvt_pk4_fp8(float a, float b, float c, float d) { int w = 0; w = __builtin_amdgcn_cvt_pk_fp8_f32(a, b, w, false); w = __builtin_amdgcn_cvt_pk_fp8_f32(c, d, w, true); return (unsigned)w; }
;     __device__ __forceinline__ void operator()(const f32x4 (&acc)[2][2][4][2], const Unit& u, int wr, int wc, int fr, int fq, LAS unsigned char* lds, int par) const {
;     ...
;         for (int ai = 0; ai < 2; ++ai)
; #pragma unroll
;             for (int mp = 0; mp < 2; ++mp) {
;                 u32x2 wv[2][2];
; #pragma unroll
;                 for (int mm = 0; mm < 2; ++mm) {
;                     const int ru = ai * HALF + wr * 64 + (mp * 2 + mm) * 16 + fr;
;                     const float g = tb[256 + ru] * Y8_SCALE;
; #pragma unroll
;                     for (int bj = 0; bj < 2; ++bj) {
;                         const int colu = bj * HALF + wc * 32 + 8 * fq;
;                         const f32x4 bd0 = *(LAS const f32x4*)(tb + colu), bd1 = *(LAS const f32x4*)(tb + colu + 4);
;                         const f32x4 v0 = (acc[ai][bj][mp * 2 + mm][0] * (1.f / (W8_SCALE * ACT8_SCALE * MX_SCALE)) + bd0) * g;
;                         const f32x4 v1 = (acc[ai][bj][mp * 2 + mm][1] * (1.f / (W8_SCALE * ACT8_SCALE * MX_SCALE)) + bd1) * g;
;                         wv[mm][bj].x = cvt_pk4_fp8(v0[0], v0[1], v0[2], v0[3]); wv[mm][bj].y = cvt_pk4_fp8(v1[0], v1[1], v1[2], v1[3]);
;                     }
;                 }
;                 const int ro = u.rowbase + u.rt * BM + ai * HALF + wr * 64 + (mp * 2 + (fq & 1)) * 16 + fr;
; #pragma unroll
;                 for (int bj = 0; bj < 2; ++bj) {
;                     const u32x2 sx = __builtin_amdgcn_permlane16_swap(wv[0][bj].x, wv[1][bj].x, false, false), sy = __builtin_amdgcn_permlane16_swap(wv[0][bj].y, wv[1][bj].y, false, false);
;                     *(u32x4*)(y + (size_t)ro * D + u.pn * BM + bj * HALF + wc * 32 + 8 * (fq & ~1)) = (u32x4){sx.x, sy.x, sx.y, sy.y};
;                 }
	v_mul_f32_e32 v74, 0x41800000, v74
	v_pk_mul_f32 v[48:49], v[48:49], v[74:75] op_sel_hi:[1,0]
	v_pk_mul_f32 v[80:81], v[74:75], v[44:45] op_sel_hi:[0,1]
	v_mov_b32_e32 v44, v35
	v_cvt_pk_fp8_f32 v44, v48, v49
	v_pk_mul_f32 v[50:51], v[50:51], v[74:75] op_sel_hi:[1,0]
	v_mov_b32_e32 v45, v35
	v_pk_fma_f32 v[48:49], v[76:77], s[2:3], v[114:115] op_sel_hi:[1,0,1]
	v_cvt_pk_fp8_f32 v44, v50, v51 op_sel:[0,0,1]
	v_cvt_pk_fp8_f32 v45, v80, v81
	v_pk_mul_f32 v[50:51], v[74:75], v[48:49] op_sel_hi:[0,1]
	v_pk_fma_f32 v[48:49], v[70:71], s[2:3], v[120:121] op_sel_hi:[1,0,1]
	v_pk_mul_f32 v[46:47], v[74:75], v[46:47] op_sel_hi:[0,1]
	v_pk_mul_f32 v[70:71], v[74:75], v[48:49] op_sel_hi:[0,1]
	v_mov_b32_e32 v48, v35
	v_cvt_pk_fp8_f32 v48, v50, v51
	v_cvt_pk_fp8_f32 v45, v46, v47 op_sel:[0,0,1]
	v_pk_fma_f32 v[46:47], v[78:79], s[2:3], v[116:117] op_sel_hi:[1,0,1]
	v_mul_f32_e32 v50, 0x41800000, v75
	v_pk_mul_f32 v[46:47], v[74:75], v[46:47] op_sel_hi:[0,1]
	v_pk_fma_f32 v[40:41], v[40:41], s[2:3], v[102:103] op_sel_hi:[1,0,1]
	v_pk_fma_f32 v[36:37], v[36:37], s[2:3], v[106:107] op_sel_hi:[1,0,1]
	v_cvt_pk_fp8_f32 v48, v46, v47 op_sel:[0,0,1]
	v_pk_mul_f32 v[40:41], v[40:41], v[50:51] op_sel_hi:[1,0]
	v_pk_mul_f32 v[36:37], v[36:37], v[50:51] op_sel_hi:[1,0]
	v_mov_b32_e32 v46, v35
	v_mov_b32_e32 v47, v35
	v_cvt_pk_fp8_f32 v46, v40, v41
	v_cvt_pk_fp8_f32 v47, v36, v37
	v_pk_fma_f32 v[42:43], v[42:43], s[2:3], v[104:105] op_sel_hi:[1,0,1]
	v_pk_fma_f32 v[38:39], v[38:39], s[2:3], v[108:109] op_sel_hi:[1,0,1]
	v_pk_mul_f32 v[42:43], v[42:43], v[50:51] op_sel_hi:[1,0]
	v_pk_mul_f32 v[38:39], v[38:39], v[50:51] op_sel_hi:[1,0]
	v_cvt_pk_fp8_f32 v46, v42, v43 op_sel:[0,0,1]
	v_cvt_pk_fp8_f32 v47, v38, v39 op_sel:[0,0,1]
	v_pk_fma_f32 v[36:37], v[58:59], s[2:3], v[116:117] op_sel_hi:[1,0,1]
	v_pk_fma_f32 v[38:39], v[56:57], s[2:3], v[114:115] op_sel_hi:[1,0,1]
	v_pk_fma_f32 v[40:41], v[54:55], s[2:3], v[120:121] op_sel_hi:[1,0,1]
	v_pk_fma_f32 v[42:43], v[52:53], s[2:3], v[118:119] op_sel_hi:[1,0,1]
	v_pk_mul_f32 v[36:37], v[36:37], v[50:51] op_sel_hi:[1,0]
	v_pk_mul_f32 v[38:39], v[38:39], v[50:51] op_sel_hi:[1,0]
	v_pk_mul_f32 v[40:41], v[40:41], v[50:51] op_sel_hi:[1,0]
	v_pk_mul_f32 v[42:43], v[42:43], v[50:51] op_sel_hi:[1,0]
	v_mov_b32_e32 v50, v35
	v_pk_fma_f32 v[68:69], v[68:69], s[2:3], v[118:119] op_sel_hi:[1,0,1]
	v_cvt_pk_fp8_f32 v50, v38, v39
	v_pk_mul_f32 v[68:69], v[74:75], v[68:69] op_sel_hi:[0,1]
	v_mov_b32_e32 v49, v35
	v_mov_b32_e32 v51, v35
	v_cvt_pk_fp8_f32 v49, v68, v69
	v_cvt_pk_fp8_f32 v51, v42, v43
	v_cvt_pk_fp8_f32 v50, v36, v37 op_sel:[0,0,1]
	v_add_u32_e32 v36, 32, v72
	v_ashrrev_i32_e32 v37, 31, v36
	v_cvt_pk_fp8_f32 v49, v70, v71 op_sel:[0,0,1]
	v_cvt_pk_fp8_f32 v51, v40, v41 op_sel:[0,0,1]
	v_lshlrev_b64 v[36:37], 10, v[36:37]
	ds_read2_b32 v[38:39], v140 offset0:128 offset1:144
	v_lshl_add_u64 v[36:37], s[10:11], 0, v[36:37]
	v_lshl_add_u64 v[36:37], v[36:37], 0, s[20:21]
	v_lshl_add_u64 v[36:37], v[36:37], 0, s[90:91]
	v_permlane16_swap_b32_e32 v44, v46
	v_permlane16_swap_b32_e32 v45, v47
	v_lshl_add_u64 v[36:37], v[36:37], 0, v[34:35]
	v_permlane16_swap_b32_e32 v48, v50
	v_permlane16_swap_b32_e32 v49, v51
	global_store_dwordx4 v[36:37], v[44:47], off
	global_store_dwordx4 v[36:37], v[48:51], off offset:128
	s_waitcnt lgkmcnt(0)
	v_mul_f32_e32 v38, 0x41800000, v38
	v_pk_fma_f32 v[36:37], v[130:131], s[2:3], v[104:105] op_sel_hi:[1,0,1]
	v_pk_fma_f32 v[40:41], v[128:129], s[2:3], v[102:103] op_sel_hi:[1,0,1]
	v_pk_mul_f32 v[42:43], v[36:37], v[38:39] op_sel_hi:[1,0]
	v_pk_fma_f32 v[36:37], v[94:95], s[2:3], v[108:109] op_sel_hi:[1,0,1]
	v_pk_fma_f32 v[44:45], v[92:93], s[2:3], v[106:107] op_sel_hi:[1,0,1]
	v_pk_mul_f32 v[40:41], v[40:41], v[38:39] op_sel_hi:[1,0]
	v_pk_mul_f32 v[46:47], v[38:39], v[36:37] op_sel_hi:[0,1]
	v_pk_mul_f32 v[44:45], v[38:39], v[44:45] op_sel_hi:[0,1]
	v_mov_b32_e32 v36, v35
	v_mov_b32_e32 v37, v35
	v_cvt_pk_fp8_f32 v36, v40, v41
	v_cvt_pk_fp8_f32 v37, v44, v45
	v_pk_fma_f32 v[40:41], v[134:135], s[2:3], v[116:117] op_sel_hi:[1,0,1]
	s_xor_b32 s63, s63, 1
	v_cvt_pk_fp8_f32 v36, v42, v43 op_sel:[0,0,1]
	v_cvt_pk_fp8_f32 v37, v46, v47 op_sel:[0,0,1]
	v_pk_fma_f32 v[42:43], v[132:133], s[2:3], v[114:115] op_sel_hi:[1,0,1]
	v_pk_mul_f32 v[44:45], v[38:39], v[40:41] op_sel_hi:[0,1]
	v_pk_fma_f32 v[40:41], v[100:101], s[2:3], v[120:121] op_sel_hi:[1,0,1]
	v_pk_fma_f32 v[46:47], v[98:99], s[2:3], v[118:119] op_sel_hi:[1,0,1]
	v_pk_mul_f32 v[42:43], v[38:39], v[42:43] op_sel_hi:[0,1]
	v_pk_mul_f32 v[48:49], v[38:39], v[40:41] op_sel_hi:[0,1]
	v_pk_mul_f32 v[46:47], v[38:39], v[46:47] op_sel_hi:[0,1]
	v_mov_b32_e32 v40, v35
	v_mov_b32_e32 v41, v35
	v_cvt_pk_fp8_f32 v40, v42, v43
	v_cvt_pk_fp8_f32 v41, v46, v47
	v_mul_f32_e32 v42, 0x41800000, v39
	v_pk_fma_f32 v[38:39], v[66:67], s[2:3], v[104:105] op_sel_hi:[1,0,1]
	v_cvt_pk_fp8_f32 v40, v44, v45 op_sel:[0,0,1]
	v_cvt_pk_fp8_f32 v41, v48, v49 op_sel:[0,0,1]
	v_pk_fma_f32 v[44:45], v[64:65], s[2:3], v[102:103] op_sel_hi:[1,0,1]
	v_pk_mul_f32 v[46:47], v[38:39], v[42:43] op_sel_hi:[1,0]
	v_pk_fma_f32 v[38:39], v[62:63], s[2:3], v[108:109] op_sel_hi:[1,0,1]
	v_pk_fma_f32 v[48:49], v[60:61], s[2:3], v[106:107] op_sel_hi:[1,0,1]
	v_pk_mul_f32 v[44:45], v[44:45], v[42:43] op_sel_hi:[1,0]
	v_pk_mul_f32 v[50:51], v[38:39], v[42:43] op_sel_hi:[1,0]
	v_pk_mul_f32 v[48:49], v[48:49], v[42:43] op_sel_hi:[1,0]
	v_mov_b32_e32 v38, v35
; #define LAS __attribute__((address_space(3)))
; template <class Epi, class Src>
; __device__ __forceinline__ void gemm_phase(LAS unsigned char* lds, const Src S, const Epi E) {
;     ...
;         if (!has_next) break;
; #pragma unroll
;         for (int a = 0; a < 2; ++a)
; #pragma unroll
;             for (int b = 0; b < 2; ++b)
; #pragma unroll
;                 for (int m = 0; m < 4; ++m)
; #pragma unroll
;                     for (int n = 0; n < 2; ++n) acc[a][b][m][n] = (f32x4){0.f, 0.f, 0.f, 0.f};
;         cur = nxt; cB = nB; cA = nA; ++ui; par ^= 1;
;     __device__ __forceinline__ void operator()(const f32x4 (&acc)[2][2][4][2], const Unit& u, int wr, int wc, int fr, int fq, LAS unsigned char* lds, int par) const {
;     ...
;         for (int ai = 0; ai < 2; ++ai)
; #pragma unroll
;             for (int mp = 0; mp < 2; ++mp) {
;                 u32x2 wv[2][2];
; #pragma unroll
;                 for (int mm = 0; mm < 2; ++mm) {
;                     const int ru = ai * HALF + wr * 64 + (mp * 2 + mm) * 16 + fr;
;                     const float g = tb[256 + ru] * Y8_SCALE;
; #pragma unroll
;                     for (int bj = 0; bj < 2; ++bj) {
;                         const int colu = bj * HALF + wc * 32 + 8 * fq;
;                         const f32x4 bd0 = *(LAS const f32x4*)(tb + colu), bd1 = *(LAS const f32x4*)(tb + colu + 4);
;                         const f32x4 v0 = (acc[ai][bj][mp * 2 + mm][0] * (1.f / (W8_SCALE * ACT8_SCALE * MX_SCALE)) + bd0) * g;
;                         const f32x4 v1 = (acc[ai][bj][mp * 2 + mm][1] * (1.f / (W8_SCALE * ACT8_SCALE * MX_SCALE)) + bd1) * g;
;                         wv[mm][bj].x = cvt_pk4_fp8(v0[0], v0[1], v0[2], v0[3]); wv[mm][bj].y = cvt_pk4_fp8(v1[0], v1[1], v1[2], v1[3]);
;                     }
;                 }
;                 const int ro = u.rowbase + u.rt * BM + ai * HALF + wr * 64 + (mp * 2 + (fq & 1)) * 16 + fr;
; #pragma unroll
;                 for (int bj = 0; bj < 2; ++bj) {
;                     const u32x2 sx = __builtin_amdgcn_permlane16_swap(wv[0][bj].x, wv[1][bj].x, false, false), sy = __builtin_amdgcn_permlane16_swap(wv[0][bj].y, wv[1][bj].y, false, false);
;                     *(u32x4*)(y + (size_t)ro * D + u.pn * BM + bj * HALF + wc * 32 + 8 * (fq & ~1)) = (u32x4){sx.x, sy.x, sx.y, sy.y};
;                 }
	v_mov_b32_e32 v39, v35
	v_cvt_pk_fp8_f32 v38, v44, v45
	v_cvt_pk_fp8_f32 v39, v48, v49
	v_pk_fma_f32 v[44:45], v[90:91], s[2:3], v[116:117] op_sel_hi:[1,0,1]
	v_pk_fma_f32 v[48:49], v[86:87], s[2:3], v[120:121] op_sel_hi:[1,0,1]
	v_cvt_pk_fp8_f32 v38, v46, v47 op_sel:[0,0,1]
	v_cvt_pk_fp8_f32 v39, v50, v51 op_sel:[0,0,1]
	v_pk_fma_f32 v[46:47], v[88:89], s[2:3], v[114:115] op_sel_hi:[1,0,1]
	v_pk_fma_f32 v[50:51], v[84:85], s[2:3], v[118:119] op_sel_hi:[1,0,1]
	v_pk_mul_f32 v[44:45], v[44:45], v[42:43] op_sel_hi:[1,0]
	v_pk_mul_f32 v[46:47], v[46:47], v[42:43] op_sel_hi:[1,0]
	v_pk_mul_f32 v[48:49], v[48:49], v[42:43] op_sel_hi:[1,0]
	v_pk_mul_f32 v[50:51], v[50:51], v[42:43] op_sel_hi:[1,0]
	v_mov_b32_e32 v42, v35
	v_cvt_pk_fp8_f32 v42, v46, v47
	v_mov_b32_e32 v43, v35
	v_cvt_pk_fp8_f32 v43, v50, v51
	v_permlane16_swap_b32_e32 v36, v38
	v_cvt_pk_fp8_f32 v42, v44, v45 op_sel:[0,0,1]
	v_add_u32_e32 v44, 0x80, v72
	v_ashrrev_i32_e32 v45, 31, v44
	v_cvt_pk_fp8_f32 v43, v48, v49 op_sel:[0,0,1]
	v_lshlrev_b64 v[44:45], 10, v[44:45]
	v_lshl_add_u64 v[44:45], s[10:11], 0, v[44:45]
	v_lshl_add_u64 v[44:45], v[44:45], 0, s[20:21]
	v_lshl_add_u64 v[44:45], v[44:45], 0, s[90:91]
	v_permlane16_swap_b32_e32 v37, v39
	v_lshl_add_u64 v[44:45], v[44:45], 0, v[34:35]
	v_permlane16_swap_b32_e32 v40, v42
	v_permlane16_swap_b32_e32 v41, v43
	global_store_dwordx4 v[44:45], v[36:39], off
	global_store_dwordx4 v[44:45], v[40:43], off offset:128
	ds_read2_b32 v[48:49], v140 offset0:160 offset1:176
	ds_read_b128 v[36:39], v96
	ds_read_b128 v[40:43], v96 offset:16
	s_andn2_b64 vcc, exec, s[16:17]
	s_mov_b32 s68, s67
	s_mov_b32 s70, s65
	s_waitcnt lgkmcnt(0)
	v_mul_f32_e32 v48, 0x41800000, v48
	v_pk_fma_f32 v[30:31], v[30:31], s[2:3], v[36:37] op_sel_hi:[1,0,1]
	v_pk_fma_f32 v[26:27], v[26:27], s[2:3], v[40:41] op_sel_hi:[1,0,1]
	v_pk_mul_f32 v[30:31], v[30:31], v[48:49] op_sel_hi:[1,0]
	v_pk_mul_f32 v[44:45], v[48:49], v[26:27] op_sel_hi:[0,1]
	v_mov_b32_e32 v26, v35
	v_cvt_pk_fp8_f32 v26, v30, v31
	v_pk_fma_f32 v[32:33], v[32:33], s[2:3], v[38:39] op_sel_hi:[1,0,1]
	v_mov_b32_e32 v27, v35
	v_pk_mul_f32 v[32:33], v[32:33], v[48:49] op_sel_hi:[1,0]
	v_cvt_pk_fp8_f32 v27, v44, v45
	v_cvt_pk_fp8_f32 v26, v32, v33 op_sel:[0,0,1]
	ds_read_b128 v[30:33], v96 offset:512
	ds_read_b128 v[44:47], v96 offset:528
	v_pk_fma_f32 v[28:29], v[28:29], s[2:3], v[42:43] op_sel_hi:[1,0,1]
	v_pk_fma_f32 v[16:17], v[16:17], s[2:3], v[38:39] op_sel_hi:[1,0,1]
	v_pk_mul_f32 v[28:29], v[48:49], v[28:29] op_sel_hi:[0,1]
	v_cvt_pk_fp8_f32 v27, v28, v29 op_sel:[0,0,1]
	s_waitcnt lgkmcnt(0)
	v_pk_fma_f32 v[18:19], v[18:19], s[2:3], v[44:45] op_sel_hi:[1,0,1]
	v_pk_fma_f32 v[20:21], v[20:21], s[2:3], v[46:47] op_sel_hi:[1,0,1]
	v_pk_mul_f32 v[28:29], v[48:49], v[18:19] op_sel_hi:[0,1]
	v_mov_b32_e32 v19, v35
	v_cvt_pk_fp8_f32 v19, v28, v29
	v_pk_mul_f32 v[20:21], v[48:49], v[20:21] op_sel_hi:[0,1]
	v_pk_fma_f32 v[22:23], v[22:23], s[2:3], v[30:31] op_sel_hi:[1,0,1]
	v_pk_fma_f32 v[14:15], v[14:15], s[2:3], v[36:37] op_sel_hi:[1,0,1]
	v_cvt_pk_fp8_f32 v19, v20, v21 op_sel:[0,0,1]
	v_mul_f32_e32 v20, 0x41800000, v49
	v_pk_fma_f32 v[12:13], v[12:13], s[2:3], v[42:43] op_sel_hi:[1,0,1]
	v_pk_fma_f32 v[10:11], v[10:11], s[2:3], v[40:41] op_sel_hi:[1,0,1]
	v_pk_fma_f32 v[8:9], v[8:9], s[2:3], v[32:33] op_sel_hi:[1,0,1]
	v_pk_fma_f32 v[6:7], v[6:7], s[2:3], v[30:31] op_sel_hi:[1,0,1]
	v_pk_fma_f32 v[4:5], v[4:5], s[2:3], v[46:47] op_sel_hi:[1,0,1]
	v_pk_fma_f32 v[2:3], v[2:3], s[2:3], v[44:45] op_sel_hi:[1,0,1]
	v_pk_mul_f32 v[22:23], v[48:49], v[22:23] op_sel_hi:[0,1]
	v_mov_b32_e32 v18, v35
	v_pk_mul_f32 v[16:17], v[16:17], v[20:21] op_sel_hi:[1,0]
	v_pk_mul_f32 v[14:15], v[14:15], v[20:21] op_sel_hi:[1,0]
	v_pk_mul_f32 v[12:13], v[12:13], v[20:21] op_sel_hi:[1,0]
	v_pk_mul_f32 v[10:11], v[10:11], v[20:21] op_sel_hi:[1,0]
	v_mov_b32_e32 v28, v35
	v_mov_b32_e32 v29, v35
	v_pk_mul_f32 v[8:9], v[8:9], v[20:21] op_sel_hi:[1,0]
	v_pk_mul_f32 v[6:7], v[6:7], v[20:21] op_sel_hi:[1,0]
	v_pk_mul_f32 v[4:5], v[4:5], v[20:21] op_sel_hi:[1,0]
	v_pk_mul_f32 v[2:3], v[2:3], v[20:21] op_sel_hi:[1,0]
	v_mov_b32_e32 v20, v35
	v_mov_b32_e32 v21, v35
	v_cvt_pk_fp8_f32 v18, v22, v23
	v_cvt_pk_fp8_f32 v28, v14, v15
	v_cvt_pk_fp8_f32 v29, v10, v11
	v_cvt_pk_fp8_f32 v20, v6, v7
	v_cvt_pk_fp8_f32 v21, v2, v3
	v_pk_fma_f32 v[24:25], v[24:25], s[2:3], v[32:33] op_sel_hi:[1,0,1]
	v_add_u32_e32 v2, 0xa0, v72
	v_pk_mul_f32 v[24:25], v[48:49], v[24:25] op_sel_hi:[0,1]
	v_ashrrev_i32_e32 v3, 31, v2
	v_cvt_pk_fp8_f32 v18, v24, v25 op_sel:[0,0,1]
	v_cvt_pk_fp8_f32 v28, v16, v17 op_sel:[0,0,1]
	v_cvt_pk_fp8_f32 v29, v12, v13 op_sel:[0,0,1]
	v_cvt_pk_fp8_f32 v20, v8, v9 op_sel:[0,0,1]
	v_cvt_pk_fp8_f32 v21, v4, v5 op_sel:[0,0,1]
	v_lshlrev_b64 v[2:3], 10, v[2:3]
	v_lshl_add_u64 v[2:3], s[10:11], 0, v[2:3]
	v_lshl_add_u64 v[2:3], v[2:3], 0, s[20:21]
	v_lshl_add_u64 v[2:3], v[2:3], 0, s[90:91]
	v_permlane16_swap_b32_e32 v26, v28
	v_permlane16_swap_b32_e32 v27, v29
	v_lshl_add_u64 v[2:3], v[2:3], 0, v[34:35]
	v_permlane16_swap_b32_e32 v18, v20
	v_permlane16_swap_b32_e32 v19, v21
	s_mov_b32 s26, s14
	s_mov_b32 s69, s66
	s_mov_b32 s24, s6
	s_mov_b32 s21, s67
	s_mov_b32 s20, s65
	s_mov_b32 s7, s14
	s_mov_b32 s15, s66
	s_mov_b32 s25, s6
	s_mov_b64 s[0:1], s[22:23]
	s_mov_b64 s[2:3], s[18:19]
	global_store_dwordx4 v[2:3], v[26:29], off
	global_store_dwordx4 v[2:3], v[18:21], off offset:128
	s_cbranch_vccz .LBB0_1421
